# final3 + 389 provably dead zero-init v_mov before fp8/bf8 pack pairs removed kernel-wide (same basic block: plain cvt writes low half, op_sel cvt writes high half)
# speedup vs baseline: 1.0003x; 1.0003x over previous
; __device__ __forceinline__ u32x4 pack8(const f32x4 a, const f32x4 b) { u32x4 w; w.x = cvt_pk_bf16(a[0], a[1]); w.y = cvt_pk_bf16(a[2], a[3]); w.z = cvt_pk_bf16(b[0], b[1]); w.w = cvt_pk_bf16(b[2], b[3]); return w; }
;     __device__ __forceinline__ void operator()(const f32x4 (&acc)[2][2][4][2], const Unit& u, int wr, int wc, int fr_in, int fq_in) const {
;     ...
;             for (int ai = 0; ai < 2; ++ai)
; #pragma unroll
;                 for (int m = 0; m < 4; ++m) {
;                     const int row = row0 + ai * HALF + m * 16; const float r = t[ai * 64 + m * 16 + fr] * sc;
;                     f32x4 v0 = acc[ai][bj][m][0] * r, v1 = acc[ai][bj][m][1] * r;
;                     if (kind == 2) rope8(v0, v1, rcos, rsin, row & (SEQ_ - 1), fq);
;                     *(u32x4*)(dst + (size_t)row * pitch + 8 * fq) = pack8(v0, v1);
;                     if (f8ch && colg >= 768 && colg < 1280) { u32x2 w8; w8.x = pack4_fp8_x16(v0); w8.y = pack4_fp8_x16(v1); *(u32x2*)(ws + WS_QB8 + (size_t)row * 512 + (colg - 768) + 8 * fq) = w8; }
;                     if (f8ch && colg >= 1280 && colg < 1792) { u32x2 w8; w8.x = pack4_fp8_x8(v0); w8.y = pack4_fp8_x8(v1); *(u32x2*)(ws + WS_KB8 + (size_t)row * 512 + (colg - 1280) + 8 * fq) = w8; }
;                     if (f8ch && colg >= 1792) {
;                         const int c0_ = colg - 1792 + 8 * fq, bb_ = row >> 13, pos_ = row & (SEQ_ - 1), key_ = pos_ & 63, k32_ = key_ & 31;
;                         unsigned char* p_ = ws + WS_VB8T + ((((size_t)(bb_ * 8 + (c0_ >> 6)) * 128 + (pos_ >> 6)) * 64 + (c0_ & 63)) * 64) + 32 * ((k32_ >> 2) & 1) + 16 * (key_ >> 5) + (k32_ & 3) + 4 * (k32_ >> 3);
;                         const unsigned w0_ = pack4_fp8_x8(v0), w1_ = pack4_fp8_x8(v1);
; #pragma unroll
;                         for (int e_ = 0; e_ < 4; ++e_) { p_[e_ * 64] = (unsigned char)((w0_ >> (8 * e_)) & 0xffu); p_[(4 + e_) * 64] = (unsigned char)((w1_ >> (8 * e_)) & 0xffu); }
;                     }
;                     if (kind == 2 && f8qk) { u32x2 w8; w8.x = pack4_fp8_x8(v0); w8.y = pack4_fp8_x8(v1); *(u32x2*)(ws + WS_KR8 + (size_t)row * 32 + 8 * fq) = w8; }
.LBB0_75:
	v_ashrrev_i32_e32 v15, 31, v14
	v_mul_lo_u32 v30, s55, v14
	v_mul_lo_u32 v31, s54, v15
	v_mad_u64_u32 v[28:29], s[14:15], s54, v14, 0
	v_lshl_add_u64 v[16:17], v[6:7], 1, s[12:13]
	v_add3_u32 v29, v29, v31, v30
	s_add_i32 s9, s94, 0xfffffd00
	v_cvt_pk_bf16_f32 v22, v2, v3
	v_cvt_pk_bf16_f32 v23, v4, v5
	v_lshl_add_u64 v[28:29], v[28:29], 1, v[16:17]
	s_cmpk_lt_u32 s9, 0x200
	v_cvt_pk_bf16_f32 v24, v20, v21
	v_cvt_pk_bf16_f32 v25, v18, v19
	global_store_dwordx4 v[28:29], v[22:25], off
	s_cselect_b64 s[12:13], -1, 0
	s_cmpk_gt_u32 s9, 0x1ff
	v_lshlrev_b64 v[22:23], 9, v[14:15]
	v_lshl_add_u64 v[22:23], s[18:19], 0, v[22:23]
	s_cbranch_scc1 .LBB0_77
	v_mul_f32_e32 v24, 0x41800000, v2
	v_med3_f32 v25, v24, s64, v250
	v_mul_f32_e32 v24, 0x41800000, v3
	v_med3_f32 v28, v24, s64, v250
	v_cvt_pk_fp8_f32 v24, v25, v28
	v_mul_f32_e32 v25, 0x41800000, v4
	v_mul_f32_e32 v28, 0x41800000, v5
	v_med3_f32 v25, v25, s64, v250
	v_med3_f32 v28, v28, s64, v250
	v_cvt_pk_fp8_f32 v24, v25, v28 op_sel:[0,0,1]
	v_mul_f32_e32 v25, 0x41800000, v20
	v_med3_f32 v28, v25, s64, v250
	v_mul_f32_e32 v25, 0x41800000, v21
	v_med3_f32 v29, v25, s64, v250
	v_cvt_pk_fp8_f32 v25, v28, v29
	v_mul_f32_e32 v28, 0x41800000, v18
	v_mul_f32_e32 v29, 0x41800000, v19
	v_med3_f32 v28, v28, s64, v250
	v_med3_f32 v29, v29, s64, v250
	v_cvt_pk_fp8_f32 v25, v28, v29 op_sel:[0,0,1]
	v_lshl_add_u64 v[28:29], v[22:23], 0, s[68:69]
	v_lshl_add_u64 v[28:29], v[28:29], 0, v[6:7]
	v_add_co_u32_e32 v28, vcc, 0x332ff000, v28
	s_nop 1
	v_addc_co_u32_e32 v29, vcc, 0, v29, vcc
	global_store_dwordx2 v[28:29], v[24:25], off offset:3328
.LBB0_77:
	s_add_i32 s9, s94, 0xfffffb00
	s_cmpk_lt_u32 s9, 0x200
	v_mul_f32_e32 v24, 0x41000000, v2
	v_mul_f32_e32 v25, 0x41000000, v3
	v_mul_f32_e32 v28, 0x41000000, v4
	v_mul_f32_e32 v29, 0x41000000, v5
	v_mul_f32_e32 v30, 0x41000000, v20
	v_mul_f32_e32 v33, 0x41000000, v21
	v_mul_f32_e32 v156, 0x41000000, v18
	v_mul_f32_e32 v157, 0x41000000, v19
	s_cselect_b64 s[14:15], -1, 0
	s_cmpk_gt_u32 s9, 0x1ff
	v_med3_f32 v31, v24, s64, v250
	v_med3_f32 v154, v25, s64, v250
	v_med3_f32 v24, v28, s64, v250
	v_med3_f32 v25, v29, s64, v250
	v_med3_f32 v32, v30, s64, v250
	v_med3_f32 v155, v33, s64, v250
	v_med3_f32 v30, v156, s64, v250
	v_med3_f32 v33, v157, s64, v250
	s_cbranch_scc1 .LBB0_79
	v_cvt_pk_fp8_f32 v28, v31, v154
	v_cvt_pk_fp8_f32 v29, v32, v155
	v_lshl_add_u64 v[22:23], v[22:23], 0, s[68:69]
	v_lshl_add_u64 v[22:23], v[22:23], 0, v[6:7]
	v_cvt_pk_fp8_f32 v28, v24, v25 op_sel:[0,0,1]
	v_cvt_pk_fp8_f32 v29, v30, v33 op_sel:[0,0,1]
	v_add_co_u32_e32 v22, vcc, 0x342ff000, v22
	s_nop 1
	v_addc_co_u32_e32 v23, vcc, 0, v23, vcc
	global_store_dwordx2 v[22:23], v[28:29], off offset:2816
.LBB0_79:
	s_cmpk_gt_i32 s68, 0x6ff
	v_add_u32_e32 v22, s68, v27
	s_cselect_b64 s[58:59], -1, 0
	s_cmpk_lt_i32 s68, 0x700
	v_ashrrev_i32_e32 v29, 6, v22
	v_and_b32_e32 v28, 56, v22
	s_cbranch_scc1 .LBB0_81
	v_ashrrev_i32_e32 v22, 10, v14
	v_and_b32_e32 v22, -8, v22
	v_add_u32_e32 v22, v29, v22
	v_ashrrev_i32_e32 v23, 31, v22
	v_lshlrev_b64 v[22:23], 13, v[22:23]
	v_and_or_b32 v22, v14, s50, v22
	v_or_b32_e32 v22, v22, v28
	v_lshlrev_b64 v[22:23], 6, v[22:23]
	v_lshl_add_u64 v[22:23], s[24:25], 0, v[22:23]
	v_lshrrev_b32_e32 v158, 1, v14
	v_lshl_add_u64 v[22:23], v[22:23], 0, v[0:1]
	v_and_b32_e32 v156, 16, v158
	v_mov_b32_e32 v157, v1
	v_lshl_add_u64 v[22:23], v[22:23], 0, v[156:157]
	v_lshl_add_u64 v[22:23], v[22:23], 0, v[8:9]
	v_and_b32_e32 v156, 12, v158
	v_lshl_add_u64 v[22:23], v[22:23], 0, v[156:157]
	v_cvt_pk_fp8_f32 v156, v31, v154
	v_cvt_pk_fp8_f32 v157, v32, v155
	v_cvt_pk_fp8_f32 v156, v24, v25 op_sel:[0,0,1]
	v_cvt_pk_fp8_f32 v157, v30, v33 op_sel:[0,0,1]
	global_store_byte v[22:23], v156, off
	global_store_byte v[22:23], v157, off offset:256
	v_lshrrev_b32_e32 v158, 8, v156
	global_store_byte v[22:23], v158, off offset:64
	v_lshrrev_b32_e32 v158, 8, v157
	global_store_byte v[22:23], v158, off offset:320
	global_store_byte_d16_hi v[22:23], v156, off offset:128
	global_store_byte_d16_hi v[22:23], v157, off offset:384
	v_lshrrev_b32_e32 v156, 24, v156
	global_store_byte v[22:23], v156, off offset:192
	v_lshrrev_b32_e32 v156, 24, v157
	global_store_byte v[22:23], v156, off offset:448
.LBB0_81:
	s_and_b64 vcc, exec, s[6:7]
	s_cbranch_vccnz .LBB0_83
	v_cvt_pk_fp8_f32 v22, v31, v154
	v_cvt_pk_fp8_f32 v23, v32, v155
	v_cvt_pk_fp8_f32 v22, v24, v25 op_sel:[0,0,1]
	v_cvt_pk_fp8_f32 v23, v30, v33 op_sel:[0,0,1]
	v_lshlrev_b64 v[24:25], 5, v[14:15]
	v_lshl_add_u64 v[24:25], s[34:35], 0, v[24:25]
	v_lshl_add_u64 v[24:25], v[24:25], 0, v[6:7]
	global_store_dwordx2 v[24:25], v[22:23], off

; __device__ __forceinline__ u32x4 pack8(const f32x4 a, const f32x4 b) { u32x4 w; w.x = cvt_pk_bf16(a[0], a[1]); w.y = cvt_pk_bf16(a[2], a[3]); w.z = cvt_pk_bf16(b[0], b[1]); w.w = cvt_pk_bf16(b[2], b[3]); return w; }
;     __device__ __forceinline__ void operator()(const f32x4 (&acc)[2][2][4][2], const Unit& u, int wr, int wc, int fr_in, int fq_in) const {
;     ...
;                     const int row = row0 + ai * HALF + m * 16; const float r = t[ai * 64 + m * 16 + fr] * sc;
;                     f32x4 v0 = acc[ai][bj][m][0] * r, v1 = acc[ai][bj][m][1] * r;
;                     if (kind == 2) rope8(v0, v1, rcos, rsin, row & (SEQ_ - 1), fq);
;                     *(u32x4*)(dst + (size_t)row * pitch + 8 * fq) = pack8(v0, v1);
;                     if (f8ch && colg >= 768 && colg < 1280) { u32x2 w8; w8.x = pack4_fp8_x16(v0); w8.y = pack4_fp8_x16(v1); *(u32x2*)(ws + WS_QB8 + (size_t)row * 512 + (colg - 768) + 8 * fq) = w8; }
;                     if (f8ch && colg >= 1280 && colg < 1792) { u32x2 w8; w8.x = pack4_fp8_x8(v0); w8.y = pack4_fp8_x8(v1); *(u32x2*)(ws + WS_KB8 + (size_t)row * 512 + (colg - 1280) + 8 * fq) = w8; }
.LBB0_89:
	v_ashrrev_i32_e32 v19, 31, v18
	v_mul_lo_u32 v15, s55, v18
	v_mul_lo_u32 v146, s54, v19
	v_mad_u64_u32 v[24:25], s[10:11], s54, v18, 0
	v_add3_u32 v25, v25, v146, v15
	v_lshl_add_u64 v[24:25], v[24:25], 1, v[16:17]
	v_cvt_pk_bf16_f32 v30, v2, v3
	v_cvt_pk_bf16_f32 v31, v4, v5
	v_cvt_pk_bf16_f32 v32, v22, v23
	v_cvt_pk_bf16_f32 v33, v20, v21
	global_store_dwordx4 v[24:25], v[30:33], off
	v_cndmask_b32_e64 v15, 0, 1, s[12:13]
	v_lshlrev_b64 v[24:25], 9, v[18:19]
	v_cmp_ne_u32_e64 s[10:11], 1, v15
	s_andn2_b64 vcc, exec, s[12:13]
	v_lshl_add_u64 v[24:25], s[18:19], 0, v[24:25]
	s_cbranch_vccnz .LBB0_91
	v_mul_f32_e32 v15, 0x41800000, v2
	v_mul_f32_e32 v30, 0x41800000, v3
	v_med3_f32 v15, v15, s64, v250
	v_med3_f32 v31, v30, s64, v250
	v_cvt_pk_fp8_f32 v30, v15, v31
	v_mul_f32_e32 v15, 0x41800000, v4
	v_mul_f32_e32 v31, 0x41800000, v5
	v_med3_f32 v15, v15, s64, v250
	v_med3_f32 v31, v31, s64, v250
	v_cvt_pk_fp8_f32 v30, v15, v31 op_sel:[0,0,1]
	v_mul_f32_e32 v15, 0x41800000, v22
	v_mul_f32_e32 v31, 0x41800000, v23
	v_med3_f32 v15, v15, s64, v250
	v_med3_f32 v32, v31, s64, v250
	v_cvt_pk_fp8_f32 v31, v15, v32
	v_mul_f32_e32 v15, 0x41800000, v20
	v_mul_f32_e32 v32, 0x41800000, v21
	v_med3_f32 v15, v15, s64, v250
	v_med3_f32 v32, v32, s64, v250
	v_cvt_pk_fp8_f32 v31, v15, v32 op_sel:[0,0,1]
	v_lshl_add_u64 v[32:33], v[24:25], 0, s[68:69]
	v_lshl_add_u64 v[32:33], v[32:33], 0, v[6:7]
	v_add_co_u32_e32 v32, vcc, 0x332ff000, v32
	s_nop 1
	v_addc_co_u32_e32 v33, vcc, 0, v33, vcc
	global_store_dwordx2 v[32:33], v[30:31], off offset:3328
.LBB0_91:
	v_cndmask_b32_e64 v15, 0, 1, s[14:15]
	v_cmp_ne_u32_e64 s[12:13], 1, v15
	v_mul_f32_e32 v15, 0x41000000, v2
	v_mul_f32_e32 v30, 0x41000000, v3
	v_mul_f32_e32 v31, 0x41000000, v4
	v_mul_f32_e32 v33, 0x41000000, v5
	v_mul_f32_e32 v146, 0x41000000, v22
	v_mul_f32_e32 v148, 0x41000000, v23
	v_mul_f32_e32 v149, 0x41000000, v20
	v_mul_f32_e32 v150, 0x41000000, v21
	s_andn2_b64 vcc, exec, s[14:15]
	v_med3_f32 v32, v15, s64, v250
	v_med3_f32 v147, v30, s64, v250
	v_med3_f32 v15, v31, s64, v250
	v_med3_f32 v30, v33, s64, v250
	v_med3_f32 v33, v146, s64, v250
	v_med3_f32 v148, v148, s64, v250
	v_med3_f32 v31, v149, s64, v250
	v_med3_f32 v146, v150, s64, v250
	s_cbranch_vccnz .LBB0_95
	v_cvt_pk_fp8_f32 v150, v32, v147
	v_cvt_pk_fp8_f32 v151, v33, v148
	v_lshl_add_u64 v[24:25], v[24:25], 0, s[68:69]
	v_lshl_add_u64 v[24:25], v[24:25], 0, v[6:7]
	v_cvt_pk_fp8_f32 v150, v15, v30 op_sel:[0,0,1]
	v_cvt_pk_fp8_f32 v151, v31, v146 op_sel:[0,0,1]
	v_add_co_u32_e32 v24, vcc, 0x342ff000, v24
	s_nop 1
	v_addc_co_u32_e32 v25, vcc, 0, v25, vcc
	global_store_dwordx2 v[24:25], v[150:151], off offset:2816
	v_cndmask_b32_e64 v24, 0, 1, s[58:59]
	v_cmp_ne_u32_e64 s[14:15], 1, v24
	s_andn2_b64 vcc, exec, s[58:59]
	s_cbranch_vccz .LBB0_96

;     __device__ __forceinline__ void operator()(const f32x4 (&acc)[2][2][4][2], const Unit& u, int wr, int wc, int fr_in, int fq_in) const {
;     ...
;                     if (kind == 2 && f8qk) { u32x2 w8; w8.x = pack4_fp8_x8(v0); w8.y = pack4_fp8_x8(v1); *(u32x2*)(ws + WS_KR8 + (size_t)row * 32 + 8 * fq) = w8; }
.LBB0_94:
	v_cvt_pk_fp8_f32 v24, v32, v147
	v_cvt_pk_fp8_f32 v25, v33, v148
	v_cvt_pk_fp8_f32 v24, v15, v30 op_sel:[0,0,1]
	v_cvt_pk_fp8_f32 v25, v31, v146 op_sel:[0,0,1]
	v_lshlrev_b64 v[30:31], 5, v[18:19]
	v_lshl_add_u64 v[30:31], s[34:35], 0, v[30:31]
	v_lshl_add_u64 v[30:31], v[30:31], 0, v[6:7]
	global_store_dwordx2 v[30:31], v[24:25], off
	s_and_b64 vcc, exec, s[8:9]
	s_cbranch_vccnz .LBB0_101
	s_branch .LBB0_98

;     __device__ __forceinline__ void operator()(const f32x4 (&acc)[2][2][4][2], const Unit& u, int wr, int wc, int fr_in, int fq_in) const {
;     ...
;                     if (f8ch && colg >= 1792) {
;                         const int c0_ = colg - 1792 + 8 * fq, bb_ = row >> 13, pos_ = row & (SEQ_ - 1), key_ = pos_ & 63, k32_ = key_ & 31;
;                         unsigned char* p_ = ws + WS_VB8T + ((((size_t)(bb_ * 8 + (c0_ >> 6)) * 128 + (pos_ >> 6)) * 64 + (c0_ & 63)) * 64) + 32 * ((k32_ >> 2) & 1) + 16 * (key_ >> 5) + (k32_ & 3) + 4 * (k32_ >> 3);
;                         const unsigned w0_ = pack4_fp8_x8(v0), w1_ = pack4_fp8_x8(v1);
; #pragma unroll
;                         for (int e_ = 0; e_ < 4; ++e_) { p_[e_ * 64] = (unsigned char)((w0_ >> (8 * e_)) & 0xffu); p_[(4 + e_) * 64] = (unsigned char)((w1_ >> (8 * e_)) & 0xffu); }
;                     }
.LBB0_96:
	v_ashrrev_i32_e32 v24, 10, v18
	v_and_b32_e32 v24, -8, v24
	v_add_u32_e32 v24, v24, v29
	v_ashrrev_i32_e32 v25, 31, v24
	v_lshlrev_b64 v[24:25], 13, v[24:25]
	v_and_or_b32 v24, v18, s50, v24
	v_or_b32_e32 v24, v24, v28
	v_lshlrev_b64 v[24:25], 6, v[24:25]
	v_lshl_add_u64 v[24:25], s[24:25], 0, v[24:25]
	v_lshrrev_b32_e32 v149, 1, v18
	v_lshl_add_u64 v[24:25], v[24:25], 0, v[0:1]
	v_and_b32_e32 v150, 16, v149
	v_mov_b32_e32 v151, v1
	v_lshl_add_u64 v[24:25], v[24:25], 0, v[150:151]
	v_lshl_add_u64 v[24:25], v[24:25], 0, v[8:9]
	v_and_b32_e32 v150, 12, v149
	v_lshl_add_u64 v[24:25], v[24:25], 0, v[150:151]
	v_cvt_pk_fp8_f32 v149, v32, v147
	v_cvt_pk_fp8_f32 v150, v33, v148
	v_cvt_pk_fp8_f32 v149, v15, v30 op_sel:[0,0,1]
	v_cvt_pk_fp8_f32 v150, v31, v146 op_sel:[0,0,1]
	global_store_byte v[24:25], v149, off
	global_store_byte v[24:25], v150, off offset:256
	v_lshrrev_b32_e32 v151, 8, v149
	global_store_byte v[24:25], v151, off offset:64
	v_lshrrev_b32_e32 v151, 8, v150
	global_store_byte v[24:25], v151, off offset:320
	global_store_byte_d16_hi v[24:25], v149, off offset:128
	global_store_byte_d16_hi v[24:25], v150, off offset:384
	v_lshrrev_b32_e32 v149, 24, v149
	global_store_byte v[24:25], v149, off offset:192
	v_lshrrev_b32_e32 v149, 24, v150
	global_store_byte v[24:25], v149, off offset:448
	s_and_b64 vcc, exec, s[6:7]
	s_cbranch_vccz .LBB0_94

; __device__ __forceinline__ u32x4 pack8(const f32x4 a, const f32x4 b) { u32x4 w; w.x = cvt_pk_bf16(a[0], a[1]); w.y = cvt_pk_bf16(a[2], a[3]); w.z = cvt_pk_bf16(b[0], b[1]); w.w = cvt_pk_bf16(b[2], b[3]); return w; }
;     __device__ __forceinline__ void operator()(const f32x4 (&acc)[2][2][4][2], const Unit& u, int wr, int wc, int fr_in, int fq_in) const {
;     ...
;                     const int row = row0 + ai * HALF + m * 16; const float r = t[ai * 64 + m * 16 + fr] * sc;
;                     f32x4 v0 = acc[ai][bj][m][0] * r, v1 = acc[ai][bj][m][1] * r;
;                     if (kind == 2) rope8(v0, v1, rcos, rsin, row & (SEQ_ - 1), fq);
;                     *(u32x4*)(dst + (size_t)row * pitch + 8 * fq) = pack8(v0, v1);
;                     if (f8ch && colg >= 768 && colg < 1280) { u32x2 w8; w8.x = pack4_fp8_x16(v0); w8.y = pack4_fp8_x16(v1); *(u32x2*)(ws + WS_QB8 + (size_t)row * 512 + (colg - 768) + 8 * fq) = w8; }
;                     if (f8ch && colg >= 1280 && colg < 1792) { u32x2 w8; w8.x = pack4_fp8_x8(v0); w8.y = pack4_fp8_x8(v1); *(u32x2*)(ws + WS_KB8 + (size_t)row * 512 + (colg - 1280) + 8 * fq) = w8; }
.LBB0_103:
	v_ashrrev_i32_e32 v19, 31, v18
	v_mul_lo_u32 v15, s55, v18
	v_mul_lo_u32 v138, s54, v19
	v_mad_u64_u32 v[24:25], s[58:59], s54, v18, 0
	v_add3_u32 v25, v25, v138, v15
	v_lshl_add_u64 v[24:25], v[24:25], 1, v[16:17]
	v_cvt_pk_bf16_f32 v30, v2, v3
	v_cvt_pk_bf16_f32 v31, v4, v5
	v_cvt_pk_bf16_f32 v32, v22, v23
	v_cvt_pk_bf16_f32 v33, v20, v21
	global_store_dwordx4 v[24:25], v[30:33], off
	v_lshlrev_b64 v[24:25], 9, v[18:19]
	s_and_b64 vcc, exec, s[10:11]
	v_lshl_add_u64 v[24:25], s[18:19], 0, v[24:25]
	s_cbranch_vccnz .LBB0_105
	v_mul_f32_e32 v15, 0x41800000, v2
	v_mul_f32_e32 v30, 0x41800000, v3
	v_med3_f32 v15, v15, s64, v250
	v_med3_f32 v31, v30, s64, v250
	v_cvt_pk_fp8_f32 v30, v15, v31
	v_mul_f32_e32 v15, 0x41800000, v4
	v_mul_f32_e32 v31, 0x41800000, v5
	v_med3_f32 v15, v15, s64, v250
	v_med3_f32 v31, v31, s64, v250
	v_cvt_pk_fp8_f32 v30, v15, v31 op_sel:[0,0,1]
	v_mul_f32_e32 v15, 0x41800000, v22
	v_mul_f32_e32 v31, 0x41800000, v23
	v_med3_f32 v15, v15, s64, v250
	v_med3_f32 v32, v31, s64, v250
	v_cvt_pk_fp8_f32 v31, v15, v32
	v_mul_f32_e32 v15, 0x41800000, v20
	v_mul_f32_e32 v32, 0x41800000, v21
	v_med3_f32 v15, v15, s64, v250
	v_med3_f32 v32, v32, s64, v250
	v_cvt_pk_fp8_f32 v31, v15, v32 op_sel:[0,0,1]
	v_lshl_add_u64 v[32:33], v[24:25], 0, s[68:69]
	v_lshl_add_u64 v[32:33], v[32:33], 0, v[6:7]
	v_add_co_u32_e32 v32, vcc, 0x332ff000, v32
	s_nop 1
	v_addc_co_u32_e32 v33, vcc, 0, v33, vcc
	global_store_dwordx2 v[32:33], v[30:31], off offset:3328
.LBB0_105:
	v_mul_f32_e32 v15, 0x41000000, v2
	v_mul_f32_e32 v30, 0x41000000, v3
	v_mul_f32_e32 v31, 0x41000000, v4
	v_mul_f32_e32 v33, 0x41000000, v5
	v_mul_f32_e32 v138, 0x41000000, v22
	v_mul_f32_e32 v140, 0x41000000, v23
	v_mul_f32_e32 v141, 0x41000000, v20
	v_mul_f32_e32 v142, 0x41000000, v21
	s_and_b64 vcc, exec, s[12:13]
	v_med3_f32 v32, v15, s64, v250
	v_med3_f32 v139, v30, s64, v250
	v_med3_f32 v15, v31, s64, v250
	v_med3_f32 v30, v33, s64, v250
	v_med3_f32 v33, v138, s64, v250
	v_med3_f32 v140, v140, s64, v250
	v_med3_f32 v31, v141, s64, v250
	v_med3_f32 v138, v142, s64, v250
	s_cbranch_vccnz .LBB0_109
	v_cvt_pk_fp8_f32 v142, v32, v139
	v_cvt_pk_fp8_f32 v143, v33, v140
	v_lshl_add_u64 v[24:25], v[24:25], 0, s[68:69]
	v_lshl_add_u64 v[24:25], v[24:25], 0, v[6:7]
	v_cvt_pk_fp8_f32 v142, v15, v30 op_sel:[0,0,1]
	v_cvt_pk_fp8_f32 v143, v31, v138 op_sel:[0,0,1]
	v_add_co_u32_e32 v24, vcc, 0x342ff000, v24
	s_nop 1
	v_addc_co_u32_e32 v25, vcc, 0, v25, vcc
	global_store_dwordx2 v[24:25], v[142:143], off offset:2816
	s_and_b64 vcc, exec, s[14:15]
	s_cbranch_vccz .LBB0_110

;     __device__ __forceinline__ void operator()(const f32x4 (&acc)[2][2][4][2], const Unit& u, int wr, int wc, int fr_in, int fq_in) const {
;     ...
;                     if (kind == 2 && f8qk) { u32x2 w8; w8.x = pack4_fp8_x8(v0); w8.y = pack4_fp8_x8(v1); *(u32x2*)(ws + WS_KR8 + (size_t)row * 32 + 8 * fq) = w8; }
.LBB0_108:
	v_cvt_pk_fp8_f32 v24, v32, v139
	v_cvt_pk_fp8_f32 v25, v33, v140
	v_cvt_pk_fp8_f32 v24, v15, v30 op_sel:[0,0,1]
	v_cvt_pk_fp8_f32 v25, v31, v138 op_sel:[0,0,1]
	v_lshlrev_b64 v[30:31], 5, v[18:19]
	v_lshl_add_u64 v[30:31], s[34:35], 0, v[30:31]
	v_lshl_add_u64 v[30:31], v[30:31], 0, v[6:7]
	global_store_dwordx2 v[30:31], v[24:25], off
	s_and_b64 vcc, exec, s[8:9]
	s_cbranch_vccnz .LBB0_115
	s_branch .LBB0_112

;     __device__ __forceinline__ void operator()(const f32x4 (&acc)[2][2][4][2], const Unit& u, int wr, int wc, int fr_in, int fq_in) const {
;     ...
;                     if (f8ch && colg >= 1792) {
;                         const int c0_ = colg - 1792 + 8 * fq, bb_ = row >> 13, pos_ = row & (SEQ_ - 1), key_ = pos_ & 63, k32_ = key_ & 31;
;                         unsigned char* p_ = ws + WS_VB8T + ((((size_t)(bb_ * 8 + (c0_ >> 6)) * 128 + (pos_ >> 6)) * 64 + (c0_ & 63)) * 64) + 32 * ((k32_ >> 2) & 1) + 16 * (key_ >> 5) + (k32_ & 3) + 4 * (k32_ >> 3);
;                         const unsigned w0_ = pack4_fp8_x8(v0), w1_ = pack4_fp8_x8(v1);
; #pragma unroll
;                         for (int e_ = 0; e_ < 4; ++e_) { p_[e_ * 64] = (unsigned char)((w0_ >> (8 * e_)) & 0xffu); p_[(4 + e_) * 64] = (unsigned char)((w1_ >> (8 * e_)) & 0xffu); }
;                     }
.LBB0_110:
	v_ashrrev_i32_e32 v24, 10, v18
	v_and_b32_e32 v24, -8, v24
	v_add_u32_e32 v24, v24, v29
	v_ashrrev_i32_e32 v25, 31, v24
	v_lshlrev_b64 v[24:25], 13, v[24:25]
	v_and_or_b32 v24, v18, s50, v24
	v_or_b32_e32 v24, v24, v28
	v_lshlrev_b64 v[24:25], 6, v[24:25]
	v_lshl_add_u64 v[24:25], s[24:25], 0, v[24:25]
	v_lshrrev_b32_e32 v141, 1, v18
	v_lshl_add_u64 v[24:25], v[24:25], 0, v[0:1]
	v_and_b32_e32 v142, 16, v141
	v_mov_b32_e32 v143, v1
	v_lshl_add_u64 v[24:25], v[24:25], 0, v[142:143]
	v_lshl_add_u64 v[24:25], v[24:25], 0, v[8:9]
	v_and_b32_e32 v142, 12, v141
	v_lshl_add_u64 v[24:25], v[24:25], 0, v[142:143]
	v_cvt_pk_fp8_f32 v141, v32, v139
	v_cvt_pk_fp8_f32 v142, v33, v140
	v_cvt_pk_fp8_f32 v141, v15, v30 op_sel:[0,0,1]
	v_cvt_pk_fp8_f32 v142, v31, v138 op_sel:[0,0,1]
	global_store_byte v[24:25], v141, off
	global_store_byte v[24:25], v142, off offset:256
	v_lshrrev_b32_e32 v143, 8, v141
	global_store_byte v[24:25], v143, off offset:64
	v_lshrrev_b32_e32 v143, 8, v142
	global_store_byte v[24:25], v143, off offset:320
	global_store_byte_d16_hi v[24:25], v141, off offset:128
	global_store_byte_d16_hi v[24:25], v142, off offset:384
	v_lshrrev_b32_e32 v141, 24, v141
	global_store_byte v[24:25], v141, off offset:192
	v_lshrrev_b32_e32 v141, 24, v142
	global_store_byte v[24:25], v141, off offset:448
	s_and_b64 vcc, exec, s[6:7]
	s_cbranch_vccz .LBB0_108

; __device__ __forceinline__ u32x4 pack8(const f32x4 a, const f32x4 b) { u32x4 w; w.x = cvt_pk_bf16(a[0], a[1]); w.y = cvt_pk_bf16(a[2], a[3]); w.z = cvt_pk_bf16(b[0], b[1]); w.w = cvt_pk_bf16(b[2], b[3]); return w; }
;     __device__ __forceinline__ void operator()(const f32x4 (&acc)[2][2][4][2], const Unit& u, int wr, int wc, int fr_in, int fq_in) const {
;     ...
;                     const int row = row0 + ai * HALF + m * 16; const float r = t[ai * 64 + m * 16 + fr] * sc;
;                     f32x4 v0 = acc[ai][bj][m][0] * r, v1 = acc[ai][bj][m][1] * r;
;                     if (kind == 2) rope8(v0, v1, rcos, rsin, row & (SEQ_ - 1), fq);
;                     *(u32x4*)(dst + (size_t)row * pitch + 8 * fq) = pack8(v0, v1);
;                     if (f8ch && colg >= 768 && colg < 1280) { u32x2 w8; w8.x = pack4_fp8_x16(v0); w8.y = pack4_fp8_x16(v1); *(u32x2*)(ws + WS_QB8 + (size_t)row * 512 + (colg - 768) + 8 * fq) = w8; }
;                     if (f8ch && colg >= 1280 && colg < 1792) { u32x2 w8; w8.x = pack4_fp8_x8(v0); w8.y = pack4_fp8_x8(v1); *(u32x2*)(ws + WS_KB8 + (size_t)row * 512 + (colg - 1280) + 8 * fq) = w8; }
.LBB0_117:
	v_ashrrev_i32_e32 v19, 31, v18
	v_mul_lo_u32 v15, s55, v18
	v_mul_lo_u32 v130, s54, v19
	v_mad_u64_u32 v[24:25], s[58:59], s54, v18, 0
	v_add3_u32 v25, v25, v130, v15
	v_lshl_add_u64 v[24:25], v[24:25], 1, v[16:17]
	v_cvt_pk_bf16_f32 v30, v2, v3
	v_cvt_pk_bf16_f32 v31, v4, v5
	v_cvt_pk_bf16_f32 v32, v22, v23
	v_cvt_pk_bf16_f32 v33, v20, v21
	global_store_dwordx4 v[24:25], v[30:33], off
	v_lshlrev_b64 v[24:25], 9, v[18:19]
	s_and_b64 vcc, exec, s[10:11]
	v_lshl_add_u64 v[24:25], s[18:19], 0, v[24:25]
	s_cbranch_vccnz .LBB0_119
	v_mul_f32_e32 v15, 0x41800000, v2
	v_mul_f32_e32 v30, 0x41800000, v3
	v_med3_f32 v15, v15, s64, v250
	v_med3_f32 v31, v30, s64, v250
	v_cvt_pk_fp8_f32 v30, v15, v31
	v_mul_f32_e32 v15, 0x41800000, v4
	v_mul_f32_e32 v31, 0x41800000, v5
	v_med3_f32 v15, v15, s64, v250
	v_med3_f32 v31, v31, s64, v250
	v_cvt_pk_fp8_f32 v30, v15, v31 op_sel:[0,0,1]
	v_mul_f32_e32 v15, 0x41800000, v22
	v_mul_f32_e32 v31, 0x41800000, v23
	v_med3_f32 v15, v15, s64, v250
	v_med3_f32 v32, v31, s64, v250
	v_cvt_pk_fp8_f32 v31, v15, v32
	v_mul_f32_e32 v15, 0x41800000, v20
	v_mul_f32_e32 v32, 0x41800000, v21
	v_med3_f32 v15, v15, s64, v250
	v_med3_f32 v32, v32, s64, v250
	v_cvt_pk_fp8_f32 v31, v15, v32 op_sel:[0,0,1]
	v_lshl_add_u64 v[32:33], v[24:25], 0, s[68:69]
	v_lshl_add_u64 v[32:33], v[32:33], 0, v[6:7]
	v_add_co_u32_e32 v32, vcc, 0x332ff000, v32
	s_nop 1
	v_addc_co_u32_e32 v33, vcc, 0, v33, vcc
	global_store_dwordx2 v[32:33], v[30:31], off offset:3328
.LBB0_119:
	v_mul_f32_e32 v15, 0x41000000, v2
	v_mul_f32_e32 v30, 0x41000000, v3
	v_mul_f32_e32 v31, 0x41000000, v4
	v_mul_f32_e32 v33, 0x41000000, v5
	v_mul_f32_e32 v130, 0x41000000, v22
	v_mul_f32_e32 v132, 0x41000000, v23
	v_mul_f32_e32 v133, 0x41000000, v20
	v_mul_f32_e32 v134, 0x41000000, v21
	s_and_b64 vcc, exec, s[12:13]
	v_med3_f32 v32, v15, s64, v250
	v_med3_f32 v131, v30, s64, v250
	v_med3_f32 v15, v31, s64, v250
	v_med3_f32 v30, v33, s64, v250
	v_med3_f32 v33, v130, s64, v250
	v_med3_f32 v132, v132, s64, v250
	v_med3_f32 v31, v133, s64, v250
	v_med3_f32 v130, v134, s64, v250
	s_cbranch_vccnz .LBB0_123
	v_cvt_pk_fp8_f32 v134, v32, v131
	v_cvt_pk_fp8_f32 v135, v33, v132
	v_lshl_add_u64 v[24:25], v[24:25], 0, s[68:69]
	v_lshl_add_u64 v[24:25], v[24:25], 0, v[6:7]
	v_cvt_pk_fp8_f32 v134, v15, v30 op_sel:[0,0,1]
	v_cvt_pk_fp8_f32 v135, v31, v130 op_sel:[0,0,1]
	v_add_co_u32_e32 v24, vcc, 0x342ff000, v24
	s_nop 1
	v_addc_co_u32_e32 v25, vcc, 0, v25, vcc
	global_store_dwordx2 v[24:25], v[134:135], off offset:2816
	s_and_b64 vcc, exec, s[14:15]
	s_cbranch_vccz .LBB0_124

;     __device__ __forceinline__ void operator()(const f32x4 (&acc)[2][2][4][2], const Unit& u, int wr, int wc, int fr_in, int fq_in) const {
;     ...
;                     if (kind == 2 && f8qk) { u32x2 w8; w8.x = pack4_fp8_x8(v0); w8.y = pack4_fp8_x8(v1); *(u32x2*)(ws + WS_KR8 + (size_t)row * 32 + 8 * fq) = w8; }
.LBB0_122:
	v_cvt_pk_fp8_f32 v24, v32, v131
	v_cvt_pk_fp8_f32 v25, v33, v132
	v_cvt_pk_fp8_f32 v24, v15, v30 op_sel:[0,0,1]
	v_cvt_pk_fp8_f32 v25, v31, v130 op_sel:[0,0,1]
	v_lshlrev_b64 v[30:31], 5, v[18:19]
	v_lshl_add_u64 v[30:31], s[34:35], 0, v[30:31]
	v_lshl_add_u64 v[30:31], v[30:31], 0, v[6:7]
	global_store_dwordx2 v[30:31], v[24:25], off
	s_and_b64 vcc, exec, s[8:9]
	s_cbranch_vccnz .LBB0_129
	s_branch .LBB0_126

;     __device__ __forceinline__ void operator()(const f32x4 (&acc)[2][2][4][2], const Unit& u, int wr, int wc, int fr_in, int fq_in) const {
;     ...
;                     if (f8ch && colg >= 1792) {
;                         const int c0_ = colg - 1792 + 8 * fq, bb_ = row >> 13, pos_ = row & (SEQ_ - 1), key_ = pos_ & 63, k32_ = key_ & 31;
;                         unsigned char* p_ = ws + WS_VB8T + ((((size_t)(bb_ * 8 + (c0_ >> 6)) * 128 + (pos_ >> 6)) * 64 + (c0_ & 63)) * 64) + 32 * ((k32_ >> 2) & 1) + 16 * (key_ >> 5) + (k32_ & 3) + 4 * (k32_ >> 3);
;                         const unsigned w0_ = pack4_fp8_x8(v0), w1_ = pack4_fp8_x8(v1);
; #pragma unroll
;                         for (int e_ = 0; e_ < 4; ++e_) { p_[e_ * 64] = (unsigned char)((w0_ >> (8 * e_)) & 0xffu); p_[(4 + e_) * 64] = (unsigned char)((w1_ >> (8 * e_)) & 0xffu); }
;                     }
.LBB0_124:
	v_ashrrev_i32_e32 v24, 10, v18
	v_and_b32_e32 v24, -8, v24
	v_add_u32_e32 v24, v24, v29
	v_ashrrev_i32_e32 v25, 31, v24
	v_lshlrev_b64 v[24:25], 13, v[24:25]
	v_and_or_b32 v24, v18, s50, v24
	v_or_b32_e32 v24, v24, v28
	v_lshlrev_b64 v[24:25], 6, v[24:25]
	v_lshl_add_u64 v[24:25], s[24:25], 0, v[24:25]
	v_lshrrev_b32_e32 v133, 1, v18
	v_lshl_add_u64 v[24:25], v[24:25], 0, v[0:1]
	v_and_b32_e32 v134, 16, v133
	v_mov_b32_e32 v135, v1
	v_lshl_add_u64 v[24:25], v[24:25], 0, v[134:135]
	v_lshl_add_u64 v[24:25], v[24:25], 0, v[8:9]
	v_and_b32_e32 v134, 12, v133
	v_lshl_add_u64 v[24:25], v[24:25], 0, v[134:135]
	v_cvt_pk_fp8_f32 v133, v32, v131
	v_cvt_pk_fp8_f32 v134, v33, v132
	v_cvt_pk_fp8_f32 v133, v15, v30 op_sel:[0,0,1]
	v_cvt_pk_fp8_f32 v134, v31, v130 op_sel:[0,0,1]
	global_store_byte v[24:25], v133, off
	global_store_byte v[24:25], v134, off offset:256
	v_lshrrev_b32_e32 v135, 8, v133
	global_store_byte v[24:25], v135, off offset:64
	v_lshrrev_b32_e32 v135, 8, v134
	global_store_byte v[24:25], v135, off offset:320
	global_store_byte_d16_hi v[24:25], v133, off offset:128
	global_store_byte_d16_hi v[24:25], v134, off offset:384
	v_lshrrev_b32_e32 v133, 24, v133
	global_store_byte v[24:25], v133, off offset:192
	v_lshrrev_b32_e32 v133, 24, v134
	global_store_byte v[24:25], v133, off offset:448
	s_and_b64 vcc, exec, s[6:7]
	s_cbranch_vccz .LBB0_122

; __device__ __forceinline__ u32x4 pack8(const f32x4 a, const f32x4 b) { u32x4 w; w.x = cvt_pk_bf16(a[0], a[1]); w.y = cvt_pk_bf16(a[2], a[3]); w.z = cvt_pk_bf16(b[0], b[1]); w.w = cvt_pk_bf16(b[2], b[3]); return w; }
;     __device__ __forceinline__ void operator()(const f32x4 (&acc)[2][2][4][2], const Unit& u, int wr, int wc, int fr_in, int fq_in) const {
;     ...
;                     const int row = row0 + ai * HALF + m * 16; const float r = t[ai * 64 + m * 16 + fr] * sc;
;                     f32x4 v0 = acc[ai][bj][m][0] * r, v1 = acc[ai][bj][m][1] * r;
;                     if (kind == 2) rope8(v0, v1, rcos, rsin, row & (SEQ_ - 1), fq);
;                     *(u32x4*)(dst + (size_t)row * pitch + 8 * fq) = pack8(v0, v1);
;                     if (f8ch && colg >= 768 && colg < 1280) { u32x2 w8; w8.x = pack4_fp8_x16(v0); w8.y = pack4_fp8_x16(v1); *(u32x2*)(ws + WS_QB8 + (size_t)row * 512 + (colg - 768) + 8 * fq) = w8; }
;                     if (f8ch && colg >= 1280 && colg < 1792) { u32x2 w8; w8.x = pack4_fp8_x8(v0); w8.y = pack4_fp8_x8(v1); *(u32x2*)(ws + WS_KB8 + (size_t)row * 512 + (colg - 1280) + 8 * fq) = w8; }
.LBB0_131:
	v_ashrrev_i32_e32 v19, 31, v18
	v_mul_lo_u32 v15, s55, v18
	v_mul_lo_u32 v122, s54, v19
	v_mad_u64_u32 v[24:25], s[58:59], s54, v18, 0
	v_add3_u32 v25, v25, v122, v15
	v_lshl_add_u64 v[24:25], v[24:25], 1, v[16:17]
	v_cvt_pk_bf16_f32 v30, v2, v3
	v_cvt_pk_bf16_f32 v31, v4, v5
	v_cvt_pk_bf16_f32 v32, v22, v23
	v_cvt_pk_bf16_f32 v33, v20, v21
	global_store_dwordx4 v[24:25], v[30:33], off
	v_lshlrev_b64 v[24:25], 9, v[18:19]
	s_and_b64 vcc, exec, s[10:11]
	v_lshl_add_u64 v[24:25], s[18:19], 0, v[24:25]
	s_cbranch_vccnz .LBB0_133
	v_mul_f32_e32 v15, 0x41800000, v2
	v_mul_f32_e32 v30, 0x41800000, v3
	v_med3_f32 v15, v15, s64, v250
	v_med3_f32 v31, v30, s64, v250
	v_cvt_pk_fp8_f32 v30, v15, v31
	v_mul_f32_e32 v15, 0x41800000, v4
	v_mul_f32_e32 v31, 0x41800000, v5
	v_med3_f32 v15, v15, s64, v250
	v_med3_f32 v31, v31, s64, v250
	v_cvt_pk_fp8_f32 v30, v15, v31 op_sel:[0,0,1]
	v_mul_f32_e32 v15, 0x41800000, v22
	v_mul_f32_e32 v31, 0x41800000, v23
	v_med3_f32 v15, v15, s64, v250
	v_med3_f32 v32, v31, s64, v250
	v_cvt_pk_fp8_f32 v31, v15, v32
	v_mul_f32_e32 v15, 0x41800000, v20
	v_mul_f32_e32 v32, 0x41800000, v21
	v_med3_f32 v15, v15, s64, v250
	v_med3_f32 v32, v32, s64, v250
	v_cvt_pk_fp8_f32 v31, v15, v32 op_sel:[0,0,1]
	v_lshl_add_u64 v[32:33], v[24:25], 0, s[68:69]
	v_lshl_add_u64 v[32:33], v[32:33], 0, v[6:7]
	v_add_co_u32_e32 v32, vcc, 0x332ff000, v32
	s_nop 1
	v_addc_co_u32_e32 v33, vcc, 0, v33, vcc
	global_store_dwordx2 v[32:33], v[30:31], off offset:3328
.LBB0_133:
	v_mul_f32_e32 v15, 0x41000000, v2
	v_mul_f32_e32 v30, 0x41000000, v3
	v_mul_f32_e32 v31, 0x41000000, v4
	v_mul_f32_e32 v33, 0x41000000, v5
	v_mul_f32_e32 v122, 0x41000000, v22
	v_mul_f32_e32 v124, 0x41000000, v23
	v_mul_f32_e32 v125, 0x41000000, v20
	v_mul_f32_e32 v126, 0x41000000, v21
	s_and_b64 vcc, exec, s[12:13]
	v_med3_f32 v32, v15, s64, v250
	v_med3_f32 v123, v30, s64, v250
	v_med3_f32 v15, v31, s64, v250
	v_med3_f32 v30, v33, s64, v250
	v_med3_f32 v33, v122, s64, v250
	v_med3_f32 v124, v124, s64, v250
	v_med3_f32 v31, v125, s64, v250
	v_med3_f32 v122, v126, s64, v250
	s_cbranch_vccnz .LBB0_137
	v_cvt_pk_fp8_f32 v126, v32, v123
	v_cvt_pk_fp8_f32 v127, v33, v124
	v_lshl_add_u64 v[24:25], v[24:25], 0, s[68:69]
	v_lshl_add_u64 v[24:25], v[24:25], 0, v[6:7]
	v_cvt_pk_fp8_f32 v126, v15, v30 op_sel:[0,0,1]
	v_cvt_pk_fp8_f32 v127, v31, v122 op_sel:[0,0,1]
	v_add_co_u32_e32 v24, vcc, 0x342ff000, v24
	s_nop 1
	v_addc_co_u32_e32 v25, vcc, 0, v25, vcc
	global_store_dwordx2 v[24:25], v[126:127], off offset:2816
	s_and_b64 vcc, exec, s[14:15]
	s_cbranch_vccz .LBB0_138

;     __device__ __forceinline__ void operator()(const f32x4 (&acc)[2][2][4][2], const Unit& u, int wr, int wc, int fr_in, int fq_in) const {
;     ...
;                     if (kind == 2 && f8qk) { u32x2 w8; w8.x = pack4_fp8_x8(v0); w8.y = pack4_fp8_x8(v1); *(u32x2*)(ws + WS_KR8 + (size_t)row * 32 + 8 * fq) = w8; }
.LBB0_136:
	v_cvt_pk_fp8_f32 v24, v32, v123
	v_cvt_pk_fp8_f32 v25, v33, v124
	v_cvt_pk_fp8_f32 v24, v15, v30 op_sel:[0,0,1]
	v_cvt_pk_fp8_f32 v25, v31, v122 op_sel:[0,0,1]
	v_lshlrev_b64 v[30:31], 5, v[18:19]
	v_lshl_add_u64 v[30:31], s[34:35], 0, v[30:31]
	v_lshl_add_u64 v[30:31], v[30:31], 0, v[6:7]
	global_store_dwordx2 v[30:31], v[24:25], off
	s_and_b64 vcc, exec, s[8:9]
	s_cbranch_vccnz .LBB0_143
	s_branch .LBB0_140

;     __device__ __forceinline__ void operator()(const f32x4 (&acc)[2][2][4][2], const Unit& u, int wr, int wc, int fr_in, int fq_in) const {
;     ...
;                     if (f8ch && colg >= 1792) {
;                         const int c0_ = colg - 1792 + 8 * fq, bb_ = row >> 13, pos_ = row & (SEQ_ - 1), key_ = pos_ & 63, k32_ = key_ & 31;
;                         unsigned char* p_ = ws + WS_VB8T + ((((size_t)(bb_ * 8 + (c0_ >> 6)) * 128 + (pos_ >> 6)) * 64 + (c0_ & 63)) * 64) + 32 * ((k32_ >> 2) & 1) + 16 * (key_ >> 5) + (k32_ & 3) + 4 * (k32_ >> 3);
;                         const unsigned w0_ = pack4_fp8_x8(v0), w1_ = pack4_fp8_x8(v1);
; #pragma unroll
;                         for (int e_ = 0; e_ < 4; ++e_) { p_[e_ * 64] = (unsigned char)((w0_ >> (8 * e_)) & 0xffu); p_[(4 + e_) * 64] = (unsigned char)((w1_ >> (8 * e_)) & 0xffu); }
;                     }
.LBB0_138:
	v_ashrrev_i32_e32 v24, 10, v18
	v_and_b32_e32 v24, -8, v24
	v_add_u32_e32 v24, v24, v29
	v_ashrrev_i32_e32 v25, 31, v24
	v_lshlrev_b64 v[24:25], 13, v[24:25]
	v_and_or_b32 v24, v18, s50, v24
	v_or_b32_e32 v24, v24, v28
	v_lshlrev_b64 v[24:25], 6, v[24:25]
	v_lshl_add_u64 v[24:25], s[24:25], 0, v[24:25]
	v_lshrrev_b32_e32 v125, 1, v18
	v_lshl_add_u64 v[24:25], v[24:25], 0, v[0:1]
	v_and_b32_e32 v126, 16, v125
	v_mov_b32_e32 v127, v1
	v_lshl_add_u64 v[24:25], v[24:25], 0, v[126:127]
	v_lshl_add_u64 v[24:25], v[24:25], 0, v[8:9]
	v_and_b32_e32 v126, 12, v125
	v_lshl_add_u64 v[24:25], v[24:25], 0, v[126:127]
	v_cvt_pk_fp8_f32 v125, v32, v123
	v_cvt_pk_fp8_f32 v126, v33, v124
	v_cvt_pk_fp8_f32 v125, v15, v30 op_sel:[0,0,1]
	v_cvt_pk_fp8_f32 v126, v31, v122 op_sel:[0,0,1]
	global_store_byte v[24:25], v125, off
	global_store_byte v[24:25], v126, off offset:256
	v_lshrrev_b32_e32 v127, 8, v125
	global_store_byte v[24:25], v127, off offset:64
	v_lshrrev_b32_e32 v127, 8, v126
	global_store_byte v[24:25], v127, off offset:320
	global_store_byte_d16_hi v[24:25], v125, off offset:128
	global_store_byte_d16_hi v[24:25], v126, off offset:384
	v_lshrrev_b32_e32 v125, 24, v125
	global_store_byte v[24:25], v125, off offset:192
	v_lshrrev_b32_e32 v125, 24, v126
	global_store_byte v[24:25], v125, off offset:448
	s_and_b64 vcc, exec, s[6:7]
	s_cbranch_vccz .LBB0_136

; __device__ __forceinline__ u32x4 pack8(const f32x4 a, const f32x4 b) { u32x4 w; w.x = cvt_pk_bf16(a[0], a[1]); w.y = cvt_pk_bf16(a[2], a[3]); w.z = cvt_pk_bf16(b[0], b[1]); w.w = cvt_pk_bf16(b[2], b[3]); return w; }
;     __device__ __forceinline__ void operator()(const f32x4 (&acc)[2][2][4][2], const Unit& u, int wr, int wc, int fr_in, int fq_in) const {
;     ...
;                     const int row = row0 + ai * HALF + m * 16; const float r = t[ai * 64 + m * 16 + fr] * sc;
;                     f32x4 v0 = acc[ai][bj][m][0] * r, v1 = acc[ai][bj][m][1] * r;
;                     if (kind == 2) rope8(v0, v1, rcos, rsin, row & (SEQ_ - 1), fq);
;                     *(u32x4*)(dst + (size_t)row * pitch + 8 * fq) = pack8(v0, v1);
;                     if (f8ch && colg >= 768 && colg < 1280) { u32x2 w8; w8.x = pack4_fp8_x16(v0); w8.y = pack4_fp8_x16(v1); *(u32x2*)(ws + WS_QB8 + (size_t)row * 512 + (colg - 768) + 8 * fq) = w8; }
;                     if (f8ch && colg >= 1280 && colg < 1792) { u32x2 w8; w8.x = pack4_fp8_x8(v0); w8.y = pack4_fp8_x8(v1); *(u32x2*)(ws + WS_KB8 + (size_t)row * 512 + (colg - 1280) + 8 * fq) = w8; }
.LBB0_145:
	v_ashrrev_i32_e32 v19, 31, v18
	v_mul_lo_u32 v15, s55, v18
	v_mul_lo_u32 v114, s54, v19
	v_mad_u64_u32 v[24:25], s[58:59], s54, v18, 0
	v_add3_u32 v25, v25, v114, v15
	v_lshl_add_u64 v[24:25], v[24:25], 1, v[16:17]
	v_cvt_pk_bf16_f32 v30, v2, v3
	v_cvt_pk_bf16_f32 v31, v4, v5
	v_cvt_pk_bf16_f32 v32, v22, v23
	v_cvt_pk_bf16_f32 v33, v20, v21
	global_store_dwordx4 v[24:25], v[30:33], off
	v_lshlrev_b64 v[24:25], 9, v[18:19]
	s_and_b64 vcc, exec, s[10:11]
	v_lshl_add_u64 v[24:25], s[18:19], 0, v[24:25]
	s_cbranch_vccnz .LBB0_147
	v_mul_f32_e32 v15, 0x41800000, v2
	v_mul_f32_e32 v30, 0x41800000, v3
	v_med3_f32 v15, v15, s64, v250
	v_med3_f32 v31, v30, s64, v250
	v_cvt_pk_fp8_f32 v30, v15, v31
	v_mul_f32_e32 v15, 0x41800000, v4
	v_mul_f32_e32 v31, 0x41800000, v5
	v_med3_f32 v15, v15, s64, v250
	v_med3_f32 v31, v31, s64, v250
	v_cvt_pk_fp8_f32 v30, v15, v31 op_sel:[0,0,1]
	v_mul_f32_e32 v15, 0x41800000, v22
	v_mul_f32_e32 v31, 0x41800000, v23
	v_med3_f32 v15, v15, s64, v250
	v_med3_f32 v32, v31, s64, v250
	v_cvt_pk_fp8_f32 v31, v15, v32
	v_mul_f32_e32 v15, 0x41800000, v20
	v_mul_f32_e32 v32, 0x41800000, v21
	v_med3_f32 v15, v15, s64, v250
	v_med3_f32 v32, v32, s64, v250
	v_cvt_pk_fp8_f32 v31, v15, v32 op_sel:[0,0,1]
	v_lshl_add_u64 v[32:33], v[24:25], 0, s[68:69]
	v_lshl_add_u64 v[32:33], v[32:33], 0, v[6:7]
	v_add_co_u32_e32 v32, vcc, 0x332ff000, v32
	s_nop 1
	v_addc_co_u32_e32 v33, vcc, 0, v33, vcc
	global_store_dwordx2 v[32:33], v[30:31], off offset:3328
.LBB0_147:
	v_mul_f32_e32 v15, 0x41000000, v2
	v_mul_f32_e32 v30, 0x41000000, v3
	v_mul_f32_e32 v31, 0x41000000, v4
	v_mul_f32_e32 v33, 0x41000000, v5
	v_mul_f32_e32 v114, 0x41000000, v22
	v_mul_f32_e32 v116, 0x41000000, v23
	v_mul_f32_e32 v117, 0x41000000, v20
	v_mul_f32_e32 v118, 0x41000000, v21
	s_and_b64 vcc, exec, s[12:13]
	v_med3_f32 v32, v15, s64, v250
	v_med3_f32 v115, v30, s64, v250
	v_med3_f32 v15, v31, s64, v250
	v_med3_f32 v30, v33, s64, v250
	v_med3_f32 v33, v114, s64, v250
	v_med3_f32 v116, v116, s64, v250
	v_med3_f32 v31, v117, s64, v250
	v_med3_f32 v114, v118, s64, v250
	s_cbranch_vccnz .LBB0_151
	v_cvt_pk_fp8_f32 v118, v32, v115
	v_cvt_pk_fp8_f32 v119, v33, v116
	v_lshl_add_u64 v[24:25], v[24:25], 0, s[68:69]
	v_lshl_add_u64 v[24:25], v[24:25], 0, v[6:7]
	v_cvt_pk_fp8_f32 v118, v15, v30 op_sel:[0,0,1]
	v_cvt_pk_fp8_f32 v119, v31, v114 op_sel:[0,0,1]
	v_add_co_u32_e32 v24, vcc, 0x342ff000, v24
	s_nop 1
	v_addc_co_u32_e32 v25, vcc, 0, v25, vcc
	global_store_dwordx2 v[24:25], v[118:119], off offset:2816
	s_and_b64 vcc, exec, s[14:15]
	s_cbranch_vccz .LBB0_152

;     __device__ __forceinline__ void operator()(const f32x4 (&acc)[2][2][4][2], const Unit& u, int wr, int wc, int fr_in, int fq_in) const {
;     ...
;                     if (kind == 2 && f8qk) { u32x2 w8; w8.x = pack4_fp8_x8(v0); w8.y = pack4_fp8_x8(v1); *(u32x2*)(ws + WS_KR8 + (size_t)row * 32 + 8 * fq) = w8; }
.LBB0_150:
	v_cvt_pk_fp8_f32 v24, v32, v115
	v_cvt_pk_fp8_f32 v25, v33, v116
	v_cvt_pk_fp8_f32 v24, v15, v30 op_sel:[0,0,1]
	v_cvt_pk_fp8_f32 v25, v31, v114 op_sel:[0,0,1]
	v_lshlrev_b64 v[30:31], 5, v[18:19]
	v_lshl_add_u64 v[30:31], s[34:35], 0, v[30:31]
	v_lshl_add_u64 v[30:31], v[30:31], 0, v[6:7]
	global_store_dwordx2 v[30:31], v[24:25], off
	s_and_b64 vcc, exec, s[8:9]
	s_cbranch_vccnz .LBB0_157
	s_branch .LBB0_154

;     __device__ __forceinline__ void operator()(const f32x4 (&acc)[2][2][4][2], const Unit& u, int wr, int wc, int fr_in, int fq_in) const {
;     ...
;                     if (f8ch && colg >= 1792) {
;                         const int c0_ = colg - 1792 + 8 * fq, bb_ = row >> 13, pos_ = row & (SEQ_ - 1), key_ = pos_ & 63, k32_ = key_ & 31;
;                         unsigned char* p_ = ws + WS_VB8T + ((((size_t)(bb_ * 8 + (c0_ >> 6)) * 128 + (pos_ >> 6)) * 64 + (c0_ & 63)) * 64) + 32 * ((k32_ >> 2) & 1) + 16 * (key_ >> 5) + (k32_ & 3) + 4 * (k32_ >> 3);
;                         const unsigned w0_ = pack4_fp8_x8(v0), w1_ = pack4_fp8_x8(v1);
; #pragma unroll
;                         for (int e_ = 0; e_ < 4; ++e_) { p_[e_ * 64] = (unsigned char)((w0_ >> (8 * e_)) & 0xffu); p_[(4 + e_) * 64] = (unsigned char)((w1_ >> (8 * e_)) & 0xffu); }
;                     }
.LBB0_152:
	v_ashrrev_i32_e32 v24, 10, v18
	v_and_b32_e32 v24, -8, v24
	v_add_u32_e32 v24, v24, v29
	v_ashrrev_i32_e32 v25, 31, v24
	v_lshlrev_b64 v[24:25], 13, v[24:25]
	v_and_or_b32 v24, v18, s50, v24
	v_or_b32_e32 v24, v24, v28
	v_lshlrev_b64 v[24:25], 6, v[24:25]
	v_lshl_add_u64 v[24:25], s[24:25], 0, v[24:25]
	v_lshrrev_b32_e32 v117, 1, v18
	v_lshl_add_u64 v[24:25], v[24:25], 0, v[0:1]
	v_and_b32_e32 v118, 16, v117
	v_mov_b32_e32 v119, v1
	v_lshl_add_u64 v[24:25], v[24:25], 0, v[118:119]
	v_lshl_add_u64 v[24:25], v[24:25], 0, v[8:9]
	v_and_b32_e32 v118, 12, v117
	v_lshl_add_u64 v[24:25], v[24:25], 0, v[118:119]
	v_cvt_pk_fp8_f32 v117, v32, v115
	v_cvt_pk_fp8_f32 v118, v33, v116
	v_cvt_pk_fp8_f32 v117, v15, v30 op_sel:[0,0,1]
	v_cvt_pk_fp8_f32 v118, v31, v114 op_sel:[0,0,1]
	global_store_byte v[24:25], v117, off
	global_store_byte v[24:25], v118, off offset:256
	v_lshrrev_b32_e32 v119, 8, v117
	global_store_byte v[24:25], v119, off offset:64
	v_lshrrev_b32_e32 v119, 8, v118
	global_store_byte v[24:25], v119, off offset:320
	global_store_byte_d16_hi v[24:25], v117, off offset:128
	global_store_byte_d16_hi v[24:25], v118, off offset:384
	v_lshrrev_b32_e32 v117, 24, v117
	global_store_byte v[24:25], v117, off offset:192
	v_lshrrev_b32_e32 v117, 24, v118
	global_store_byte v[24:25], v117, off offset:448
	s_and_b64 vcc, exec, s[6:7]
	s_cbranch_vccz .LBB0_150

; __device__ __forceinline__ u32x4 pack8(const f32x4 a, const f32x4 b) { u32x4 w; w.x = cvt_pk_bf16(a[0], a[1]); w.y = cvt_pk_bf16(a[2], a[3]); w.z = cvt_pk_bf16(b[0], b[1]); w.w = cvt_pk_bf16(b[2], b[3]); return w; }
;     __device__ __forceinline__ void operator()(const f32x4 (&acc)[2][2][4][2], const Unit& u, int wr, int wc, int fr_in, int fq_in) const {
;     ...
;                     const int row = row0 + ai * HALF + m * 16; const float r = t[ai * 64 + m * 16 + fr] * sc;
;                     f32x4 v0 = acc[ai][bj][m][0] * r, v1 = acc[ai][bj][m][1] * r;
;                     if (kind == 2) rope8(v0, v1, rcos, rsin, row & (SEQ_ - 1), fq);
;                     *(u32x4*)(dst + (size_t)row * pitch + 8 * fq) = pack8(v0, v1);
;                     if (f8ch && colg >= 768 && colg < 1280) { u32x2 w8; w8.x = pack4_fp8_x16(v0); w8.y = pack4_fp8_x16(v1); *(u32x2*)(ws + WS_QB8 + (size_t)row * 512 + (colg - 768) + 8 * fq) = w8; }
;                     if (f8ch && colg >= 1280 && colg < 1792) { u32x2 w8; w8.x = pack4_fp8_x8(v0); w8.y = pack4_fp8_x8(v1); *(u32x2*)(ws + WS_KB8 + (size_t)row * 512 + (colg - 1280) + 8 * fq) = w8; }
.LBB0_159:
	v_ashrrev_i32_e32 v19, 31, v18
	v_mul_lo_u32 v15, s55, v18
	v_mul_lo_u32 v106, s54, v19
	v_mad_u64_u32 v[24:25], s[58:59], s54, v18, 0
	v_add3_u32 v25, v25, v106, v15
	v_lshl_add_u64 v[24:25], v[24:25], 1, v[16:17]
	v_cvt_pk_bf16_f32 v30, v2, v3
	v_cvt_pk_bf16_f32 v31, v4, v5
	v_cvt_pk_bf16_f32 v32, v22, v23
	v_cvt_pk_bf16_f32 v33, v20, v21
	global_store_dwordx4 v[24:25], v[30:33], off
	v_lshlrev_b64 v[24:25], 9, v[18:19]
	s_and_b64 vcc, exec, s[10:11]
	v_lshl_add_u64 v[24:25], s[18:19], 0, v[24:25]
	s_cbranch_vccnz .LBB0_161
	v_mul_f32_e32 v15, 0x41800000, v2
	v_mul_f32_e32 v30, 0x41800000, v3
	v_med3_f32 v15, v15, s64, v250
	v_med3_f32 v31, v30, s64, v250
	v_cvt_pk_fp8_f32 v30, v15, v31
	v_mul_f32_e32 v15, 0x41800000, v4
	v_mul_f32_e32 v31, 0x41800000, v5
	v_med3_f32 v15, v15, s64, v250
	v_med3_f32 v31, v31, s64, v250
	v_cvt_pk_fp8_f32 v30, v15, v31 op_sel:[0,0,1]
	v_mul_f32_e32 v15, 0x41800000, v22
	v_mul_f32_e32 v31, 0x41800000, v23
	v_med3_f32 v15, v15, s64, v250
	v_med3_f32 v32, v31, s64, v250
	v_cvt_pk_fp8_f32 v31, v15, v32
	v_mul_f32_e32 v15, 0x41800000, v20
	v_mul_f32_e32 v32, 0x41800000, v21
	v_med3_f32 v15, v15, s64, v250
	v_med3_f32 v32, v32, s64, v250
	v_cvt_pk_fp8_f32 v31, v15, v32 op_sel:[0,0,1]
	v_lshl_add_u64 v[32:33], v[24:25], 0, s[68:69]
	v_lshl_add_u64 v[32:33], v[32:33], 0, v[6:7]
	v_add_co_u32_e32 v32, vcc, 0x332ff000, v32
	s_nop 1
	v_addc_co_u32_e32 v33, vcc, 0, v33, vcc
	global_store_dwordx2 v[32:33], v[30:31], off offset:3328
.LBB0_161:
	v_mul_f32_e32 v15, 0x41000000, v2
	v_mul_f32_e32 v30, 0x41000000, v3
	v_mul_f32_e32 v31, 0x41000000, v4
	v_mul_f32_e32 v33, 0x41000000, v5
	v_mul_f32_e32 v106, 0x41000000, v22
	v_mul_f32_e32 v108, 0x41000000, v23
	v_mul_f32_e32 v109, 0x41000000, v20
	v_mul_f32_e32 v110, 0x41000000, v21
	s_and_b64 vcc, exec, s[12:13]
	v_med3_f32 v32, v15, s64, v250
	v_med3_f32 v107, v30, s64, v250
	v_med3_f32 v15, v31, s64, v250
	v_med3_f32 v30, v33, s64, v250
	v_med3_f32 v33, v106, s64, v250
	v_med3_f32 v108, v108, s64, v250
	v_med3_f32 v31, v109, s64, v250
	v_med3_f32 v106, v110, s64, v250
	s_cbranch_vccnz .LBB0_165
	v_cvt_pk_fp8_f32 v110, v32, v107
	v_cvt_pk_fp8_f32 v111, v33, v108
	v_lshl_add_u64 v[24:25], v[24:25], 0, s[68:69]
	v_lshl_add_u64 v[24:25], v[24:25], 0, v[6:7]
	v_cvt_pk_fp8_f32 v110, v15, v30 op_sel:[0,0,1]
	v_cvt_pk_fp8_f32 v111, v31, v106 op_sel:[0,0,1]
	v_add_co_u32_e32 v24, vcc, 0x342ff000, v24
	s_nop 1
	v_addc_co_u32_e32 v25, vcc, 0, v25, vcc
	global_store_dwordx2 v[24:25], v[110:111], off offset:2816
	s_and_b64 vcc, exec, s[14:15]
	s_cbranch_vccz .LBB0_166

;     __device__ __forceinline__ void operator()(const f32x4 (&acc)[2][2][4][2], const Unit& u, int wr, int wc, int fr_in, int fq_in) const {
;     ...
;                     if (kind == 2 && f8qk) { u32x2 w8; w8.x = pack4_fp8_x8(v0); w8.y = pack4_fp8_x8(v1); *(u32x2*)(ws + WS_KR8 + (size_t)row * 32 + 8 * fq) = w8; }
.LBB0_164:
	v_cvt_pk_fp8_f32 v24, v32, v107
	v_cvt_pk_fp8_f32 v25, v33, v108
	v_cvt_pk_fp8_f32 v24, v15, v30 op_sel:[0,0,1]
	v_cvt_pk_fp8_f32 v25, v31, v106 op_sel:[0,0,1]
	v_lshlrev_b64 v[30:31], 5, v[18:19]
	v_lshl_add_u64 v[30:31], s[34:35], 0, v[30:31]
	v_lshl_add_u64 v[30:31], v[30:31], 0, v[6:7]
	global_store_dwordx2 v[30:31], v[24:25], off
	s_and_b64 vcc, exec, s[8:9]
	s_cbranch_vccnz .LBB0_171
	s_branch .LBB0_168

;     __device__ __forceinline__ void operator()(const f32x4 (&acc)[2][2][4][2], const Unit& u, int wr, int wc, int fr_in, int fq_in) const {
;     ...
;                     if (f8ch && colg >= 1792) {
;                         const int c0_ = colg - 1792 + 8 * fq, bb_ = row >> 13, pos_ = row & (SEQ_ - 1), key_ = pos_ & 63, k32_ = key_ & 31;
;                         unsigned char* p_ = ws + WS_VB8T + ((((size_t)(bb_ * 8 + (c0_ >> 6)) * 128 + (pos_ >> 6)) * 64 + (c0_ & 63)) * 64) + 32 * ((k32_ >> 2) & 1) + 16 * (key_ >> 5) + (k32_ & 3) + 4 * (k32_ >> 3);
;                         const unsigned w0_ = pack4_fp8_x8(v0), w1_ = pack4_fp8_x8(v1);
; #pragma unroll
;                         for (int e_ = 0; e_ < 4; ++e_) { p_[e_ * 64] = (unsigned char)((w0_ >> (8 * e_)) & 0xffu); p_[(4 + e_) * 64] = (unsigned char)((w1_ >> (8 * e_)) & 0xffu); }
;                     }
.LBB0_166:
	v_ashrrev_i32_e32 v24, 10, v18
	v_and_b32_e32 v24, -8, v24
	v_add_u32_e32 v24, v24, v29
	v_ashrrev_i32_e32 v25, 31, v24
	v_lshlrev_b64 v[24:25], 13, v[24:25]
	v_and_or_b32 v24, v18, s50, v24
	v_or_b32_e32 v24, v24, v28
	v_lshlrev_b64 v[24:25], 6, v[24:25]
	v_lshl_add_u64 v[24:25], s[24:25], 0, v[24:25]
	v_lshrrev_b32_e32 v109, 1, v18
	v_lshl_add_u64 v[24:25], v[24:25], 0, v[0:1]
	v_and_b32_e32 v110, 16, v109
	v_mov_b32_e32 v111, v1
	v_lshl_add_u64 v[24:25], v[24:25], 0, v[110:111]
	v_lshl_add_u64 v[24:25], v[24:25], 0, v[8:9]
	v_and_b32_e32 v110, 12, v109
	v_lshl_add_u64 v[24:25], v[24:25], 0, v[110:111]
	v_cvt_pk_fp8_f32 v109, v32, v107
	v_cvt_pk_fp8_f32 v110, v33, v108
	v_cvt_pk_fp8_f32 v109, v15, v30 op_sel:[0,0,1]
	v_cvt_pk_fp8_f32 v110, v31, v106 op_sel:[0,0,1]
	global_store_byte v[24:25], v109, off
	global_store_byte v[24:25], v110, off offset:256
	v_lshrrev_b32_e32 v111, 8, v109
	global_store_byte v[24:25], v111, off offset:64
	v_lshrrev_b32_e32 v111, 8, v110
	global_store_byte v[24:25], v111, off offset:320
	global_store_byte_d16_hi v[24:25], v109, off offset:128
	global_store_byte_d16_hi v[24:25], v110, off offset:384
	v_lshrrev_b32_e32 v109, 24, v109
	global_store_byte v[24:25], v109, off offset:192
	v_lshrrev_b32_e32 v109, 24, v110
	global_store_byte v[24:25], v109, off offset:448
	s_and_b64 vcc, exec, s[6:7]
	s_cbranch_vccz .LBB0_164

; __device__ __forceinline__ u32x4 pack8(const f32x4 a, const f32x4 b) { u32x4 w; w.x = cvt_pk_bf16(a[0], a[1]); w.y = cvt_pk_bf16(a[2], a[3]); w.z = cvt_pk_bf16(b[0], b[1]); w.w = cvt_pk_bf16(b[2], b[3]); return w; }
;     __device__ __forceinline__ void operator()(const f32x4 (&acc)[2][2][4][2], const Unit& u, int wr, int wc, int fr_in, int fq_in) const {
;     ...
;                     const int row = row0 + ai * HALF + m * 16; const float r = t[ai * 64 + m * 16 + fr] * sc;
;                     f32x4 v0 = acc[ai][bj][m][0] * r, v1 = acc[ai][bj][m][1] * r;
;                     if (kind == 2) rope8(v0, v1, rcos, rsin, row & (SEQ_ - 1), fq);
;                     *(u32x4*)(dst + (size_t)row * pitch + 8 * fq) = pack8(v0, v1);
;                     if (f8ch && colg >= 768 && colg < 1280) { u32x2 w8; w8.x = pack4_fp8_x16(v0); w8.y = pack4_fp8_x16(v1); *(u32x2*)(ws + WS_QB8 + (size_t)row * 512 + (colg - 768) + 8 * fq) = w8; }
;                     if (f8ch && colg >= 1280 && colg < 1792) { u32x2 w8; w8.x = pack4_fp8_x8(v0); w8.y = pack4_fp8_x8(v1); *(u32x2*)(ws + WS_KB8 + (size_t)row * 512 + (colg - 1280) + 8 * fq) = w8; }
.LBB0_173:
	v_ashrrev_i32_e32 v19, 31, v18
	v_mul_lo_u32 v15, s55, v18
	v_mul_lo_u32 v98, s54, v19
	v_mad_u64_u32 v[24:25], s[54:55], s54, v18, 0
	v_add3_u32 v25, v25, v98, v15
	v_lshl_add_u64 v[16:17], v[24:25], 1, v[16:17]
	v_cvt_pk_bf16_f32 v30, v2, v3
	v_cvt_pk_bf16_f32 v31, v4, v5
	v_cvt_pk_bf16_f32 v32, v22, v23
	v_cvt_pk_bf16_f32 v33, v20, v21
	global_store_dwordx4 v[16:17], v[30:33], off
	v_lshlrev_b64 v[16:17], 9, v[18:19]
	s_and_b64 vcc, exec, s[10:11]
	v_lshl_add_u64 v[16:17], s[18:19], 0, v[16:17]
	s_cbranch_vccnz .LBB0_175
	v_mul_f32_e32 v15, 0x41800000, v2
	v_mul_f32_e32 v24, 0x41800000, v3
	v_med3_f32 v15, v15, s64, v250
	v_med3_f32 v25, v24, s64, v250
	v_cvt_pk_fp8_f32 v24, v15, v25
	v_mul_f32_e32 v15, 0x41800000, v4
	v_mul_f32_e32 v25, 0x41800000, v5
	v_med3_f32 v15, v15, s64, v250
	v_med3_f32 v25, v25, s64, v250
	v_cvt_pk_fp8_f32 v24, v15, v25 op_sel:[0,0,1]
	v_mul_f32_e32 v15, 0x41800000, v22
	v_mul_f32_e32 v25, 0x41800000, v23
	v_med3_f32 v15, v15, s64, v250
	v_med3_f32 v30, v25, s64, v250
	v_cvt_pk_fp8_f32 v25, v15, v30
	v_mul_f32_e32 v15, 0x41800000, v20
	v_mul_f32_e32 v30, 0x41800000, v21
	v_med3_f32 v15, v15, s64, v250
	v_med3_f32 v30, v30, s64, v250
	v_cvt_pk_fp8_f32 v25, v15, v30 op_sel:[0,0,1]
	v_lshl_add_u64 v[30:31], v[16:17], 0, s[68:69]
	v_lshl_add_u64 v[30:31], v[30:31], 0, v[6:7]
	v_add_co_u32_e32 v30, vcc, 0x332ff000, v30
	s_nop 1
	v_addc_co_u32_e32 v31, vcc, 0, v31, vcc
	global_store_dwordx2 v[30:31], v[24:25], off offset:3328
.LBB0_175:
	v_mul_f32_e32 v15, 0x41000000, v2
	v_mul_f32_e32 v24, 0x41000000, v3
	v_mul_f32_e32 v25, 0x41000000, v4
	v_mul_f32_e32 v31, 0x41000000, v5
	v_mul_f32_e32 v32, 0x41000000, v22
	v_mul_f32_e32 v98, 0x41000000, v23
	v_mul_f32_e32 v99, 0x41000000, v20
	v_mul_f32_e32 v100, 0x41000000, v21
	s_and_b64 vcc, exec, s[12:13]
	v_med3_f32 v30, v15, s64, v250
	v_med3_f32 v33, v24, s64, v250
	v_med3_f32 v15, v25, s64, v250
	v_med3_f32 v24, v31, s64, v250
	v_med3_f32 v31, v32, s64, v250
	v_med3_f32 v98, v98, s64, v250
	v_med3_f32 v25, v99, s64, v250
	v_med3_f32 v32, v100, s64, v250
	s_cbranch_vccnz .LBB0_179
	v_cvt_pk_fp8_f32 v100, v30, v33
	v_cvt_pk_fp8_f32 v101, v31, v98
	v_lshl_add_u64 v[16:17], v[16:17], 0, s[68:69]
	v_lshl_add_u64 v[16:17], v[16:17], 0, v[6:7]
	v_cvt_pk_fp8_f32 v100, v15, v24 op_sel:[0,0,1]
	v_cvt_pk_fp8_f32 v101, v25, v32 op_sel:[0,0,1]
	v_add_co_u32_e32 v16, vcc, 0x342ff000, v16
	s_nop 1
	v_addc_co_u32_e32 v17, vcc, 0, v17, vcc
	global_store_dwordx2 v[16:17], v[100:101], off offset:2816
	s_and_b64 vcc, exec, s[14:15]
	s_cbranch_vccz .LBB0_180

;     __device__ __forceinline__ void operator()(const f32x4 (&acc)[2][2][4][2], const Unit& u, int wr, int wc, int fr_in, int fq_in) const {
;     ...
;                     if (kind == 2 && f8qk) { u32x2 w8; w8.x = pack4_fp8_x8(v0); w8.y = pack4_fp8_x8(v1); *(u32x2*)(ws + WS_KR8 + (size_t)row * 32 + 8 * fq) = w8; }
.LBB0_178:
	v_cvt_pk_fp8_f32 v16, v30, v33
	v_cvt_pk_fp8_f32 v17, v31, v98
	v_cvt_pk_fp8_f32 v16, v15, v24 op_sel:[0,0,1]
	v_cvt_pk_fp8_f32 v17, v25, v32 op_sel:[0,0,1]
	v_lshlrev_b64 v[24:25], 5, v[18:19]
	v_lshl_add_u64 v[24:25], s[34:35], 0, v[24:25]
	v_lshl_add_u64 v[24:25], v[24:25], 0, v[6:7]
	global_store_dwordx2 v[24:25], v[16:17], off
	s_and_b64 vcc, exec, s[8:9]
	s_cbranch_vccnz .LBB0_185
	s_branch .LBB0_182

;     __device__ __forceinline__ void operator()(const f32x4 (&acc)[2][2][4][2], const Unit& u, int wr, int wc, int fr_in, int fq_in) const {
;     ...
;                     if (f8ch && colg >= 1792) {
;                         const int c0_ = colg - 1792 + 8 * fq, bb_ = row >> 13, pos_ = row & (SEQ_ - 1), key_ = pos_ & 63, k32_ = key_ & 31;
;                         unsigned char* p_ = ws + WS_VB8T + ((((size_t)(bb_ * 8 + (c0_ >> 6)) * 128 + (pos_ >> 6)) * 64 + (c0_ & 63)) * 64) + 32 * ((k32_ >> 2) & 1) + 16 * (key_ >> 5) + (k32_ & 3) + 4 * (k32_ >> 3);
;                         const unsigned w0_ = pack4_fp8_x8(v0), w1_ = pack4_fp8_x8(v1);
; #pragma unroll
;                         for (int e_ = 0; e_ < 4; ++e_) { p_[e_ * 64] = (unsigned char)((w0_ >> (8 * e_)) & 0xffu); p_[(4 + e_) * 64] = (unsigned char)((w1_ >> (8 * e_)) & 0xffu); }
;                     }
.LBB0_180:
	v_ashrrev_i32_e32 v16, 10, v18
	v_and_b32_e32 v16, -8, v16
	v_add_u32_e32 v16, v16, v29
	v_ashrrev_i32_e32 v17, 31, v16
	v_lshlrev_b64 v[16:17], 13, v[16:17]
	v_and_or_b32 v16, v18, s50, v16
	v_or_b32_e32 v16, v16, v28
	v_lshlrev_b64 v[16:17], 6, v[16:17]
	v_lshl_add_u64 v[16:17], s[24:25], 0, v[16:17]
	v_lshrrev_b32_e32 v99, 1, v18
	v_lshl_add_u64 v[16:17], v[16:17], 0, v[0:1]
	v_and_b32_e32 v28, 16, v99
	v_mov_b32_e32 v29, v1
	v_lshl_add_u64 v[16:17], v[16:17], 0, v[28:29]
	v_lshl_add_u64 v[16:17], v[16:17], 0, v[8:9]
	v_and_b32_e32 v28, 12, v99
	v_lshl_add_u64 v[16:17], v[16:17], 0, v[28:29]
	v_cvt_pk_fp8_f32 v28, v30, v33
	v_cvt_pk_fp8_f32 v29, v31, v98
	v_cvt_pk_fp8_f32 v28, v15, v24 op_sel:[0,0,1]
	v_cvt_pk_fp8_f32 v29, v25, v32 op_sel:[0,0,1]
	global_store_byte v[16:17], v28, off
	global_store_byte v[16:17], v29, off offset:256
	v_lshrrev_b32_e32 v99, 8, v28
	global_store_byte v[16:17], v99, off offset:64
	v_lshrrev_b32_e32 v99, 8, v29
	global_store_byte v[16:17], v99, off offset:320
	global_store_byte_d16_hi v[16:17], v28, off offset:128
	global_store_byte_d16_hi v[16:17], v29, off offset:384
	v_lshrrev_b32_e32 v28, 24, v28
	global_store_byte v[16:17], v28, off offset:192
	v_lshrrev_b32_e32 v28, 24, v29
	global_store_byte v[16:17], v28, off offset:448
	s_and_b64 vcc, exec, s[6:7]
	s_cbranch_vccz .LBB0_178

; __device__ __forceinline__ u32x4 pack8(const f32x4 a, const f32x4 b) { u32x4 w; w.x = cvt_pk_bf16(a[0], a[1]); w.y = cvt_pk_bf16(a[2], a[3]); w.z = cvt_pk_bf16(b[0], b[1]); w.w = cvt_pk_bf16(b[2], b[3]); return w; }
;     __device__ __forceinline__ void operator()(const f32x4 (&acc)[2][2][4][2], const Unit& u, int wr, int wc, int fr_in, int fq_in) const {
;     ...
;             for (int ai = 0; ai < 2; ++ai)
; #pragma unroll
;                 for (int m = 0; m < 4; ++m) {
;                     const int row = row0 + ai * HALF + m * 16; const float r = t[ai * 64 + m * 16 + fr] * sc;
;                     f32x4 v0 = acc[ai][bj][m][0] * r, v1 = acc[ai][bj][m][1] * r;
;                     if (kind == 2) rope8(v0, v1, rcos, rsin, row & (SEQ_ - 1), fq);
;                     *(u32x4*)(dst + (size_t)row * pitch + 8 * fq) = pack8(v0, v1);
;                     if (f8ch && colg >= 768 && colg < 1280) { u32x2 w8; w8.x = pack4_fp8_x16(v0); w8.y = pack4_fp8_x16(v1); *(u32x2*)(ws + WS_QB8 + (size_t)row * 512 + (colg - 768) + 8 * fq) = w8; }
;                     if (f8ch && colg >= 1280 && colg < 1792) { u32x2 w8; w8.x = pack4_fp8_x8(v0); w8.y = pack4_fp8_x8(v1); *(u32x2*)(ws + WS_KB8 + (size_t)row * 512 + (colg - 1280) + 8 * fq) = w8; }
;                     if (f8ch && colg >= 1792) {
;                         const int c0_ = colg - 1792 + 8 * fq, bb_ = row >> 13, pos_ = row & (SEQ_ - 1), key_ = pos_ & 63, k32_ = key_ & 31;
;                         unsigned char* p_ = ws + WS_VB8T + ((((size_t)(bb_ * 8 + (c0_ >> 6)) * 128 + (pos_ >> 6)) * 64 + (c0_ & 63)) * 64) + 32 * ((k32_ >> 2) & 1) + 16 * (key_ >> 5) + (k32_ & 3) + 4 * (k32_ >> 3);
;                         const unsigned w0_ = pack4_fp8_x8(v0), w1_ = pack4_fp8_x8(v1);
; #pragma unroll
;                         for (int e_ = 0; e_ < 4; ++e_) { p_[e_ * 64] = (unsigned char)((w0_ >> (8 * e_)) & 0xffu); p_[(4 + e_) * 64] = (unsigned char)((w1_ >> (8 * e_)) & 0xffu); }
;                     }
;                     if (kind == 2 && f8qk) { u32x2 w8; w8.x = pack4_fp8_x8(v0); w8.y = pack4_fp8_x8(v1); *(u32x2*)(ws + WS_KR8 + (size_t)row * 32 + 8 * fq) = w8; }
.LBB0_206:
	v_ashrrev_i32_e32 v15, 31, v14
	v_mul_lo_u32 v30, s55, v14
	v_mul_lo_u32 v31, s54, v15
	v_mad_u64_u32 v[28:29], s[56:57], s54, v14, 0
	v_lshl_add_u64 v[16:17], v[6:7], 1, s[14:15]
	v_add3_u32 v29, v29, v31, v30
	s_add_i32 s9, s94, 0xfffffd80
	v_cvt_pk_bf16_f32 v22, v2, v3
	v_cvt_pk_bf16_f32 v23, v4, v5
	v_lshl_add_u64 v[28:29], v[28:29], 1, v[16:17]
	s_cmpk_lt_u32 s9, 0x200
	v_cvt_pk_bf16_f32 v24, v20, v21
	v_cvt_pk_bf16_f32 v25, v18, v19
	global_store_dwordx4 v[28:29], v[22:25], off
	s_cselect_b64 s[14:15], -1, 0
	s_cmpk_gt_u32 s9, 0x1ff
	v_lshlrev_b64 v[22:23], 9, v[14:15]
	v_lshl_add_u64 v[22:23], s[18:19], 0, v[22:23]
	s_cbranch_scc1 .LBB0_208
	v_mul_f32_e32 v24, 0x41800000, v2
	v_med3_f32 v25, v24, s64, v250
	v_mul_f32_e32 v24, 0x41800000, v3
	v_med3_f32 v28, v24, s64, v250
	v_cvt_pk_fp8_f32 v24, v25, v28
	v_mul_f32_e32 v25, 0x41800000, v4
	v_mul_f32_e32 v28, 0x41800000, v5
	v_med3_f32 v25, v25, s64, v250
	v_med3_f32 v28, v28, s64, v250
	v_cvt_pk_fp8_f32 v24, v25, v28 op_sel:[0,0,1]
	v_mul_f32_e32 v25, 0x41800000, v20
	v_med3_f32 v28, v25, s64, v250
	v_mul_f32_e32 v25, 0x41800000, v21
	v_med3_f32 v29, v25, s64, v250
	v_cvt_pk_fp8_f32 v25, v28, v29
	v_mul_f32_e32 v28, 0x41800000, v18
	v_mul_f32_e32 v29, 0x41800000, v19
	v_med3_f32 v28, v28, s64, v250
	v_med3_f32 v29, v29, s64, v250
	s_add_i32 s68, s94, s46
	v_cvt_pk_fp8_f32 v25, v28, v29 op_sel:[0,0,1]
	v_lshl_add_u64 v[28:29], v[22:23], 0, s[68:69]
	v_lshl_add_u64 v[28:29], v[28:29], 0, v[6:7]
	v_add_co_u32_e32 v28, vcc, 0x332ff000, v28
	s_nop 1
	v_addc_co_u32_e32 v29, vcc, 0, v29, vcc
	global_store_dwordx2 v[28:29], v[24:25], off offset:3456
.LBB0_208:
	s_add_i32 s9, s94, 0xfffffb80
	s_cmpk_lt_u32 s9, 0x200
	v_mul_f32_e32 v24, 0x41000000, v2
	v_mul_f32_e32 v25, 0x41000000, v3
	v_mul_f32_e32 v28, 0x41000000, v4
	v_mul_f32_e32 v29, 0x41000000, v5
	v_mul_f32_e32 v31, 0x41000000, v20
	v_mul_f32_e32 v32, 0x41000000, v21
	v_mul_f32_e32 v91, 0x41000000, v18
	v_mul_f32_e32 v92, 0x41000000, v19
	s_cselect_b64 s[58:59], -1, 0
	s_cmpk_gt_u32 s9, 0x1ff
	v_med3_f32 v30, v24, s64, v250
	v_med3_f32 v33, v25, s64, v250
	v_med3_f32 v24, v28, s64, v250
	v_med3_f32 v25, v29, s64, v250
	v_med3_f32 v31, v31, s64, v250
	v_med3_f32 v90, v32, s64, v250
	v_med3_f32 v29, v91, s64, v250
	v_med3_f32 v32, v92, s64, v250
	s_cbranch_scc1 .LBB0_210
	v_cvt_pk_fp8_f32 v92, v30, v33
	v_cvt_pk_fp8_f32 v93, v31, v90
	s_add_i32 s68, s94, s46
	v_lshl_add_u64 v[22:23], v[22:23], 0, s[68:69]
	v_cvt_pk_fp8_f32 v92, v24, v25 op_sel:[0,0,1]
	v_cvt_pk_fp8_f32 v93, v29, v32 op_sel:[0,0,1]
	v_lshl_add_u64 v[22:23], v[22:23], 0, v[6:7]
	v_add_co_u32_e32 v22, vcc, 0x342ff000, v22
	s_nop 1
	v_addc_co_u32_e32 v23, vcc, 0, v23, vcc
	global_store_dwordx2 v[22:23], v[92:93], off offset:2944
.LBB0_210:
	s_cmpk_gt_i32 s8, 0x6ff
	v_add_u32_e32 v22, s8, v27
	s_cselect_b64 s[60:61], -1, 0
	s_cmpk_lt_i32 s8, 0x700
	v_ashrrev_i32_e32 v28, 6, v22
	v_and_b32_e32 v27, 56, v22
	s_cbranch_scc1 .LBB0_212
	v_ashrrev_i32_e32 v22, 10, v14
	v_and_b32_e32 v22, -8, v22
	v_add_u32_e32 v22, v28, v22
	v_ashrrev_i32_e32 v23, 31, v22
	v_lshlrev_b64 v[22:23], 13, v[22:23]
	v_and_or_b32 v22, v14, s50, v22
	v_or_b32_e32 v22, v22, v27
	v_lshlrev_b64 v[22:23], 6, v[22:23]
	v_lshl_add_u64 v[22:23], s[24:25], 0, v[22:23]
	v_lshrrev_b32_e32 v91, 1, v14
	v_lshl_add_u64 v[22:23], v[22:23], 0, v[0:1]
	v_and_b32_e32 v92, 16, v91
	v_mov_b32_e32 v93, v1
	v_lshl_add_u64 v[22:23], v[22:23], 0, v[92:93]
	v_lshl_add_u64 v[22:23], v[22:23], 0, v[8:9]
	v_and_b32_e32 v92, 12, v91
	v_lshl_add_u64 v[22:23], v[22:23], 0, v[92:93]
	v_cvt_pk_fp8_f32 v91, v30, v33
	v_cvt_pk_fp8_f32 v92, v31, v90
	v_cvt_pk_fp8_f32 v91, v24, v25 op_sel:[0,0,1]
	v_cvt_pk_fp8_f32 v92, v29, v32 op_sel:[0,0,1]
	global_store_byte v[22:23], v91, off
	global_store_byte v[22:23], v92, off offset:256
	v_lshrrev_b32_e32 v93, 8, v91
	global_store_byte v[22:23], v93, off offset:64
	v_lshrrev_b32_e32 v93, 8, v92
	global_store_byte v[22:23], v93, off offset:320
	global_store_byte_d16_hi v[22:23], v91, off offset:128
	global_store_byte_d16_hi v[22:23], v92, off offset:384
	v_lshrrev_b32_e32 v91, 24, v91
	global_store_byte v[22:23], v91, off offset:192
	v_lshrrev_b32_e32 v91, 24, v92
	global_store_byte v[22:23], v91, off offset:448
.LBB0_212:
	s_and_b64 vcc, exec, s[6:7]
	s_cbranch_vccnz .LBB0_214
	v_cvt_pk_fp8_f32 v22, v30, v33
	v_cvt_pk_fp8_f32 v23, v31, v90
	v_cvt_pk_fp8_f32 v22, v24, v25 op_sel:[0,0,1]
	v_cvt_pk_fp8_f32 v23, v29, v32 op_sel:[0,0,1]
	v_lshlrev_b64 v[24:25], 5, v[14:15]
	v_lshl_add_u64 v[24:25], s[34:35], 0, v[24:25]
	v_lshl_add_u64 v[24:25], v[24:25], 0, v[6:7]
	global_store_dwordx2 v[24:25], v[22:23], off

; __device__ __forceinline__ u32x4 pack8(const f32x4 a, const f32x4 b) { u32x4 w; w.x = cvt_pk_bf16(a[0], a[1]); w.y = cvt_pk_bf16(a[2], a[3]); w.z = cvt_pk_bf16(b[0], b[1]); w.w = cvt_pk_bf16(b[2], b[3]); return w; }
;     __device__ __forceinline__ void operator()(const f32x4 (&acc)[2][2][4][2], const Unit& u, int wr, int wc, int fr_in, int fq_in) const {
;     ...
;                     const int row = row0 + ai * HALF + m * 16; const float r = t[ai * 64 + m * 16 + fr] * sc;
;                     f32x4 v0 = acc[ai][bj][m][0] * r, v1 = acc[ai][bj][m][1] * r;
;                     if (kind == 2) rope8(v0, v1, rcos, rsin, row & (SEQ_ - 1), fq);
;                     *(u32x4*)(dst + (size_t)row * pitch + 8 * fq) = pack8(v0, v1);
;                     if (f8ch && colg >= 768 && colg < 1280) { u32x2 w8; w8.x = pack4_fp8_x16(v0); w8.y = pack4_fp8_x16(v1); *(u32x2*)(ws + WS_QB8 + (size_t)row * 512 + (colg - 768) + 8 * fq) = w8; }
;                     if (f8ch && colg >= 1280 && colg < 1792) { u32x2 w8; w8.x = pack4_fp8_x8(v0); w8.y = pack4_fp8_x8(v1); *(u32x2*)(ws + WS_KB8 + (size_t)row * 512 + (colg - 1280) + 8 * fq) = w8; }
.LBB0_220:
	v_ashrrev_i32_e32 v19, 31, v18
	v_mul_lo_u32 v15, s55, v18
	v_mul_lo_u32 v29, s54, v19
	v_mad_u64_u32 v[24:25], s[10:11], s54, v18, 0
	v_add3_u32 v25, v25, v29, v15
	v_lshl_add_u64 v[24:25], v[24:25], 1, v[16:17]
	v_cvt_pk_bf16_f32 v30, v2, v3
	v_cvt_pk_bf16_f32 v31, v4, v5
	v_cvt_pk_bf16_f32 v32, v22, v23
	v_cvt_pk_bf16_f32 v33, v20, v21
	global_store_dwordx4 v[24:25], v[30:33], off
	v_cndmask_b32_e64 v15, 0, 1, s[14:15]
	v_lshlrev_b64 v[24:25], 9, v[18:19]
	v_cmp_ne_u32_e64 s[10:11], 1, v15
	s_andn2_b64 vcc, exec, s[14:15]
	v_lshl_add_u64 v[24:25], s[18:19], 0, v[24:25]
	s_cbranch_vccnz .LBB0_222
	v_mul_f32_e32 v15, 0x41800000, v2
	v_mul_f32_e32 v29, 0x41800000, v3
	v_med3_f32 v15, v15, s64, v250
	v_med3_f32 v29, v29, s64, v250
	v_cvt_pk_fp8_f32 v30, v15, v29
	v_mul_f32_e32 v15, 0x41800000, v4
	v_mul_f32_e32 v29, 0x41800000, v5
	v_med3_f32 v15, v15, s64, v250
	v_med3_f32 v29, v29, s64, v250
	v_cvt_pk_fp8_f32 v30, v15, v29 op_sel:[0,0,1]
	v_mul_f32_e32 v15, 0x41800000, v22
	v_mul_f32_e32 v29, 0x41800000, v23
	v_med3_f32 v15, v15, s64, v250
	v_med3_f32 v29, v29, s64, v250
	v_cvt_pk_fp8_f32 v31, v15, v29
	v_mul_f32_e32 v15, 0x41800000, v20
	v_mul_f32_e32 v29, 0x41800000, v21
	v_med3_f32 v15, v15, s64, v250
	v_med3_f32 v29, v29, s64, v250
	s_add_i32 s68, s94, s46
	v_cvt_pk_fp8_f32 v31, v15, v29 op_sel:[0,0,1]
	v_lshl_add_u64 v[32:33], v[24:25], 0, s[68:69]
	v_lshl_add_u64 v[32:33], v[32:33], 0, v[6:7]
	v_add_co_u32_e32 v32, vcc, 0x332ff000, v32
	s_nop 1
	v_addc_co_u32_e32 v33, vcc, 0, v33, vcc
	global_store_dwordx2 v[32:33], v[30:31], off offset:3456
.LBB0_222:
	v_cndmask_b32_e64 v15, 0, 1, s[58:59]
	v_cmp_ne_u32_e64 s[12:13], 1, v15
	v_mul_f32_e32 v15, 0x41000000, v2
	v_mul_f32_e32 v29, 0x41000000, v3
	v_mul_f32_e32 v30, 0x41000000, v4
	v_mul_f32_e32 v32, 0x41000000, v5
	v_mul_f32_e32 v33, 0x41000000, v22
	v_mul_f32_e32 v83, 0x41000000, v23
	v_mul_f32_e32 v84, 0x41000000, v20
	v_mul_f32_e32 v85, 0x41000000, v21
	s_andn2_b64 vcc, exec, s[58:59]
	v_med3_f32 v31, v15, s64, v250
	v_med3_f32 v82, v29, s64, v250
	v_med3_f32 v15, v30, s64, v250
	v_med3_f32 v29, v32, s64, v250
	v_med3_f32 v32, v33, s64, v250
	v_med3_f32 v83, v83, s64, v250
	v_med3_f32 v30, v84, s64, v250
	v_med3_f32 v33, v85, s64, v250
	s_cbranch_vccnz .LBB0_226
	v_cvt_pk_fp8_f32 v84, v31, v82
	v_cvt_pk_fp8_f32 v85, v32, v83
	s_add_i32 s68, s94, s46
	v_lshl_add_u64 v[24:25], v[24:25], 0, s[68:69]
	v_cvt_pk_fp8_f32 v84, v15, v29 op_sel:[0,0,1]
	v_cvt_pk_fp8_f32 v85, v30, v33 op_sel:[0,0,1]
	v_lshl_add_u64 v[24:25], v[24:25], 0, v[6:7]
	v_add_co_u32_e32 v24, vcc, 0x342ff000, v24
	s_nop 1
	v_addc_co_u32_e32 v25, vcc, 0, v25, vcc
	global_store_dwordx2 v[24:25], v[84:85], off offset:2944
	v_cndmask_b32_e64 v24, 0, 1, s[60:61]
	v_cmp_ne_u32_e64 s[14:15], 1, v24
	s_andn2_b64 vcc, exec, s[60:61]
	s_cbranch_vccz .LBB0_227

;     __device__ __forceinline__ void operator()(const f32x4 (&acc)[2][2][4][2], const Unit& u, int wr, int wc, int fr_in, int fq_in) const {
;     ...
;                     if (kind == 2 && f8qk) { u32x2 w8; w8.x = pack4_fp8_x8(v0); w8.y = pack4_fp8_x8(v1); *(u32x2*)(ws + WS_KR8 + (size_t)row * 32 + 8 * fq) = w8; }
.LBB0_225:
	v_cvt_pk_fp8_f32 v24, v31, v82
	v_cvt_pk_fp8_f32 v25, v32, v83
	v_cvt_pk_fp8_f32 v24, v15, v29 op_sel:[0,0,1]
	v_cvt_pk_fp8_f32 v25, v30, v33 op_sel:[0,0,1]
	v_lshlrev_b64 v[30:31], 5, v[18:19]
	v_lshl_add_u64 v[30:31], s[34:35], 0, v[30:31]
	v_lshl_add_u64 v[30:31], v[30:31], 0, v[6:7]
	global_store_dwordx2 v[30:31], v[24:25], off
	s_and_b64 vcc, exec, s[8:9]
	s_cbranch_vccnz .LBB0_232
	s_branch .LBB0_229

;     __device__ __forceinline__ void operator()(const f32x4 (&acc)[2][2][4][2], const Unit& u, int wr, int wc, int fr_in, int fq_in) const {
;     ...
;                     if (f8ch && colg >= 1792) {
;                         const int c0_ = colg - 1792 + 8 * fq, bb_ = row >> 13, pos_ = row & (SEQ_ - 1), key_ = pos_ & 63, k32_ = key_ & 31;
;                         unsigned char* p_ = ws + WS_VB8T + ((((size_t)(bb_ * 8 + (c0_ >> 6)) * 128 + (pos_ >> 6)) * 64 + (c0_ & 63)) * 64) + 32 * ((k32_ >> 2) & 1) + 16 * (key_ >> 5) + (k32_ & 3) + 4 * (k32_ >> 3);
;                         const unsigned w0_ = pack4_fp8_x8(v0), w1_ = pack4_fp8_x8(v1);
; #pragma unroll
;                         for (int e_ = 0; e_ < 4; ++e_) { p_[e_ * 64] = (unsigned char)((w0_ >> (8 * e_)) & 0xffu); p_[(4 + e_) * 64] = (unsigned char)((w1_ >> (8 * e_)) & 0xffu); }
;                     }
.LBB0_227:
	v_ashrrev_i32_e32 v24, 10, v18
	v_and_b32_e32 v24, -8, v24
	v_add_u32_e32 v24, v24, v28
	v_ashrrev_i32_e32 v25, 31, v24
	v_lshlrev_b64 v[24:25], 13, v[24:25]
	v_and_or_b32 v24, v18, s50, v24
	v_or_b32_e32 v24, v24, v27
	v_lshlrev_b64 v[24:25], 6, v[24:25]
	v_lshl_add_u64 v[24:25], s[24:25], 0, v[24:25]
	v_lshrrev_b32_e32 v86, 1, v18
	v_lshl_add_u64 v[24:25], v[24:25], 0, v[0:1]
	v_and_b32_e32 v84, 16, v86
	v_mov_b32_e32 v85, v1
	v_lshl_add_u64 v[24:25], v[24:25], 0, v[84:85]
	v_lshl_add_u64 v[24:25], v[24:25], 0, v[8:9]
	v_and_b32_e32 v84, 12, v86
	v_lshl_add_u64 v[24:25], v[24:25], 0, v[84:85]
	v_cvt_pk_fp8_f32 v84, v31, v82
	v_cvt_pk_fp8_f32 v85, v32, v83
	v_cvt_pk_fp8_f32 v84, v15, v29 op_sel:[0,0,1]
	v_cvt_pk_fp8_f32 v85, v30, v33 op_sel:[0,0,1]
	global_store_byte v[24:25], v84, off
	global_store_byte v[24:25], v85, off offset:256
	v_lshrrev_b32_e32 v86, 8, v84
	global_store_byte v[24:25], v86, off offset:64
	v_lshrrev_b32_e32 v86, 8, v85
	global_store_byte v[24:25], v86, off offset:320
	global_store_byte_d16_hi v[24:25], v84, off offset:128
	global_store_byte_d16_hi v[24:25], v85, off offset:384
	v_lshrrev_b32_e32 v84, 24, v84
	global_store_byte v[24:25], v84, off offset:192
	v_lshrrev_b32_e32 v84, 24, v85
	global_store_byte v[24:25], v84, off offset:448
	s_and_b64 vcc, exec, s[6:7]
	s_cbranch_vccz .LBB0_225

; __device__ __forceinline__ u32x4 pack8(const f32x4 a, const f32x4 b) { u32x4 w; w.x = cvt_pk_bf16(a[0], a[1]); w.y = cvt_pk_bf16(a[2], a[3]); w.z = cvt_pk_bf16(b[0], b[1]); w.w = cvt_pk_bf16(b[2], b[3]); return w; }
;     __device__ __forceinline__ void operator()(const f32x4 (&acc)[2][2][4][2], const Unit& u, int wr, int wc, int fr_in, int fq_in) const {
;     ...
;                     const int row = row0 + ai * HALF + m * 16; const float r = t[ai * 64 + m * 16 + fr] * sc;
;                     f32x4 v0 = acc[ai][bj][m][0] * r, v1 = acc[ai][bj][m][1] * r;
;                     if (kind == 2) rope8(v0, v1, rcos, rsin, row & (SEQ_ - 1), fq);
;                     *(u32x4*)(dst + (size_t)row * pitch + 8 * fq) = pack8(v0, v1);
;                     if (f8ch && colg >= 768 && colg < 1280) { u32x2 w8; w8.x = pack4_fp8_x16(v0); w8.y = pack4_fp8_x16(v1); *(u32x2*)(ws + WS_QB8 + (size_t)row * 512 + (colg - 768) + 8 * fq) = w8; }
;                     if (f8ch && colg >= 1280 && colg < 1792) { u32x2 w8; w8.x = pack4_fp8_x8(v0); w8.y = pack4_fp8_x8(v1); *(u32x2*)(ws + WS_KB8 + (size_t)row * 512 + (colg - 1280) + 8 * fq) = w8; }
.LBB0_234:
	v_ashrrev_i32_e32 v19, 31, v18
	v_mul_lo_u32 v15, s55, v18
	v_mul_lo_u32 v29, s54, v19
	v_mad_u64_u32 v[24:25], s[58:59], s54, v18, 0
	v_add3_u32 v25, v25, v29, v15
	v_lshl_add_u64 v[24:25], v[24:25], 1, v[16:17]
	v_cvt_pk_bf16_f32 v30, v2, v3
	v_cvt_pk_bf16_f32 v31, v4, v5
	v_cvt_pk_bf16_f32 v32, v22, v23
	v_cvt_pk_bf16_f32 v33, v20, v21
	global_store_dwordx4 v[24:25], v[30:33], off
	v_lshlrev_b64 v[24:25], 9, v[18:19]
	s_and_b64 vcc, exec, s[10:11]
	v_lshl_add_u64 v[24:25], s[18:19], 0, v[24:25]
	s_cbranch_vccnz .LBB0_236
	v_mul_f32_e32 v15, 0x41800000, v2
	v_mul_f32_e32 v29, 0x41800000, v3
	v_med3_f32 v15, v15, s64, v250
	v_med3_f32 v29, v29, s64, v250
	v_cvt_pk_fp8_f32 v30, v15, v29
	v_mul_f32_e32 v15, 0x41800000, v4
	v_mul_f32_e32 v29, 0x41800000, v5
	v_med3_f32 v15, v15, s64, v250
	v_med3_f32 v29, v29, s64, v250
	v_cvt_pk_fp8_f32 v30, v15, v29 op_sel:[0,0,1]
	v_mul_f32_e32 v15, 0x41800000, v22
	v_mul_f32_e32 v29, 0x41800000, v23
	v_med3_f32 v15, v15, s64, v250
	v_med3_f32 v29, v29, s64, v250
	v_cvt_pk_fp8_f32 v31, v15, v29
	v_mul_f32_e32 v15, 0x41800000, v20
	v_mul_f32_e32 v29, 0x41800000, v21
	v_med3_f32 v15, v15, s64, v250
	v_med3_f32 v29, v29, s64, v250
	s_add_i32 s68, s94, s46
	v_cvt_pk_fp8_f32 v31, v15, v29 op_sel:[0,0,1]
	v_lshl_add_u64 v[32:33], v[24:25], 0, s[68:69]
	v_lshl_add_u64 v[32:33], v[32:33], 0, v[6:7]
	v_add_co_u32_e32 v32, vcc, 0x332ff000, v32
	s_nop 1
	v_addc_co_u32_e32 v33, vcc, 0, v33, vcc
	global_store_dwordx2 v[32:33], v[30:31], off offset:3456
.LBB0_236:
	v_mul_f32_e32 v15, 0x41000000, v2
	v_mul_f32_e32 v29, 0x41000000, v3
	v_mul_f32_e32 v30, 0x41000000, v4
	v_mul_f32_e32 v32, 0x41000000, v5
	v_mul_f32_e32 v33, 0x41000000, v22
	v_mul_f32_e32 v75, 0x41000000, v23
	v_mul_f32_e32 v76, 0x41000000, v20
	v_mul_f32_e32 v77, 0x41000000, v21
	s_and_b64 vcc, exec, s[12:13]
	v_med3_f32 v31, v15, s64, v250
	v_med3_f32 v74, v29, s64, v250
	v_med3_f32 v15, v30, s64, v250
	v_med3_f32 v29, v32, s64, v250
	v_med3_f32 v32, v33, s64, v250
	v_med3_f32 v75, v75, s64, v250
	v_med3_f32 v30, v76, s64, v250
	v_med3_f32 v33, v77, s64, v250
	s_cbranch_vccnz .LBB0_240
	v_cvt_pk_fp8_f32 v76, v31, v74
	v_cvt_pk_fp8_f32 v77, v32, v75
	s_add_i32 s68, s94, s46
	v_lshl_add_u64 v[24:25], v[24:25], 0, s[68:69]
	v_cvt_pk_fp8_f32 v76, v15, v29 op_sel:[0,0,1]
	v_cvt_pk_fp8_f32 v77, v30, v33 op_sel:[0,0,1]
	v_lshl_add_u64 v[24:25], v[24:25], 0, v[6:7]
	v_add_co_u32_e32 v24, vcc, 0x342ff000, v24
	s_nop 1
	v_addc_co_u32_e32 v25, vcc, 0, v25, vcc
	global_store_dwordx2 v[24:25], v[76:77], off offset:2944
	s_and_b64 vcc, exec, s[14:15]
	s_cbranch_vccz .LBB0_241

;     __device__ __forceinline__ void operator()(const f32x4 (&acc)[2][2][4][2], const Unit& u, int wr, int wc, int fr_in, int fq_in) const {
;     ...
;                     if (kind == 2 && f8qk) { u32x2 w8; w8.x = pack4_fp8_x8(v0); w8.y = pack4_fp8_x8(v1); *(u32x2*)(ws + WS_KR8 + (size_t)row * 32 + 8 * fq) = w8; }
.LBB0_239:
	v_cvt_pk_fp8_f32 v24, v31, v74
	v_cvt_pk_fp8_f32 v25, v32, v75
	v_cvt_pk_fp8_f32 v24, v15, v29 op_sel:[0,0,1]
	v_cvt_pk_fp8_f32 v25, v30, v33 op_sel:[0,0,1]
	v_lshlrev_b64 v[30:31], 5, v[18:19]
	v_lshl_add_u64 v[30:31], s[34:35], 0, v[30:31]
	v_lshl_add_u64 v[30:31], v[30:31], 0, v[6:7]
	global_store_dwordx2 v[30:31], v[24:25], off
	s_and_b64 vcc, exec, s[8:9]
	s_cbranch_vccnz .LBB0_246
	s_branch .LBB0_243

;     __device__ __forceinline__ void operator()(const f32x4 (&acc)[2][2][4][2], const Unit& u, int wr, int wc, int fr_in, int fq_in) const {
;     ...
;                     if (f8ch && colg >= 1792) {
;                         const int c0_ = colg - 1792 + 8 * fq, bb_ = row >> 13, pos_ = row & (SEQ_ - 1), key_ = pos_ & 63, k32_ = key_ & 31;
;                         unsigned char* p_ = ws + WS_VB8T + ((((size_t)(bb_ * 8 + (c0_ >> 6)) * 128 + (pos_ >> 6)) * 64 + (c0_ & 63)) * 64) + 32 * ((k32_ >> 2) & 1) + 16 * (key_ >> 5) + (k32_ & 3) + 4 * (k32_ >> 3);
;                         const unsigned w0_ = pack4_fp8_x8(v0), w1_ = pack4_fp8_x8(v1);
; #pragma unroll
;                         for (int e_ = 0; e_ < 4; ++e_) { p_[e_ * 64] = (unsigned char)((w0_ >> (8 * e_)) & 0xffu); p_[(4 + e_) * 64] = (unsigned char)((w1_ >> (8 * e_)) & 0xffu); }
;                     }
.LBB0_241:
	v_ashrrev_i32_e32 v24, 10, v18
	v_and_b32_e32 v24, -8, v24
	v_add_u32_e32 v24, v24, v28
	v_ashrrev_i32_e32 v25, 31, v24
	v_lshlrev_b64 v[24:25], 13, v[24:25]
	v_and_or_b32 v24, v18, s50, v24
	v_or_b32_e32 v24, v24, v27
	v_lshlrev_b64 v[24:25], 6, v[24:25]
	v_lshl_add_u64 v[24:25], s[24:25], 0, v[24:25]
	v_lshrrev_b32_e32 v78, 1, v18
	v_lshl_add_u64 v[24:25], v[24:25], 0, v[0:1]
	v_and_b32_e32 v76, 16, v78
	v_mov_b32_e32 v77, v1
	v_lshl_add_u64 v[24:25], v[24:25], 0, v[76:77]
	v_lshl_add_u64 v[24:25], v[24:25], 0, v[8:9]
	v_and_b32_e32 v76, 12, v78
	v_lshl_add_u64 v[24:25], v[24:25], 0, v[76:77]
	v_cvt_pk_fp8_f32 v76, v31, v74
	v_cvt_pk_fp8_f32 v77, v32, v75
	v_cvt_pk_fp8_f32 v76, v15, v29 op_sel:[0,0,1]
	v_cvt_pk_fp8_f32 v77, v30, v33 op_sel:[0,0,1]
	global_store_byte v[24:25], v76, off
	global_store_byte v[24:25], v77, off offset:256
	v_lshrrev_b32_e32 v78, 8, v76
	global_store_byte v[24:25], v78, off offset:64
	v_lshrrev_b32_e32 v78, 8, v77
	global_store_byte v[24:25], v78, off offset:320
	global_store_byte_d16_hi v[24:25], v76, off offset:128
	global_store_byte_d16_hi v[24:25], v77, off offset:384
	v_lshrrev_b32_e32 v76, 24, v76
	global_store_byte v[24:25], v76, off offset:192
	v_lshrrev_b32_e32 v76, 24, v77
	global_store_byte v[24:25], v76, off offset:448
	s_and_b64 vcc, exec, s[6:7]
	s_cbranch_vccz .LBB0_239

; __device__ __forceinline__ u32x4 pack8(const f32x4 a, const f32x4 b) { u32x4 w; w.x = cvt_pk_bf16(a[0], a[1]); w.y = cvt_pk_bf16(a[2], a[3]); w.z = cvt_pk_bf16(b[0], b[1]); w.w = cvt_pk_bf16(b[2], b[3]); return w; }
;     __device__ __forceinline__ void operator()(const f32x4 (&acc)[2][2][4][2], const Unit& u, int wr, int wc, int fr_in, int fq_in) const {
;     ...
;                     const int row = row0 + ai * HALF + m * 16; const float r = t[ai * 64 + m * 16 + fr] * sc;
;                     f32x4 v0 = acc[ai][bj][m][0] * r, v1 = acc[ai][bj][m][1] * r;
;                     if (kind == 2) rope8(v0, v1, rcos, rsin, row & (SEQ_ - 1), fq);
;                     *(u32x4*)(dst + (size_t)row * pitch + 8 * fq) = pack8(v0, v1);
;                     if (f8ch && colg >= 768 && colg < 1280) { u32x2 w8; w8.x = pack4_fp8_x16(v0); w8.y = pack4_fp8_x16(v1); *(u32x2*)(ws + WS_QB8 + (size_t)row * 512 + (colg - 768) + 8 * fq) = w8; }
;                     if (f8ch && colg >= 1280 && colg < 1792) { u32x2 w8; w8.x = pack4_fp8_x8(v0); w8.y = pack4_fp8_x8(v1); *(u32x2*)(ws + WS_KB8 + (size_t)row * 512 + (colg - 1280) + 8 * fq) = w8; }
.LBB0_250:
	v_mul_f32_e32 v15, 0x41000000, v2
	v_mul_f32_e32 v29, 0x41000000, v3
	v_mul_f32_e32 v30, 0x41000000, v4
	v_mul_f32_e32 v32, 0x41000000, v5
	v_mul_f32_e32 v33, 0x41000000, v22
	v_mul_f32_e32 v67, 0x41000000, v23
	v_mul_f32_e32 v68, 0x41000000, v20
	v_mul_f32_e32 v69, 0x41000000, v21
	s_and_b64 vcc, exec, s[12:13]
	v_med3_f32 v31, v15, s64, v250
	v_med3_f32 v66, v29, s64, v250
	v_med3_f32 v15, v30, s64, v250
	v_med3_f32 v29, v32, s64, v250
	v_med3_f32 v32, v33, s64, v250
	v_med3_f32 v67, v67, s64, v250
	v_med3_f32 v30, v68, s64, v250
	v_med3_f32 v33, v69, s64, v250
	s_cbranch_vccnz .LBB0_254
	v_cvt_pk_fp8_f32 v68, v31, v66
	v_cvt_pk_fp8_f32 v69, v32, v67
	s_add_i32 s68, s94, s46
	v_lshl_add_u64 v[24:25], v[24:25], 0, s[68:69]
	v_cvt_pk_fp8_f32 v68, v15, v29 op_sel:[0,0,1]
	v_cvt_pk_fp8_f32 v69, v30, v33 op_sel:[0,0,1]
	v_lshl_add_u64 v[24:25], v[24:25], 0, v[6:7]
	v_add_co_u32_e32 v24, vcc, 0x342ff000, v24
	s_nop 1
	v_addc_co_u32_e32 v25, vcc, 0, v25, vcc
	global_store_dwordx2 v[24:25], v[68:69], off offset:2944
	s_and_b64 vcc, exec, s[14:15]
	s_cbranch_vccz .LBB0_255

;     __device__ __forceinline__ void operator()(const f32x4 (&acc)[2][2][4][2], const Unit& u, int wr, int wc, int fr_in, int fq_in) const {
;     ...
;                     if (kind == 2 && f8qk) { u32x2 w8; w8.x = pack4_fp8_x8(v0); w8.y = pack4_fp8_x8(v1); *(u32x2*)(ws + WS_KR8 + (size_t)row * 32 + 8 * fq) = w8; }
.LBB0_253:
	v_cvt_pk_fp8_f32 v24, v31, v66
	v_cvt_pk_fp8_f32 v25, v32, v67
	v_cvt_pk_fp8_f32 v24, v15, v29 op_sel:[0,0,1]
	v_cvt_pk_fp8_f32 v25, v30, v33 op_sel:[0,0,1]
	v_lshlrev_b64 v[30:31], 5, v[18:19]
	v_lshl_add_u64 v[30:31], s[34:35], 0, v[30:31]
	v_lshl_add_u64 v[30:31], v[30:31], 0, v[6:7]
	global_store_dwordx2 v[30:31], v[24:25], off
	s_and_b64 vcc, exec, s[8:9]
	s_cbranch_vccnz .LBB0_260
	s_branch .LBB0_257

;     __device__ __forceinline__ void operator()(const f32x4 (&acc)[2][2][4][2], const Unit& u, int wr, int wc, int fr_in, int fq_in) const {
;     ...
;                     if (f8ch && colg >= 1792) {
;                         const int c0_ = colg - 1792 + 8 * fq, bb_ = row >> 13, pos_ = row & (SEQ_ - 1), key_ = pos_ & 63, k32_ = key_ & 31;
;                         unsigned char* p_ = ws + WS_VB8T + ((((size_t)(bb_ * 8 + (c0_ >> 6)) * 128 + (pos_ >> 6)) * 64 + (c0_ & 63)) * 64) + 32 * ((k32_ >> 2) & 1) + 16 * (key_ >> 5) + (k32_ & 3) + 4 * (k32_ >> 3);
;                         const unsigned w0_ = pack4_fp8_x8(v0), w1_ = pack4_fp8_x8(v1);
; #pragma unroll
;                         for (int e_ = 0; e_ < 4; ++e_) { p_[e_ * 64] = (unsigned char)((w0_ >> (8 * e_)) & 0xffu); p_[(4 + e_) * 64] = (unsigned char)((w1_ >> (8 * e_)) & 0xffu); }
;                     }
.LBB0_255:
	v_ashrrev_i32_e32 v24, 10, v18
	v_and_b32_e32 v24, -8, v24
	v_add_u32_e32 v24, v24, v28
	v_ashrrev_i32_e32 v25, 31, v24
	v_lshlrev_b64 v[24:25], 13, v[24:25]
	v_and_or_b32 v24, v18, s50, v24
	v_or_b32_e32 v24, v24, v27
	v_lshlrev_b64 v[24:25], 6, v[24:25]
	v_lshl_add_u64 v[24:25], s[24:25], 0, v[24:25]
	v_lshrrev_b32_e32 v70, 1, v18
	v_lshl_add_u64 v[24:25], v[24:25], 0, v[0:1]
	v_and_b32_e32 v68, 16, v70
	v_mov_b32_e32 v69, v1
	v_lshl_add_u64 v[24:25], v[24:25], 0, v[68:69]
	v_lshl_add_u64 v[24:25], v[24:25], 0, v[8:9]
	v_and_b32_e32 v68, 12, v70
	v_lshl_add_u64 v[24:25], v[24:25], 0, v[68:69]
	v_cvt_pk_fp8_f32 v68, v31, v66
	v_cvt_pk_fp8_f32 v69, v32, v67
	v_cvt_pk_fp8_f32 v68, v15, v29 op_sel:[0,0,1]
	v_cvt_pk_fp8_f32 v69, v30, v33 op_sel:[0,0,1]
	global_store_byte v[24:25], v68, off
	global_store_byte v[24:25], v69, off offset:256
	v_lshrrev_b32_e32 v70, 8, v68
	global_store_byte v[24:25], v70, off offset:64
	v_lshrrev_b32_e32 v70, 8, v69
	global_store_byte v[24:25], v70, off offset:320
	global_store_byte_d16_hi v[24:25], v68, off offset:128
	global_store_byte_d16_hi v[24:25], v69, off offset:384
	v_lshrrev_b32_e32 v68, 24, v68
	global_store_byte v[24:25], v68, off offset:192
	v_lshrrev_b32_e32 v68, 24, v69
	global_store_byte v[24:25], v68, off offset:448
	s_and_b64 vcc, exec, s[6:7]
	s_cbranch_vccz .LBB0_253

; __device__ __forceinline__ u32x4 pack8(const f32x4 a, const f32x4 b) { u32x4 w; w.x = cvt_pk_bf16(a[0], a[1]); w.y = cvt_pk_bf16(a[2], a[3]); w.z = cvt_pk_bf16(b[0], b[1]); w.w = cvt_pk_bf16(b[2], b[3]); return w; }
;     __device__ __forceinline__ void operator()(const f32x4 (&acc)[2][2][4][2], const Unit& u, int wr, int wc, int fr_in, int fq_in) const {
;     ...
;                     const int row = row0 + ai * HALF + m * 16; const float r = t[ai * 64 + m * 16 + fr] * sc;
;                     f32x4 v0 = acc[ai][bj][m][0] * r, v1 = acc[ai][bj][m][1] * r;
;                     if (kind == 2) rope8(v0, v1, rcos, rsin, row & (SEQ_ - 1), fq);
;                     *(u32x4*)(dst + (size_t)row * pitch + 8 * fq) = pack8(v0, v1);
;                     if (f8ch && colg >= 768 && colg < 1280) { u32x2 w8; w8.x = pack4_fp8_x16(v0); w8.y = pack4_fp8_x16(v1); *(u32x2*)(ws + WS_QB8 + (size_t)row * 512 + (colg - 768) + 8 * fq) = w8; }
;                     if (f8ch && colg >= 1280 && colg < 1792) { u32x2 w8; w8.x = pack4_fp8_x8(v0); w8.y = pack4_fp8_x8(v1); *(u32x2*)(ws + WS_KB8 + (size_t)row * 512 + (colg - 1280) + 8 * fq) = w8; }
.LBB0_264:
	v_mul_f32_e32 v15, 0x41000000, v2
	v_mul_f32_e32 v29, 0x41000000, v3
	v_mul_f32_e32 v30, 0x41000000, v4
	v_mul_f32_e32 v32, 0x41000000, v5
	v_mul_f32_e32 v33, 0x41000000, v22
	v_mul_f32_e32 v59, 0x41000000, v23
	v_mul_f32_e32 v60, 0x41000000, v20
	v_mul_f32_e32 v61, 0x41000000, v21
	s_and_b64 vcc, exec, s[12:13]
	v_med3_f32 v31, v15, s64, v250
	v_med3_f32 v58, v29, s64, v250
	v_med3_f32 v15, v30, s64, v250
	v_med3_f32 v29, v32, s64, v250
	v_med3_f32 v32, v33, s64, v250
	v_med3_f32 v59, v59, s64, v250
	v_med3_f32 v30, v60, s64, v250
	v_med3_f32 v33, v61, s64, v250
	s_cbranch_vccnz .LBB0_268
	v_cvt_pk_fp8_f32 v60, v31, v58
	v_cvt_pk_fp8_f32 v61, v32, v59
	s_add_i32 s68, s94, s46
	v_lshl_add_u64 v[24:25], v[24:25], 0, s[68:69]
	v_cvt_pk_fp8_f32 v60, v15, v29 op_sel:[0,0,1]
	v_cvt_pk_fp8_f32 v61, v30, v33 op_sel:[0,0,1]
	v_lshl_add_u64 v[24:25], v[24:25], 0, v[6:7]
	v_add_co_u32_e32 v24, vcc, 0x342ff000, v24
	s_nop 1
	v_addc_co_u32_e32 v25, vcc, 0, v25, vcc
	global_store_dwordx2 v[24:25], v[60:61], off offset:2944
	s_and_b64 vcc, exec, s[14:15]
	s_cbranch_vccz .LBB0_269

;     __device__ __forceinline__ void operator()(const f32x4 (&acc)[2][2][4][2], const Unit& u, int wr, int wc, int fr_in, int fq_in) const {
;     ...
;                     if (kind == 2 && f8qk) { u32x2 w8; w8.x = pack4_fp8_x8(v0); w8.y = pack4_fp8_x8(v1); *(u32x2*)(ws + WS_KR8 + (size_t)row * 32 + 8 * fq) = w8; }
.LBB0_267:
	v_cvt_pk_fp8_f32 v24, v31, v58
	v_cvt_pk_fp8_f32 v25, v32, v59
	v_cvt_pk_fp8_f32 v24, v15, v29 op_sel:[0,0,1]
	v_cvt_pk_fp8_f32 v25, v30, v33 op_sel:[0,0,1]
	v_lshlrev_b64 v[30:31], 5, v[18:19]
	v_lshl_add_u64 v[30:31], s[34:35], 0, v[30:31]
	v_lshl_add_u64 v[30:31], v[30:31], 0, v[6:7]
	global_store_dwordx2 v[30:31], v[24:25], off
	s_and_b64 vcc, exec, s[8:9]
	s_cbranch_vccnz .LBB0_274
	s_branch .LBB0_271

;     __device__ __forceinline__ void operator()(const f32x4 (&acc)[2][2][4][2], const Unit& u, int wr, int wc, int fr_in, int fq_in) const {
;     ...
;                     if (f8ch && colg >= 1792) {
;                         const int c0_ = colg - 1792 + 8 * fq, bb_ = row >> 13, pos_ = row & (SEQ_ - 1), key_ = pos_ & 63, k32_ = key_ & 31;
;                         unsigned char* p_ = ws + WS_VB8T + ((((size_t)(bb_ * 8 + (c0_ >> 6)) * 128 + (pos_ >> 6)) * 64 + (c0_ & 63)) * 64) + 32 * ((k32_ >> 2) & 1) + 16 * (key_ >> 5) + (k32_ & 3) + 4 * (k32_ >> 3);
;                         const unsigned w0_ = pack4_fp8_x8(v0), w1_ = pack4_fp8_x8(v1);
; #pragma unroll
;                         for (int e_ = 0; e_ < 4; ++e_) { p_[e_ * 64] = (unsigned char)((w0_ >> (8 * e_)) & 0xffu); p_[(4 + e_) * 64] = (unsigned char)((w1_ >> (8 * e_)) & 0xffu); }
;                     }
.LBB0_269:
	v_ashrrev_i32_e32 v24, 10, v18
	v_and_b32_e32 v24, -8, v24
	v_add_u32_e32 v24, v24, v28
	v_ashrrev_i32_e32 v25, 31, v24
	v_lshlrev_b64 v[24:25], 13, v[24:25]
	v_and_or_b32 v24, v18, s50, v24
	v_or_b32_e32 v24, v24, v27
	v_lshlrev_b64 v[24:25], 6, v[24:25]
	v_lshl_add_u64 v[24:25], s[24:25], 0, v[24:25]
	v_lshrrev_b32_e32 v62, 1, v18
	v_lshl_add_u64 v[24:25], v[24:25], 0, v[0:1]
	v_and_b32_e32 v60, 16, v62
	v_mov_b32_e32 v61, v1
	v_lshl_add_u64 v[24:25], v[24:25], 0, v[60:61]
	v_lshl_add_u64 v[24:25], v[24:25], 0, v[8:9]
	v_and_b32_e32 v60, 12, v62
	v_lshl_add_u64 v[24:25], v[24:25], 0, v[60:61]
	v_cvt_pk_fp8_f32 v60, v31, v58
	v_cvt_pk_fp8_f32 v61, v32, v59
	v_cvt_pk_fp8_f32 v60, v15, v29 op_sel:[0,0,1]
	v_cvt_pk_fp8_f32 v61, v30, v33 op_sel:[0,0,1]
	global_store_byte v[24:25], v60, off
	global_store_byte v[24:25], v61, off offset:256
	v_lshrrev_b32_e32 v62, 8, v60
	global_store_byte v[24:25], v62, off offset:64
	v_lshrrev_b32_e32 v62, 8, v61
	global_store_byte v[24:25], v62, off offset:320
	global_store_byte_d16_hi v[24:25], v60, off offset:128
	global_store_byte_d16_hi v[24:25], v61, off offset:384
	v_lshrrev_b32_e32 v60, 24, v60
	global_store_byte v[24:25], v60, off offset:192
	v_lshrrev_b32_e32 v60, 24, v61
	global_store_byte v[24:25], v60, off offset:448
	s_and_b64 vcc, exec, s[6:7]
	s_cbranch_vccz .LBB0_267

; __device__ __forceinline__ u32x4 pack8(const f32x4 a, const f32x4 b) { u32x4 w; w.x = cvt_pk_bf16(a[0], a[1]); w.y = cvt_pk_bf16(a[2], a[3]); w.z = cvt_pk_bf16(b[0], b[1]); w.w = cvt_pk_bf16(b[2], b[3]); return w; }
;     __device__ __forceinline__ void operator()(const f32x4 (&acc)[2][2][4][2], const Unit& u, int wr, int wc, int fr_in, int fq_in) const {
;     ...
;                     const int row = row0 + ai * HALF + m * 16; const float r = t[ai * 64 + m * 16 + fr] * sc;
;                     f32x4 v0 = acc[ai][bj][m][0] * r, v1 = acc[ai][bj][m][1] * r;
;                     if (kind == 2) rope8(v0, v1, rcos, rsin, row & (SEQ_ - 1), fq);
;                     *(u32x4*)(dst + (size_t)row * pitch + 8 * fq) = pack8(v0, v1);
;                     if (f8ch && colg >= 768 && colg < 1280) { u32x2 w8; w8.x = pack4_fp8_x16(v0); w8.y = pack4_fp8_x16(v1); *(u32x2*)(ws + WS_QB8 + (size_t)row * 512 + (colg - 768) + 8 * fq) = w8; }
;                     if (f8ch && colg >= 1280 && colg < 1792) { u32x2 w8; w8.x = pack4_fp8_x8(v0); w8.y = pack4_fp8_x8(v1); *(u32x2*)(ws + WS_KB8 + (size_t)row * 512 + (colg - 1280) + 8 * fq) = w8; }
.LBB0_278:
	v_mul_f32_e32 v15, 0x41000000, v2
	v_mul_f32_e32 v29, 0x41000000, v3
	v_mul_f32_e32 v30, 0x41000000, v4
	v_mul_f32_e32 v32, 0x41000000, v5
	v_mul_f32_e32 v33, 0x41000000, v22
	v_mul_f32_e32 v51, 0x41000000, v23
	v_mul_f32_e32 v52, 0x41000000, v20
	v_mul_f32_e32 v53, 0x41000000, v21
	s_and_b64 vcc, exec, s[12:13]
	v_med3_f32 v31, v15, s64, v250
	v_med3_f32 v50, v29, s64, v250
	v_med3_f32 v15, v30, s64, v250
	v_med3_f32 v29, v32, s64, v250
	v_med3_f32 v32, v33, s64, v250
	v_med3_f32 v51, v51, s64, v250
	v_med3_f32 v30, v52, s64, v250
	v_med3_f32 v33, v53, s64, v250
	s_cbranch_vccnz .LBB0_282
	v_cvt_pk_fp8_f32 v52, v31, v50
	v_cvt_pk_fp8_f32 v53, v32, v51
	s_add_i32 s68, s94, s46
	v_lshl_add_u64 v[24:25], v[24:25], 0, s[68:69]
	v_cvt_pk_fp8_f32 v52, v15, v29 op_sel:[0,0,1]
	v_cvt_pk_fp8_f32 v53, v30, v33 op_sel:[0,0,1]
	v_lshl_add_u64 v[24:25], v[24:25], 0, v[6:7]
	v_add_co_u32_e32 v24, vcc, 0x342ff000, v24
	s_nop 1
	v_addc_co_u32_e32 v25, vcc, 0, v25, vcc
	global_store_dwordx2 v[24:25], v[52:53], off offset:2944
	s_and_b64 vcc, exec, s[14:15]
	s_cbranch_vccz .LBB0_283

;     __device__ __forceinline__ void operator()(const f32x4 (&acc)[2][2][4][2], const Unit& u, int wr, int wc, int fr_in, int fq_in) const {
;     ...
;                     if (kind == 2 && f8qk) { u32x2 w8; w8.x = pack4_fp8_x8(v0); w8.y = pack4_fp8_x8(v1); *(u32x2*)(ws + WS_KR8 + (size_t)row * 32 + 8 * fq) = w8; }
.LBB0_281:
	v_cvt_pk_fp8_f32 v24, v31, v50
	v_cvt_pk_fp8_f32 v25, v32, v51
	v_cvt_pk_fp8_f32 v24, v15, v29 op_sel:[0,0,1]
	v_cvt_pk_fp8_f32 v25, v30, v33 op_sel:[0,0,1]
	v_lshlrev_b64 v[30:31], 5, v[18:19]
	v_lshl_add_u64 v[30:31], s[34:35], 0, v[30:31]
	v_lshl_add_u64 v[30:31], v[30:31], 0, v[6:7]
	global_store_dwordx2 v[30:31], v[24:25], off
	s_and_b64 vcc, exec, s[8:9]
	s_cbranch_vccnz .LBB0_288
	s_branch .LBB0_285

;     __device__ __forceinline__ void operator()(const f32x4 (&acc)[2][2][4][2], const Unit& u, int wr, int wc, int fr_in, int fq_in) const {
;     ...
;                     if (f8ch && colg >= 1792) {
;                         const int c0_ = colg - 1792 + 8 * fq, bb_ = row >> 13, pos_ = row & (SEQ_ - 1), key_ = pos_ & 63, k32_ = key_ & 31;
;                         unsigned char* p_ = ws + WS_VB8T + ((((size_t)(bb_ * 8 + (c0_ >> 6)) * 128 + (pos_ >> 6)) * 64 + (c0_ & 63)) * 64) + 32 * ((k32_ >> 2) & 1) + 16 * (key_ >> 5) + (k32_ & 3) + 4 * (k32_ >> 3);
;                         const unsigned w0_ = pack4_fp8_x8(v0), w1_ = pack4_fp8_x8(v1);
; #pragma unroll
;                         for (int e_ = 0; e_ < 4; ++e_) { p_[e_ * 64] = (unsigned char)((w0_ >> (8 * e_)) & 0xffu); p_[(4 + e_) * 64] = (unsigned char)((w1_ >> (8 * e_)) & 0xffu); }
;                     }
.LBB0_283:
	v_ashrrev_i32_e32 v24, 10, v18
	v_and_b32_e32 v24, -8, v24
	v_add_u32_e32 v24, v24, v28
	v_ashrrev_i32_e32 v25, 31, v24
	v_lshlrev_b64 v[24:25], 13, v[24:25]
	v_and_or_b32 v24, v18, s50, v24
	v_or_b32_e32 v24, v24, v27
	v_lshlrev_b64 v[24:25], 6, v[24:25]
	v_lshl_add_u64 v[24:25], s[24:25], 0, v[24:25]
	v_lshrrev_b32_e32 v54, 1, v18
	v_lshl_add_u64 v[24:25], v[24:25], 0, v[0:1]
	v_and_b32_e32 v52, 16, v54
	v_mov_b32_e32 v53, v1
	v_lshl_add_u64 v[24:25], v[24:25], 0, v[52:53]
	v_lshl_add_u64 v[24:25], v[24:25], 0, v[8:9]
	v_and_b32_e32 v52, 12, v54
	v_lshl_add_u64 v[24:25], v[24:25], 0, v[52:53]
	v_cvt_pk_fp8_f32 v52, v31, v50
	v_cvt_pk_fp8_f32 v53, v32, v51
	v_cvt_pk_fp8_f32 v52, v15, v29 op_sel:[0,0,1]
	v_cvt_pk_fp8_f32 v53, v30, v33 op_sel:[0,0,1]
	global_store_byte v[24:25], v52, off
	global_store_byte v[24:25], v53, off offset:256
	v_lshrrev_b32_e32 v54, 8, v52
	global_store_byte v[24:25], v54, off offset:64
	v_lshrrev_b32_e32 v54, 8, v53
	global_store_byte v[24:25], v54, off offset:320
	global_store_byte_d16_hi v[24:25], v52, off offset:128
	global_store_byte_d16_hi v[24:25], v53, off offset:384
	v_lshrrev_b32_e32 v52, 24, v52
	global_store_byte v[24:25], v52, off offset:192
	v_lshrrev_b32_e32 v52, 24, v53
	global_store_byte v[24:25], v52, off offset:448
	s_and_b64 vcc, exec, s[6:7]
	s_cbranch_vccz .LBB0_281

; __device__ __forceinline__ u32x4 pack8(const f32x4 a, const f32x4 b) { u32x4 w; w.x = cvt_pk_bf16(a[0], a[1]); w.y = cvt_pk_bf16(a[2], a[3]); w.z = cvt_pk_bf16(b[0], b[1]); w.w = cvt_pk_bf16(b[2], b[3]); return w; }
;     __device__ __forceinline__ void operator()(const f32x4 (&acc)[2][2][4][2], const Unit& u, int wr, int wc, int fr_in, int fq_in) const {
;     ...
;                     const int row = row0 + ai * HALF + m * 16; const float r = t[ai * 64 + m * 16 + fr] * sc;
;                     f32x4 v0 = acc[ai][bj][m][0] * r, v1 = acc[ai][bj][m][1] * r;
;                     if (kind == 2) rope8(v0, v1, rcos, rsin, row & (SEQ_ - 1), fq);
;                     *(u32x4*)(dst + (size_t)row * pitch + 8 * fq) = pack8(v0, v1);
;                     if (f8ch && colg >= 768 && colg < 1280) { u32x2 w8; w8.x = pack4_fp8_x16(v0); w8.y = pack4_fp8_x16(v1); *(u32x2*)(ws + WS_QB8 + (size_t)row * 512 + (colg - 768) + 8 * fq) = w8; }
;                     if (f8ch && colg >= 1280 && colg < 1792) { u32x2 w8; w8.x = pack4_fp8_x8(v0); w8.y = pack4_fp8_x8(v1); *(u32x2*)(ws + WS_KB8 + (size_t)row * 512 + (colg - 1280) + 8 * fq) = w8; }
.LBB0_292:
	v_mul_f32_e32 v15, 0x41000000, v2
	v_mul_f32_e32 v29, 0x41000000, v3
	v_mul_f32_e32 v30, 0x41000000, v4
	v_mul_f32_e32 v32, 0x41000000, v5
	v_mul_f32_e32 v33, 0x41000000, v22
	v_mul_f32_e32 v43, 0x41000000, v23
	v_mul_f32_e32 v44, 0x41000000, v20
	v_mul_f32_e32 v45, 0x41000000, v21
	s_and_b64 vcc, exec, s[12:13]
	v_med3_f32 v31, v15, s64, v250
	v_med3_f32 v42, v29, s64, v250
	v_med3_f32 v15, v30, s64, v250
	v_med3_f32 v29, v32, s64, v250
	v_med3_f32 v32, v33, s64, v250
	v_med3_f32 v43, v43, s64, v250
	v_med3_f32 v30, v44, s64, v250
	v_med3_f32 v33, v45, s64, v250
	s_cbranch_vccnz .LBB0_296
	v_cvt_pk_fp8_f32 v44, v31, v42
	v_cvt_pk_fp8_f32 v45, v32, v43
	s_add_i32 s68, s94, s46
	v_lshl_add_u64 v[24:25], v[24:25], 0, s[68:69]
	v_cvt_pk_fp8_f32 v44, v15, v29 op_sel:[0,0,1]
	v_cvt_pk_fp8_f32 v45, v30, v33 op_sel:[0,0,1]
	v_lshl_add_u64 v[24:25], v[24:25], 0, v[6:7]
	v_add_co_u32_e32 v24, vcc, 0x342ff000, v24
	s_nop 1
	v_addc_co_u32_e32 v25, vcc, 0, v25, vcc
	global_store_dwordx2 v[24:25], v[44:45], off offset:2944
	s_and_b64 vcc, exec, s[14:15]
	s_cbranch_vccz .LBB0_297

;     __device__ __forceinline__ void operator()(const f32x4 (&acc)[2][2][4][2], const Unit& u, int wr, int wc, int fr_in, int fq_in) const {
;     ...
;                     if (kind == 2 && f8qk) { u32x2 w8; w8.x = pack4_fp8_x8(v0); w8.y = pack4_fp8_x8(v1); *(u32x2*)(ws + WS_KR8 + (size_t)row * 32 + 8 * fq) = w8; }
.LBB0_295:
	v_cvt_pk_fp8_f32 v24, v31, v42
	v_cvt_pk_fp8_f32 v25, v32, v43
	v_cvt_pk_fp8_f32 v24, v15, v29 op_sel:[0,0,1]
	v_cvt_pk_fp8_f32 v25, v30, v33 op_sel:[0,0,1]
	v_lshlrev_b64 v[30:31], 5, v[18:19]
	v_lshl_add_u64 v[30:31], s[34:35], 0, v[30:31]
	v_lshl_add_u64 v[30:31], v[30:31], 0, v[6:7]
	global_store_dwordx2 v[30:31], v[24:25], off
	s_and_b64 vcc, exec, s[8:9]
	s_cbranch_vccnz .LBB0_302
	s_branch .LBB0_299

;     __device__ __forceinline__ void operator()(const f32x4 (&acc)[2][2][4][2], const Unit& u, int wr, int wc, int fr_in, int fq_in) const {
;     ...
;                     if (f8ch && colg >= 1792) {
;                         const int c0_ = colg - 1792 + 8 * fq, bb_ = row >> 13, pos_ = row & (SEQ_ - 1), key_ = pos_ & 63, k32_ = key_ & 31;
;                         unsigned char* p_ = ws + WS_VB8T + ((((size_t)(bb_ * 8 + (c0_ >> 6)) * 128 + (pos_ >> 6)) * 64 + (c0_ & 63)) * 64) + 32 * ((k32_ >> 2) & 1) + 16 * (key_ >> 5) + (k32_ & 3) + 4 * (k32_ >> 3);
;                         const unsigned w0_ = pack4_fp8_x8(v0), w1_ = pack4_fp8_x8(v1);
; #pragma unroll
;                         for (int e_ = 0; e_ < 4; ++e_) { p_[e_ * 64] = (unsigned char)((w0_ >> (8 * e_)) & 0xffu); p_[(4 + e_) * 64] = (unsigned char)((w1_ >> (8 * e_)) & 0xffu); }
;                     }
.LBB0_297:
	v_ashrrev_i32_e32 v24, 10, v18
	v_and_b32_e32 v24, -8, v24
	v_add_u32_e32 v24, v24, v28
	v_ashrrev_i32_e32 v25, 31, v24
	v_lshlrev_b64 v[24:25], 13, v[24:25]
	v_and_or_b32 v24, v18, s50, v24
	v_or_b32_e32 v24, v24, v27
	v_lshlrev_b64 v[24:25], 6, v[24:25]
	v_lshl_add_u64 v[24:25], s[24:25], 0, v[24:25]
	v_lshrrev_b32_e32 v46, 1, v18
	v_lshl_add_u64 v[24:25], v[24:25], 0, v[0:1]
	v_and_b32_e32 v44, 16, v46
	v_mov_b32_e32 v45, v1
	v_lshl_add_u64 v[24:25], v[24:25], 0, v[44:45]
	v_lshl_add_u64 v[24:25], v[24:25], 0, v[8:9]
	v_and_b32_e32 v44, 12, v46
	v_lshl_add_u64 v[24:25], v[24:25], 0, v[44:45]
	v_cvt_pk_fp8_f32 v44, v31, v42
	v_cvt_pk_fp8_f32 v45, v32, v43
	v_cvt_pk_fp8_f32 v44, v15, v29 op_sel:[0,0,1]
	v_cvt_pk_fp8_f32 v45, v30, v33 op_sel:[0,0,1]
	global_store_byte v[24:25], v44, off
	global_store_byte v[24:25], v45, off offset:256
	v_lshrrev_b32_e32 v46, 8, v44
	global_store_byte v[24:25], v46, off offset:64
	v_lshrrev_b32_e32 v46, 8, v45
	global_store_byte v[24:25], v46, off offset:320
	global_store_byte_d16_hi v[24:25], v44, off offset:128
	global_store_byte_d16_hi v[24:25], v45, off offset:384
	v_lshrrev_b32_e32 v44, 24, v44
	global_store_byte v[24:25], v44, off offset:192
	v_lshrrev_b32_e32 v44, 24, v45
	global_store_byte v[24:25], v44, off offset:448
	s_and_b64 vcc, exec, s[6:7]
	s_cbranch_vccz .LBB0_295

; __device__ __forceinline__ u32x4 pack8(const f32x4 a, const f32x4 b) { u32x4 w; w.x = cvt_pk_bf16(a[0], a[1]); w.y = cvt_pk_bf16(a[2], a[3]); w.z = cvt_pk_bf16(b[0], b[1]); w.w = cvt_pk_bf16(b[2], b[3]); return w; }
;     __device__ __forceinline__ void operator()(const f32x4 (&acc)[2][2][4][2], const Unit& u, int wr, int wc, int fr_in, int fq_in) const {
;     ...
;                     const int row = row0 + ai * HALF + m * 16; const float r = t[ai * 64 + m * 16 + fr] * sc;
;                     f32x4 v0 = acc[ai][bj][m][0] * r, v1 = acc[ai][bj][m][1] * r;
;                     if (kind == 2) rope8(v0, v1, rcos, rsin, row & (SEQ_ - 1), fq);
;                     *(u32x4*)(dst + (size_t)row * pitch + 8 * fq) = pack8(v0, v1);
;                     if (f8ch && colg >= 768 && colg < 1280) { u32x2 w8; w8.x = pack4_fp8_x16(v0); w8.y = pack4_fp8_x16(v1); *(u32x2*)(ws + WS_QB8 + (size_t)row * 512 + (colg - 768) + 8 * fq) = w8; }
;                     if (f8ch && colg >= 1280 && colg < 1792) { u32x2 w8; w8.x = pack4_fp8_x8(v0); w8.y = pack4_fp8_x8(v1); *(u32x2*)(ws + WS_KB8 + (size_t)row * 512 + (colg - 1280) + 8 * fq) = w8; }
.LBB0_304:
	v_ashrrev_i32_e32 v15, 31, v14
	v_mul_lo_u32 v24, s55, v14
	v_mul_lo_u32 v25, s54, v15
	v_mad_u64_u32 v[22:23], s[54:55], s54, v14, 0
	v_add3_u32 v23, v23, v25, v24
	v_cvt_pk_bf16_f32 v10, v2, v3
	v_cvt_pk_bf16_f32 v11, v4, v5
	v_lshl_add_u64 v[16:17], v[22:23], 1, v[16:17]
	v_cvt_pk_bf16_f32 v12, v20, v21
	v_cvt_pk_bf16_f32 v13, v18, v19
	global_store_dwordx4 v[16:17], v[10:13], off
	s_and_b64 vcc, exec, s[10:11]
	s_nop 0
	v_lshlrev_b64 v[10:11], 9, v[14:15]
	v_lshl_add_u64 v[10:11], s[18:19], 0, v[10:11]
	s_cbranch_vccnz .LBB0_306
	v_mul_f32_e32 v12, 0x41800000, v2
	v_med3_f32 v13, v12, s64, v250
	v_mul_f32_e32 v12, 0x41800000, v3
	v_med3_f32 v16, v12, s64, v250
	v_cvt_pk_fp8_f32 v12, v13, v16
	v_mul_f32_e32 v13, 0x41800000, v4
	v_mul_f32_e32 v16, 0x41800000, v5
	v_med3_f32 v13, v13, s64, v250
	v_med3_f32 v16, v16, s64, v250
	v_cvt_pk_fp8_f32 v12, v13, v16 op_sel:[0,0,1]
	v_mul_f32_e32 v13, 0x41800000, v20
	v_med3_f32 v16, v13, s64, v250
	v_mul_f32_e32 v13, 0x41800000, v21
	v_med3_f32 v17, v13, s64, v250
	v_cvt_pk_fp8_f32 v13, v16, v17
	v_mul_f32_e32 v16, 0x41800000, v18
	v_mul_f32_e32 v17, 0x41800000, v19
	v_med3_f32 v16, v16, s64, v250
	v_med3_f32 v17, v17, s64, v250
	s_add_i32 s68, s94, s46
	v_cvt_pk_fp8_f32 v13, v16, v17 op_sel:[0,0,1]
	v_lshl_add_u64 v[16:17], v[10:11], 0, s[68:69]
	v_lshl_add_u64 v[16:17], v[16:17], 0, v[6:7]
	v_add_co_u32_e32 v16, vcc, 0x332ff000, v16
	s_nop 1
	v_addc_co_u32_e32 v17, vcc, 0, v17, vcc
	global_store_dwordx2 v[16:17], v[12:13], off offset:3456
.LBB0_306:
	v_mul_f32_e32 v12, 0x41000000, v2
	v_mul_f32_e32 v13, 0x41000000, v3
	v_mul_f32_e32 v16, 0x41000000, v4
	v_mul_f32_e32 v22, 0x41000000, v5
	v_mul_f32_e32 v23, 0x41000000, v20
	v_mul_f32_e32 v25, 0x41000000, v21
	v_mul_f32_e32 v26, 0x41000000, v18
	v_mul_f32_e32 v29, 0x41000000, v19
	s_and_b64 vcc, exec, s[12:13]
	v_med3_f32 v17, v12, s64, v250
	v_med3_f32 v24, v13, s64, v250
	v_med3_f32 v12, v16, s64, v250
	v_med3_f32 v13, v22, s64, v250
	v_med3_f32 v22, v23, s64, v250
	v_med3_f32 v25, v25, s64, v250
	v_med3_f32 v16, v26, s64, v250
	v_med3_f32 v23, v29, s64, v250
	s_cbranch_vccnz .LBB0_313
	v_cvt_pk_fp8_f32 v30, v17, v24
	v_cvt_pk_fp8_f32 v31, v22, v25
	s_add_i32 s68, s94, s46
	v_lshl_add_u64 v[10:11], v[10:11], 0, s[68:69]
	v_cvt_pk_fp8_f32 v30, v12, v13 op_sel:[0,0,1]
	v_cvt_pk_fp8_f32 v31, v16, v23 op_sel:[0,0,1]
	v_lshl_add_u64 v[10:11], v[10:11], 0, v[6:7]
	v_add_co_u32_e32 v10, vcc, 0x342ff000, v10
	s_nop 1
	v_addc_co_u32_e32 v11, vcc, 0, v11, vcc
	global_store_dwordx2 v[10:11], v[30:31], off offset:2944
	s_and_b64 vcc, exec, s[14:15]
	s_cbranch_vccz .LBB0_314

;     __device__ __forceinline__ void operator()(const f32x4 (&acc)[2][2][4][2], const Unit& u, int wr, int wc, int fr_in, int fq_in) const {
;     ...
;                     if (kind == 2 && f8qk) { u32x2 w8; w8.x = pack4_fp8_x8(v0); w8.y = pack4_fp8_x8(v1); *(u32x2*)(ws + WS_KR8 + (size_t)row * 32 + 8 * fq) = w8; }
.LBB0_309:
	v_cvt_pk_fp8_f32 v8, v17, v24
	v_cvt_pk_fp8_f32 v9, v22, v25
	v_lshlrev_b64 v[10:11], 5, v[14:15]
	v_lshl_add_u64 v[10:11], s[34:35], 0, v[10:11]
	v_cvt_pk_fp8_f32 v8, v12, v13 op_sel:[0,0,1]
	v_cvt_pk_fp8_f32 v9, v16, v23 op_sel:[0,0,1]
	v_lshl_add_u64 v[6:7], v[10:11], 0, v[6:7]
	global_store_dwordx2 v[6:7], v[8:9], off
	s_and_b64 vcc, exec, s[8:9]
	s_cbranch_vccz .LBB0_316

;     __device__ __forceinline__ void operator()(const f32x4 (&acc)[2][2][4][2], const Unit& u, int wr, int wc, int fr_in, int fq_in) const {
;     ...
;                     if (f8ch && colg >= 1792) {
;                         const int c0_ = colg - 1792 + 8 * fq, bb_ = row >> 13, pos_ = row & (SEQ_ - 1), key_ = pos_ & 63, k32_ = key_ & 31;
;                         unsigned char* p_ = ws + WS_VB8T + ((((size_t)(bb_ * 8 + (c0_ >> 6)) * 128 + (pos_ >> 6)) * 64 + (c0_ & 63)) * 64) + 32 * ((k32_ >> 2) & 1) + 16 * (key_ >> 5) + (k32_ & 3) + 4 * (k32_ >> 3);
;                         const unsigned w0_ = pack4_fp8_x8(v0), w1_ = pack4_fp8_x8(v1);
; #pragma unroll
;                         for (int e_ = 0; e_ < 4; ++e_) { p_[e_ * 64] = (unsigned char)((w0_ >> (8 * e_)) & 0xffu); p_[(4 + e_) * 64] = (unsigned char)((w1_ >> (8 * e_)) & 0xffu); }
;                     }
.LBB0_314:
	v_ashrrev_i32_e32 v10, 10, v14
	v_and_b32_e32 v10, -8, v10
	v_add_u32_e32 v10, v10, v28
	v_ashrrev_i32_e32 v11, 31, v10
	v_lshlrev_b64 v[10:11], 13, v[10:11]
	v_and_or_b32 v10, v14, s50, v10
	v_or_b32_e32 v10, v10, v27
	v_lshlrev_b64 v[10:11], 6, v[10:11]
	v_lshl_add_u64 v[10:11], s[24:25], 0, v[10:11]
	v_lshrrev_b32_e32 v26, 1, v14
	v_lshl_add_u64 v[10:11], v[10:11], 0, v[0:1]
	v_and_b32_e32 v0, 16, v26
	v_lshl_add_u64 v[10:11], v[10:11], 0, v[0:1]
	v_lshl_add_u64 v[8:9], v[10:11], 0, v[8:9]
	v_and_b32_e32 v0, 12, v26
	v_lshl_add_u64 v[8:9], v[8:9], 0, v[0:1]
	v_cvt_pk_fp8_f32 v0, v17, v24
	v_cvt_pk_fp8_f32 v10, v22, v25
	v_cvt_pk_fp8_f32 v0, v12, v13 op_sel:[0,0,1]
	v_cvt_pk_fp8_f32 v10, v16, v23 op_sel:[0,0,1]
	global_store_byte v[8:9], v0, off
	global_store_byte v[8:9], v10, off offset:256
	v_lshrrev_b32_e32 v11, 8, v0
	global_store_byte v[8:9], v11, off offset:64
	v_lshrrev_b32_e32 v11, 8, v10
	global_store_byte v[8:9], v11, off offset:320
	global_store_byte_d16_hi v[8:9], v0, off offset:128
	global_store_byte_d16_hi v[8:9], v10, off offset:384
	v_lshrrev_b32_e32 v0, 24, v0
	global_store_byte v[8:9], v0, off offset:192
	v_lshrrev_b32_e32 v0, 24, v10
	global_store_byte v[8:9], v0, off offset:448
	s_and_b64 vcc, exec, s[6:7]
	s_cbranch_vccz .LBB0_309

; #define LDS_WAIT() asm volatile("s_waitcnt lgkmcnt(0)" ::: "memory")
; __device__ __forceinline__ void tr_item(const TrJob& J, int item, LAS float* scr, int lane) {
;     const int nblk = J.N / 32, kb = item / nblk, nb = item % nblk, k0 = 64 * kb, n0 = 32 * nb;
;     float wv[32];
; #pragma unroll
;     for (int i = 0; i < 32; ++i) wv[i] = __builtin_nontemporal_load(J.W + (size_t)(k0 + 2 * i + (lane >> 5)) * J.N + n0 + (lane & 31));
; #pragma unroll
;     for (int i = 0; i < 32; ++i) scr[(2 * i + (lane >> 5)) * 33 + (lane & 31)] = wv[i];
;     LDS_WAIT(); asm volatile("" ::: "memory");
; __device__ __forceinline__ void moe_job(const KP* kp, unsigned char* ws, int l, int g, TrJob& J, int& it) {
;     const int mj = l >> 1, j = g / IT_FF; it = g % IT_FF;
;     unsigned char* WM13 = ws + WS_WM; unsigned char* WM2 = WM13 + (size_t)NEXP * 2 * FF_ * D_ * 2; const int eb = f8_layer(l) ? 1 : 2;
;     if (j < 2 * NEXP) { const int e = j >> 1;
;         if ((j & 1) == 0) J = TrJob{kp->in[14] + (size_t)(mj * NEXP + e) * D_ * FF_, D_, FF_, (bf16*)(WM13 + (size_t)e * 2 * FF_ * D_ * eb), kp->in[9] + l * D_, TM_W1, (int)f8_layer(l)};
;         else J = TrJob{kp->in[15] + (size_t)(mj * NEXP + e) * D_ * FF_, D_, FF_, (bf16*)(WM13 + (size_t)e * 2 * FF_ * D_ * eb), kp->in[9] + l * D_, TM_W3, (int)f8_layer(l)};
;     } else { const int e = j - 2 * NEXP; J = TrJob{kp->in[16] + (size_t)(mj * NEXP + e) * FF_ * D_, FF_, D_, (bf16*)(WM2 + (size_t)e * FF_ * D_ * eb), nullptr, TM_ID, (int)f8_layer(l)}; }
.LBB0_327:
	s_mul_hi_i32 s4, s1, 0x92492493
	s_add_i32 s4, s4, s1
	s_lshr_b32 s5, s4, 31
	s_ashr_i32 s4, s4, 10
	s_add_i32 s4, s4, s5
	s_mul_i32 s5, s4, 0xfffff900
	s_add_i32 s8, s1, s5
	s_ashr_i32 s5, s4, 1
	s_and_b32 s14, s4, 1
	s_add_i32 s6, s5, s10
	s_mul_hi_i32 s7, s5, 0x700000
	s_mul_i32 s5, s5, 0x700000
	s_add_u32 s4, s11, s5
	s_addc_u32 s5, s12, s7
	s_cmp_eq_u32 s14, 0
	s_mul_hi_i32 s9, s6, 0xe00000
	s_mul_i32 s15, s6, 0xe00000
	s_cselect_b32 s6, s28, 0x78
	s_add_u32 s6, s16, s6
	s_addc_u32 s7, s17, 0
	s_load_dwordx2 s[6:7], s[6:7], 0x0
	s_waitcnt lgkmcnt(0)
	s_add_u32 s15, s6, s15
	s_mul_i32 s6, s8, 0x4925
	s_addc_u32 s20, s7, s9
	s_lshr_b32 s7, s6, 31
	s_ashr_i32 s6, s6, 21
	s_add_i32 s6, s6, s7
	s_sext_i32_i16 s9, s6
	s_mulk_i32 s6, 0x70
	s_sub_i32 s6, s8, s6
	s_sext_i32_i16 s7, s6
	s_lshl_b32 s8, s7, 5
	s_lshl_b32 s6, s9, 6
	s_ashr_i32 s9, s8, 31
	s_lshl_b64 s[18:19], s[8:9], 2
	s_add_u32 s18, s15, s18
	s_addc_u32 s19, s20, s19
	v_add_u32_e32 v40, s6, v14
	v_lshl_add_u64 v[36:37], s[18:19], 0, v[0:1]
	v_mad_i64_i32 v[2:3], s[18:19], v40, s33, v[36:37]
	global_load_dword v41, v[2:3], off nt
	v_add_u32_e32 v2, 2, v40
	v_mad_i64_i32 v[2:3], s[18:19], v2, s33, v[36:37]
	global_load_dword v42, v[2:3], off nt
	v_add_u32_e32 v2, 4, v40
	v_mad_i64_i32 v[2:3], s[18:19], v2, s33, v[36:37]
	global_load_dword v43, v[2:3], off nt
	v_add_u32_e32 v2, 6, v40
	v_mad_i64_i32 v[2:3], s[18:19], v2, s33, v[36:37]
	global_load_dword v44, v[2:3], off nt
	v_add_u32_e32 v2, 8, v40
	v_mad_i64_i32 v[2:3], s[18:19], v2, s33, v[36:37]
	global_load_dword v2, v[2:3], off nt
	v_add_u32_e32 v3, 10, v40
	v_mad_i64_i32 v[4:5], s[18:19], v3, s33, v[36:37]
	v_add_u32_e32 v3, 12, v40
	v_mad_i64_i32 v[6:7], s[18:19], v3, s33, v[36:37]
	v_add_u32_e32 v3, 14, v40
	global_load_dword v5, v[4:5], off nt
	v_add_u32_e32 v8, 34, v40
	global_load_dword v9, v[6:7], off nt
	v_mad_i64_i32 v[6:7], s[18:19], v3, s33, v[36:37]
	v_add_u32_e32 v3, 16, v40
	global_load_dword v23, v[6:7], off nt
	v_mad_i64_i32 v[6:7], s[18:19], v3, s33, v[36:37]
	v_add_u32_e32 v4, 18, v40
	global_load_dword v3, v[6:7], off nt
	v_mad_i64_i32 v[6:7], s[18:19], v4, s33, v[36:37]
	v_add_u32_e32 v4, 20, v40
	v_mad_i64_i32 v[12:13], s[18:19], v4, s33, v[36:37]
	v_add_u32_e32 v4, 22, v40
	global_load_dword v7, v[6:7], off nt
	v_add_u32_e32 v28, 58, v40
	global_load_dword v18, v[12:13], off nt
	v_mad_i64_i32 v[12:13], s[18:19], v4, s33, v[36:37]
	v_add_u32_e32 v4, 24, v40
	global_load_dword v26, v[12:13], off nt
	v_mad_i64_i32 v[12:13], s[18:19], v4, s33, v[36:37]
	v_add_u32_e32 v6, 26, v40
	global_load_dword v4, v[12:13], off nt
	v_mad_i64_i32 v[12:13], s[18:19], v6, s33, v[36:37]
	v_add_u32_e32 v6, 28, v40
	v_mad_i64_i32 v[20:21], s[18:19], v6, s33, v[36:37]
	v_add_u32_e32 v6, 30, v40
	v_mad_i64_i32 v[24:25], s[18:19], v6, s33, v[36:37]
	v_add_u32_e32 v6, 32, v40
	global_load_dword v12, v[12:13], off nt
	s_lshl_b32 s7, s7, 6
	global_load_dword v21, v[20:21], off nt
	s_and_b32 s7, s7, 0xffffff00
	global_load_dword v29, v[24:25], off nt
	v_mad_i64_i32 v[24:25], s[18:19], v6, s33, v[36:37]
	global_load_dword v6, v[24:25], off nt
	v_mad_i64_i32 v[24:25], s[18:19], v8, s33, v[36:37]
	v_add_u32_e32 v8, 36, v40
	global_load_dword v19, v[24:25], off nt
	v_mad_i64_i32 v[24:25], s[18:19], v8, s33, v[36:37]
	v_add_u32_e32 v8, 38, v40
	v_mad_i64_i32 v[30:31], s[18:19], v8, s33, v[36:37]
	v_add_u32_e32 v8, 40, v40
	v_mad_i64_i32 v[32:33], s[18:19], v8, s33, v[36:37]
	v_add_u32_e32 v13, 42, v40
	global_load_dword v24, v[24:25], off nt
	v_add_u32_e32 v20, 50, v40
	global_load_dword v31, v[30:31], off nt
	s_and_b32 s8, s8, 0x60
	global_load_dword v8, v[32:33], off nt
	v_mad_i64_i32 v[32:33], s[18:19], v13, s33, v[36:37]
	v_add_u32_e32 v13, 44, v40
	global_load_dword v22, v[32:33], off nt
	v_mad_i64_i32 v[32:33], s[18:19], v13, s33, v[36:37]
	v_add_u32_e32 v13, 46, v40
	global_load_dword v27, v[32:33], off nt
	v_mad_i64_i32 v[32:33], s[18:19], v13, s33, v[36:37]
	v_add_u32_e32 v13, 48, v40
	v_mad_i64_i32 v[34:35], s[18:19], v13, s33, v[36:37]
	global_load_dword v33, v[32:33], off nt
	s_or_b32 s8, s7, s8
	global_load_dword v13, v[34:35], off nt
	v_mad_i64_i32 v[34:35], s[18:19], v20, s33, v[36:37]
	v_add_u32_e32 v20, 52, v40
	global_load_dword v25, v[34:35], off nt
	v_mad_i64_i32 v[34:35], s[18:19], v20, s33, v[36:37]
	v_add_u32_e32 v20, 54, v40
	global_load_dword v30, v[34:35], off nt
	v_mad_i64_i32 v[34:35], s[18:19], v20, s33, v[36:37]
	v_add_u32_e32 v20, 56, v40
	v_mad_i64_i32 v[38:39], s[18:19], v20, s33, v[36:37]
	global_load_dword v34, v[34:35], off nt
	v_add_u32_e32 v32, 60, v40
	global_load_dword v20, v[38:39], off nt
	v_mad_i64_i32 v[38:39], s[18:19], v28, s33, v[36:37]
	v_add_u32_e32 v35, 62, v40
	global_load_dword v28, v[38:39], off nt
	v_mad_i64_i32 v[38:39], s[18:19], v32, s33, v[36:37]
	v_mad_i64_i32 v[36:37], s[18:19], v35, s33, v[36:37]
	global_load_dword v32, v[38:39], off nt
	global_load_dword v35, v[36:37], off nt
	v_add_u32_e32 v36, 0x400, v17
	s_waitcnt vmcnt(0)
	ds_write2_b32 v17, v41, v42 offset1:66
	s_waitcnt vmcnt(28)
	ds_write2_b32 v17, v43, v44 offset0:132 offset1:198
	s_waitcnt vmcnt(26)
	ds_write2_b32 v36, v2, v5 offset0:8 offset1:74
	s_waitcnt vmcnt(24)
	ds_write2_b32 v36, v9, v23 offset0:140 offset1:206
	v_add_u32_e32 v2, 0x800, v17
	s_waitcnt vmcnt(22)
	ds_write2_b32 v2, v3, v7 offset0:16 offset1:82
	s_waitcnt vmcnt(20)
	ds_write2_b32 v2, v18, v26 offset0:148 offset1:214
	v_add_u32_e32 v2, 0xc00, v17
	s_waitcnt vmcnt(18)
	ds_write2_b32 v2, v4, v12 offset0:24 offset1:90
	s_waitcnt vmcnt(16)
	ds_write2_b32 v2, v21, v29 offset0:156 offset1:222
	v_add_u32_e32 v2, 0x1000, v17
	s_waitcnt vmcnt(14)
; #define GAS __attribute__((address_space(1)))
; #define LAS __attribute__((address_space(3)))
; #define LDS_WAIT() asm volatile("s_waitcnt lgkmcnt(0)" ::: "memory")
; __device__ __forceinline__ unsigned pk2(float lo, float hi) { return f2bf(lo) | (f2bf(hi) << 16); }
; __device__ __forceinline__ void tr_item(const TrJob& J, int item, LAS float* scr, int lane) {
;     ...
;     for (int i = 0; i < 32; ++i) scr[(2 * i + (lane >> 5)) * 33 + (lane & 31)] = wv[i];
;     LDS_WAIT(); asm volatile("" ::: "memory");
;     const int c = lane & 7; float g[8];
; #pragma unroll
;     for (int e = 0; e < 8; ++e) g[e] = J.gain ? J.gain[k0 + 8 * c + e] : 1.f;
; #pragma unroll
;     for (int j = 0; j < 4; ++j) { const int n = (lane >> 3) + 8 * j; const LAS float* s = scr + (8 * c) * 33 + n;
;         if (J.f8) { int w0 = 0, w1 = 0;
;             w0 = __builtin_amdgcn_cvt_pk_fp8_f32(s[0 * 33] * g[0] * 64.0f, s[1 * 33] * g[1] * 64.0f, w0, false); w0 = __builtin_amdgcn_cvt_pk_fp8_f32(s[2 * 33] * g[2] * 64.0f, s[3 * 33] * g[3] * 64.0f, w0, true);
;             w1 = __builtin_amdgcn_cvt_pk_fp8_f32(s[4 * 33] * g[4] * 64.0f, s[5 * 33] * g[5] * 64.0f, w1, false); w1 = __builtin_amdgcn_cvt_pk_fp8_f32(s[6 * 33] * g[6] * 64.0f, s[7 * 33] * g[7] * 64.0f, w1, true);
;             v2u o; o.x = (unsigned)w0; o.y = (unsigned)w1; *(GAS v2u*)((unsigned char*)J.dst + (size_t)tr_dest_row(J.mode, n0, n) * J.K + k0 + 8 * c) = o; }
;         else { v4u o; o.x = pk2(s[0 * 33] * g[0], s[1 * 33] * g[1]); o.y = pk2(s[2 * 33] * g[2], s[3 * 33] * g[3]); o.z = pk2(s[4 * 33] * g[4], s[5 * 33] * g[5]); o.w = pk2(s[6 * 33] * g[6], s[7 * 33] * g[7]);
;         *(GAS v4u*)(J.dst + (size_t)tr_dest_row(J.mode, n0, n) * J.K + k0 + 8 * c) = o; } }
	ds_write2_b32 v2, v6, v19 offset0:32 offset1:98
	s_waitcnt vmcnt(12)
	ds_write2_b32 v2, v24, v31 offset0:164 offset1:230
	v_add_u32_e32 v2, 0x1400, v17
	s_waitcnt vmcnt(10)
	ds_write2_b32 v2, v8, v22 offset0:40 offset1:106
	s_waitcnt vmcnt(8)
	ds_write2_b32 v2, v27, v33 offset0:172 offset1:238
	v_add_u32_e32 v2, 0x1800, v17
	s_waitcnt vmcnt(6)
	ds_write2_b32 v2, v13, v25 offset0:48 offset1:114
	s_waitcnt vmcnt(4)
	ds_write2_b32 v2, v30, v34 offset0:180 offset1:246
	v_add_u32_e32 v2, 0x1c00, v17
	s_waitcnt vmcnt(2)
	ds_write2_b32 v2, v20, v28 offset0:56 offset1:122
	s_waitcnt vmcnt(0)
	ds_write2_b32 v2, v32, v35 offset0:188 offset1:254
	v_or_b32_e32 v2, s6, v10
	s_waitcnt lgkmcnt(0)
	v_ashrrev_i32_e32 v3, 31, v2
	v_lshl_add_u64 v[6:7], v[2:3], 2, s[2:3]
	global_load_dwordx4 v[2:5], v[6:7], off offset:16
	s_nop 0
	global_load_dwordx4 v[6:9], v[6:7], off
	ds_read2_b32 v[18:19], v16 offset1:8
	ds_read2_b32 v[20:21], v16 offset0:33 offset1:41
	ds_read2_b32 v[24:25], v16 offset0:66 offset1:74
	ds_read2_b32 v[26:27], v16 offset0:99 offset1:107
	ds_read2_b32 v[28:29], v16 offset0:132 offset1:140
	ds_read2_b32 v[30:31], v16 offset0:165 offset1:173
	ds_read2_b32 v[32:33], v16 offset0:198 offset1:206
	ds_read2_b32 v[34:35], v16 offset0:231 offset1:239
	s_lshl_b32 s9, s14, 7
	s_or_b32 s8, s8, s9
	s_ashr_i32 s7, s6, 31
	s_add_i32 s1, s1, s13
	s_cmp_lt_i32 s1, s0
	s_waitcnt vmcnt(0) lgkmcnt(7)
	v_mul_f32_e32 v12, v6, v18
	s_waitcnt lgkmcnt(6)
	v_mul_f32_e32 v13, v7, v20
	v_mul_f32_e32 v12, 0x42800000, v12
	v_mul_f32_e32 v13, 0x42800000, v13
	v_cvt_pk_fp8_f32 v22, v12, v13
	s_waitcnt lgkmcnt(5)
	v_mul_f32_e32 v12, v8, v24
	s_waitcnt lgkmcnt(4)
	v_mul_f32_e32 v13, v9, v26
	v_mul_f32_e32 v12, 0x42800000, v12
	v_mul_f32_e32 v13, 0x42800000, v13
	v_cvt_pk_fp8_f32 v22, v12, v13 op_sel:[0,0,1]
	s_waitcnt lgkmcnt(3)
	v_mul_f32_e32 v12, v2, v28
	s_waitcnt lgkmcnt(2)
	v_mul_f32_e32 v13, v3, v30
	v_mul_f32_e32 v12, 0x42800000, v12
	v_mul_f32_e32 v13, 0x42800000, v13
	v_cvt_pk_fp8_f32 v23, v12, v13
	s_waitcnt lgkmcnt(1)
	v_mul_f32_e32 v12, v4, v32
	s_waitcnt lgkmcnt(0)
	v_mul_f32_e32 v13, v5, v34
	v_mul_f32_e32 v12, 0x42800000, v12
	v_mul_f32_e32 v13, 0x42800000, v13
	v_cvt_pk_fp8_f32 v23, v12, v13 op_sel:[0,0,1]
	v_add_u32_e32 v12, s8, v15
	v_ashrrev_i32_e32 v13, 31, v12
	v_lshlrev_b64 v[36:37], 10, v[12:13]
	v_mul_f32_e32 v13, v6, v19
	v_mul_f32_e32 v18, v7, v21
	v_mul_f32_e32 v13, 0x42800000, v13
	v_mul_f32_e32 v19, 0x42800000, v18
	v_cvt_pk_fp8_f32 v18, v13, v19
	v_mul_f32_e32 v13, v8, v25
	v_mul_f32_e32 v19, v9, v27
	v_mul_f32_e32 v13, 0x42800000, v13
	v_mul_f32_e32 v19, 0x42800000, v19
	v_cvt_pk_fp8_f32 v18, v13, v19 op_sel:[0,0,1]
	v_mul_f32_e32 v13, v2, v29
	v_mul_f32_e32 v19, v3, v31
	v_mul_f32_e32 v13, 0x42800000, v13
	v_mul_f32_e32 v20, 0x42800000, v19
	v_cvt_pk_fp8_f32 v19, v13, v20
	v_mul_f32_e32 v13, v4, v33
	v_mul_f32_e32 v20, v5, v35
	v_mul_f32_e32 v13, 0x42800000, v13
	v_mul_f32_e32 v20, 0x42800000, v20
	v_cvt_pk_fp8_f32 v19, v13, v20 op_sel:[0,0,1]
	v_add_u32_e32 v20, 8, v12
	v_ashrrev_i32_e32 v21, 31, v20
	v_lshlrev_b64 v[20:21], 10, v[20:21]
	v_lshl_add_u64 v[20:21], s[4:5], 0, v[20:21]
	v_lshl_add_u64 v[20:21], v[20:21], 0, s[6:7]
	v_lshl_add_u64 v[20:21], v[20:21], 0, v[10:11]
	global_store_dwordx2 v[20:21], v[18:19], off
	ds_read2_b32 v[18:19], v16 offset0:16 offset1:24
	ds_read2_b32 v[20:21], v16 offset0:49 offset1:57
	v_lshl_add_u64 v[36:37], s[4:5], 0, v[36:37]
	v_lshl_add_u64 v[36:37], v[36:37], 0, s[6:7]
	ds_read2_b32 v[24:25], v16 offset0:82 offset1:90
	ds_read2_b32 v[26:27], v16 offset0:115 offset1:123
	v_lshl_add_u64 v[36:37], v[36:37], 0, v[10:11]
	s_waitcnt lgkmcnt(3)
	v_mul_f32_e32 v13, v6, v18
	s_waitcnt lgkmcnt(2)
	v_mul_f32_e32 v18, v7, v20
	global_store_dwordx2 v[36:37], v[22:23], off
	v_mul_f32_e32 v13, 0x42800000, v13
	v_mul_f32_e32 v18, 0x42800000, v18
	ds_read2_b32 v[28:29], v16 offset0:148 offset1:156
	ds_read2_b32 v[30:31], v16 offset0:181 offset1:189
	v_cvt_pk_fp8_f32 v22, v13, v18
	s_waitcnt lgkmcnt(3)
	v_mul_f32_e32 v13, v8, v24
	s_waitcnt lgkmcnt(2)
	v_mul_f32_e32 v18, v9, v26
	v_mul_f32_e32 v13, 0x42800000, v13
	v_mul_f32_e32 v18, 0x42800000, v18
	ds_read2_b32 v[32:33], v16 offset0:214 offset1:222
	ds_read2_b32 v[34:35], v16 offset0:247 offset1:255
	v_cvt_pk_fp8_f32 v22, v13, v18 op_sel:[0,0,1]
	s_waitcnt lgkmcnt(3)
	v_mul_f32_e32 v13, v2, v28
	s_waitcnt lgkmcnt(2)
	v_mul_f32_e32 v18, v3, v30
	v_mul_f32_e32 v13, 0x42800000, v13
	v_mul_f32_e32 v18, 0x42800000, v18
	v_cvt_pk_fp8_f32 v23, v13, v18
	s_waitcnt lgkmcnt(1)
	v_mul_f32_e32 v13, v4, v32
	s_waitcnt lgkmcnt(0)
	v_mul_f32_e32 v18, v5, v34
	v_mul_f32_e32 v13, 0x42800000, v13
	v_mul_f32_e32 v18, 0x42800000, v18
	v_mul_f32_e32 v6, v6, v19
	v_cvt_pk_fp8_f32 v23, v13, v18 op_sel:[0,0,1]
	v_mul_f32_e32 v13, 0x42800000, v6
	v_mul_f32_e32 v6, v7, v21
	v_mul_f32_e32 v7, 0x42800000, v6
	v_cvt_pk_fp8_f32 v6, v13, v7
	v_mul_f32_e32 v7, v8, v25
	v_mul_f32_e32 v8, v9, v27
	v_mul_f32_e32 v7, 0x42800000, v7
	v_mul_f32_e32 v8, 0x42800000, v8
	v_mul_f32_e32 v2, v2, v29
	v_mul_f32_e32 v3, v3, v31
	v_cvt_pk_fp8_f32 v6, v7, v8 op_sel:[0,0,1]
	v_mul_f32_e32 v2, 0x42800000, v2
	v_mul_f32_e32 v3, 0x42800000, v3
	v_cvt_pk_fp8_f32 v7, v2, v3
	v_mul_f32_e32 v2, v4, v33
	v_mul_f32_e32 v3, v5, v35
	v_mul_f32_e32 v2, 0x42800000, v2
	v_mul_f32_e32 v3, 0x42800000, v3
	v_add_u32_e32 v36, 16, v12
	v_cvt_pk_fp8_f32 v7, v2, v3 op_sel:[0,0,1]
	v_add_u32_e32 v2, 24, v12
	v_ashrrev_i32_e32 v37, 31, v36
	v_ashrrev_i32_e32 v3, 31, v2
	v_lshlrev_b64 v[36:37], 10, v[36:37]
	v_lshlrev_b64 v[2:3], 10, v[2:3]
	v_lshl_add_u64 v[36:37], s[4:5], 0, v[36:37]
	v_lshl_add_u64 v[2:3], s[4:5], 0, v[2:3]
	v_lshl_add_u64 v[36:37], v[36:37], 0, s[6:7]
	v_lshl_add_u64 v[2:3], v[2:3], 0, s[6:7]
	v_lshl_add_u64 v[36:37], v[36:37], 0, v[10:11]
	v_lshl_add_u64 v[2:3], v[2:3], 0, v[10:11]
	global_store_dwordx2 v[36:37], v[22:23], off
	global_store_dwordx2 v[2:3], v[6:7], off
	s_waitcnt lgkmcnt(0)
	s_cbranch_scc1 .LBB0_327

; __device__ __forceinline__ u32x4 pack8(const f32x4 a, const f32x4 b) { u32x4 w; w.x = cvt_pk_bf16(a[0], a[1]); w.y = cvt_pk_bf16(a[2], a[3]); w.z = cvt_pk_bf16(b[0], b[1]); w.w = cvt_pk_bf16(b[2], b[3]); return w; }
;     __device__ __forceinline__ void operator()(const f32x4 (&acc)[2][2][4][2], const Unit& u, int wr, int wc, int fr, int fq) const {
;     ...
;             for (int ai = 0; ai < 2; ++ai)
; #pragma unroll
;                 for (int m = 0; m < 4; ++m) {
;                     const int row = row0 + ai * HALF + m * 16; const float r = t[ai * 64 + m * 16 + fr] * qscale;
;                     f32x4 v0 = acc[ai][bj][m][0] * r, v1 = acc[ai][bj][m][1] * r;
;                     if (rope) rope8(v0, v1, rcos, rsin, row & (SEQ_ - 1), fq);
;                     if (!f8qk) *(u32x4*)(q + (size_t)row * 768 + colg + 8 * fq) = pack8(v0, v1);
;                     if (f8qk) { u32x2 w8; w8.x = pack4_fp8_x16(v0); w8.y = pack4_fp8_x16(v1); *(u32x2*)(ws + WS_Q8 + (size_t)row * 768 + colg + 8 * fq) = w8; }
;                 }
.LBB0_399:
	v_mul_f32_e32 v122, 0x41800000, v122
	v_med3_f32 v157, v122, s64, v250
	v_mul_f32_e32 v122, 0x41800000, v123
	v_med3_f32 v123, v122, s64, v250
	v_cvt_pk_fp8_f32 v122, v157, v123
	v_mul_f32_e32 v123, 0x41800000, v124
	v_mul_f32_e32 v124, 0x41800000, v125
	v_med3_f32 v123, v123, s64, v250
	v_med3_f32 v124, v124, s64, v250
	v_cvt_pk_fp8_f32 v122, v123, v124 op_sel:[0,0,1]
	v_mul_f32_e32 v123, 0x41800000, v126
	v_med3_f32 v124, v123, s64, v250
	v_mul_f32_e32 v123, 0x41800000, v127
	v_med3_f32 v125, v123, s64, v250
	v_cvt_pk_fp8_f32 v123, v124, v125
	v_mul_f32_e32 v124, 0x41800000, v128
	v_mul_f32_e32 v125, 0x41800000, v129
	v_med3_f32 v124, v124, s64, v250
	v_med3_f32 v125, v125, s64, v250
	ds_read_b32 v126, v155 offset:64
	v_cvt_pk_fp8_f32 v123, v124, v125 op_sel:[0,0,1]
	v_mov_b64_e32 v[124:125], s[22:23]
	s_ashr_i32 s29, s28, 31
	v_mad_i64_i32 v[124:125], s[4:5], v149, s67, v[124:125]
	v_lshl_add_u64 v[124:125], v[124:125], 0, s[28:29]
	v_lshl_add_u64 v[124:125], v[124:125], 0, v[138:139]
	global_store_dwordx2 v[124:125], v[122:123], off
	v_or_b32_e32 v123, 16, v149
	s_waitcnt lgkmcnt(0)
	v_mul_f32_e32 v122, 0x3e16c740, v126
	v_pk_mul_f32 v[126:127], v[116:117], v[122:123] op_sel_hi:[1,0]
	v_cndmask_b32_e64 v116, 0, 1, s[30:31]
	v_cmp_ne_u32_e64 s[4:5], 1, v116
	v_lshlrev_b32_e32 v116, 6, v123
	v_pk_mul_f32 v[120:121], v[120:121], v[122:123] op_sel_hi:[1,0]
	v_pk_mul_f32 v[118:119], v[118:119], v[122:123] op_sel_hi:[1,0]
	v_pk_mul_f32 v[114:115], v[114:115], v[122:123] op_sel_hi:[1,0]
	s_andn2_b64 vcc, exec, s[30:31]
	v_and_b32_e32 v116, 0x7f7c0, v116
	s_cbranch_vccnz .LBB0_401
	v_mov_b32_e32 v117, v1
	v_add_u32_e32 v244, 160, v192
	v_lshlrev_b32_e32 v244, 6, v244
	v_and_b32_e32 v244, 0x7ffc0, v244
	v_lshl_add_u64 v[204:205], v[142:143], 0, v[244:245]
	global_load_dwordx4 v[204:207], v[204:205], off
	v_lshl_add_u64 v[208:209], v[140:141], 0, v[244:245]
	global_load_dwordx4 v[208:211], v[208:209], off
	v_pk_mul_f32 v[128:129], v[126:127], v[214:215]
	v_pk_mul_f32 v[168:169], v[114:115], v[212:213]
	v_pk_mul_f32 v[214:215], v[120:121], v[214:215]
	v_pk_mul_f32 v[212:213], v[118:119], v[212:213]
	v_pk_fma_f32 v[120:121], v[120:121], v[218:219], v[128:129] neg_lo:[0,0,1] neg_hi:[0,0,1]
	v_pk_fma_f32 v[118:119], v[118:119], v[216:217], v[168:169] neg_lo:[0,0,1] neg_hi:[0,0,1]
	v_pk_fma_f32 v[126:127], v[126:127], v[218:219], v[214:215]
	v_pk_fma_f32 v[114:115], v[114:115], v[216:217], v[212:213]
.LBB0_401:
	v_mul_f32_e32 v117, 0x41800000, v118
	v_mul_f32_e32 v118, 0x41800000, v119
	v_med3_f32 v117, v117, s64, v250
	v_med3_f32 v118, v118, s64, v250
	v_cvt_pk_fp8_f32 v128, v117, v118
	v_mul_f32_e32 v114, 0x41800000, v114
	v_mul_f32_e32 v115, 0x41800000, v115
	v_med3_f32 v114, v114, s64, v250
	v_med3_f32 v115, v115, s64, v250
	v_mul_f32_e32 v117, 0x41800000, v120
	v_mul_f32_e32 v118, 0x41800000, v121
	v_cvt_pk_fp8_f32 v129, v114, v115
	v_med3_f32 v117, v117, s64, v250
	v_med3_f32 v118, v118, s64, v250
	v_cvt_pk_fp8_f32 v128, v117, v118 op_sel:[0,0,1]
	v_mul_f32_e32 v114, 0x41800000, v126
	v_mul_f32_e32 v115, 0x41800000, v127
	ds_read_b32 v117, v155 offset:128
	v_med3_f32 v114, v114, s64, v250
	v_med3_f32 v115, v115, s64, v250
	v_cvt_pk_fp8_f32 v129, v114, v115 op_sel:[0,0,1]
	v_mov_b64_e32 v[114:115], s[22:23]
	v_mad_i64_i32 v[114:115], s[30:31], v123, s67, v[114:115]
	v_lshl_add_u64 v[114:115], v[114:115], 0, s[28:29]
	v_lshl_add_u64 v[118:119], v[114:115], 0, v[138:139]
	v_or_b32_e32 v115, 32, v149
	s_waitcnt lgkmcnt(0)
	v_mul_f32_e32 v114, 0x3e16c740, v117
	v_pk_mul_f32 v[120:121], v[108:109], v[114:115] op_sel_hi:[1,0]
	v_lshlrev_b32_e32 v108, 6, v115
	v_pk_mul_f32 v[112:113], v[112:113], v[114:115] op_sel_hi:[1,0]
	v_pk_mul_f32 v[110:111], v[110:111], v[114:115] op_sel_hi:[1,0]
	v_pk_mul_f32 v[106:107], v[106:107], v[114:115] op_sel_hi:[1,0]
	s_and_b64 vcc, exec, s[4:5]
	v_and_b32_e32 v108, 0x7fbc0, v108
	global_store_dwordx2 v[118:119], v[128:129], off
	s_cbranch_vccnz .LBB0_403
	v_mov_b32_e32 v109, v1
	v_add_u32_e32 v244, 176, v192
	v_lshlrev_b32_e32 v244, 6, v244
	v_and_b32_e32 v244, 0x7ffc0, v244
	v_lshl_add_u64 v[212:213], v[142:143], 0, v[244:245]
	global_load_dwordx4 v[212:215], v[212:213], off
	v_lshl_add_u64 v[216:217], v[140:141], 0, v[244:245]
	global_load_dwordx4 v[216:219], v[216:217], off
	v_pk_mul_f32 v[164:165], v[120:121], v[222:223]
	v_pk_mul_f32 v[166:167], v[106:107], v[220:221]
	v_pk_mul_f32 v[222:223], v[112:113], v[222:223]
	v_pk_mul_f32 v[220:221], v[110:111], v[220:221]
	v_pk_fma_f32 v[112:113], v[112:113], v[226:227], v[164:165] neg_lo:[0,0,1] neg_hi:[0,0,1]
	v_pk_fma_f32 v[110:111], v[110:111], v[224:225], v[166:167] neg_lo:[0,0,1] neg_hi:[0,0,1]
	v_pk_fma_f32 v[120:121], v[120:121], v[226:227], v[222:223]
	v_pk_fma_f32 v[106:107], v[106:107], v[224:225], v[220:221]
; __device__ __forceinline__ u32x4 pack8(const f32x4 a, const f32x4 b) { u32x4 w; w.x = cvt_pk_bf16(a[0], a[1]); w.y = cvt_pk_bf16(a[2], a[3]); w.z = cvt_pk_bf16(b[0], b[1]); w.w = cvt_pk_bf16(b[2], b[3]); return w; }
;     __device__ __forceinline__ void operator()(const f32x4 (&acc)[2][2][4][2], const Unit& u, int wr, int wc, int fr, int fq) const {
;     ...
;             for (int ai = 0; ai < 2; ++ai)
; #pragma unroll
;                 for (int m = 0; m < 4; ++m) {
;                     const int row = row0 + ai * HALF + m * 16; const float r = t[ai * 64 + m * 16 + fr] * qscale;
;                     f32x4 v0 = acc[ai][bj][m][0] * r, v1 = acc[ai][bj][m][1] * r;
;                     if (rope) rope8(v0, v1, rcos, rsin, row & (SEQ_ - 1), fq);
;                     if (!f8qk) *(u32x4*)(q + (size_t)row * 768 + colg + 8 * fq) = pack8(v0, v1);
;                     if (f8qk) { u32x2 w8; w8.x = pack4_fp8_x16(v0); w8.y = pack4_fp8_x16(v1); *(u32x2*)(ws + WS_Q8 + (size_t)row * 768 + colg + 8 * fq) = w8; }
;                 }
.LBB0_403:
	v_mul_f32_e32 v109, 0x41800000, v110
	v_mul_f32_e32 v110, 0x41800000, v111
	v_med3_f32 v109, v109, s64, v250
	v_med3_f32 v110, v110, s64, v250
	v_cvt_pk_fp8_f32 v126, v109, v110
	v_mul_f32_e32 v106, 0x41800000, v106
	v_mul_f32_e32 v107, 0x41800000, v107
	v_med3_f32 v106, v106, s64, v250
	v_med3_f32 v107, v107, s64, v250
	v_mul_f32_e32 v109, 0x41800000, v112
	v_mul_f32_e32 v110, 0x41800000, v113
	v_cvt_pk_fp8_f32 v127, v106, v107
	v_med3_f32 v109, v109, s64, v250
	v_med3_f32 v110, v110, s64, v250
	v_cvt_pk_fp8_f32 v126, v109, v110 op_sel:[0,0,1]
	v_mul_f32_e32 v106, 0x41800000, v120
	v_mul_f32_e32 v107, 0x41800000, v121
	ds_read_b32 v109, v155 offset:192
	v_med3_f32 v106, v106, s64, v250
	v_med3_f32 v107, v107, s64, v250
	v_cvt_pk_fp8_f32 v127, v106, v107 op_sel:[0,0,1]
	v_mov_b64_e32 v[106:107], s[22:23]
	v_mad_i64_i32 v[106:107], s[30:31], v115, s67, v[106:107]
	v_lshl_add_u64 v[106:107], v[106:107], 0, s[28:29]
	v_lshl_add_u64 v[110:111], v[106:107], 0, v[138:139]
	v_or_b32_e32 v107, 48, v149
	s_waitcnt lgkmcnt(0)
	v_mul_f32_e32 v106, 0x3e16c740, v109
	v_pk_mul_f32 v[112:113], v[100:101], v[106:107] op_sel_hi:[1,0]
	v_lshlrev_b32_e32 v100, 6, v107
	v_pk_mul_f32 v[104:105], v[104:105], v[106:107] op_sel_hi:[1,0]
	v_pk_mul_f32 v[102:103], v[102:103], v[106:107] op_sel_hi:[1,0]
	v_pk_mul_f32 v[98:99], v[98:99], v[106:107] op_sel_hi:[1,0]
	s_and_b64 vcc, exec, s[4:5]
	v_and_b32_e32 v100, 0x7ffc0, v100
	global_store_dwordx2 v[110:111], v[126:127], off
	s_cbranch_vccnz .LBB0_405
	v_mov_b32_e32 v101, v1
	v_pk_mul_f32 v[120:121], v[112:113], v[230:231]
	v_pk_mul_f32 v[164:165], v[98:99], v[228:229]
	v_pk_mul_f32 v[230:231], v[104:105], v[230:231]
	v_pk_mul_f32 v[228:229], v[102:103], v[228:229]
	v_pk_fma_f32 v[104:105], v[104:105], v[234:235], v[120:121] neg_lo:[0,0,1] neg_hi:[0,0,1]
	v_pk_fma_f32 v[102:103], v[102:103], v[232:233], v[164:165] neg_lo:[0,0,1] neg_hi:[0,0,1]
	v_pk_fma_f32 v[112:113], v[112:113], v[234:235], v[230:231]
	v_pk_fma_f32 v[98:99], v[98:99], v[232:233], v[228:229]
.LBB0_405:
	v_mul_f32_e32 v101, 0x41800000, v102
	v_mul_f32_e32 v102, 0x41800000, v103
	v_med3_f32 v101, v101, s64, v250
	v_med3_f32 v102, v102, s64, v250
	v_cvt_pk_fp8_f32 v120, v101, v102
	v_mul_f32_e32 v98, 0x41800000, v98
	v_mul_f32_e32 v99, 0x41800000, v99
	v_med3_f32 v98, v98, s64, v250
	v_med3_f32 v99, v99, s64, v250
	v_mul_f32_e32 v101, 0x41800000, v104
	v_mul_f32_e32 v102, 0x41800000, v105
	v_cvt_pk_fp8_f32 v121, v98, v99
	v_med3_f32 v101, v101, s64, v250
	v_med3_f32 v102, v102, s64, v250
	v_cvt_pk_fp8_f32 v120, v101, v102 op_sel:[0,0,1]
	v_mul_f32_e32 v98, 0x41800000, v112
	v_mul_f32_e32 v99, 0x41800000, v113
	ds_read_b32 v101, v155 offset:256
	v_med3_f32 v98, v98, s64, v250
	v_med3_f32 v99, v99, s64, v250
	v_cvt_pk_fp8_f32 v121, v98, v99 op_sel:[0,0,1]
	v_mov_b64_e32 v[98:99], s[22:23]
	v_mad_i64_i32 v[98:99], s[30:31], v107, s67, v[98:99]
	v_lshl_add_u64 v[98:99], v[98:99], 0, s[28:29]
	v_lshl_add_u64 v[102:103], v[98:99], 0, v[138:139]
	v_add_u32_e32 v99, 0x80, v149
	s_waitcnt lgkmcnt(0)
	v_mul_f32_e32 v98, 0x3e16c740, v101
	v_pk_mul_f32 v[104:105], v[92:93], v[98:99] op_sel_hi:[1,0]
	v_lshlrev_b32_e32 v92, 6, v99
	v_pk_mul_f32 v[96:97], v[96:97], v[98:99] op_sel_hi:[1,0]
	v_pk_mul_f32 v[94:95], v[94:95], v[98:99] op_sel_hi:[1,0]
	v_pk_mul_f32 v[90:91], v[90:91], v[98:99] op_sel_hi:[1,0]
	s_and_b64 vcc, exec, s[4:5]
	v_and_b32_e32 v92, 0x7f3c0, v92
	global_store_dwordx2 v[102:103], v[120:121], off
	s_cbranch_vccnz .LBB0_407
	v_mov_b32_e32 v93, v1
	v_pk_mul_f32 v[112:113], v[104:105], v[238:239]
	v_pk_mul_f32 v[120:121], v[90:91], v[236:237]
	v_pk_mul_f32 v[238:239], v[96:97], v[238:239]
	v_pk_mul_f32 v[236:237], v[94:95], v[236:237]
	v_pk_fma_f32 v[96:97], v[96:97], v[242:243], v[112:113] neg_lo:[0,0,1] neg_hi:[0,0,1]
	v_pk_fma_f32 v[94:95], v[94:95], v[240:241], v[120:121] neg_lo:[0,0,1] neg_hi:[0,0,1]
	v_pk_fma_f32 v[104:105], v[104:105], v[242:243], v[238:239]
	v_pk_fma_f32 v[90:91], v[90:91], v[240:241], v[236:237]
.LBB0_407:
	v_mul_f32_e32 v93, 0x41800000, v94
	v_mul_f32_e32 v94, 0x41800000, v95
	v_med3_f32 v93, v93, s64, v250
	v_med3_f32 v94, v94, s64, v250
	v_cvt_pk_fp8_f32 v112, v93, v94
	v_mul_f32_e32 v90, 0x41800000, v90
	v_mul_f32_e32 v91, 0x41800000, v91
	v_med3_f32 v90, v90, s64, v250
	v_med3_f32 v91, v91, s64, v250
	v_mul_f32_e32 v93, 0x41800000, v96
	v_mul_f32_e32 v94, 0x41800000, v97
	v_cvt_pk_fp8_f32 v113, v90, v91
	v_med3_f32 v93, v93, s64, v250
	v_med3_f32 v94, v94, s64, v250
	v_cvt_pk_fp8_f32 v112, v93, v94 op_sel:[0,0,1]
	v_mul_f32_e32 v90, 0x41800000, v104
	v_mul_f32_e32 v91, 0x41800000, v105
	ds_read_b32 v93, v155 offset:320
	v_med3_f32 v90, v90, s64, v250
	v_med3_f32 v91, v91, s64, v250
	v_cvt_pk_fp8_f32 v113, v90, v91 op_sel:[0,0,1]
	v_mov_b64_e32 v[90:91], s[22:23]
	v_mad_i64_i32 v[90:91], s[30:31], v99, s67, v[90:91]
	v_lshl_add_u64 v[90:91], v[90:91], 0, s[28:29]
	v_lshl_add_u64 v[94:95], v[90:91], 0, v[138:139]
	v_add_u32_e32 v91, 0x90, v149
	s_waitcnt lgkmcnt(0)
	v_mul_f32_e32 v90, 0x3e16c740, v93
	v_pk_mul_f32 v[96:97], v[84:85], v[90:91] op_sel_hi:[1,0]
	v_lshlrev_b32_e32 v84, 6, v91
	v_pk_mul_f32 v[88:89], v[88:89], v[90:91] op_sel_hi:[1,0]
	v_pk_mul_f32 v[86:87], v[86:87], v[90:91] op_sel_hi:[1,0]
	v_pk_mul_f32 v[82:83], v[82:83], v[90:91] op_sel_hi:[1,0]
	s_and_b64 vcc, exec, s[4:5]
	v_and_b32_e32 v84, 0x7f7c0, v84
	global_store_dwordx2 v[94:95], v[112:113], off
	s_cbranch_vccnz .LBB0_409
	v_mov_b32_e32 v85, v1
	v_pk_mul_f32 v[104:105], v[96:97], v[190:191]
	v_pk_mul_f32 v[112:113], v[82:83], v[188:189]
	v_pk_mul_f32 v[120:121], v[88:89], v[190:191]
	v_pk_mul_f32 v[188:189], v[86:87], v[188:189]
	v_pk_fma_f32 v[88:89], v[88:89], v[198:199], v[104:105] neg_lo:[0,0,1] neg_hi:[0,0,1]
	v_pk_fma_f32 v[86:87], v[86:87], v[196:197], v[112:113] neg_lo:[0,0,1] neg_hi:[0,0,1]
	v_pk_fma_f32 v[96:97], v[96:97], v[198:199], v[120:121]
	v_pk_fma_f32 v[82:83], v[82:83], v[196:197], v[188:189]
; __device__ __forceinline__ u32x4 pack8(const f32x4 a, const f32x4 b) { u32x4 w; w.x = cvt_pk_bf16(a[0], a[1]); w.y = cvt_pk_bf16(a[2], a[3]); w.z = cvt_pk_bf16(b[0], b[1]); w.w = cvt_pk_bf16(b[2], b[3]); return w; }
;     __device__ __forceinline__ void operator()(const f32x4 (&acc)[2][2][4][2], const Unit& u, int wr, int wc, int fr, int fq) const {
;     ...
;             for (int ai = 0; ai < 2; ++ai)
; #pragma unroll
;                 for (int m = 0; m < 4; ++m) {
;                     const int row = row0 + ai * HALF + m * 16; const float r = t[ai * 64 + m * 16 + fr] * qscale;
;                     f32x4 v0 = acc[ai][bj][m][0] * r, v1 = acc[ai][bj][m][1] * r;
;                     if (rope) rope8(v0, v1, rcos, rsin, row & (SEQ_ - 1), fq);
;                     if (!f8qk) *(u32x4*)(q + (size_t)row * 768 + colg + 8 * fq) = pack8(v0, v1);
;                     if (f8qk) { u32x2 w8; w8.x = pack4_fp8_x16(v0); w8.y = pack4_fp8_x16(v1); *(u32x2*)(ws + WS_Q8 + (size_t)row * 768 + colg + 8 * fq) = w8; }
;                 }
.LBB0_409:
	v_mul_f32_e32 v85, 0x41800000, v86
	v_mul_f32_e32 v86, 0x41800000, v87
	v_med3_f32 v85, v85, s64, v250
	v_med3_f32 v86, v86, s64, v250
	v_cvt_pk_fp8_f32 v104, v85, v86
	v_mul_f32_e32 v82, 0x41800000, v82
	v_mul_f32_e32 v83, 0x41800000, v83
	v_med3_f32 v82, v82, s64, v250
	v_med3_f32 v83, v83, s64, v250
	v_mul_f32_e32 v85, 0x41800000, v88
	v_mul_f32_e32 v86, 0x41800000, v89
	v_cvt_pk_fp8_f32 v105, v82, v83
	v_med3_f32 v85, v85, s64, v250
	v_med3_f32 v86, v86, s64, v250
	v_cvt_pk_fp8_f32 v104, v85, v86 op_sel:[0,0,1]
	v_mul_f32_e32 v82, 0x41800000, v96
	v_mul_f32_e32 v83, 0x41800000, v97
	ds_read_b32 v85, v155 offset:384
	v_med3_f32 v82, v82, s64, v250
	v_med3_f32 v83, v83, s64, v250
	v_cvt_pk_fp8_f32 v105, v82, v83 op_sel:[0,0,1]
	v_mov_b64_e32 v[82:83], s[22:23]
	v_mad_i64_i32 v[82:83], s[30:31], v91, s67, v[82:83]
	v_lshl_add_u64 v[82:83], v[82:83], 0, s[28:29]
	v_lshl_add_u64 v[86:87], v[82:83], 0, v[138:139]
	v_add_u32_e32 v83, 0xa0, v149
	s_waitcnt lgkmcnt(0)
	v_mul_f32_e32 v82, 0x3e16c740, v85
	v_pk_mul_f32 v[88:89], v[76:77], v[82:83] op_sel_hi:[1,0]
	v_lshlrev_b32_e32 v76, 6, v83
	v_pk_mul_f32 v[80:81], v[80:81], v[82:83] op_sel_hi:[1,0]
	v_pk_mul_f32 v[78:79], v[78:79], v[82:83] op_sel_hi:[1,0]
	v_pk_mul_f32 v[74:75], v[74:75], v[82:83] op_sel_hi:[1,0]
	s_and_b64 vcc, exec, s[4:5]
	v_and_b32_e32 v76, 0x7fbc0, v76
	global_store_dwordx2 v[86:87], v[104:105], off
	s_cbranch_vccnz .LBB0_411
	v_mov_b32_e32 v77, v1
	s_waitcnt vmcnt(6)
	v_pk_mul_f32 v[96:97], v[88:89], v[206:207]
	v_pk_mul_f32 v[104:105], v[74:75], v[204:205]
	v_pk_mul_f32 v[112:113], v[80:81], v[206:207]
	v_pk_mul_f32 v[120:121], v[78:79], v[204:205]
	v_pk_fma_f32 v[80:81], v[80:81], v[210:211], v[96:97] neg_lo:[0,0,1] neg_hi:[0,0,1]
	v_pk_fma_f32 v[78:79], v[78:79], v[208:209], v[104:105] neg_lo:[0,0,1] neg_hi:[0,0,1]
	v_pk_fma_f32 v[88:89], v[88:89], v[210:211], v[112:113]
	v_pk_fma_f32 v[74:75], v[74:75], v[208:209], v[120:121]
.LBB0_411:
	v_mul_f32_e32 v77, 0x41800000, v78
	v_mul_f32_e32 v78, 0x41800000, v79
	v_med3_f32 v77, v77, s64, v250
	v_med3_f32 v78, v78, s64, v250
	v_cvt_pk_fp8_f32 v96, v77, v78
	v_mul_f32_e32 v74, 0x41800000, v74
	v_mul_f32_e32 v75, 0x41800000, v75
	v_med3_f32 v74, v74, s64, v250
	v_med3_f32 v75, v75, s64, v250
	v_mul_f32_e32 v77, 0x41800000, v80
	v_mul_f32_e32 v78, 0x41800000, v81
	v_cvt_pk_fp8_f32 v97, v74, v75
	v_med3_f32 v77, v77, s64, v250
	v_med3_f32 v78, v78, s64, v250
	v_cvt_pk_fp8_f32 v96, v77, v78 op_sel:[0,0,1]
	v_mul_f32_e32 v74, 0x41800000, v88
	v_mul_f32_e32 v75, 0x41800000, v89
	ds_read_b32 v77, v155 offset:448
	v_med3_f32 v74, v74, s64, v250
	v_med3_f32 v75, v75, s64, v250
	v_cvt_pk_fp8_f32 v97, v74, v75 op_sel:[0,0,1]
	v_mov_b64_e32 v[74:75], s[22:23]
	v_mad_i64_i32 v[74:75], s[30:31], v83, s67, v[74:75]
	v_lshl_add_u64 v[74:75], v[74:75], 0, s[28:29]
	v_lshl_add_u64 v[78:79], v[74:75], 0, v[138:139]
	v_add_u32_e32 v75, 0xb0, v149
	s_waitcnt lgkmcnt(0)
	v_mul_f32_e32 v74, 0x3e16c740, v77
	v_pk_mul_f32 v[80:81], v[66:67], v[74:75] op_sel_hi:[1,0]
	v_lshlrev_b32_e32 v66, 6, v75
	v_pk_mul_f32 v[72:73], v[72:73], v[74:75] op_sel_hi:[1,0]
	v_pk_mul_f32 v[70:71], v[70:71], v[74:75] op_sel_hi:[1,0]
	v_pk_mul_f32 v[68:69], v[68:69], v[74:75] op_sel_hi:[1,0]
	s_and_b64 vcc, exec, s[4:5]
	v_and_b32_e32 v66, 0x7ffc0, v66
	global_store_dwordx2 v[78:79], v[96:97], off
	s_cbranch_vccnz .LBB0_413
	v_mov_b32_e32 v67, v1
	s_waitcnt vmcnt(4)
	v_pk_mul_f32 v[88:89], v[68:69], v[214:215]
	v_pk_mul_f32 v[96:97], v[80:81], v[212:213]
	v_pk_mul_f32 v[104:105], v[72:73], v[214:215]
	v_pk_mul_f32 v[112:113], v[70:71], v[212:213]
	v_pk_fma_f32 v[72:73], v[72:73], v[218:219], v[88:89] neg_lo:[0,0,1] neg_hi:[0,0,1]
	v_pk_fma_f32 v[70:71], v[70:71], v[216:217], v[96:97] neg_lo:[0,0,1] neg_hi:[0,0,1]
	v_pk_fma_f32 v[68:69], v[68:69], v[218:219], v[104:105]
	v_pk_fma_f32 v[80:81], v[80:81], v[216:217], v[112:113]
.LBB0_413:
	v_mul_f32_e32 v67, 0x41800000, v70
	v_mul_f32_e32 v70, 0x41800000, v71
	v_med3_f32 v67, v67, s64, v250
	v_med3_f32 v71, v70, s64, v250
	v_cvt_pk_fp8_f32 v70, v67, v71
	v_mul_f32_e32 v67, 0x41800000, v72
	v_mul_f32_e32 v71, 0x41800000, v73
	v_med3_f32 v67, v67, s64, v250
	v_med3_f32 v71, v71, s64, v250
	v_cvt_pk_fp8_f32 v70, v67, v71 op_sel:[0,0,1]
	v_mul_f32_e32 v67, 0x41800000, v80
	v_mul_f32_e32 v71, 0x41800000, v81
	v_med3_f32 v67, v67, s64, v250
	v_med3_f32 v72, v71, s64, v250
	v_cvt_pk_fp8_f32 v71, v67, v72
	v_mul_f32_e32 v67, 0x41800000, v68
	v_mul_f32_e32 v68, 0x41800000, v69
	v_med3_f32 v67, v67, s64, v250
	v_med3_f32 v68, v68, s64, v250
	v_cvt_pk_fp8_f32 v71, v67, v68 op_sel:[0,0,1]
	v_mov_b64_e32 v[68:69], s[22:23]
	v_mad_i64_i32 v[68:69], s[4:5], v75, s67, v[68:69]
	s_or_b32 s4, s28, 0x80
	s_ashr_i32 s4, s4, 5
	s_mul_hi_i32 s5, s4, 0x55555556
	v_lshl_add_u64 v[68:69], v[68:69], 0, s[28:29]
	s_lshr_b32 s28, s5, 31
	s_add_i32 s5, s5, s28
	s_mul_i32 s5, s5, 3
	v_lshl_add_u64 v[68:69], v[68:69], 0, v[138:139]
	s_sub_i32 s4, s4, s5
	v_mov_b32_e32 v149, v148
	global_store_dwordx2 v[68:69], v[70:71], off
	s_cmp_eq_u32 s4, 2
	v_mov_b32_e32 v70, v148
	v_mov_b32_e32 v71, v148
	s_cselect_b64 s[28:29], -1, 0
	s_cmp_lg_u32 s4, 2
	v_pk_mul_f32 v[64:65], v[64:65], v[70:71]
	v_pk_mul_f32 v[62:63], v[62:63], v[148:149]
	v_pk_mul_f32 v[60:61], v[60:61], v[70:71]
	v_pk_mul_f32 v[58:59], v[58:59], v[148:149]
	s_cbranch_scc1 .LBB0_415
; __device__ __forceinline__ u32x4 pack8(const f32x4 a, const f32x4 b) { u32x4 w; w.x = cvt_pk_bf16(a[0], a[1]); w.y = cvt_pk_bf16(a[2], a[3]); w.z = cvt_pk_bf16(b[0], b[1]); w.w = cvt_pk_bf16(b[2], b[3]); return w; }
;     __device__ __forceinline__ void operator()(const f32x4 (&acc)[2][2][4][2], const Unit& u, int wr, int wc, int fr, int fq) const {
;     ...
;             for (int ai = 0; ai < 2; ++ai)
; #pragma unroll
;                 for (int m = 0; m < 4; ++m) {
;                     const int row = row0 + ai * HALF + m * 16; const float r = t[ai * 64 + m * 16 + fr] * qscale;
;                     f32x4 v0 = acc[ai][bj][m][0] * r, v1 = acc[ai][bj][m][1] * r;
;                     if (rope) rope8(v0, v1, rcos, rsin, row & (SEQ_ - 1), fq);
;                     if (!f8qk) *(u32x4*)(q + (size_t)row * 768 + colg + 8 * fq) = pack8(v0, v1);
;                     if (f8qk) { u32x2 w8; w8.x = pack4_fp8_x16(v0); w8.y = pack4_fp8_x16(v1); *(u32x2*)(ws + WS_Q8 + (size_t)row * 768 + colg + 8 * fq) = w8; }
;                 }
	v_mov_b32_e32 v245, v1
	v_add_u32_e32 v244, 0, v192
	v_lshlrev_b32_e32 v244, 6, v244
	v_and_b32_e32 v244, 0x7ffc0, v244
	v_lshl_add_u64 v[204:205], v[142:143], 0, v[244:245]
	global_load_dwordx4 v[204:207], v[204:205], off
	v_lshl_add_u64 v[208:209], v[140:141], 0, v[244:245]
	global_load_dwordx4 v[208:211], v[208:209], off
	v_add_u32_e32 v244, 16, v192
	v_lshlrev_b32_e32 v244, 6, v244
	v_and_b32_e32 v244, 0x7ffc0, v244
	v_lshl_add_u64 v[212:213], v[142:143], 0, v[244:245]
	global_load_dwordx4 v[212:215], v[212:213], off
	v_lshl_add_u64 v[216:217], v[140:141], 0, v[244:245]
	global_load_dwordx4 v[216:219], v[216:217], off
	v_add_u32_e32 v244, 32, v192
	v_lshlrev_b32_e32 v244, 6, v244
	v_and_b32_e32 v244, 0x7ffc0, v244
	v_lshl_add_u64 v[220:221], v[142:143], 0, v[244:245]
	global_load_dwordx4 v[220:223], v[220:221], off
	v_lshl_add_u64 v[224:225], v[140:141], 0, v[244:245]
	global_load_dwordx4 v[224:227], v[224:225], off
	v_add_u32_e32 v244, 48, v192
	v_lshlrev_b32_e32 v244, 6, v244
	v_and_b32_e32 v244, 0x7ffc0, v244
	v_lshl_add_u64 v[228:229], v[142:143], 0, v[244:245]
	global_load_dwordx4 v[228:231], v[228:229], off
	v_lshl_add_u64 v[232:233], v[140:141], 0, v[244:245]
	global_load_dwordx4 v[232:235], v[232:233], off
	v_add_u32_e32 v244, 128, v192
	v_lshlrev_b32_e32 v244, 6, v244
	v_and_b32_e32 v244, 0x7ffc0, v244
	v_lshl_add_u64 v[236:237], v[142:143], 0, v[244:245]
	global_load_dwordx4 v[236:239], v[236:237], off
	v_lshl_add_u64 v[240:241], v[140:141], 0, v[244:245]
	global_load_dwordx4 v[240:243], v[240:241], off
	v_add_u32_e32 v244, 144, v192
	v_lshlrev_b32_e32 v244, 6, v244
	v_and_b32_e32 v244, 0x7ffc0, v244
	v_lshl_add_u64 v[188:189], v[142:143], 0, v[244:245]
	global_load_dwordx4 v[188:191], v[188:189], off
	v_lshl_add_u64 v[196:197], v[140:141], 0, v[244:245]
	global_load_dwordx4 v[196:199], v[196:197], off
	s_waitcnt vmcnt(0)
	v_pk_mul_f32 v[80:81], v[60:61], v[206:207]
	v_pk_mul_f32 v[88:89], v[58:59], v[204:205]
	v_pk_mul_f32 v[206:207], v[64:65], v[206:207]
	v_pk_mul_f32 v[204:205], v[62:63], v[204:205]
	v_pk_fma_f32 v[64:65], v[64:65], v[210:211], v[80:81] neg_lo:[0,0,1] neg_hi:[0,0,1]
	v_pk_fma_f32 v[62:63], v[62:63], v[208:209], v[88:89] neg_lo:[0,0,1] neg_hi:[0,0,1]
	v_pk_fma_f32 v[60:61], v[60:61], v[210:211], v[206:207]
	v_pk_fma_f32 v[58:59], v[58:59], v[208:209], v[204:205]
.LBB0_415:
	v_mul_f32_e32 v0, 0x41800000, v62
	v_mul_f32_e32 v62, 0x41800000, v63
	v_med3_f32 v0, v0, s64, v250
	v_med3_f32 v63, v62, s64, v250
	v_cvt_pk_fp8_f32 v62, v0, v63
	v_mul_f32_e32 v0, 0x41800000, v64
	v_mul_f32_e32 v63, 0x41800000, v65
	v_med3_f32 v0, v0, s64, v250
	v_med3_f32 v63, v63, s64, v250
	v_cvt_pk_fp8_f32 v62, v0, v63 op_sel:[0,0,1]
	v_mul_f32_e32 v0, 0x41800000, v58
	v_mul_f32_e32 v58, 0x41800000, v59
	v_med3_f32 v0, v0, s64, v250
	v_med3_f32 v58, v58, s64, v250
	v_cvt_pk_fp8_f32 v63, v0, v58
	v_mul_f32_e32 v0, 0x41800000, v60
	v_mul_f32_e32 v58, 0x41800000, v61
	v_med3_f32 v0, v0, s64, v250
	v_med3_f32 v58, v58, s64, v250
	v_cvt_pk_fp8_f32 v63, v0, v58 op_sel:[0,0,1]
	v_mov_b32_e32 v123, v122
	v_mov_b32_e32 v58, v122
	v_mov_b32_e32 v59, v122
	v_cndmask_b32_e64 v0, 0, 1, s[28:29]
	v_pk_mul_f32 v[56:57], v[56:57], v[58:59]
	v_pk_mul_f32 v[54:55], v[54:55], v[122:123]
	v_pk_mul_f32 v[52:53], v[52:53], v[58:59]
	v_cmp_ne_u32_e64 s[4:5], 1, v0
	s_andn2_b64 vcc, exec, s[28:29]
	v_pk_mul_f32 v[50:51], v[50:51], v[122:123]
	global_store_dwordx2 v[124:125], v[62:63], off offset:128
	s_cbranch_vccnz .LBB0_417
	v_mov_b32_e32 v117, v1
	v_add_u32_e32 v244, 160, v192
	v_lshlrev_b32_e32 v244, 6, v244
	v_and_b32_e32 v244, 0x7ffc0, v244
	v_lshl_add_u64 v[204:205], v[142:143], 0, v[244:245]
	global_load_dwordx4 v[204:207], v[204:205], off
	v_lshl_add_u64 v[208:209], v[140:141], 0, v[244:245]
	global_load_dwordx4 v[208:211], v[208:209], off
	v_pk_mul_f32 v[70:71], v[52:53], v[214:215]
	v_pk_mul_f32 v[72:73], v[50:51], v[212:213]
	v_pk_mul_f32 v[214:215], v[56:57], v[214:215]
	v_pk_mul_f32 v[212:213], v[54:55], v[212:213]
	v_pk_fma_f32 v[56:57], v[56:57], v[218:219], v[70:71] neg_lo:[0,0,1] neg_hi:[0,0,1]
	v_pk_fma_f32 v[54:55], v[54:55], v[216:217], v[72:73] neg_lo:[0,0,1] neg_hi:[0,0,1]
	v_pk_fma_f32 v[52:53], v[52:53], v[218:219], v[214:215]
	v_pk_fma_f32 v[50:51], v[50:51], v[216:217], v[212:213]
.LBB0_417:
	v_mul_f32_e32 v0, 0x41800000, v54
	v_mul_f32_e32 v54, 0x41800000, v55
	v_med3_f32 v0, v0, s64, v250
	v_med3_f32 v55, v54, s64, v250
	v_cvt_pk_fp8_f32 v54, v0, v55
	v_mul_f32_e32 v0, 0x41800000, v56
	v_mul_f32_e32 v55, 0x41800000, v57
	v_med3_f32 v0, v0, s64, v250
	v_med3_f32 v55, v55, s64, v250
	v_cvt_pk_fp8_f32 v54, v0, v55 op_sel:[0,0,1]
	v_mul_f32_e32 v0, 0x41800000, v50
	v_mul_f32_e32 v50, 0x41800000, v51
	v_med3_f32 v0, v0, s64, v250
	v_med3_f32 v50, v50, s64, v250
	v_cvt_pk_fp8_f32 v55, v0, v50
	v_mul_f32_e32 v0, 0x41800000, v52
	v_mul_f32_e32 v50, 0x41800000, v53
	v_med3_f32 v0, v0, s64, v250
	v_med3_f32 v50, v50, s64, v250
	v_cvt_pk_fp8_f32 v55, v0, v50 op_sel:[0,0,1]
	v_mov_b32_e32 v115, v114
	v_mov_b32_e32 v50, v114
	v_mov_b32_e32 v51, v114
	v_pk_mul_f32 v[48:49], v[48:49], v[50:51]
	v_pk_mul_f32 v[46:47], v[46:47], v[114:115]
	v_pk_mul_f32 v[44:45], v[44:45], v[50:51]
	s_and_b64 vcc, exec, s[4:5]
	v_pk_mul_f32 v[42:43], v[42:43], v[114:115]
	global_store_dwordx2 v[118:119], v[54:55], off offset:128
	s_cbranch_vccnz .LBB0_419
	v_mov_b32_e32 v109, v1
	v_add_u32_e32 v244, 176, v192
	v_lshlrev_b32_e32 v244, 6, v244
	v_and_b32_e32 v244, 0x7ffc0, v244
	v_lshl_add_u64 v[212:213], v[142:143], 0, v[244:245]
	global_load_dwordx4 v[212:215], v[212:213], off
	v_lshl_add_u64 v[216:217], v[140:141], 0, v[244:245]
	global_load_dwordx4 v[216:219], v[216:217], off
	v_pk_mul_f32 v[58:59], v[44:45], v[222:223]
	v_pk_mul_f32 v[60:61], v[42:43], v[220:221]
	v_pk_mul_f32 v[222:223], v[48:49], v[222:223]
	v_pk_mul_f32 v[220:221], v[46:47], v[220:221]
	v_pk_fma_f32 v[48:49], v[48:49], v[226:227], v[58:59] neg_lo:[0,0,1] neg_hi:[0,0,1]
	v_pk_fma_f32 v[46:47], v[46:47], v[224:225], v[60:61] neg_lo:[0,0,1] neg_hi:[0,0,1]
	v_pk_fma_f32 v[44:45], v[44:45], v[226:227], v[222:223]
	v_pk_fma_f32 v[42:43], v[42:43], v[224:225], v[220:221]
; __device__ __forceinline__ u32x4 pack8(const f32x4 a, const f32x4 b) { u32x4 w; w.x = cvt_pk_bf16(a[0], a[1]); w.y = cvt_pk_bf16(a[2], a[3]); w.z = cvt_pk_bf16(b[0], b[1]); w.w = cvt_pk_bf16(b[2], b[3]); return w; }
;     __device__ __forceinline__ void operator()(const f32x4 (&acc)[2][2][4][2], const Unit& u, int wr, int wc, int fr, int fq) const {
;     ...
;             for (int ai = 0; ai < 2; ++ai)
; #pragma unroll
;                 for (int m = 0; m < 4; ++m) {
;                     const int row = row0 + ai * HALF + m * 16; const float r = t[ai * 64 + m * 16 + fr] * qscale;
;                     f32x4 v0 = acc[ai][bj][m][0] * r, v1 = acc[ai][bj][m][1] * r;
;                     if (rope) rope8(v0, v1, rcos, rsin, row & (SEQ_ - 1), fq);
;                     if (!f8qk) *(u32x4*)(q + (size_t)row * 768 + colg + 8 * fq) = pack8(v0, v1);
;                     if (f8qk) { u32x2 w8; w8.x = pack4_fp8_x16(v0); w8.y = pack4_fp8_x16(v1); *(u32x2*)(ws + WS_Q8 + (size_t)row * 768 + colg + 8 * fq) = w8; }
;                 }
.LBB0_419:
	v_mul_f32_e32 v0, 0x41800000, v46
	v_mul_f32_e32 v46, 0x41800000, v47
	v_med3_f32 v0, v0, s64, v250
	v_med3_f32 v47, v46, s64, v250
	v_cvt_pk_fp8_f32 v46, v0, v47
	v_mul_f32_e32 v0, 0x41800000, v48
	v_mul_f32_e32 v47, 0x41800000, v49
	v_med3_f32 v0, v0, s64, v250
	v_med3_f32 v47, v47, s64, v250
	v_cvt_pk_fp8_f32 v46, v0, v47 op_sel:[0,0,1]
	v_mul_f32_e32 v0, 0x41800000, v42
	v_mul_f32_e32 v42, 0x41800000, v43
	v_med3_f32 v0, v0, s64, v250
	v_med3_f32 v42, v42, s64, v250
	v_cvt_pk_fp8_f32 v47, v0, v42
	v_mul_f32_e32 v0, 0x41800000, v44
	v_mul_f32_e32 v42, 0x41800000, v45
	v_med3_f32 v0, v0, s64, v250
	v_med3_f32 v42, v42, s64, v250
	v_cvt_pk_fp8_f32 v47, v0, v42 op_sel:[0,0,1]
	v_mov_b32_e32 v107, v106
	v_mov_b32_e32 v42, v106
	v_mov_b32_e32 v43, v106
	v_pk_mul_f32 v[40:41], v[40:41], v[42:43]
	v_pk_mul_f32 v[38:39], v[38:39], v[106:107]
	v_pk_mul_f32 v[36:37], v[36:37], v[42:43]
	s_and_b64 vcc, exec, s[4:5]
	v_pk_mul_f32 v[34:35], v[34:35], v[106:107]
	global_store_dwordx2 v[110:111], v[46:47], off offset:128
	s_cbranch_vccnz .LBB0_421
	v_mov_b32_e32 v101, v1
	v_pk_mul_f32 v[50:51], v[36:37], v[230:231]
	v_pk_mul_f32 v[52:53], v[34:35], v[228:229]
	v_pk_mul_f32 v[230:231], v[40:41], v[230:231]
	v_pk_mul_f32 v[228:229], v[38:39], v[228:229]
	v_pk_fma_f32 v[40:41], v[40:41], v[234:235], v[50:51] neg_lo:[0,0,1] neg_hi:[0,0,1]
	v_pk_fma_f32 v[38:39], v[38:39], v[232:233], v[52:53] neg_lo:[0,0,1] neg_hi:[0,0,1]
	v_pk_fma_f32 v[36:37], v[36:37], v[234:235], v[230:231]
	v_pk_fma_f32 v[34:35], v[34:35], v[232:233], v[228:229]
.LBB0_421:
	v_mul_f32_e32 v0, 0x41800000, v38
	v_mul_f32_e32 v38, 0x41800000, v39
	v_med3_f32 v0, v0, s64, v250
	v_med3_f32 v39, v38, s64, v250
	v_cvt_pk_fp8_f32 v38, v0, v39
	v_mul_f32_e32 v0, 0x41800000, v40
	v_mul_f32_e32 v39, 0x41800000, v41
	v_med3_f32 v0, v0, s64, v250
	v_med3_f32 v39, v39, s64, v250
	v_cvt_pk_fp8_f32 v38, v0, v39 op_sel:[0,0,1]
	v_mul_f32_e32 v0, 0x41800000, v34
	v_mul_f32_e32 v34, 0x41800000, v35
	v_med3_f32 v0, v0, s64, v250
	v_med3_f32 v34, v34, s64, v250
	v_cvt_pk_fp8_f32 v39, v0, v34
	v_mul_f32_e32 v0, 0x41800000, v36
	v_mul_f32_e32 v34, 0x41800000, v37
	v_med3_f32 v0, v0, s64, v250
	v_med3_f32 v34, v34, s64, v250
	v_cvt_pk_fp8_f32 v39, v0, v34 op_sel:[0,0,1]
	v_mov_b32_e32 v99, v98
	v_mov_b32_e32 v34, v98
	v_mov_b32_e32 v35, v98
	v_pk_mul_f32 v[32:33], v[32:33], v[34:35]
	v_pk_mul_f32 v[30:31], v[30:31], v[98:99]
	v_pk_mul_f32 v[28:29], v[28:29], v[34:35]
	s_and_b64 vcc, exec, s[4:5]
	v_pk_mul_f32 v[26:27], v[26:27], v[98:99]
	global_store_dwordx2 v[102:103], v[38:39], off offset:128
	s_cbranch_vccnz .LBB0_423
	v_mov_b32_e32 v93, v1
	v_pk_mul_f32 v[42:43], v[28:29], v[238:239]
	v_pk_mul_f32 v[44:45], v[26:27], v[236:237]
	v_pk_mul_f32 v[238:239], v[32:33], v[238:239]
	v_pk_mul_f32 v[236:237], v[30:31], v[236:237]
	v_pk_fma_f32 v[32:33], v[32:33], v[242:243], v[42:43] neg_lo:[0,0,1] neg_hi:[0,0,1]
	v_pk_fma_f32 v[30:31], v[30:31], v[240:241], v[44:45] neg_lo:[0,0,1] neg_hi:[0,0,1]
	v_pk_fma_f32 v[28:29], v[28:29], v[242:243], v[238:239]
	v_pk_fma_f32 v[26:27], v[26:27], v[240:241], v[236:237]
.LBB0_423:
	v_mul_f32_e32 v0, 0x41800000, v30
	v_mul_f32_e32 v30, 0x41800000, v31
	v_med3_f32 v0, v0, s64, v250
	v_med3_f32 v31, v30, s64, v250
	v_cvt_pk_fp8_f32 v30, v0, v31
	v_mul_f32_e32 v0, 0x41800000, v32
	v_mul_f32_e32 v31, 0x41800000, v33
	v_med3_f32 v0, v0, s64, v250
	v_med3_f32 v31, v31, s64, v250
	v_cvt_pk_fp8_f32 v30, v0, v31 op_sel:[0,0,1]
	v_mul_f32_e32 v0, 0x41800000, v26
	v_mul_f32_e32 v26, 0x41800000, v27
	v_med3_f32 v0, v0, s64, v250
	v_med3_f32 v26, v26, s64, v250
	v_cvt_pk_fp8_f32 v31, v0, v26
	v_mul_f32_e32 v0, 0x41800000, v28
	v_mul_f32_e32 v26, 0x41800000, v29
	v_med3_f32 v0, v0, s64, v250
	v_med3_f32 v26, v26, s64, v250
	v_cvt_pk_fp8_f32 v31, v0, v26 op_sel:[0,0,1]
	v_mov_b32_e32 v91, v90
	v_mov_b32_e32 v26, v90
	v_mov_b32_e32 v27, v90
	v_pk_mul_f32 v[24:25], v[24:25], v[26:27]
	v_pk_mul_f32 v[22:23], v[22:23], v[90:91]
	v_pk_mul_f32 v[20:21], v[20:21], v[26:27]
	s_and_b64 vcc, exec, s[4:5]
	v_pk_mul_f32 v[18:19], v[18:19], v[90:91]
	global_store_dwordx2 v[94:95], v[30:31], off offset:128
	s_cbranch_vccnz .LBB0_425
	v_mov_b32_e32 v85, v1
	v_pk_mul_f32 v[34:35], v[20:21], v[190:191]
	v_pk_mul_f32 v[36:37], v[18:19], v[188:189]
	v_pk_mul_f32 v[190:191], v[24:25], v[190:191]
	v_pk_mul_f32 v[188:189], v[22:23], v[188:189]
	v_pk_fma_f32 v[24:25], v[24:25], v[198:199], v[34:35] neg_lo:[0,0,1] neg_hi:[0,0,1]
	v_pk_fma_f32 v[22:23], v[22:23], v[196:197], v[36:37] neg_lo:[0,0,1] neg_hi:[0,0,1]
	v_pk_fma_f32 v[20:21], v[20:21], v[198:199], v[190:191]
	v_pk_fma_f32 v[18:19], v[18:19], v[196:197], v[188:189]
; __device__ __forceinline__ u32x4 pack8(const f32x4 a, const f32x4 b) { u32x4 w; w.x = cvt_pk_bf16(a[0], a[1]); w.y = cvt_pk_bf16(a[2], a[3]); w.z = cvt_pk_bf16(b[0], b[1]); w.w = cvt_pk_bf16(b[2], b[3]); return w; }
; #define PG8_BAR __builtin_amdgcn_s_barrier()
;     __device__ __forceinline__ void operator()(const f32x4 (&acc)[2][2][4][2], const Unit& u, int wr, int wc, int fr, int fq) const {
;     ...
;             for (int ai = 0; ai < 2; ++ai)
; #pragma unroll
;                 for (int m = 0; m < 4; ++m) {
;                     const int row = row0 + ai * HALF + m * 16; const float r = t[ai * 64 + m * 16 + fr] * qscale;
;                     f32x4 v0 = acc[ai][bj][m][0] * r, v1 = acc[ai][bj][m][1] * r;
;                     if (rope) rope8(v0, v1, rcos, rsin, row & (SEQ_ - 1), fq);
;                     if (!f8qk) *(u32x4*)(q + (size_t)row * 768 + colg + 8 * fq) = pack8(v0, v1);
;                     if (f8qk) { u32x2 w8; w8.x = pack4_fp8_x16(v0); w8.y = pack4_fp8_x16(v1); *(u32x2*)(ws + WS_Q8 + (size_t)row * 768 + colg + 8 * fq) = w8; }
;                 }
; template <class Epi, class Sched, bool ALIGN_EPI = false, bool SP2 = false, bool F8 = false>
; __device__ __forceinline__ void gemm_phase(PG8_LAS unsigned char* lds, const Gemm g, const Sched& S, const Epi& E, const int tidb  ) {
;     ...
;         if constexpr (ALIGN_EPI) { if (wr == 0) PG8_BAR; }
;         if constexpr (F8) asm volatile("s_nop 15\n\ts_nop 15" ::: "memory");
;         if constexpr (!Epi::AFTER_DRAIN) { E(acc, cur, wr, wc, fr, fq); S.done(cur); }
;         if (!has_next) break;
; #pragma unroll
;         for (int a = 0; a < 2; ++a)
; #pragma unroll
;             for (int b = 0; b < 2; ++b)
; #pragma unroll
;                 for (int m = 0; m < 4; ++m)
; #pragma unroll
;                     for (int n = 0; n < 2; ++n) acc[a][b][m][n] = (f32x4){0.f, 0.f, 0.f, 0.f};
;         cur = nxt; cA = nA; cB = nB; ++ui;
;         if constexpr (ALIGN_EPI) { if (wr == 1) PG8_BAR; }
.LBB0_425:
	v_mul_f32_e32 v0, 0x41800000, v22
	v_mul_f32_e32 v22, 0x41800000, v23
	v_med3_f32 v0, v0, s64, v250
	v_med3_f32 v23, v22, s64, v250
	v_cvt_pk_fp8_f32 v22, v0, v23
	v_mul_f32_e32 v0, 0x41800000, v24
	v_mul_f32_e32 v23, 0x41800000, v25
	v_med3_f32 v0, v0, s64, v250
	v_med3_f32 v23, v23, s64, v250
	v_cvt_pk_fp8_f32 v22, v0, v23 op_sel:[0,0,1]
	v_mul_f32_e32 v0, 0x41800000, v18
	v_mul_f32_e32 v18, 0x41800000, v19
	v_med3_f32 v0, v0, s64, v250
	v_med3_f32 v18, v18, s64, v250
	v_cvt_pk_fp8_f32 v23, v0, v18
	v_mul_f32_e32 v0, 0x41800000, v20
	v_mul_f32_e32 v18, 0x41800000, v21
	v_med3_f32 v0, v0, s64, v250
	v_med3_f32 v18, v18, s64, v250
	v_cvt_pk_fp8_f32 v23, v0, v18 op_sel:[0,0,1]
	v_mov_b32_e32 v83, v82
	v_mov_b32_e32 v18, v82
	v_mov_b32_e32 v19, v82
	v_pk_mul_f32 v[16:17], v[16:17], v[18:19]
	v_pk_mul_f32 v[14:15], v[14:15], v[82:83]
	v_pk_mul_f32 v[12:13], v[12:13], v[18:19]
	s_and_b64 vcc, exec, s[4:5]
	v_pk_mul_f32 v[10:11], v[10:11], v[82:83]
	global_store_dwordx2 v[86:87], v[22:23], off offset:128
	s_cbranch_vccnz .LBB0_427
	v_mov_b32_e32 v77, v1
	s_waitcnt vmcnt(6)
	v_pk_mul_f32 v[26:27], v[12:13], v[206:207]
	v_pk_mul_f32 v[28:29], v[10:11], v[204:205]
	v_pk_mul_f32 v[206:207], v[16:17], v[206:207]
	v_pk_mul_f32 v[204:205], v[14:15], v[204:205]
	v_pk_fma_f32 v[16:17], v[16:17], v[210:211], v[26:27] neg_lo:[0,0,1] neg_hi:[0,0,1]
	v_pk_fma_f32 v[14:15], v[14:15], v[208:209], v[28:29] neg_lo:[0,0,1] neg_hi:[0,0,1]
	v_pk_fma_f32 v[12:13], v[12:13], v[210:211], v[206:207]
	v_pk_fma_f32 v[10:11], v[10:11], v[208:209], v[204:205]
.LBB0_427:
	v_mul_f32_e32 v0, 0x41800000, v14
	v_mul_f32_e32 v14, 0x41800000, v15
	v_med3_f32 v0, v0, s64, v250
	v_med3_f32 v15, v14, s64, v250
	v_cvt_pk_fp8_f32 v14, v0, v15
	v_mul_f32_e32 v0, 0x41800000, v16
	v_mul_f32_e32 v15, 0x41800000, v17
	v_med3_f32 v0, v0, s64, v250
	v_med3_f32 v15, v15, s64, v250
	v_cvt_pk_fp8_f32 v14, v0, v15 op_sel:[0,0,1]
	v_mul_f32_e32 v0, 0x41800000, v10
	v_mul_f32_e32 v10, 0x41800000, v11
	v_med3_f32 v0, v0, s64, v250
	v_med3_f32 v10, v10, s64, v250
	v_cvt_pk_fp8_f32 v15, v0, v10
	v_mul_f32_e32 v0, 0x41800000, v12
	v_mul_f32_e32 v10, 0x41800000, v13
	v_med3_f32 v0, v0, s64, v250
	v_med3_f32 v10, v10, s64, v250
	v_cvt_pk_fp8_f32 v15, v0, v10 op_sel:[0,0,1]
	v_mov_b32_e32 v75, v74
	v_mov_b32_e32 v10, v74
	v_mov_b32_e32 v11, v74
	v_pk_mul_f32 v[8:9], v[8:9], v[10:11]
	v_pk_mul_f32 v[6:7], v[6:7], v[74:75]
	v_pk_mul_f32 v[4:5], v[4:5], v[10:11]
	s_and_b64 vcc, exec, s[4:5]
	v_pk_mul_f32 v[2:3], v[2:3], v[74:75]
	global_store_dwordx2 v[78:79], v[14:15], off offset:128
	s_cbranch_vccnz .LBB0_429
	v_mov_b32_e32 v67, v1
	s_waitcnt vmcnt(4)
	v_pk_mul_f32 v[18:19], v[4:5], v[214:215]
	v_pk_mul_f32 v[20:21], v[2:3], v[212:213]
	v_pk_mul_f32 v[214:215], v[8:9], v[214:215]
	v_pk_mul_f32 v[212:213], v[6:7], v[212:213]
	v_pk_fma_f32 v[8:9], v[8:9], v[218:219], v[18:19] neg_lo:[0,0,1] neg_hi:[0,0,1]
	v_pk_fma_f32 v[6:7], v[6:7], v[216:217], v[20:21] neg_lo:[0,0,1] neg_hi:[0,0,1]
	v_pk_fma_f32 v[4:5], v[4:5], v[218:219], v[214:215]
	v_pk_fma_f32 v[2:3], v[2:3], v[216:217], v[212:213]
.LBB0_429:
	v_mul_f32_e32 v0, 0x41800000, v6
	v_mul_f32_e32 v6, 0x41800000, v7
	v_med3_f32 v0, v0, s64, v250
	v_med3_f32 v7, v6, s64, v250
	v_cvt_pk_fp8_f32 v6, v0, v7
	v_mul_f32_e32 v0, 0x41800000, v8
	v_mul_f32_e32 v7, 0x41800000, v9
	v_med3_f32 v0, v0, s64, v250
	v_med3_f32 v7, v7, s64, v250
	v_cvt_pk_fp8_f32 v6, v0, v7 op_sel:[0,0,1]
	v_mul_f32_e32 v0, 0x41800000, v2
	v_mul_f32_e32 v2, 0x41800000, v3
	v_med3_f32 v0, v0, s64, v250
	v_med3_f32 v2, v2, s64, v250
	v_cvt_pk_fp8_f32 v7, v0, v2
	v_mul_f32_e32 v0, 0x41800000, v4
	v_mul_f32_e32 v2, 0x41800000, v5
	v_med3_f32 v0, v0, s64, v250
	v_med3_f32 v2, v2, s64, v250
	v_cvt_pk_fp8_f32 v7, v0, v2 op_sel:[0,0,1]
	s_and_b64 vcc, exec, s[2:3]
	s_mov_b64 s[2:3], -1
	global_store_dwordx2 v[68:69], v[6:7], off offset:128
	s_cbranch_vccnz .LBB0_384
	s_andn2_b64 vcc, exec, s[14:15]
	s_cbranch_vccnz .LBB0_383
	s_barrier
	s_branch .LBB0_383

; #define LDS_WAIT() asm volatile("s_waitcnt lgkmcnt(0)" ::: "memory")
; __device__ __forceinline__ void tr_item(const TrJob& J, int item, LAS float* scr, int lane) {
;     const int nblk = J.N / 32, kb = item / nblk, nb = item % nblk, k0 = 64 * kb, n0 = 32 * nb;
;     float wv[32];
; #pragma unroll
;     for (int i = 0; i < 32; ++i) wv[i] = __builtin_nontemporal_load(J.W + (size_t)(k0 + 2 * i + (lane >> 5)) * J.N + n0 + (lane & 31));
; #pragma unroll
;     for (int i = 0; i < 32; ++i) scr[(2 * i + (lane >> 5)) * 33 + (lane & 31)] = wv[i];
;     LDS_WAIT(); asm volatile("" ::: "memory");
; __device__ __forceinline__ void moe_job(const KP* kp, unsigned char* ws, int l, int g, TrJob& J, int& it) {
;     const int mj = l >> 1, j = g / IT_FF; it = g % IT_FF;
;     unsigned char* WM13 = ws + WS_WM; unsigned char* WM2 = WM13 + (size_t)NEXP * 2 * FF_ * D_ * 2; const int eb = f8_layer(l) ? 1 : 2;
;     if (j < 2 * NEXP) { const int e = j >> 1;
;         if ((j & 1) == 0) J = TrJob{kp->in[14] + (size_t)(mj * NEXP + e) * D_ * FF_, D_, FF_, (bf16*)(WM13 + (size_t)e * 2 * FF_ * D_ * eb), kp->in[9] + l * D_, TM_W1, (int)f8_layer(l)};
;         else J = TrJob{kp->in[15] + (size_t)(mj * NEXP + e) * D_ * FF_, D_, FF_, (bf16*)(WM13 + (size_t)e * 2 * FF_ * D_ * eb), kp->in[9] + l * D_, TM_W3, (int)f8_layer(l)};
;     } else { const int e = j - 2 * NEXP; J = TrJob{kp->in[16] + (size_t)(mj * NEXP + e) * FF_ * D_, FF_, D_, (bf16*)(WM2 + (size_t)e * FF_ * D_ * eb), nullptr, TM_ID, (int)f8_layer(l)}; }
.LBB0_440:
	s_mul_hi_i32 s4, s13, 0x92492493
	s_add_i32 s4, s4, s13
	s_lshr_b32 s5, s4, 31
	s_ashr_i32 s4, s4, 10
	s_add_i32 s4, s4, s5
	s_mul_i32 s5, s4, 0xfffff900
	s_add_i32 s10, s13, s5
	s_ashr_i32 s5, s4, 1
	s_and_b32 s17, s4, 1
	s_add_i32 s8, s5, s1
	s_mul_hi_i32 s9, s5, 0x700000
	s_mul_i32 s5, s5, 0x700000
	s_add_u32 s4, s14, s5
	s_addc_u32 s5, s15, s9
	s_cmp_eq_u32 s17, 0
	s_mul_hi_i32 s11, s8, 0xe00000
	s_mul_i32 s18, s8, 0xe00000
	s_cselect_b32 s8, s22, 0x78
	s_add_u32 s8, s6, s8
	s_addc_u32 s9, s7, 0
	s_load_dwordx2 s[8:9], s[8:9], 0x0
	s_waitcnt lgkmcnt(0)
	s_add_u32 s20, s8, s18
	s_mul_i32 s8, s10, 0x4925
	s_addc_u32 s21, s9, s11
	s_lshr_b32 s9, s8, 31
	s_ashr_i32 s8, s8, 21
	s_add_i32 s8, s8, s9
	s_sext_i32_i16 s11, s8
	s_mulk_i32 s8, 0x70
	s_sub_i32 s8, s10, s8
	s_sext_i32_i16 s9, s8
	s_lshl_b32 s10, s9, 5
	s_lshl_b32 s8, s11, 6
	s_ashr_i32 s11, s10, 31
	s_lshl_b64 s[18:19], s[10:11], 2
	s_add_u32 s18, s20, s18
	s_addc_u32 s19, s21, s19
	v_add_u32_e32 v40, s8, v14
	v_lshl_add_u64 v[36:37], s[18:19], 0, v[0:1]
	v_mad_i64_i32 v[2:3], s[18:19], v40, s33, v[36:37]
	global_load_dword v41, v[2:3], off nt
	v_add_u32_e32 v2, 2, v40
	v_mad_i64_i32 v[2:3], s[18:19], v2, s33, v[36:37]
	global_load_dword v42, v[2:3], off nt
	v_add_u32_e32 v2, 4, v40
	v_mad_i64_i32 v[2:3], s[18:19], v2, s33, v[36:37]
	global_load_dword v43, v[2:3], off nt
	v_add_u32_e32 v2, 6, v40
	v_mad_i64_i32 v[2:3], s[18:19], v2, s33, v[36:37]
	global_load_dword v44, v[2:3], off nt
	v_add_u32_e32 v2, 8, v40
	v_mad_i64_i32 v[2:3], s[18:19], v2, s33, v[36:37]
	global_load_dword v2, v[2:3], off nt
	v_add_u32_e32 v3, 10, v40
	v_mad_i64_i32 v[4:5], s[18:19], v3, s33, v[36:37]
	v_add_u32_e32 v3, 12, v40
	v_mad_i64_i32 v[6:7], s[18:19], v3, s33, v[36:37]
	v_add_u32_e32 v3, 14, v40
	global_load_dword v5, v[4:5], off nt
	v_add_u32_e32 v8, 34, v40
	global_load_dword v9, v[6:7], off nt
	v_mad_i64_i32 v[6:7], s[18:19], v3, s33, v[36:37]
	v_add_u32_e32 v3, 16, v40
	global_load_dword v23, v[6:7], off nt
	v_mad_i64_i32 v[6:7], s[18:19], v3, s33, v[36:37]
	v_add_u32_e32 v4, 18, v40
	global_load_dword v3, v[6:7], off nt
	v_mad_i64_i32 v[6:7], s[18:19], v4, s33, v[36:37]
	v_add_u32_e32 v4, 20, v40
	v_mad_i64_i32 v[12:13], s[18:19], v4, s33, v[36:37]
	v_add_u32_e32 v4, 22, v40
	global_load_dword v7, v[6:7], off nt
	v_add_u32_e32 v28, 58, v40
	global_load_dword v18, v[12:13], off nt
	v_mad_i64_i32 v[12:13], s[18:19], v4, s33, v[36:37]
	v_add_u32_e32 v4, 24, v40
	global_load_dword v26, v[12:13], off nt
	v_mad_i64_i32 v[12:13], s[18:19], v4, s33, v[36:37]
	v_add_u32_e32 v6, 26, v40
	global_load_dword v4, v[12:13], off nt
	v_mad_i64_i32 v[12:13], s[18:19], v6, s33, v[36:37]
	v_add_u32_e32 v6, 28, v40
	v_mad_i64_i32 v[20:21], s[18:19], v6, s33, v[36:37]
	v_add_u32_e32 v6, 30, v40
	v_mad_i64_i32 v[24:25], s[18:19], v6, s33, v[36:37]
	v_add_u32_e32 v6, 32, v40
	global_load_dword v12, v[12:13], off nt
	s_lshl_b32 s9, s9, 6
	global_load_dword v21, v[20:21], off nt
	s_and_b32 s9, s9, 0xffffff00
	global_load_dword v29, v[24:25], off nt
	v_mad_i64_i32 v[24:25], s[18:19], v6, s33, v[36:37]
	global_load_dword v6, v[24:25], off nt
	v_mad_i64_i32 v[24:25], s[18:19], v8, s33, v[36:37]
	v_add_u32_e32 v8, 36, v40
	global_load_dword v19, v[24:25], off nt
	v_mad_i64_i32 v[24:25], s[18:19], v8, s33, v[36:37]
	v_add_u32_e32 v8, 38, v40
	v_mad_i64_i32 v[30:31], s[18:19], v8, s33, v[36:37]
	v_add_u32_e32 v8, 40, v40
	v_mad_i64_i32 v[32:33], s[18:19], v8, s33, v[36:37]
	v_add_u32_e32 v13, 42, v40
	global_load_dword v24, v[24:25], off nt
	v_add_u32_e32 v20, 50, v40
	global_load_dword v31, v[30:31], off nt
	s_and_b32 s10, s10, 0x60
	global_load_dword v8, v[32:33], off nt
	v_mad_i64_i32 v[32:33], s[18:19], v13, s33, v[36:37]
	v_add_u32_e32 v13, 44, v40
	global_load_dword v22, v[32:33], off nt
	v_mad_i64_i32 v[32:33], s[18:19], v13, s33, v[36:37]
	v_add_u32_e32 v13, 46, v40
	global_load_dword v27, v[32:33], off nt
	v_mad_i64_i32 v[32:33], s[18:19], v13, s33, v[36:37]
	v_add_u32_e32 v13, 48, v40
	v_mad_i64_i32 v[34:35], s[18:19], v13, s33, v[36:37]
	global_load_dword v33, v[32:33], off nt
	s_or_b32 s10, s9, s10
	global_load_dword v13, v[34:35], off nt
	v_mad_i64_i32 v[34:35], s[18:19], v20, s33, v[36:37]
	v_add_u32_e32 v20, 52, v40
	global_load_dword v25, v[34:35], off nt
	v_mad_i64_i32 v[34:35], s[18:19], v20, s33, v[36:37]
	v_add_u32_e32 v20, 54, v40
	global_load_dword v30, v[34:35], off nt
	v_mad_i64_i32 v[34:35], s[18:19], v20, s33, v[36:37]
	v_add_u32_e32 v20, 56, v40
	v_mad_i64_i32 v[38:39], s[18:19], v20, s33, v[36:37]
	global_load_dword v34, v[34:35], off nt
	v_add_u32_e32 v32, 60, v40
	global_load_dword v20, v[38:39], off nt
	v_mad_i64_i32 v[38:39], s[18:19], v28, s33, v[36:37]
	v_add_u32_e32 v35, 62, v40
	global_load_dword v28, v[38:39], off nt
	v_mad_i64_i32 v[38:39], s[18:19], v32, s33, v[36:37]
	v_mad_i64_i32 v[36:37], s[18:19], v35, s33, v[36:37]
	global_load_dword v32, v[38:39], off nt
	global_load_dword v35, v[36:37], off nt
	v_add_u32_e32 v36, 0x400, v17
	s_waitcnt vmcnt(0)
	ds_write2_b32 v17, v41, v42 offset1:66
	s_waitcnt vmcnt(28)
	ds_write2_b32 v17, v43, v44 offset0:132 offset1:198
	s_waitcnt vmcnt(26)
	ds_write2_b32 v36, v2, v5 offset0:8 offset1:74
	s_waitcnt vmcnt(24)
	ds_write2_b32 v36, v9, v23 offset0:140 offset1:206
	v_add_u32_e32 v2, 0x800, v17
	s_waitcnt vmcnt(22)
	ds_write2_b32 v2, v3, v7 offset0:16 offset1:82
	s_waitcnt vmcnt(20)
	ds_write2_b32 v2, v18, v26 offset0:148 offset1:214
	v_add_u32_e32 v2, 0xc00, v17
	s_waitcnt vmcnt(18)
	ds_write2_b32 v2, v4, v12 offset0:24 offset1:90
	s_waitcnt vmcnt(16)
	ds_write2_b32 v2, v21, v29 offset0:156 offset1:222
	v_add_u32_e32 v2, 0x1000, v17
	s_waitcnt vmcnt(14)
; #define GAS __attribute__((address_space(1)))
; #define LAS __attribute__((address_space(3)))
; #define LDS_WAIT() asm volatile("s_waitcnt lgkmcnt(0)" ::: "memory")
; __device__ __forceinline__ void tr_item(const TrJob& J, int item, LAS float* scr, int lane) {
;     ...
;     for (int i = 0; i < 32; ++i) wv[i] = __builtin_nontemporal_load(J.W + (size_t)(k0 + 2 * i + (lane >> 5)) * J.N + n0 + (lane & 31));
; #pragma unroll
;     for (int i = 0; i < 32; ++i) scr[(2 * i + (lane >> 5)) * 33 + (lane & 31)] = wv[i];
;     LDS_WAIT(); asm volatile("" ::: "memory");
;     const int c = lane & 7; float g[8];
; #pragma unroll
;     for (int e = 0; e < 8; ++e) g[e] = J.gain ? J.gain[k0 + 8 * c + e] : 1.f;
; #pragma unroll
;     for (int j = 0; j < 4; ++j) { const int n = (lane >> 3) + 8 * j; const LAS float* s = scr + (8 * c) * 33 + n;
;         if (J.f8) { int w0 = 0, w1 = 0;
;             w0 = __builtin_amdgcn_cvt_pk_fp8_f32(s[0 * 33] * g[0] * 64.0f, s[1 * 33] * g[1] * 64.0f, w0, false); w0 = __builtin_amdgcn_cvt_pk_fp8_f32(s[2 * 33] * g[2] * 64.0f, s[3 * 33] * g[3] * 64.0f, w0, true);
;             w1 = __builtin_amdgcn_cvt_pk_fp8_f32(s[4 * 33] * g[4] * 64.0f, s[5 * 33] * g[5] * 64.0f, w1, false); w1 = __builtin_amdgcn_cvt_pk_fp8_f32(s[6 * 33] * g[6] * 64.0f, s[7 * 33] * g[7] * 64.0f, w1, true);
;             v2u o; o.x = (unsigned)w0; o.y = (unsigned)w1; *(GAS v2u*)((unsigned char*)J.dst + (size_t)tr_dest_row(J.mode, n0, n) * J.K + k0 + 8 * c) = o; }
; __device__ __forceinline__ void moe_fill(const KP* kp, unsigned char* ws, int l, int a, int b, int nwg, int G, int c, int wave, LAS unsigned char* lds, int lane) {
;     ...
;     if (pidx >= 0) { LAS float* scr = (LAS float*)(lds + wave * 16384);
;         for (int g = a + pidx * NWAVES + wave; g < b; g += P * NWAVES) { TrJob J; int it; moe_job(kp, ws, l, g, J, it); tr_item(J, it, scr, lane); } }
	ds_write2_b32 v2, v6, v19 offset0:32 offset1:98
	s_waitcnt vmcnt(12)
	ds_write2_b32 v2, v24, v31 offset0:164 offset1:230
	v_add_u32_e32 v2, 0x1400, v17
	s_waitcnt vmcnt(10)
	ds_write2_b32 v2, v8, v22 offset0:40 offset1:106
	s_waitcnt vmcnt(8)
	ds_write2_b32 v2, v27, v33 offset0:172 offset1:238
	v_add_u32_e32 v2, 0x1800, v17
	s_waitcnt vmcnt(6)
	ds_write2_b32 v2, v13, v25 offset0:48 offset1:114
	s_waitcnt vmcnt(4)
	ds_write2_b32 v2, v30, v34 offset0:180 offset1:246
	v_add_u32_e32 v2, 0x1c00, v17
	s_waitcnt vmcnt(2)
	ds_write2_b32 v2, v20, v28 offset0:56 offset1:122
	s_waitcnt vmcnt(0)
	ds_write2_b32 v2, v32, v35 offset0:188 offset1:254
	v_or_b32_e32 v2, s8, v10
	s_waitcnt lgkmcnt(0)
	v_ashrrev_i32_e32 v3, 31, v2
	v_lshl_add_u64 v[6:7], v[2:3], 2, s[2:3]
	global_load_dwordx4 v[2:5], v[6:7], off offset:16
	s_nop 0
	global_load_dwordx4 v[6:9], v[6:7], off
	ds_read2_b32 v[18:19], v16 offset1:8
	ds_read2_b32 v[20:21], v16 offset0:33 offset1:41
	ds_read2_b32 v[24:25], v16 offset0:66 offset1:74
	ds_read2_b32 v[26:27], v16 offset0:99 offset1:107
	ds_read2_b32 v[28:29], v16 offset0:132 offset1:140
	ds_read2_b32 v[30:31], v16 offset0:165 offset1:173
	ds_read2_b32 v[32:33], v16 offset0:198 offset1:206
	ds_read2_b32 v[34:35], v16 offset0:231 offset1:239
	s_lshl_b32 s11, s17, 7
	s_or_b32 s10, s10, s11
	s_ashr_i32 s9, s8, 31
	s_add_i32 s13, s13, s16
	s_cmp_lt_i32 s13, s12
	s_waitcnt vmcnt(0) lgkmcnt(7)
	v_mul_f32_e32 v12, v6, v18
	s_waitcnt lgkmcnt(6)
	v_mul_f32_e32 v13, v7, v20
	v_mul_f32_e32 v12, 0x42800000, v12
	v_mul_f32_e32 v13, 0x42800000, v13
	v_cvt_pk_fp8_f32 v22, v12, v13
	s_waitcnt lgkmcnt(5)
	v_mul_f32_e32 v12, v8, v24
	s_waitcnt lgkmcnt(4)
	v_mul_f32_e32 v13, v9, v26
	v_mul_f32_e32 v12, 0x42800000, v12
	v_mul_f32_e32 v13, 0x42800000, v13
	v_cvt_pk_fp8_f32 v22, v12, v13 op_sel:[0,0,1]
	s_waitcnt lgkmcnt(3)
	v_mul_f32_e32 v12, v2, v28
	s_waitcnt lgkmcnt(2)
	v_mul_f32_e32 v13, v3, v30
	v_mul_f32_e32 v12, 0x42800000, v12
	v_mul_f32_e32 v13, 0x42800000, v13
	v_cvt_pk_fp8_f32 v23, v12, v13
	s_waitcnt lgkmcnt(1)
	v_mul_f32_e32 v12, v4, v32
	s_waitcnt lgkmcnt(0)
	v_mul_f32_e32 v13, v5, v34
	v_mul_f32_e32 v12, 0x42800000, v12
	v_mul_f32_e32 v13, 0x42800000, v13
	v_cvt_pk_fp8_f32 v23, v12, v13 op_sel:[0,0,1]
	v_add_u32_e32 v12, s10, v15
	v_ashrrev_i32_e32 v13, 31, v12
	v_lshlrev_b64 v[36:37], 10, v[12:13]
	v_mul_f32_e32 v13, v6, v19
	v_mul_f32_e32 v18, v7, v21
	v_mul_f32_e32 v13, 0x42800000, v13
	v_mul_f32_e32 v19, 0x42800000, v18
	v_cvt_pk_fp8_f32 v18, v13, v19
	v_mul_f32_e32 v13, v8, v25
	v_mul_f32_e32 v19, v9, v27
	v_mul_f32_e32 v13, 0x42800000, v13
	v_mul_f32_e32 v19, 0x42800000, v19
	v_cvt_pk_fp8_f32 v18, v13, v19 op_sel:[0,0,1]
	v_mul_f32_e32 v13, v2, v29
	v_mul_f32_e32 v19, v3, v31
	v_mul_f32_e32 v13, 0x42800000, v13
	v_mul_f32_e32 v20, 0x42800000, v19
	v_cvt_pk_fp8_f32 v19, v13, v20
	v_mul_f32_e32 v13, v4, v33
	v_mul_f32_e32 v20, v5, v35
	v_mul_f32_e32 v13, 0x42800000, v13
	v_mul_f32_e32 v20, 0x42800000, v20
	v_cvt_pk_fp8_f32 v19, v13, v20 op_sel:[0,0,1]
	v_add_u32_e32 v20, 8, v12
	v_ashrrev_i32_e32 v21, 31, v20
	v_lshlrev_b64 v[20:21], 10, v[20:21]
	v_lshl_add_u64 v[20:21], s[4:5], 0, v[20:21]
	v_lshl_add_u64 v[20:21], v[20:21], 0, s[8:9]
	v_lshl_add_u64 v[20:21], v[20:21], 0, v[10:11]
	global_store_dwordx2 v[20:21], v[18:19], off
	ds_read2_b32 v[18:19], v16 offset0:16 offset1:24
	ds_read2_b32 v[20:21], v16 offset0:49 offset1:57
	v_lshl_add_u64 v[36:37], s[4:5], 0, v[36:37]
	v_lshl_add_u64 v[36:37], v[36:37], 0, s[8:9]
	ds_read2_b32 v[24:25], v16 offset0:82 offset1:90
	ds_read2_b32 v[26:27], v16 offset0:115 offset1:123
	v_lshl_add_u64 v[36:37], v[36:37], 0, v[10:11]
	s_waitcnt lgkmcnt(3)
	v_mul_f32_e32 v13, v6, v18
	s_waitcnt lgkmcnt(2)
	v_mul_f32_e32 v18, v7, v20
	global_store_dwordx2 v[36:37], v[22:23], off
	v_mul_f32_e32 v13, 0x42800000, v13
	v_mul_f32_e32 v18, 0x42800000, v18
	ds_read2_b32 v[28:29], v16 offset0:148 offset1:156
	ds_read2_b32 v[30:31], v16 offset0:181 offset1:189
	v_cvt_pk_fp8_f32 v22, v13, v18
	s_waitcnt lgkmcnt(3)
	v_mul_f32_e32 v13, v8, v24
	s_waitcnt lgkmcnt(2)
	v_mul_f32_e32 v18, v9, v26
	v_mul_f32_e32 v13, 0x42800000, v13
	v_mul_f32_e32 v18, 0x42800000, v18
	ds_read2_b32 v[32:33], v16 offset0:214 offset1:222
	ds_read2_b32 v[34:35], v16 offset0:247 offset1:255
	v_cvt_pk_fp8_f32 v22, v13, v18 op_sel:[0,0,1]
	s_waitcnt lgkmcnt(3)
	v_mul_f32_e32 v13, v2, v28
	s_waitcnt lgkmcnt(2)
	v_mul_f32_e32 v18, v3, v30
	v_mul_f32_e32 v13, 0x42800000, v13
	v_mul_f32_e32 v18, 0x42800000, v18
	v_cvt_pk_fp8_f32 v23, v13, v18
	s_waitcnt lgkmcnt(1)
	v_mul_f32_e32 v13, v4, v32
	s_waitcnt lgkmcnt(0)
	v_mul_f32_e32 v18, v5, v34
	v_mul_f32_e32 v13, 0x42800000, v13
	v_mul_f32_e32 v18, 0x42800000, v18
	v_mul_f32_e32 v6, v6, v19
	v_cvt_pk_fp8_f32 v23, v13, v18 op_sel:[0,0,1]
	v_mul_f32_e32 v13, 0x42800000, v6
	v_mul_f32_e32 v6, v7, v21
	v_mul_f32_e32 v7, 0x42800000, v6
	v_cvt_pk_fp8_f32 v6, v13, v7
	v_mul_f32_e32 v7, v8, v25
	v_mul_f32_e32 v8, v9, v27
	v_mul_f32_e32 v7, 0x42800000, v7
	v_mul_f32_e32 v8, 0x42800000, v8
	v_mul_f32_e32 v2, v2, v29
	v_mul_f32_e32 v3, v3, v31
	v_cvt_pk_fp8_f32 v6, v7, v8 op_sel:[0,0,1]
	v_mul_f32_e32 v2, 0x42800000, v2
	v_mul_f32_e32 v3, 0x42800000, v3
	v_cvt_pk_fp8_f32 v7, v2, v3
	v_mul_f32_e32 v2, v4, v33
	v_mul_f32_e32 v3, v5, v35
	v_mul_f32_e32 v2, 0x42800000, v2
	v_mul_f32_e32 v3, 0x42800000, v3
	v_add_u32_e32 v36, 16, v12
	v_cvt_pk_fp8_f32 v7, v2, v3 op_sel:[0,0,1]
	v_add_u32_e32 v2, 24, v12
	v_ashrrev_i32_e32 v37, 31, v36
	v_ashrrev_i32_e32 v3, 31, v2
	v_lshlrev_b64 v[36:37], 10, v[36:37]
	v_lshlrev_b64 v[2:3], 10, v[2:3]
	v_lshl_add_u64 v[36:37], s[4:5], 0, v[36:37]
	v_lshl_add_u64 v[2:3], s[4:5], 0, v[2:3]
	v_lshl_add_u64 v[36:37], v[36:37], 0, s[8:9]
	v_lshl_add_u64 v[2:3], v[2:3], 0, s[8:9]
	v_lshl_add_u64 v[36:37], v[36:37], 0, v[10:11]
	v_lshl_add_u64 v[2:3], v[2:3], 0, v[10:11]
	global_store_dwordx2 v[36:37], v[22:23], off
	global_store_dwordx2 v[2:3], v[6:7], off
	s_waitcnt lgkmcnt(0)
	s_cbranch_scc1 .LBB0_440

; __device__ __forceinline__ u32x4 pack8(const f32x4 a, const f32x4 b) { u32x4 w; w.x = cvt_pk_bf16(a[0], a[1]); w.y = cvt_pk_bf16(a[2], a[3]); w.z = cvt_pk_bf16(b[0], b[1]); w.w = cvt_pk_bf16(b[2], b[3]); return w; }
;     __device__ __forceinline__ void operator()(const f32x4 (&acc)[2][2][4][2], const Unit& u, int wr, int wc, int fr_in, int fq_in) const {
;     ...
;         for (int bj = 0; bj < 2; ++bj) {
;             const int colg = u.pn * BM + bj * HALF + wc * 32; bf16_t* dst = colg < 512 ? kn + colg : v + (colg - 512);
; #pragma unroll
;             for (int ai = 0; ai < 2; ++ai)
; #pragma unroll
;                 for (int m = 0; m < 4; ++m) {
;                     const int row = row0 + ai * HALF + m * 16; const float r = t[ai * 64 + m * 16 + fr];
;                     if (!(f8qk && colg < 512) && !(f8pv && colg >= 512)) *(u32x4*)(dst + (size_t)row * 512 + 8 * fq) = pack8(acc[ai][bj][m][0] * r, acc[ai][bj][m][1] * r);
;                     if (f8pv && colg >= 512) {
;                         const int c0_ = colg - 512 + 8 * fq, bb_ = row >> 13, pos_ = row & (SEQ_ - 1), key_ = pos_ & 63, k32_ = key_ & 31;
;                         unsigned char* p_ = ws + WS_V8T + ((((size_t)(bb_ * 8 + (c0_ >> 6)) * 128 + (pos_ >> 6)) * 64 + (c0_ & 63)) * 64) + 32 * ((k32_ >> 2) & 1) + 16 * (key_ >> 5) + (k32_ & 3) + 4 * (k32_ >> 3);
;                         const unsigned w0_ = pack4_fp8_x8(acc[ai][bj][m][0] * r), w1_ = pack4_fp8_x8(acc[ai][bj][m][1] * r);
;                         const int qi_ = fr & 3; unsigned char* pb_ = p_ - qi_;
;                         *(unsigned*)(pb_ + qi_ * 64) = quad_tr4(w0_, qi_); *(unsigned*)(pb_ + (4 + qi_) * 64) = quad_tr4(w1_, qi_);
;                     }
;                     if (f8qk && colg < 512) { u32x2 w8; w8.x = pack4_fp8_x8(acc[ai][bj][m][0] * r); w8.y = pack4_fp8_x8(acc[ai][bj][m][1] * r); *(u32x2*)(ws + WS_KN8 + (size_t)row * 512 + colg + 8 * fq) = w8; }
.LBB0_470:
	s_cmpk_lt_i32 s28, 0x200
	s_cselect_b64 s[30:31], -1, 0
	s_ashr_i32 s29, s28, 31
	v_ashrrev_i32_e32 v143, 31, v142
	s_cmpk_gt_i32 s28, 0x1ff
	v_ashrrev_i32_e32 v151, 31, v150
	s_cbranch_scc1 .LBB0_472
	s_waitcnt lgkmcnt(0)
	v_pk_mul_f32 v[126:127], v[126:127], v[152:153] op_sel_hi:[1,0]
	v_pk_mul_f32 v[128:129], v[128:129], v[152:153] op_sel_hi:[1,0]
	v_mul_f32_e32 v126, 0x41000000, v126
	v_med3_f32 v155, v126, s64, v250
	v_mul_f32_e32 v126, 0x41000000, v127
	v_med3_f32 v127, v126, s64, v250
	v_cvt_pk_fp8_f32 v126, v155, v127
	v_mul_f32_e32 v127, 0x41000000, v128
	v_mul_f32_e32 v128, 0x41000000, v129
	v_pk_mul_f32 v[122:123], v[122:123], v[152:153] op_sel_hi:[1,0]
	v_med3_f32 v127, v127, s64, v250
	v_med3_f32 v128, v128, s64, v250
	v_mul_f32_e32 v122, 0x41000000, v122
	v_mul_f32_e32 v123, 0x41000000, v123
	v_cvt_pk_fp8_f32 v126, v127, v128 op_sel:[0,0,1]
	v_med3_f32 v122, v122, s64, v250
	v_med3_f32 v123, v123, s64, v250
	v_cvt_pk_fp8_f32 v127, v122, v123
	v_pk_mul_f32 v[124:125], v[124:125], v[152:153] op_sel_hi:[1,0]
	s_nop 0
	v_mul_f32_e32 v122, 0x41000000, v124
	v_mul_f32_e32 v123, 0x41000000, v125
	v_med3_f32 v122, v122, s64, v250
	v_med3_f32 v123, v123, s64, v250
	v_cvt_pk_fp8_f32 v127, v122, v123 op_sel:[0,0,1]
	v_lshlrev_b64 v[122:123], 9, v[150:151]
	v_lshl_add_u64 v[122:123], s[22:23], 0, v[122:123]
	v_lshl_add_u64 v[122:123], v[122:123], 0, s[28:29]
	v_lshl_add_u64 v[122:123], v[122:123], 0, v[142:143]
	global_store_dwordx2 v[122:123], v[126:127], off
.LBB0_472:
	ds_read_b32 v124, v165 offset:64
	v_add_u32_e32 v122, 16, v150
	v_cndmask_b32_e64 v123, 0, 1, s[6:7]
	v_cmp_ne_u32_e64 s[4:5], 1, v123
	v_ashrrev_i32_e32 v123, 10, v122
	v_lshrrev_b32_e32 v126, 1, v122
	s_andn2_b64 vcc, exec, s[6:7]
	v_and_b32_e32 v125, -8, v123
	v_and_b32_e32 v128, 16, v126
	v_and_b32_e32 v126, 12, v126
	s_cbranch_vccnz .LBB0_474
	v_add_u32_e32 v170, v125, v168
	v_ashrrev_i32_e32 v171, 31, v170
	v_lshlrev_b64 v[170:171], 13, v[170:171]
	v_and_or_b32 v123, v122, s87, v170
	v_or_b32_e32 v170, v123, v167
	v_lshlrev_b64 v[170:171], 6, v[170:171]
	v_lshl_add_u64 v[170:171], s[20:21], 0, v[170:171]
	v_lshl_add_u64 v[170:171], v[170:171], 0, v[0:1]
	v_mov_b32_e32 v129, v1
	v_lshl_add_u64 v[170:171], v[170:171], 0, v[128:129]
	v_lshl_add_u64 v[170:171], v[170:171], 0, v[146:147]
	v_mov_b32_e32 v127, v1
	s_waitcnt lgkmcnt(0)
	v_pk_mul_f32 v[174:175], v[118:119], v[124:125] op_sel_hi:[1,0]
	v_lshl_add_u64 v[170:171], v[170:171], 0, v[126:127]
	v_mul_f32_e32 v123, 0x41000000, v174
	v_mul_f32_e32 v127, 0x41000000, v175
	v_med3_f32 v123, v123, s64, v250
	v_med3_f32 v127, v127, s64, v250
	v_cvt_pk_fp8_f32 v129, v123, v127
	v_pk_mul_f32 v[172:173], v[120:121], v[124:125] op_sel_hi:[1,0]
	v_pk_mul_f32 v[174:175], v[114:115], v[124:125] op_sel_hi:[1,0]
	v_mul_f32_e32 v123, 0x41000000, v172
	v_mul_f32_e32 v127, 0x41000000, v173
	v_med3_f32 v123, v123, s64, v250
	v_med3_f32 v127, v127, s64, v250
	v_cvt_pk_fp8_f32 v129, v123, v127 op_sel:[0,0,1]
	v_mul_f32_e32 v123, 0x41000000, v174
	v_mul_f32_e32 v127, 0x41000000, v175
	v_med3_f32 v123, v123, s64, v250
	v_med3_f32 v127, v127, s64, v250
	v_cvt_pk_fp8_f32 v155, v123, v127
	v_pk_mul_f32 v[172:173], v[116:117], v[124:125] op_sel_hi:[1,0]
	v_lshl_add_u64 v[170:171], v[170:171], 0, v[144:145]
	v_mul_f32_e32 v123, 0x41000000, v172
	v_mul_f32_e32 v127, 0x41000000, v173
	v_med3_f32 v123, v123, s64, v250
	v_med3_f32 v127, v127, s64, v250
	v_cvt_pk_fp8_f32 v155, v123, v127 op_sel:[0,0,1]
	v_mov_b32_dpp v123, v129 quad_perm:[1,0,3,2] row_mask:0xf bank_mask:0xf bound_ctrl:1
	v_perm_b32 v123, v123, v129, v161
	v_lshl_add_u64 v[170:171], v[170:171], 0, v[148:149]
	s_nop 0
	v_mov_b32_dpp v127, v123 quad_perm:[2,3,0,1] row_mask:0xf bank_mask:0xf bound_ctrl:1
	v_perm_b32 v123, v127, v123, v163
	global_store_dword v[170:171], v123, off
	s_nop 0
	v_mov_b32_dpp v123, v155 quad_perm:[1,0,3,2] row_mask:0xf bank_mask:0xf bound_ctrl:1
	v_perm_b32 v123, v123, v155, v161
	s_nop 1
	v_mov_b32_dpp v127, v123 quad_perm:[2,3,0,1] row_mask:0xf bank_mask:0xf bound_ctrl:1
	v_perm_b32 v123, v127, v123, v163
	global_store_dword v[170:171], v123, off offset:256
.LBB0_474:
	v_cndmask_b32_e64 v123, 0, 1, s[30:31]
	v_cmp_ne_u32_e64 s[6:7], 1, v123
	s_andn2_b64 vcc, exec, s[30:31]
	v_ashrrev_i32_e32 v123, 31, v122
	s_cbranch_vccnz .LBB0_476
	s_waitcnt lgkmcnt(0)
	v_pk_mul_f32 v[118:119], v[118:119], v[124:125] op_sel_hi:[1,0]
	v_pk_mul_f32 v[120:121], v[120:121], v[124:125] op_sel_hi:[1,0]
	v_mul_f32_e32 v118, 0x41000000, v118
	v_med3_f32 v127, v118, s64, v250
	v_mul_f32_e32 v118, 0x41000000, v119
	v_med3_f32 v119, v118, s64, v250
	v_cvt_pk_fp8_f32 v118, v127, v119
	v_mul_f32_e32 v119, 0x41000000, v120
	v_mul_f32_e32 v120, 0x41000000, v121
	v_pk_mul_f32 v[114:115], v[114:115], v[124:125] op_sel_hi:[1,0]
	v_med3_f32 v119, v119, s64, v250
	v_med3_f32 v120, v120, s64, v250
	v_mul_f32_e32 v114, 0x41000000, v114
	v_mul_f32_e32 v115, 0x41000000, v115
	v_cvt_pk_fp8_f32 v118, v119, v120 op_sel:[0,0,1]
	v_med3_f32 v114, v114, s64, v250
	v_med3_f32 v115, v115, s64, v250
	v_cvt_pk_fp8_f32 v119, v114, v115
	v_pk_mul_f32 v[116:117], v[116:117], v[124:125] op_sel_hi:[1,0]
	s_nop 0
	v_mul_f32_e32 v114, 0x41000000, v116
	v_mul_f32_e32 v115, 0x41000000, v117
	v_med3_f32 v114, v114, s64, v250
	v_med3_f32 v115, v115, s64, v250
	v_cvt_pk_fp8_f32 v119, v114, v115 op_sel:[0,0,1]
	v_lshlrev_b64 v[114:115], 9, v[122:123]
	v_lshl_add_u64 v[114:115], s[22:23], 0, v[114:115]
	v_lshl_add_u64 v[114:115], v[114:115], 0, s[28:29]
	v_lshl_add_u64 v[114:115], v[114:115], 0, v[142:143]
	global_store_dwordx2 v[114:115], v[118:119], off
; __device__ __forceinline__ u32x4 pack8(const f32x4 a, const f32x4 b) { u32x4 w; w.x = cvt_pk_bf16(a[0], a[1]); w.y = cvt_pk_bf16(a[2], a[3]); w.z = cvt_pk_bf16(b[0], b[1]); w.w = cvt_pk_bf16(b[2], b[3]); return w; }
;     __device__ __forceinline__ void operator()(const f32x4 (&acc)[2][2][4][2], const Unit& u, int wr, int wc, int fr_in, int fq_in) const {
;     ...
;         for (int bj = 0; bj < 2; ++bj) {
;             const int colg = u.pn * BM + bj * HALF + wc * 32; bf16_t* dst = colg < 512 ? kn + colg : v + (colg - 512);
; #pragma unroll
;             for (int ai = 0; ai < 2; ++ai)
; #pragma unroll
;                 for (int m = 0; m < 4; ++m) {
;                     const int row = row0 + ai * HALF + m * 16; const float r = t[ai * 64 + m * 16 + fr];
;                     if (!(f8qk && colg < 512) && !(f8pv && colg >= 512)) *(u32x4*)(dst + (size_t)row * 512 + 8 * fq) = pack8(acc[ai][bj][m][0] * r, acc[ai][bj][m][1] * r);
;                     if (f8pv && colg >= 512) {
;                         const int c0_ = colg - 512 + 8 * fq, bb_ = row >> 13, pos_ = row & (SEQ_ - 1), key_ = pos_ & 63, k32_ = key_ & 31;
;                         unsigned char* p_ = ws + WS_V8T + ((((size_t)(bb_ * 8 + (c0_ >> 6)) * 128 + (pos_ >> 6)) * 64 + (c0_ & 63)) * 64) + 32 * ((k32_ >> 2) & 1) + 16 * (key_ >> 5) + (k32_ & 3) + 4 * (k32_ >> 3);
;                         const unsigned w0_ = pack4_fp8_x8(acc[ai][bj][m][0] * r), w1_ = pack4_fp8_x8(acc[ai][bj][m][1] * r);
;                         const int qi_ = fr & 3; unsigned char* pb_ = p_ - qi_;
;                         *(unsigned*)(pb_ + qi_ * 64) = quad_tr4(w0_, qi_); *(unsigned*)(pb_ + (4 + qi_) * 64) = quad_tr4(w1_, qi_);
;                     }
;                     if (f8qk && colg < 512) { u32x2 w8; w8.x = pack4_fp8_x8(acc[ai][bj][m][0] * r); w8.y = pack4_fp8_x8(acc[ai][bj][m][1] * r); *(u32x2*)(ws + WS_KN8 + (size_t)row * 512 + colg + 8 * fq) = w8; }
.LBB0_476:
	ds_read_b32 v116, v165 offset:128
	v_add_u32_e32 v114, 32, v150
	v_ashrrev_i32_e32 v115, 10, v114
	v_lshrrev_b32_e32 v118, 1, v114
	s_and_b64 vcc, exec, s[4:5]
	v_and_b32_e32 v117, -8, v115
	v_and_b32_e32 v120, 16, v118
	v_and_b32_e32 v118, 12, v118
	s_cbranch_vccnz .LBB0_478
	v_add_u32_e32 v170, v117, v168
	v_ashrrev_i32_e32 v171, 31, v170
	v_lshlrev_b64 v[170:171], 13, v[170:171]
	v_and_or_b32 v115, v114, s87, v170
	v_or_b32_e32 v170, v115, v167
	v_lshlrev_b64 v[170:171], 6, v[170:171]
	v_lshl_add_u64 v[170:171], s[20:21], 0, v[170:171]
	v_lshl_add_u64 v[170:171], v[170:171], 0, v[0:1]
	v_mov_b32_e32 v121, v1
	v_lshl_add_u64 v[170:171], v[170:171], 0, v[120:121]
	v_lshl_add_u64 v[170:171], v[170:171], 0, v[146:147]
	v_mov_b32_e32 v119, v1
	s_waitcnt lgkmcnt(0)
	v_pk_mul_f32 v[174:175], v[110:111], v[116:117] op_sel_hi:[1,0]
	v_lshl_add_u64 v[170:171], v[170:171], 0, v[118:119]
	v_mul_f32_e32 v115, 0x41000000, v174
	v_mul_f32_e32 v119, 0x41000000, v175
	v_med3_f32 v115, v115, s64, v250
	v_med3_f32 v119, v119, s64, v250
	v_cvt_pk_fp8_f32 v121, v115, v119
	v_pk_mul_f32 v[172:173], v[112:113], v[116:117] op_sel_hi:[1,0]
	v_pk_mul_f32 v[174:175], v[106:107], v[116:117] op_sel_hi:[1,0]
	v_mul_f32_e32 v115, 0x41000000, v172
	v_mul_f32_e32 v119, 0x41000000, v173
	v_med3_f32 v115, v115, s64, v250
	v_med3_f32 v119, v119, s64, v250
	v_cvt_pk_fp8_f32 v121, v115, v119 op_sel:[0,0,1]
	v_mul_f32_e32 v115, 0x41000000, v174
	v_mul_f32_e32 v119, 0x41000000, v175
	v_med3_f32 v115, v115, s64, v250
	v_med3_f32 v119, v119, s64, v250
	v_cvt_pk_fp8_f32 v127, v115, v119
	v_pk_mul_f32 v[172:173], v[108:109], v[116:117] op_sel_hi:[1,0]
	v_lshl_add_u64 v[170:171], v[170:171], 0, v[144:145]
	v_mul_f32_e32 v115, 0x41000000, v172
	v_mul_f32_e32 v119, 0x41000000, v173
	v_med3_f32 v115, v115, s64, v250
	v_med3_f32 v119, v119, s64, v250
	v_cvt_pk_fp8_f32 v127, v115, v119 op_sel:[0,0,1]
	v_mov_b32_dpp v115, v121 quad_perm:[1,0,3,2] row_mask:0xf bank_mask:0xf bound_ctrl:1
	v_perm_b32 v115, v115, v121, v161
	v_lshl_add_u64 v[170:171], v[170:171], 0, v[148:149]
	s_nop 0
	v_mov_b32_dpp v119, v115 quad_perm:[2,3,0,1] row_mask:0xf bank_mask:0xf bound_ctrl:1
	v_perm_b32 v115, v119, v115, v163
	global_store_dword v[170:171], v115, off
	s_nop 0
	v_mov_b32_dpp v115, v127 quad_perm:[1,0,3,2] row_mask:0xf bank_mask:0xf bound_ctrl:1
	v_perm_b32 v115, v115, v127, v161
	s_nop 1
	v_mov_b32_dpp v119, v115 quad_perm:[2,3,0,1] row_mask:0xf bank_mask:0xf bound_ctrl:1
	v_perm_b32 v115, v119, v115, v163
	global_store_dword v[170:171], v115, off offset:256
.LBB0_478:
	s_and_b64 vcc, exec, s[6:7]
	v_ashrrev_i32_e32 v115, 31, v114
	s_cbranch_vccnz .LBB0_480
	s_waitcnt lgkmcnt(0)
	v_pk_mul_f32 v[110:111], v[110:111], v[116:117] op_sel_hi:[1,0]
	v_pk_mul_f32 v[112:113], v[112:113], v[116:117] op_sel_hi:[1,0]
	v_mul_f32_e32 v110, 0x41000000, v110
	v_med3_f32 v119, v110, s64, v250
	v_mul_f32_e32 v110, 0x41000000, v111
	v_med3_f32 v111, v110, s64, v250
	v_cvt_pk_fp8_f32 v110, v119, v111
	v_mul_f32_e32 v111, 0x41000000, v112
	v_mul_f32_e32 v112, 0x41000000, v113
	v_pk_mul_f32 v[106:107], v[106:107], v[116:117] op_sel_hi:[1,0]
	v_med3_f32 v111, v111, s64, v250
	v_med3_f32 v112, v112, s64, v250
	v_mul_f32_e32 v106, 0x41000000, v106
	v_mul_f32_e32 v107, 0x41000000, v107
	v_cvt_pk_fp8_f32 v110, v111, v112 op_sel:[0,0,1]
	v_med3_f32 v106, v106, s64, v250
	v_med3_f32 v107, v107, s64, v250
	v_cvt_pk_fp8_f32 v111, v106, v107
	v_pk_mul_f32 v[108:109], v[108:109], v[116:117] op_sel_hi:[1,0]
	s_nop 0
	v_mul_f32_e32 v106, 0x41000000, v108
	v_mul_f32_e32 v107, 0x41000000, v109
	v_med3_f32 v106, v106, s64, v250
	v_med3_f32 v107, v107, s64, v250
	v_cvt_pk_fp8_f32 v111, v106, v107 op_sel:[0,0,1]
	v_lshlrev_b64 v[106:107], 9, v[114:115]
	v_lshl_add_u64 v[106:107], s[22:23], 0, v[106:107]
	v_lshl_add_u64 v[106:107], v[106:107], 0, s[28:29]
	v_lshl_add_u64 v[106:107], v[106:107], 0, v[142:143]
	global_store_dwordx2 v[106:107], v[110:111], off
.LBB0_480:
	ds_read_b32 v108, v165 offset:192
	v_add_u32_e32 v106, 48, v150
	v_ashrrev_i32_e32 v107, 10, v106
	v_lshrrev_b32_e32 v110, 1, v106
	s_and_b64 vcc, exec, s[4:5]
	v_and_b32_e32 v109, -8, v107
	v_and_b32_e32 v112, 16, v110
	v_and_b32_e32 v110, 12, v110
	s_cbranch_vccnz .LBB0_482
	v_add_u32_e32 v170, v109, v168
	v_ashrrev_i32_e32 v171, 31, v170
	v_lshlrev_b64 v[170:171], 13, v[170:171]
	v_and_or_b32 v107, v106, s87, v170
	v_or_b32_e32 v170, v107, v167
	v_lshlrev_b64 v[170:171], 6, v[170:171]
	v_lshl_add_u64 v[170:171], s[20:21], 0, v[170:171]
	v_lshl_add_u64 v[170:171], v[170:171], 0, v[0:1]
	v_mov_b32_e32 v113, v1
	v_lshl_add_u64 v[170:171], v[170:171], 0, v[112:113]
	v_lshl_add_u64 v[170:171], v[170:171], 0, v[146:147]
	v_mov_b32_e32 v111, v1
	s_waitcnt lgkmcnt(0)
	v_pk_mul_f32 v[174:175], v[102:103], v[108:109] op_sel_hi:[1,0]
	v_lshl_add_u64 v[170:171], v[170:171], 0, v[110:111]
	v_mul_f32_e32 v107, 0x41000000, v174
	v_mul_f32_e32 v111, 0x41000000, v175
	v_med3_f32 v107, v107, s64, v250
	v_med3_f32 v111, v111, s64, v250
	v_cvt_pk_fp8_f32 v113, v107, v111
	v_pk_mul_f32 v[172:173], v[104:105], v[108:109] op_sel_hi:[1,0]
	v_pk_mul_f32 v[174:175], v[98:99], v[108:109] op_sel_hi:[1,0]
	v_mul_f32_e32 v107, 0x41000000, v172
	v_mul_f32_e32 v111, 0x41000000, v173
	v_med3_f32 v107, v107, s64, v250
	v_med3_f32 v111, v111, s64, v250
	v_cvt_pk_fp8_f32 v113, v107, v111 op_sel:[0,0,1]
	v_mul_f32_e32 v107, 0x41000000, v174
	v_mul_f32_e32 v111, 0x41000000, v175
	v_med3_f32 v107, v107, s64, v250
	v_med3_f32 v111, v111, s64, v250
	v_cvt_pk_fp8_f32 v119, v107, v111
	v_pk_mul_f32 v[172:173], v[100:101], v[108:109] op_sel_hi:[1,0]
	v_lshl_add_u64 v[170:171], v[170:171], 0, v[144:145]
	v_mul_f32_e32 v107, 0x41000000, v172
	v_mul_f32_e32 v111, 0x41000000, v173
	v_med3_f32 v107, v107, s64, v250
	v_med3_f32 v111, v111, s64, v250
	v_cvt_pk_fp8_f32 v119, v107, v111 op_sel:[0,0,1]
	v_mov_b32_dpp v107, v113 quad_perm:[1,0,3,2] row_mask:0xf bank_mask:0xf bound_ctrl:1
	v_perm_b32 v107, v107, v113, v161
	v_lshl_add_u64 v[170:171], v[170:171], 0, v[148:149]
	s_nop 0
	v_mov_b32_dpp v111, v107 quad_perm:[2,3,0,1] row_mask:0xf bank_mask:0xf bound_ctrl:1
	v_perm_b32 v107, v111, v107, v163
	global_store_dword v[170:171], v107, off
	s_nop 0
	v_mov_b32_dpp v107, v119 quad_perm:[1,0,3,2] row_mask:0xf bank_mask:0xf bound_ctrl:1
	v_perm_b32 v107, v107, v119, v161
	s_nop 1
	v_mov_b32_dpp v111, v107 quad_perm:[2,3,0,1] row_mask:0xf bank_mask:0xf bound_ctrl:1
	v_perm_b32 v107, v111, v107, v163
	global_store_dword v[170:171], v107, off offset:256
; __device__ __forceinline__ u32x4 pack8(const f32x4 a, const f32x4 b) { u32x4 w; w.x = cvt_pk_bf16(a[0], a[1]); w.y = cvt_pk_bf16(a[2], a[3]); w.z = cvt_pk_bf16(b[0], b[1]); w.w = cvt_pk_bf16(b[2], b[3]); return w; }
;     __device__ __forceinline__ void operator()(const f32x4 (&acc)[2][2][4][2], const Unit& u, int wr, int wc, int fr_in, int fq_in) const {
;     ...
;         for (int bj = 0; bj < 2; ++bj) {
;             const int colg = u.pn * BM + bj * HALF + wc * 32; bf16_t* dst = colg < 512 ? kn + colg : v + (colg - 512);
; #pragma unroll
;             for (int ai = 0; ai < 2; ++ai)
; #pragma unroll
;                 for (int m = 0; m < 4; ++m) {
;                     const int row = row0 + ai * HALF + m * 16; const float r = t[ai * 64 + m * 16 + fr];
;                     if (!(f8qk && colg < 512) && !(f8pv && colg >= 512)) *(u32x4*)(dst + (size_t)row * 512 + 8 * fq) = pack8(acc[ai][bj][m][0] * r, acc[ai][bj][m][1] * r);
;                     if (f8pv && colg >= 512) {
;                         const int c0_ = colg - 512 + 8 * fq, bb_ = row >> 13, pos_ = row & (SEQ_ - 1), key_ = pos_ & 63, k32_ = key_ & 31;
;                         unsigned char* p_ = ws + WS_V8T + ((((size_t)(bb_ * 8 + (c0_ >> 6)) * 128 + (pos_ >> 6)) * 64 + (c0_ & 63)) * 64) + 32 * ((k32_ >> 2) & 1) + 16 * (key_ >> 5) + (k32_ & 3) + 4 * (k32_ >> 3);
;                         const unsigned w0_ = pack4_fp8_x8(acc[ai][bj][m][0] * r), w1_ = pack4_fp8_x8(acc[ai][bj][m][1] * r);
;                         const int qi_ = fr & 3; unsigned char* pb_ = p_ - qi_;
;                         *(unsigned*)(pb_ + qi_ * 64) = quad_tr4(w0_, qi_); *(unsigned*)(pb_ + (4 + qi_) * 64) = quad_tr4(w1_, qi_);
;                     }
;                     if (f8qk && colg < 512) { u32x2 w8; w8.x = pack4_fp8_x8(acc[ai][bj][m][0] * r); w8.y = pack4_fp8_x8(acc[ai][bj][m][1] * r); *(u32x2*)(ws + WS_KN8 + (size_t)row * 512 + colg + 8 * fq) = w8; }
.LBB0_482:
	s_and_b64 vcc, exec, s[6:7]
	v_ashrrev_i32_e32 v107, 31, v106
	s_cbranch_vccnz .LBB0_484
	s_waitcnt lgkmcnt(0)
	v_pk_mul_f32 v[102:103], v[102:103], v[108:109] op_sel_hi:[1,0]
	v_pk_mul_f32 v[104:105], v[104:105], v[108:109] op_sel_hi:[1,0]
	v_mul_f32_e32 v102, 0x41000000, v102
	v_med3_f32 v111, v102, s64, v250
	v_mul_f32_e32 v102, 0x41000000, v103
	v_med3_f32 v103, v102, s64, v250
	v_cvt_pk_fp8_f32 v102, v111, v103
	v_mul_f32_e32 v103, 0x41000000, v104
	v_mul_f32_e32 v104, 0x41000000, v105
	v_pk_mul_f32 v[98:99], v[98:99], v[108:109] op_sel_hi:[1,0]
	v_med3_f32 v103, v103, s64, v250
	v_med3_f32 v104, v104, s64, v250
	v_mul_f32_e32 v98, 0x41000000, v98
	v_mul_f32_e32 v99, 0x41000000, v99
	v_cvt_pk_fp8_f32 v102, v103, v104 op_sel:[0,0,1]
	v_med3_f32 v98, v98, s64, v250
	v_med3_f32 v99, v99, s64, v250
	v_cvt_pk_fp8_f32 v103, v98, v99
	v_pk_mul_f32 v[100:101], v[100:101], v[108:109] op_sel_hi:[1,0]
	s_nop 0
	v_mul_f32_e32 v98, 0x41000000, v100
	v_mul_f32_e32 v99, 0x41000000, v101
	v_med3_f32 v98, v98, s64, v250
	v_med3_f32 v99, v99, s64, v250
	v_cvt_pk_fp8_f32 v103, v98, v99 op_sel:[0,0,1]
	v_lshlrev_b64 v[98:99], 9, v[106:107]
	v_lshl_add_u64 v[98:99], s[22:23], 0, v[98:99]
	v_lshl_add_u64 v[98:99], v[98:99], 0, s[28:29]
	v_lshl_add_u64 v[98:99], v[98:99], 0, v[142:143]
	global_store_dwordx2 v[98:99], v[102:103], off
.LBB0_484:
	ds_read_b32 v100, v165 offset:256
	v_add_u32_e32 v98, 0x80, v150
	v_ashrrev_i32_e32 v99, 10, v98
	v_lshrrev_b32_e32 v102, 1, v98
	s_and_b64 vcc, exec, s[4:5]
	v_and_b32_e32 v101, -8, v99
	v_and_b32_e32 v104, 16, v102
	v_and_b32_e32 v102, 12, v102
	s_cbranch_vccnz .LBB0_486
	v_add_u32_e32 v170, v101, v168
	v_ashrrev_i32_e32 v171, 31, v170
	v_lshlrev_b64 v[170:171], 13, v[170:171]
	v_and_or_b32 v99, v98, s87, v170
	v_or_b32_e32 v170, v99, v167
	v_lshlrev_b64 v[170:171], 6, v[170:171]
	v_lshl_add_u64 v[170:171], s[20:21], 0, v[170:171]
	v_lshl_add_u64 v[170:171], v[170:171], 0, v[0:1]
	v_mov_b32_e32 v105, v1
	v_lshl_add_u64 v[170:171], v[170:171], 0, v[104:105]
	v_lshl_add_u64 v[170:171], v[170:171], 0, v[146:147]
	v_mov_b32_e32 v103, v1
	s_waitcnt lgkmcnt(0)
	v_pk_mul_f32 v[174:175], v[94:95], v[100:101] op_sel_hi:[1,0]
	v_lshl_add_u64 v[170:171], v[170:171], 0, v[102:103]
	v_mul_f32_e32 v99, 0x41000000, v174
	v_mul_f32_e32 v103, 0x41000000, v175
	v_med3_f32 v99, v99, s64, v250
	v_med3_f32 v103, v103, s64, v250
	v_cvt_pk_fp8_f32 v105, v99, v103
	v_pk_mul_f32 v[172:173], v[96:97], v[100:101] op_sel_hi:[1,0]
	v_pk_mul_f32 v[174:175], v[90:91], v[100:101] op_sel_hi:[1,0]
	v_mul_f32_e32 v99, 0x41000000, v172
	v_mul_f32_e32 v103, 0x41000000, v173
	v_med3_f32 v99, v99, s64, v250
	v_med3_f32 v103, v103, s64, v250
	v_cvt_pk_fp8_f32 v105, v99, v103 op_sel:[0,0,1]
	v_mul_f32_e32 v99, 0x41000000, v174
	v_mul_f32_e32 v103, 0x41000000, v175
	v_med3_f32 v99, v99, s64, v250
	v_med3_f32 v103, v103, s64, v250
	v_cvt_pk_fp8_f32 v111, v99, v103
	v_pk_mul_f32 v[172:173], v[92:93], v[100:101] op_sel_hi:[1,0]
	v_lshl_add_u64 v[170:171], v[170:171], 0, v[144:145]
	v_mul_f32_e32 v99, 0x41000000, v172
	v_mul_f32_e32 v103, 0x41000000, v173
	v_med3_f32 v99, v99, s64, v250
	v_med3_f32 v103, v103, s64, v250
	v_cvt_pk_fp8_f32 v111, v99, v103 op_sel:[0,0,1]
	v_mov_b32_dpp v99, v105 quad_perm:[1,0,3,2] row_mask:0xf bank_mask:0xf bound_ctrl:1
	v_perm_b32 v99, v99, v105, v161
	v_lshl_add_u64 v[170:171], v[170:171], 0, v[148:149]
	s_nop 0
	v_mov_b32_dpp v103, v99 quad_perm:[2,3,0,1] row_mask:0xf bank_mask:0xf bound_ctrl:1
	v_perm_b32 v99, v103, v99, v163
	global_store_dword v[170:171], v99, off
	s_nop 0
	v_mov_b32_dpp v99, v111 quad_perm:[1,0,3,2] row_mask:0xf bank_mask:0xf bound_ctrl:1
	v_perm_b32 v99, v99, v111, v161
	s_nop 1
	v_mov_b32_dpp v103, v99 quad_perm:[2,3,0,1] row_mask:0xf bank_mask:0xf bound_ctrl:1
	v_perm_b32 v99, v103, v99, v163
	global_store_dword v[170:171], v99, off offset:256
.LBB0_486:
	s_and_b64 vcc, exec, s[6:7]
	v_ashrrev_i32_e32 v99, 31, v98
	s_cbranch_vccnz .LBB0_488
	s_waitcnt lgkmcnt(0)
	v_pk_mul_f32 v[94:95], v[94:95], v[100:101] op_sel_hi:[1,0]
	v_pk_mul_f32 v[96:97], v[96:97], v[100:101] op_sel_hi:[1,0]
	v_mul_f32_e32 v94, 0x41000000, v94
	v_med3_f32 v103, v94, s64, v250
	v_mul_f32_e32 v94, 0x41000000, v95
	v_med3_f32 v95, v94, s64, v250
	v_cvt_pk_fp8_f32 v94, v103, v95
	v_mul_f32_e32 v95, 0x41000000, v96
	v_mul_f32_e32 v96, 0x41000000, v97
	v_pk_mul_f32 v[90:91], v[90:91], v[100:101] op_sel_hi:[1,0]
	v_med3_f32 v95, v95, s64, v250
	v_med3_f32 v96, v96, s64, v250
	v_mul_f32_e32 v90, 0x41000000, v90
	v_mul_f32_e32 v91, 0x41000000, v91
	v_cvt_pk_fp8_f32 v94, v95, v96 op_sel:[0,0,1]
	v_med3_f32 v90, v90, s64, v250
	v_med3_f32 v91, v91, s64, v250
	v_cvt_pk_fp8_f32 v95, v90, v91
	v_pk_mul_f32 v[92:93], v[92:93], v[100:101] op_sel_hi:[1,0]
	s_nop 0
	v_mul_f32_e32 v90, 0x41000000, v92
	v_mul_f32_e32 v91, 0x41000000, v93
	v_med3_f32 v90, v90, s64, v250
	v_med3_f32 v91, v91, s64, v250
	v_cvt_pk_fp8_f32 v95, v90, v91 op_sel:[0,0,1]
	v_lshlrev_b64 v[90:91], 9, v[98:99]
	v_lshl_add_u64 v[90:91], s[22:23], 0, v[90:91]
	v_lshl_add_u64 v[90:91], v[90:91], 0, s[28:29]
	v_lshl_add_u64 v[90:91], v[90:91], 0, v[142:143]
	global_store_dwordx2 v[90:91], v[94:95], off
; __device__ __forceinline__ u32x4 pack8(const f32x4 a, const f32x4 b) { u32x4 w; w.x = cvt_pk_bf16(a[0], a[1]); w.y = cvt_pk_bf16(a[2], a[3]); w.z = cvt_pk_bf16(b[0], b[1]); w.w = cvt_pk_bf16(b[2], b[3]); return w; }
;     __device__ __forceinline__ void operator()(const f32x4 (&acc)[2][2][4][2], const Unit& u, int wr, int wc, int fr_in, int fq_in) const {
;     ...
;         for (int bj = 0; bj < 2; ++bj) {
;             const int colg = u.pn * BM + bj * HALF + wc * 32; bf16_t* dst = colg < 512 ? kn + colg : v + (colg - 512);
; #pragma unroll
;             for (int ai = 0; ai < 2; ++ai)
; #pragma unroll
;                 for (int m = 0; m < 4; ++m) {
;                     const int row = row0 + ai * HALF + m * 16; const float r = t[ai * 64 + m * 16 + fr];
;                     if (!(f8qk && colg < 512) && !(f8pv && colg >= 512)) *(u32x4*)(dst + (size_t)row * 512 + 8 * fq) = pack8(acc[ai][bj][m][0] * r, acc[ai][bj][m][1] * r);
;                     if (f8pv && colg >= 512) {
;                         const int c0_ = colg - 512 + 8 * fq, bb_ = row >> 13, pos_ = row & (SEQ_ - 1), key_ = pos_ & 63, k32_ = key_ & 31;
;                         unsigned char* p_ = ws + WS_V8T + ((((size_t)(bb_ * 8 + (c0_ >> 6)) * 128 + (pos_ >> 6)) * 64 + (c0_ & 63)) * 64) + 32 * ((k32_ >> 2) & 1) + 16 * (key_ >> 5) + (k32_ & 3) + 4 * (k32_ >> 3);
;                         const unsigned w0_ = pack4_fp8_x8(acc[ai][bj][m][0] * r), w1_ = pack4_fp8_x8(acc[ai][bj][m][1] * r);
;                         const int qi_ = fr & 3; unsigned char* pb_ = p_ - qi_;
;                         *(unsigned*)(pb_ + qi_ * 64) = quad_tr4(w0_, qi_); *(unsigned*)(pb_ + (4 + qi_) * 64) = quad_tr4(w1_, qi_);
;                     }
;                     if (f8qk && colg < 512) { u32x2 w8; w8.x = pack4_fp8_x8(acc[ai][bj][m][0] * r); w8.y = pack4_fp8_x8(acc[ai][bj][m][1] * r); *(u32x2*)(ws + WS_KN8 + (size_t)row * 512 + colg + 8 * fq) = w8; }
.LBB0_488:
	ds_read_b32 v92, v165 offset:320
	v_add_u32_e32 v90, 0x90, v150
	v_ashrrev_i32_e32 v91, 10, v90
	v_lshrrev_b32_e32 v94, 1, v90
	s_and_b64 vcc, exec, s[4:5]
	v_and_b32_e32 v93, -8, v91
	v_and_b32_e32 v96, 16, v94
	v_and_b32_e32 v94, 12, v94
	s_cbranch_vccnz .LBB0_490
	v_add_u32_e32 v170, v93, v168
	v_ashrrev_i32_e32 v171, 31, v170
	v_lshlrev_b64 v[170:171], 13, v[170:171]
	v_and_or_b32 v91, v90, s87, v170
	v_or_b32_e32 v170, v91, v167
	v_lshlrev_b64 v[170:171], 6, v[170:171]
	v_lshl_add_u64 v[170:171], s[20:21], 0, v[170:171]
	v_lshl_add_u64 v[170:171], v[170:171], 0, v[0:1]
	v_mov_b32_e32 v97, v1
	v_lshl_add_u64 v[170:171], v[170:171], 0, v[96:97]
	v_lshl_add_u64 v[170:171], v[170:171], 0, v[146:147]
	v_mov_b32_e32 v95, v1
	s_waitcnt lgkmcnt(0)
	v_pk_mul_f32 v[174:175], v[86:87], v[92:93] op_sel_hi:[1,0]
	v_lshl_add_u64 v[170:171], v[170:171], 0, v[94:95]
	v_mul_f32_e32 v91, 0x41000000, v174
	v_mul_f32_e32 v95, 0x41000000, v175
	v_med3_f32 v91, v91, s64, v250
	v_med3_f32 v95, v95, s64, v250
	v_cvt_pk_fp8_f32 v97, v91, v95
	v_pk_mul_f32 v[172:173], v[88:89], v[92:93] op_sel_hi:[1,0]
	v_pk_mul_f32 v[174:175], v[82:83], v[92:93] op_sel_hi:[1,0]
	v_mul_f32_e32 v91, 0x41000000, v172
	v_mul_f32_e32 v95, 0x41000000, v173
	v_med3_f32 v91, v91, s64, v250
	v_med3_f32 v95, v95, s64, v250
	v_cvt_pk_fp8_f32 v97, v91, v95 op_sel:[0,0,1]
	v_mul_f32_e32 v91, 0x41000000, v174
	v_mul_f32_e32 v95, 0x41000000, v175
	v_med3_f32 v91, v91, s64, v250
	v_med3_f32 v95, v95, s64, v250
	v_cvt_pk_fp8_f32 v103, v91, v95
	v_pk_mul_f32 v[172:173], v[84:85], v[92:93] op_sel_hi:[1,0]
	v_lshl_add_u64 v[170:171], v[170:171], 0, v[144:145]
	v_mul_f32_e32 v91, 0x41000000, v172
	v_mul_f32_e32 v95, 0x41000000, v173
	v_med3_f32 v91, v91, s64, v250
	v_med3_f32 v95, v95, s64, v250
	v_cvt_pk_fp8_f32 v103, v91, v95 op_sel:[0,0,1]
	v_mov_b32_dpp v91, v97 quad_perm:[1,0,3,2] row_mask:0xf bank_mask:0xf bound_ctrl:1
	v_perm_b32 v91, v91, v97, v161
	v_lshl_add_u64 v[170:171], v[170:171], 0, v[148:149]
	s_nop 0
	v_mov_b32_dpp v95, v91 quad_perm:[2,3,0,1] row_mask:0xf bank_mask:0xf bound_ctrl:1
	v_perm_b32 v91, v95, v91, v163
	global_store_dword v[170:171], v91, off
	s_nop 0
	v_mov_b32_dpp v91, v103 quad_perm:[1,0,3,2] row_mask:0xf bank_mask:0xf bound_ctrl:1
	v_perm_b32 v91, v91, v103, v161
	s_nop 1
	v_mov_b32_dpp v95, v91 quad_perm:[2,3,0,1] row_mask:0xf bank_mask:0xf bound_ctrl:1
	v_perm_b32 v91, v95, v91, v163
	global_store_dword v[170:171], v91, off offset:256
.LBB0_490:
	s_and_b64 vcc, exec, s[6:7]
	v_ashrrev_i32_e32 v91, 31, v90
	s_cbranch_vccnz .LBB0_492
	s_waitcnt lgkmcnt(0)
	v_pk_mul_f32 v[86:87], v[86:87], v[92:93] op_sel_hi:[1,0]
	v_pk_mul_f32 v[88:89], v[88:89], v[92:93] op_sel_hi:[1,0]
	v_mul_f32_e32 v86, 0x41000000, v86
	v_med3_f32 v95, v86, s64, v250
	v_mul_f32_e32 v86, 0x41000000, v87
	v_med3_f32 v87, v86, s64, v250
	v_cvt_pk_fp8_f32 v86, v95, v87
	v_mul_f32_e32 v87, 0x41000000, v88
	v_mul_f32_e32 v88, 0x41000000, v89
	v_pk_mul_f32 v[82:83], v[82:83], v[92:93] op_sel_hi:[1,0]
	v_med3_f32 v87, v87, s64, v250
	v_med3_f32 v88, v88, s64, v250
	v_mul_f32_e32 v82, 0x41000000, v82
	v_mul_f32_e32 v83, 0x41000000, v83
	v_cvt_pk_fp8_f32 v86, v87, v88 op_sel:[0,0,1]
	v_med3_f32 v82, v82, s64, v250
	v_med3_f32 v83, v83, s64, v250
	v_cvt_pk_fp8_f32 v87, v82, v83
	v_pk_mul_f32 v[84:85], v[84:85], v[92:93] op_sel_hi:[1,0]
	s_nop 0
	v_mul_f32_e32 v82, 0x41000000, v84
	v_mul_f32_e32 v83, 0x41000000, v85
	v_med3_f32 v82, v82, s64, v250
	v_med3_f32 v83, v83, s64, v250
	v_cvt_pk_fp8_f32 v87, v82, v83 op_sel:[0,0,1]
	v_lshlrev_b64 v[82:83], 9, v[90:91]
	v_lshl_add_u64 v[82:83], s[22:23], 0, v[82:83]
	v_lshl_add_u64 v[82:83], v[82:83], 0, s[28:29]
	v_lshl_add_u64 v[82:83], v[82:83], 0, v[142:143]
	global_store_dwordx2 v[82:83], v[86:87], off
.LBB0_492:
	ds_read_b32 v84, v165 offset:384
	v_add_u32_e32 v82, 0xa0, v150
	v_ashrrev_i32_e32 v83, 10, v82
	v_lshrrev_b32_e32 v86, 1, v82
	s_and_b64 vcc, exec, s[4:5]
	v_and_b32_e32 v85, -8, v83
	v_and_b32_e32 v88, 16, v86
	v_and_b32_e32 v86, 12, v86
	s_cbranch_vccnz .LBB0_494
	v_add_u32_e32 v170, v85, v168
	v_ashrrev_i32_e32 v171, 31, v170
	v_lshlrev_b64 v[170:171], 13, v[170:171]
	v_and_or_b32 v83, v82, s87, v170
	v_or_b32_e32 v170, v83, v167
	v_lshlrev_b64 v[170:171], 6, v[170:171]
	v_lshl_add_u64 v[170:171], s[20:21], 0, v[170:171]
	v_lshl_add_u64 v[170:171], v[170:171], 0, v[0:1]
	v_mov_b32_e32 v89, v1
	v_lshl_add_u64 v[170:171], v[170:171], 0, v[88:89]
	v_lshl_add_u64 v[170:171], v[170:171], 0, v[146:147]
	v_mov_b32_e32 v87, v1
	s_waitcnt lgkmcnt(0)
	v_pk_mul_f32 v[174:175], v[78:79], v[84:85] op_sel_hi:[1,0]
	v_lshl_add_u64 v[170:171], v[170:171], 0, v[86:87]
	v_mul_f32_e32 v83, 0x41000000, v174
	v_mul_f32_e32 v87, 0x41000000, v175
	v_med3_f32 v83, v83, s64, v250
	v_med3_f32 v87, v87, s64, v250
	v_cvt_pk_fp8_f32 v89, v83, v87
	v_pk_mul_f32 v[172:173], v[80:81], v[84:85] op_sel_hi:[1,0]
	v_pk_mul_f32 v[174:175], v[74:75], v[84:85] op_sel_hi:[1,0]
	v_mul_f32_e32 v83, 0x41000000, v172
	v_mul_f32_e32 v87, 0x41000000, v173
	v_med3_f32 v83, v83, s64, v250
	v_med3_f32 v87, v87, s64, v250
	v_cvt_pk_fp8_f32 v89, v83, v87 op_sel:[0,0,1]
	v_mul_f32_e32 v83, 0x41000000, v174
	v_mul_f32_e32 v87, 0x41000000, v175
	v_med3_f32 v83, v83, s64, v250
	v_med3_f32 v87, v87, s64, v250
	v_cvt_pk_fp8_f32 v95, v83, v87
	v_pk_mul_f32 v[172:173], v[76:77], v[84:85] op_sel_hi:[1,0]
	v_lshl_add_u64 v[170:171], v[170:171], 0, v[144:145]
	v_mul_f32_e32 v83, 0x41000000, v172
	v_mul_f32_e32 v87, 0x41000000, v173
	v_med3_f32 v83, v83, s64, v250
	v_med3_f32 v87, v87, s64, v250
	v_cvt_pk_fp8_f32 v95, v83, v87 op_sel:[0,0,1]
	v_mov_b32_dpp v83, v89 quad_perm:[1,0,3,2] row_mask:0xf bank_mask:0xf bound_ctrl:1
	v_perm_b32 v83, v83, v89, v161
	v_lshl_add_u64 v[170:171], v[170:171], 0, v[148:149]
	s_nop 0
	v_mov_b32_dpp v87, v83 quad_perm:[2,3,0,1] row_mask:0xf bank_mask:0xf bound_ctrl:1
	v_perm_b32 v83, v87, v83, v163
	global_store_dword v[170:171], v83, off
	s_nop 0
	v_mov_b32_dpp v83, v95 quad_perm:[1,0,3,2] row_mask:0xf bank_mask:0xf bound_ctrl:1
	v_perm_b32 v83, v83, v95, v161
	s_nop 1
	v_mov_b32_dpp v87, v83 quad_perm:[2,3,0,1] row_mask:0xf bank_mask:0xf bound_ctrl:1
	v_perm_b32 v83, v87, v83, v163
	global_store_dword v[170:171], v83, off offset:256
; __device__ __forceinline__ u32x4 pack8(const f32x4 a, const f32x4 b) { u32x4 w; w.x = cvt_pk_bf16(a[0], a[1]); w.y = cvt_pk_bf16(a[2], a[3]); w.z = cvt_pk_bf16(b[0], b[1]); w.w = cvt_pk_bf16(b[2], b[3]); return w; }
;     __device__ __forceinline__ void operator()(const f32x4 (&acc)[2][2][4][2], const Unit& u, int wr, int wc, int fr_in, int fq_in) const {
;     ...
;         for (int bj = 0; bj < 2; ++bj) {
;             const int colg = u.pn * BM + bj * HALF + wc * 32; bf16_t* dst = colg < 512 ? kn + colg : v + (colg - 512);
; #pragma unroll
;             for (int ai = 0; ai < 2; ++ai)
; #pragma unroll
;                 for (int m = 0; m < 4; ++m) {
;                     const int row = row0 + ai * HALF + m * 16; const float r = t[ai * 64 + m * 16 + fr];
;                     if (!(f8qk && colg < 512) && !(f8pv && colg >= 512)) *(u32x4*)(dst + (size_t)row * 512 + 8 * fq) = pack8(acc[ai][bj][m][0] * r, acc[ai][bj][m][1] * r);
;                     if (f8pv && colg >= 512) {
;                         const int c0_ = colg - 512 + 8 * fq, bb_ = row >> 13, pos_ = row & (SEQ_ - 1), key_ = pos_ & 63, k32_ = key_ & 31;
;                         unsigned char* p_ = ws + WS_V8T + ((((size_t)(bb_ * 8 + (c0_ >> 6)) * 128 + (pos_ >> 6)) * 64 + (c0_ & 63)) * 64) + 32 * ((k32_ >> 2) & 1) + 16 * (key_ >> 5) + (k32_ & 3) + 4 * (k32_ >> 3);
;                         const unsigned w0_ = pack4_fp8_x8(acc[ai][bj][m][0] * r), w1_ = pack4_fp8_x8(acc[ai][bj][m][1] * r);
;                         const int qi_ = fr & 3; unsigned char* pb_ = p_ - qi_;
;                         *(unsigned*)(pb_ + qi_ * 64) = quad_tr4(w0_, qi_); *(unsigned*)(pb_ + (4 + qi_) * 64) = quad_tr4(w1_, qi_);
;                     }
;                     if (f8qk && colg < 512) { u32x2 w8; w8.x = pack4_fp8_x8(acc[ai][bj][m][0] * r); w8.y = pack4_fp8_x8(acc[ai][bj][m][1] * r); *(u32x2*)(ws + WS_KN8 + (size_t)row * 512 + colg + 8 * fq) = w8; }
.LBB0_494:
	s_and_b64 vcc, exec, s[6:7]
	v_ashrrev_i32_e32 v83, 31, v82
	s_cbranch_vccnz .LBB0_496
	s_waitcnt lgkmcnt(0)
	v_pk_mul_f32 v[78:79], v[78:79], v[84:85] op_sel_hi:[1,0]
	v_pk_mul_f32 v[80:81], v[80:81], v[84:85] op_sel_hi:[1,0]
	v_mul_f32_e32 v78, 0x41000000, v78
	v_med3_f32 v87, v78, s64, v250
	v_mul_f32_e32 v78, 0x41000000, v79
	v_med3_f32 v79, v78, s64, v250
	v_cvt_pk_fp8_f32 v78, v87, v79
	v_mul_f32_e32 v79, 0x41000000, v80
	v_mul_f32_e32 v80, 0x41000000, v81
	v_pk_mul_f32 v[74:75], v[74:75], v[84:85] op_sel_hi:[1,0]
	v_med3_f32 v79, v79, s64, v250
	v_med3_f32 v80, v80, s64, v250
	v_mul_f32_e32 v74, 0x41000000, v74
	v_mul_f32_e32 v75, 0x41000000, v75
	v_cvt_pk_fp8_f32 v78, v79, v80 op_sel:[0,0,1]
	v_med3_f32 v74, v74, s64, v250
	v_med3_f32 v75, v75, s64, v250
	v_cvt_pk_fp8_f32 v79, v74, v75
	v_pk_mul_f32 v[76:77], v[76:77], v[84:85] op_sel_hi:[1,0]
	s_nop 0
	v_mul_f32_e32 v74, 0x41000000, v76
	v_mul_f32_e32 v75, 0x41000000, v77
	v_med3_f32 v74, v74, s64, v250
	v_med3_f32 v75, v75, s64, v250
	v_cvt_pk_fp8_f32 v79, v74, v75 op_sel:[0,0,1]
	v_lshlrev_b64 v[74:75], 9, v[82:83]
	v_lshl_add_u64 v[74:75], s[22:23], 0, v[74:75]
	v_lshl_add_u64 v[74:75], v[74:75], 0, s[28:29]
	v_lshl_add_u64 v[74:75], v[74:75], 0, v[142:143]
	global_store_dwordx2 v[74:75], v[78:79], off
.LBB0_496:
	ds_read_b32 v76, v165 offset:448
	v_add_u32_e32 v74, 0xb0, v150
	v_ashrrev_i32_e32 v75, 10, v74
	v_lshrrev_b32_e32 v78, 1, v74
	s_and_b64 vcc, exec, s[4:5]
	v_and_b32_e32 v77, -8, v75
	v_and_b32_e32 v80, 16, v78
	v_and_b32_e32 v78, 12, v78
	s_cbranch_vccnz .LBB0_498
	v_add_u32_e32 v168, v77, v168
	v_ashrrev_i32_e32 v169, 31, v168
	v_lshlrev_b64 v[168:169], 13, v[168:169]
	v_and_or_b32 v75, v74, s87, v168
	v_or_b32_e32 v168, v75, v167
	v_lshlrev_b64 v[168:169], 6, v[168:169]
	v_lshl_add_u64 v[168:169], s[20:21], 0, v[168:169]
	v_lshl_add_u64 v[168:169], v[168:169], 0, v[0:1]
	v_mov_b32_e32 v81, v1
	v_lshl_add_u64 v[168:169], v[168:169], 0, v[80:81]
	v_lshl_add_u64 v[168:169], v[168:169], 0, v[146:147]
	v_mov_b32_e32 v79, v1
	s_waitcnt lgkmcnt(0)
	v_pk_mul_f32 v[172:173], v[70:71], v[76:77] op_sel_hi:[1,0]
	v_lshl_add_u64 v[168:169], v[168:169], 0, v[78:79]
	v_mul_f32_e32 v75, 0x41000000, v172
	v_mul_f32_e32 v79, 0x41000000, v173
	v_med3_f32 v75, v75, s64, v250
	v_med3_f32 v79, v79, s64, v250
	v_cvt_pk_fp8_f32 v81, v75, v79
	v_pk_mul_f32 v[170:171], v[72:73], v[76:77] op_sel_hi:[1,0]
	v_pk_mul_f32 v[172:173], v[66:67], v[76:77] op_sel_hi:[1,0]
	v_mul_f32_e32 v75, 0x41000000, v170
	v_mul_f32_e32 v79, 0x41000000, v171
	v_med3_f32 v75, v75, s64, v250
	v_med3_f32 v79, v79, s64, v250
	v_cvt_pk_fp8_f32 v81, v75, v79 op_sel:[0,0,1]
	v_mul_f32_e32 v75, 0x41000000, v172
	v_mul_f32_e32 v79, 0x41000000, v173
	v_med3_f32 v75, v75, s64, v250
	v_med3_f32 v79, v79, s64, v250
	v_cvt_pk_fp8_f32 v87, v75, v79
	v_pk_mul_f32 v[170:171], v[68:69], v[76:77] op_sel_hi:[1,0]
	v_lshl_add_u64 v[168:169], v[168:169], 0, v[144:145]
	v_mul_f32_e32 v75, 0x41000000, v170
	v_mul_f32_e32 v79, 0x41000000, v171
	v_med3_f32 v75, v75, s64, v250
	v_med3_f32 v79, v79, s64, v250
	v_cvt_pk_fp8_f32 v87, v75, v79 op_sel:[0,0,1]
	v_mov_b32_dpp v75, v81 quad_perm:[1,0,3,2] row_mask:0xf bank_mask:0xf bound_ctrl:1
	v_perm_b32 v75, v75, v81, v161
	v_lshl_add_u64 v[168:169], v[168:169], 0, v[148:149]
	s_nop 0
	v_mov_b32_dpp v79, v75 quad_perm:[2,3,0,1] row_mask:0xf bank_mask:0xf bound_ctrl:1
	v_perm_b32 v75, v79, v75, v163
	global_store_dword v[168:169], v75, off
	s_nop 0
	v_mov_b32_dpp v75, v87 quad_perm:[1,0,3,2] row_mask:0xf bank_mask:0xf bound_ctrl:1
	v_perm_b32 v75, v75, v87, v161
	s_nop 1
	v_mov_b32_dpp v79, v75 quad_perm:[2,3,0,1] row_mask:0xf bank_mask:0xf bound_ctrl:1
	v_perm_b32 v75, v79, v75, v163
	global_store_dword v[168:169], v75, off offset:256
; __device__ __forceinline__ u32x4 pack8(const f32x4 a, const f32x4 b) { u32x4 w; w.x = cvt_pk_bf16(a[0], a[1]); w.y = cvt_pk_bf16(a[2], a[3]); w.z = cvt_pk_bf16(b[0], b[1]); w.w = cvt_pk_bf16(b[2], b[3]); return w; }
;     __device__ __forceinline__ void operator()(const f32x4 (&acc)[2][2][4][2], const Unit& u, int wr, int wc, int fr_in, int fq_in) const {
;     ...
;         for (int bj = 0; bj < 2; ++bj) {
;             const int colg = u.pn * BM + bj * HALF + wc * 32; bf16_t* dst = colg < 512 ? kn + colg : v + (colg - 512);
; #pragma unroll
;             for (int ai = 0; ai < 2; ++ai)
; #pragma unroll
;                 for (int m = 0; m < 4; ++m) {
;                     const int row = row0 + ai * HALF + m * 16; const float r = t[ai * 64 + m * 16 + fr];
;                     if (!(f8qk && colg < 512) && !(f8pv && colg >= 512)) *(u32x4*)(dst + (size_t)row * 512 + 8 * fq) = pack8(acc[ai][bj][m][0] * r, acc[ai][bj][m][1] * r);
;                     if (f8pv && colg >= 512) {
;                         const int c0_ = colg - 512 + 8 * fq, bb_ = row >> 13, pos_ = row & (SEQ_ - 1), key_ = pos_ & 63, k32_ = key_ & 31;
;                         unsigned char* p_ = ws + WS_V8T + ((((size_t)(bb_ * 8 + (c0_ >> 6)) * 128 + (pos_ >> 6)) * 64 + (c0_ & 63)) * 64) + 32 * ((k32_ >> 2) & 1) + 16 * (key_ >> 5) + (k32_ & 3) + 4 * (k32_ >> 3);
;                         const unsigned w0_ = pack4_fp8_x8(acc[ai][bj][m][0] * r), w1_ = pack4_fp8_x8(acc[ai][bj][m][1] * r);
;                         const int qi_ = fr & 3; unsigned char* pb_ = p_ - qi_;
;                         *(unsigned*)(pb_ + qi_ * 64) = quad_tr4(w0_, qi_); *(unsigned*)(pb_ + (4 + qi_) * 64) = quad_tr4(w1_, qi_);
;                     }
;                     if (f8qk && colg < 512) { u32x2 w8; w8.x = pack4_fp8_x8(acc[ai][bj][m][0] * r); w8.y = pack4_fp8_x8(acc[ai][bj][m][1] * r); *(u32x2*)(ws + WS_KN8 + (size_t)row * 512 + colg + 8 * fq) = w8; }
.LBB0_498:
	s_and_b64 vcc, exec, s[6:7]
	v_ashrrev_i32_e32 v75, 31, v74
	s_cbranch_vccnz .LBB0_500
	s_waitcnt lgkmcnt(0)
	v_pk_mul_f32 v[70:71], v[70:71], v[76:77] op_sel_hi:[1,0]
	v_pk_mul_f32 v[72:73], v[72:73], v[76:77] op_sel_hi:[1,0]
	v_mul_f32_e32 v70, 0x41000000, v70
	v_med3_f32 v79, v70, s64, v250
	v_mul_f32_e32 v70, 0x41000000, v71
	v_med3_f32 v71, v70, s64, v250
	v_cvt_pk_fp8_f32 v70, v79, v71
	v_mul_f32_e32 v71, 0x41000000, v72
	v_mul_f32_e32 v72, 0x41000000, v73
	v_pk_mul_f32 v[66:67], v[66:67], v[76:77] op_sel_hi:[1,0]
	v_med3_f32 v71, v71, s64, v250
	v_med3_f32 v72, v72, s64, v250
	v_mul_f32_e32 v66, 0x41000000, v66
	v_mul_f32_e32 v67, 0x41000000, v67
	v_cvt_pk_fp8_f32 v70, v71, v72 op_sel:[0,0,1]
	v_med3_f32 v66, v66, s64, v250
	v_med3_f32 v67, v67, s64, v250
	v_cvt_pk_fp8_f32 v71, v66, v67
	v_pk_mul_f32 v[68:69], v[68:69], v[76:77] op_sel_hi:[1,0]
	s_nop 0
	v_mul_f32_e32 v66, 0x41000000, v68
	v_mul_f32_e32 v67, 0x41000000, v69
	v_med3_f32 v66, v66, s64, v250
	v_med3_f32 v67, v67, s64, v250
	v_cvt_pk_fp8_f32 v71, v66, v67 op_sel:[0,0,1]
	v_lshlrev_b64 v[66:67], 9, v[74:75]
	v_lshl_add_u64 v[66:67], s[22:23], 0, v[66:67]
	v_lshl_add_u64 v[66:67], v[66:67], 0, s[28:29]
	v_lshl_add_u64 v[66:67], v[66:67], 0, v[142:143]
	global_store_dwordx2 v[66:67], v[70:71], off
.LBB0_500:
	s_or_b32 s4, s28, 0x80
	s_cmpk_gt_i32 s4, 0x1ff
	v_add_u32_e32 v66, s4, v164
	s_cselect_b64 s[6:7], -1, 0
	s_cmpk_lt_i32 s4, 0x200
	v_ashrrev_i32_e32 v67, 6, v66
	v_and_b32_e32 v66, 56, v66
	s_cbranch_scc1 .LBB0_517
	s_waitcnt lgkmcnt(0)
	v_pk_mul_f32 v[72:73], v[62:63], v[152:153] op_sel_hi:[1,0]
	v_add_u32_e32 v68, v67, v166
	v_mul_f32_e32 v72, 0x41000000, v72
	v_mul_f32_e32 v73, 0x41000000, v73
	v_med3_f32 v72, v72, s64, v250
	v_med3_f32 v73, v73, s64, v250
	v_ashrrev_i32_e32 v69, 31, v68
	v_cvt_pk_fp8_f32 v79, v72, v73
	v_lshlrev_b64 v[68:69], 13, v[68:69]
	v_pk_mul_f32 v[70:71], v[64:65], v[152:153] op_sel_hi:[1,0]
	v_pk_mul_f32 v[72:73], v[58:59], v[152:153] op_sel_hi:[1,0]
	v_and_or_b32 v68, v150, s87, v68
	v_mul_f32_e32 v70, 0x41000000, v70
	v_mul_f32_e32 v71, 0x41000000, v71
	v_mul_f32_e32 v72, 0x41000000, v72
	v_mul_f32_e32 v73, 0x41000000, v73
	v_or_b32_e32 v68, v68, v66
	v_med3_f32 v70, v70, s64, v250
	v_med3_f32 v71, v71, s64, v250
	v_med3_f32 v72, v72, s64, v250
	v_med3_f32 v73, v73, s64, v250
	v_lshlrev_b64 v[68:69], 6, v[68:69]
	v_cvt_pk_fp8_f32 v79, v70, v71 op_sel:[0,0,1]
	v_cvt_pk_fp8_f32 v81, v72, v73
	v_lshl_add_u64 v[68:69], s[20:21], 0, v[68:69]
	v_pk_mul_f32 v[70:71], v[60:61], v[152:153] op_sel_hi:[1,0]
	v_lshl_add_u64 v[68:69], v[68:69], 0, v[0:1]
	v_mov_b32_e32 v157, v1
	v_mul_f32_e32 v70, 0x41000000, v70
	v_mul_f32_e32 v71, 0x41000000, v71
	v_lshl_add_u64 v[68:69], v[68:69], 0, v[156:157]
	v_med3_f32 v70, v70, s64, v250
	v_med3_f32 v71, v71, s64, v250
	v_lshl_add_u64 v[68:69], v[68:69], 0, v[146:147]
	v_mov_b32_e32 v155, v1
	v_cvt_pk_fp8_f32 v81, v70, v71 op_sel:[0,0,1]
	v_mov_b32_dpp v70, v79 quad_perm:[1,0,3,2] row_mask:0xf bank_mask:0xf bound_ctrl:1
	v_lshl_add_u64 v[68:69], v[68:69], 0, v[154:155]
	v_perm_b32 v70, v70, v79, v161
	v_lshl_add_u64 v[68:69], v[68:69], 0, v[144:145]
	v_lshl_add_u64 v[68:69], v[68:69], 0, v[148:149]
	v_mov_b32_dpp v71, v70 quad_perm:[2,3,0,1] row_mask:0xf bank_mask:0xf bound_ctrl:1
	v_perm_b32 v70, v71, v70, v163
	global_store_dword v[68:69], v70, off
	s_nop 0
	v_mov_b32_dpp v70, v81 quad_perm:[1,0,3,2] row_mask:0xf bank_mask:0xf bound_ctrl:1
	v_perm_b32 v70, v70, v81, v161
	s_nop 1
	v_mov_b32_dpp v71, v70 quad_perm:[2,3,0,1] row_mask:0xf bank_mask:0xf bound_ctrl:1
	v_perm_b32 v70, v71, v70, v163
	global_store_dword v[68:69], v70, off offset:256
	s_cmpk_lt_i32 s4, 0x200
	s_cselect_b64 s[30:31], -1, 0
	s_cmpk_gt_i32 s4, 0x1ff
	s_cbranch_scc0 .LBB0_518

; __device__ __forceinline__ u32x4 pack8(const f32x4 a, const f32x4 b) { u32x4 w; w.x = cvt_pk_bf16(a[0], a[1]); w.y = cvt_pk_bf16(a[2], a[3]); w.z = cvt_pk_bf16(b[0], b[1]); w.w = cvt_pk_bf16(b[2], b[3]); return w; }
;     __device__ __forceinline__ void operator()(const f32x4 (&acc)[2][2][4][2], const Unit& u, int wr, int wc, int fr_in, int fq_in) const {
;     ...
;         for (int bj = 0; bj < 2; ++bj) {
;             const int colg = u.pn * BM + bj * HALF + wc * 32; bf16_t* dst = colg < 512 ? kn + colg : v + (colg - 512);
; #pragma unroll
;             for (int ai = 0; ai < 2; ++ai)
; #pragma unroll
;                 for (int m = 0; m < 4; ++m) {
;                     const int row = row0 + ai * HALF + m * 16; const float r = t[ai * 64 + m * 16 + fr];
;                     if (!(f8qk && colg < 512) && !(f8pv && colg >= 512)) *(u32x4*)(dst + (size_t)row * 512 + 8 * fq) = pack8(acc[ai][bj][m][0] * r, acc[ai][bj][m][1] * r);
;                     if (f8pv && colg >= 512) {
;                         const int c0_ = colg - 512 + 8 * fq, bb_ = row >> 13, pos_ = row & (SEQ_ - 1), key_ = pos_ & 63, k32_ = key_ & 31;
;                         unsigned char* p_ = ws + WS_V8T + ((((size_t)(bb_ * 8 + (c0_ >> 6)) * 128 + (pos_ >> 6)) * 64 + (c0_ & 63)) * 64) + 32 * ((k32_ >> 2) & 1) + 16 * (key_ >> 5) + (k32_ & 3) + 4 * (k32_ >> 3);
;                         const unsigned w0_ = pack4_fp8_x8(acc[ai][bj][m][0] * r), w1_ = pack4_fp8_x8(acc[ai][bj][m][1] * r);
;                         const int qi_ = fr & 3; unsigned char* pb_ = p_ - qi_;
;                         *(unsigned*)(pb_ + qi_ * 64) = quad_tr4(w0_, qi_); *(unsigned*)(pb_ + (4 + qi_) * 64) = quad_tr4(w1_, qi_);
;                     }
;                     if (f8qk && colg < 512) { u32x2 w8; w8.x = pack4_fp8_x8(acc[ai][bj][m][0] * r); w8.y = pack4_fp8_x8(acc[ai][bj][m][1] * r); *(u32x2*)(ws + WS_KN8 + (size_t)row * 512 + colg + 8 * fq) = w8; }
.LBB0_503:
	s_waitcnt lgkmcnt(0)
	v_pk_mul_f32 v[62:63], v[54:55], v[124:125] op_sel_hi:[1,0]
	v_add_u32_e32 v58, v125, v67
	v_mul_f32_e32 v62, 0x41000000, v62
	v_mul_f32_e32 v63, 0x41000000, v63
	v_med3_f32 v62, v62, s64, v250
	v_med3_f32 v63, v63, s64, v250
	v_ashrrev_i32_e32 v59, 31, v58
	v_cvt_pk_fp8_f32 v64, v62, v63
	v_lshlrev_b64 v[58:59], 13, v[58:59]
	v_pk_mul_f32 v[60:61], v[56:57], v[124:125] op_sel_hi:[1,0]
	v_pk_mul_f32 v[62:63], v[50:51], v[124:125] op_sel_hi:[1,0]
	v_and_or_b32 v58, v122, s87, v58
	v_mul_f32_e32 v60, 0x41000000, v60
	v_mul_f32_e32 v61, 0x41000000, v61
	v_mul_f32_e32 v62, 0x41000000, v62
	v_mul_f32_e32 v63, 0x41000000, v63
	v_or_b32_e32 v58, v58, v66
	v_med3_f32 v60, v60, s64, v250
	v_med3_f32 v61, v61, s64, v250
	v_med3_f32 v62, v62, s64, v250
	v_med3_f32 v63, v63, s64, v250
	v_lshlrev_b64 v[58:59], 6, v[58:59]
	v_cvt_pk_fp8_f32 v64, v60, v61 op_sel:[0,0,1]
	v_cvt_pk_fp8_f32 v65, v62, v63
	v_lshl_add_u64 v[58:59], s[20:21], 0, v[58:59]
	v_pk_mul_f32 v[60:61], v[52:53], v[124:125] op_sel_hi:[1,0]
	v_lshl_add_u64 v[58:59], v[58:59], 0, v[0:1]
	v_mov_b32_e32 v129, v1
	v_mul_f32_e32 v60, 0x41000000, v60
	v_mul_f32_e32 v61, 0x41000000, v61
	v_lshl_add_u64 v[58:59], v[58:59], 0, v[128:129]
	v_med3_f32 v60, v60, s64, v250
	v_med3_f32 v61, v61, s64, v250
	v_lshl_add_u64 v[58:59], v[58:59], 0, v[146:147]
	v_mov_b32_e32 v127, v1
	v_cvt_pk_fp8_f32 v65, v60, v61 op_sel:[0,0,1]
	v_mov_b32_dpp v60, v64 quad_perm:[1,0,3,2] row_mask:0xf bank_mask:0xf bound_ctrl:1
	v_lshl_add_u64 v[58:59], v[58:59], 0, v[126:127]
	v_perm_b32 v60, v60, v64, v161
	v_lshl_add_u64 v[58:59], v[58:59], 0, v[144:145]
	v_lshl_add_u64 v[58:59], v[58:59], 0, v[148:149]
	v_mov_b32_dpp v61, v60 quad_perm:[2,3,0,1] row_mask:0xf bank_mask:0xf bound_ctrl:1
	v_perm_b32 v60, v61, v60, v163
	global_store_dword v[58:59], v60, off
	s_nop 0
	v_mov_b32_dpp v60, v65 quad_perm:[1,0,3,2] row_mask:0xf bank_mask:0xf bound_ctrl:1
	v_perm_b32 v60, v60, v65, v161
	s_nop 1
	v_mov_b32_dpp v61, v60 quad_perm:[2,3,0,1] row_mask:0xf bank_mask:0xf bound_ctrl:1
	v_perm_b32 v60, v61, v60, v163
	global_store_dword v[58:59], v60, off offset:256
	v_cndmask_b32_e64 v58, 0, 1, s[30:31]
	v_cmp_ne_u32_e64 s[6:7], 1, v58
	s_andn2_b64 vcc, exec, s[30:31]
	s_cbranch_vccz .LBB0_520

; __device__ __forceinline__ u32x4 pack8(const f32x4 a, const f32x4 b) { u32x4 w; w.x = cvt_pk_bf16(a[0], a[1]); w.y = cvt_pk_bf16(a[2], a[3]); w.z = cvt_pk_bf16(b[0], b[1]); w.w = cvt_pk_bf16(b[2], b[3]); return w; }
;     __device__ __forceinline__ void operator()(const f32x4 (&acc)[2][2][4][2], const Unit& u, int wr, int wc, int fr_in, int fq_in) const {
;     ...
;         for (int bj = 0; bj < 2; ++bj) {
;             const int colg = u.pn * BM + bj * HALF + wc * 32; bf16_t* dst = colg < 512 ? kn + colg : v + (colg - 512);
; #pragma unroll
;             for (int ai = 0; ai < 2; ++ai)
; #pragma unroll
;                 for (int m = 0; m < 4; ++m) {
;                     const int row = row0 + ai * HALF + m * 16; const float r = t[ai * 64 + m * 16 + fr];
;                     if (!(f8qk && colg < 512) && !(f8pv && colg >= 512)) *(u32x4*)(dst + (size_t)row * 512 + 8 * fq) = pack8(acc[ai][bj][m][0] * r, acc[ai][bj][m][1] * r);
;                     if (f8pv && colg >= 512) {
;                         const int c0_ = colg - 512 + 8 * fq, bb_ = row >> 13, pos_ = row & (SEQ_ - 1), key_ = pos_ & 63, k32_ = key_ & 31;
;                         unsigned char* p_ = ws + WS_V8T + ((((size_t)(bb_ * 8 + (c0_ >> 6)) * 128 + (pos_ >> 6)) * 64 + (c0_ & 63)) * 64) + 32 * ((k32_ >> 2) & 1) + 16 * (key_ >> 5) + (k32_ & 3) + 4 * (k32_ >> 3);
;                         const unsigned w0_ = pack4_fp8_x8(acc[ai][bj][m][0] * r), w1_ = pack4_fp8_x8(acc[ai][bj][m][1] * r);
;                         const int qi_ = fr & 3; unsigned char* pb_ = p_ - qi_;
;                         *(unsigned*)(pb_ + qi_ * 64) = quad_tr4(w0_, qi_); *(unsigned*)(pb_ + (4 + qi_) * 64) = quad_tr4(w1_, qi_);
;                     }
;                     if (f8qk && colg < 512) { u32x2 w8; w8.x = pack4_fp8_x8(acc[ai][bj][m][0] * r); w8.y = pack4_fp8_x8(acc[ai][bj][m][1] * r); *(u32x2*)(ws + WS_KN8 + (size_t)row * 512 + colg + 8 * fq) = w8; }
.LBB0_505:
	s_waitcnt lgkmcnt(0)
	v_pk_mul_f32 v[54:55], v[46:47], v[116:117] op_sel_hi:[1,0]
	v_add_u32_e32 v50, v117, v67
	v_mul_f32_e32 v54, 0x41000000, v54
	v_mul_f32_e32 v55, 0x41000000, v55
	v_med3_f32 v54, v54, s64, v250
	v_med3_f32 v55, v55, s64, v250
	v_ashrrev_i32_e32 v51, 31, v50
	v_cvt_pk_fp8_f32 v56, v54, v55
	v_lshlrev_b64 v[50:51], 13, v[50:51]
	v_pk_mul_f32 v[52:53], v[48:49], v[116:117] op_sel_hi:[1,0]
	v_pk_mul_f32 v[54:55], v[42:43], v[116:117] op_sel_hi:[1,0]
	v_and_or_b32 v50, v114, s87, v50
	v_mul_f32_e32 v52, 0x41000000, v52
	v_mul_f32_e32 v53, 0x41000000, v53
	v_mul_f32_e32 v54, 0x41000000, v54
	v_mul_f32_e32 v55, 0x41000000, v55
	v_or_b32_e32 v50, v50, v66
	v_med3_f32 v52, v52, s64, v250
	v_med3_f32 v53, v53, s64, v250
	v_med3_f32 v54, v54, s64, v250
	v_med3_f32 v55, v55, s64, v250
	v_lshlrev_b64 v[50:51], 6, v[50:51]
	v_cvt_pk_fp8_f32 v56, v52, v53 op_sel:[0,0,1]
	v_cvt_pk_fp8_f32 v57, v54, v55
	v_lshl_add_u64 v[50:51], s[20:21], 0, v[50:51]
	v_pk_mul_f32 v[52:53], v[44:45], v[116:117] op_sel_hi:[1,0]
	v_lshl_add_u64 v[50:51], v[50:51], 0, v[0:1]
	v_mov_b32_e32 v121, v1
	v_mul_f32_e32 v52, 0x41000000, v52
	v_mul_f32_e32 v53, 0x41000000, v53
	v_lshl_add_u64 v[50:51], v[50:51], 0, v[120:121]
	v_med3_f32 v52, v52, s64, v250
	v_med3_f32 v53, v53, s64, v250
	v_lshl_add_u64 v[50:51], v[50:51], 0, v[146:147]
	v_mov_b32_e32 v119, v1
	v_cvt_pk_fp8_f32 v57, v52, v53 op_sel:[0,0,1]
	v_mov_b32_dpp v52, v56 quad_perm:[1,0,3,2] row_mask:0xf bank_mask:0xf bound_ctrl:1
	v_lshl_add_u64 v[50:51], v[50:51], 0, v[118:119]
	v_perm_b32 v52, v52, v56, v161
	v_lshl_add_u64 v[50:51], v[50:51], 0, v[144:145]
	v_lshl_add_u64 v[50:51], v[50:51], 0, v[148:149]
	v_mov_b32_dpp v53, v52 quad_perm:[2,3,0,1] row_mask:0xf bank_mask:0xf bound_ctrl:1
	v_perm_b32 v52, v53, v52, v163
	global_store_dword v[50:51], v52, off
	s_nop 0
	v_mov_b32_dpp v52, v57 quad_perm:[1,0,3,2] row_mask:0xf bank_mask:0xf bound_ctrl:1
	v_perm_b32 v52, v52, v57, v161
	s_nop 1
	v_mov_b32_dpp v53, v52 quad_perm:[2,3,0,1] row_mask:0xf bank_mask:0xf bound_ctrl:1
	v_perm_b32 v52, v53, v52, v163
	global_store_dword v[50:51], v52, off offset:256
	s_and_b64 vcc, exec, s[6:7]
	s_cbranch_vccz .LBB0_522

; __device__ __forceinline__ u32x4 pack8(const f32x4 a, const f32x4 b) { u32x4 w; w.x = cvt_pk_bf16(a[0], a[1]); w.y = cvt_pk_bf16(a[2], a[3]); w.z = cvt_pk_bf16(b[0], b[1]); w.w = cvt_pk_bf16(b[2], b[3]); return w; }
;     __device__ __forceinline__ void operator()(const f32x4 (&acc)[2][2][4][2], const Unit& u, int wr, int wc, int fr_in, int fq_in) const {
;     ...
;         for (int bj = 0; bj < 2; ++bj) {
;             const int colg = u.pn * BM + bj * HALF + wc * 32; bf16_t* dst = colg < 512 ? kn + colg : v + (colg - 512);
; #pragma unroll
;             for (int ai = 0; ai < 2; ++ai)
; #pragma unroll
;                 for (int m = 0; m < 4; ++m) {
;                     const int row = row0 + ai * HALF + m * 16; const float r = t[ai * 64 + m * 16 + fr];
;                     if (!(f8qk && colg < 512) && !(f8pv && colg >= 512)) *(u32x4*)(dst + (size_t)row * 512 + 8 * fq) = pack8(acc[ai][bj][m][0] * r, acc[ai][bj][m][1] * r);
;                     if (f8pv && colg >= 512) {
;                         const int c0_ = colg - 512 + 8 * fq, bb_ = row >> 13, pos_ = row & (SEQ_ - 1), key_ = pos_ & 63, k32_ = key_ & 31;
;                         unsigned char* p_ = ws + WS_V8T + ((((size_t)(bb_ * 8 + (c0_ >> 6)) * 128 + (pos_ >> 6)) * 64 + (c0_ & 63)) * 64) + 32 * ((k32_ >> 2) & 1) + 16 * (key_ >> 5) + (k32_ & 3) + 4 * (k32_ >> 3);
;                         const unsigned w0_ = pack4_fp8_x8(acc[ai][bj][m][0] * r), w1_ = pack4_fp8_x8(acc[ai][bj][m][1] * r);
;                         const int qi_ = fr & 3; unsigned char* pb_ = p_ - qi_;
;                         *(unsigned*)(pb_ + qi_ * 64) = quad_tr4(w0_, qi_); *(unsigned*)(pb_ + (4 + qi_) * 64) = quad_tr4(w1_, qi_);
;                     }
;                     if (f8qk && colg < 512) { u32x2 w8; w8.x = pack4_fp8_x8(acc[ai][bj][m][0] * r); w8.y = pack4_fp8_x8(acc[ai][bj][m][1] * r); *(u32x2*)(ws + WS_KN8 + (size_t)row * 512 + colg + 8 * fq) = w8; }
.LBB0_507:
	s_waitcnt lgkmcnt(0)
	v_pk_mul_f32 v[46:47], v[38:39], v[108:109] op_sel_hi:[1,0]
	v_add_u32_e32 v42, v109, v67
	v_mul_f32_e32 v46, 0x41000000, v46
	v_mul_f32_e32 v47, 0x41000000, v47
	v_med3_f32 v46, v46, s64, v250
	v_med3_f32 v47, v47, s64, v250
	v_ashrrev_i32_e32 v43, 31, v42
	v_cvt_pk_fp8_f32 v48, v46, v47
	v_lshlrev_b64 v[42:43], 13, v[42:43]
	v_pk_mul_f32 v[44:45], v[40:41], v[108:109] op_sel_hi:[1,0]
	v_pk_mul_f32 v[46:47], v[34:35], v[108:109] op_sel_hi:[1,0]
	v_and_or_b32 v42, v106, s87, v42
	v_mul_f32_e32 v44, 0x41000000, v44
	v_mul_f32_e32 v45, 0x41000000, v45
	v_mul_f32_e32 v46, 0x41000000, v46
	v_mul_f32_e32 v47, 0x41000000, v47
	v_or_b32_e32 v42, v42, v66
	v_med3_f32 v44, v44, s64, v250
	v_med3_f32 v45, v45, s64, v250
	v_med3_f32 v46, v46, s64, v250
	v_med3_f32 v47, v47, s64, v250
	v_lshlrev_b64 v[42:43], 6, v[42:43]
	v_cvt_pk_fp8_f32 v48, v44, v45 op_sel:[0,0,1]
	v_cvt_pk_fp8_f32 v49, v46, v47
	v_lshl_add_u64 v[42:43], s[20:21], 0, v[42:43]
	v_pk_mul_f32 v[44:45], v[36:37], v[108:109] op_sel_hi:[1,0]
	v_lshl_add_u64 v[42:43], v[42:43], 0, v[0:1]
	v_mov_b32_e32 v113, v1
	v_mul_f32_e32 v44, 0x41000000, v44
	v_mul_f32_e32 v45, 0x41000000, v45
	v_lshl_add_u64 v[42:43], v[42:43], 0, v[112:113]
	v_med3_f32 v44, v44, s64, v250
	v_med3_f32 v45, v45, s64, v250
	v_lshl_add_u64 v[42:43], v[42:43], 0, v[146:147]
	v_mov_b32_e32 v111, v1
	v_cvt_pk_fp8_f32 v49, v44, v45 op_sel:[0,0,1]
	v_mov_b32_dpp v44, v48 quad_perm:[1,0,3,2] row_mask:0xf bank_mask:0xf bound_ctrl:1
	v_lshl_add_u64 v[42:43], v[42:43], 0, v[110:111]
	v_perm_b32 v44, v44, v48, v161
	v_lshl_add_u64 v[42:43], v[42:43], 0, v[144:145]
	v_lshl_add_u64 v[42:43], v[42:43], 0, v[148:149]
	v_mov_b32_dpp v45, v44 quad_perm:[2,3,0,1] row_mask:0xf bank_mask:0xf bound_ctrl:1
	v_perm_b32 v44, v45, v44, v163
	global_store_dword v[42:43], v44, off
	s_nop 0
	v_mov_b32_dpp v44, v49 quad_perm:[1,0,3,2] row_mask:0xf bank_mask:0xf bound_ctrl:1
	v_perm_b32 v44, v44, v49, v161
	s_nop 1
	v_mov_b32_dpp v45, v44 quad_perm:[2,3,0,1] row_mask:0xf bank_mask:0xf bound_ctrl:1
	v_perm_b32 v44, v45, v44, v163
	global_store_dword v[42:43], v44, off offset:256
	s_and_b64 vcc, exec, s[6:7]
	s_cbranch_vccz .LBB0_524

; __device__ __forceinline__ u32x4 pack8(const f32x4 a, const f32x4 b) { u32x4 w; w.x = cvt_pk_bf16(a[0], a[1]); w.y = cvt_pk_bf16(a[2], a[3]); w.z = cvt_pk_bf16(b[0], b[1]); w.w = cvt_pk_bf16(b[2], b[3]); return w; }
;     __device__ __forceinline__ void operator()(const f32x4 (&acc)[2][2][4][2], const Unit& u, int wr, int wc, int fr_in, int fq_in) const {
;     ...
;         for (int bj = 0; bj < 2; ++bj) {
;             const int colg = u.pn * BM + bj * HALF + wc * 32; bf16_t* dst = colg < 512 ? kn + colg : v + (colg - 512);
; #pragma unroll
;             for (int ai = 0; ai < 2; ++ai)
; #pragma unroll
;                 for (int m = 0; m < 4; ++m) {
;                     const int row = row0 + ai * HALF + m * 16; const float r = t[ai * 64 + m * 16 + fr];
;                     if (!(f8qk && colg < 512) && !(f8pv && colg >= 512)) *(u32x4*)(dst + (size_t)row * 512 + 8 * fq) = pack8(acc[ai][bj][m][0] * r, acc[ai][bj][m][1] * r);
;                     if (f8pv && colg >= 512) {
;                         const int c0_ = colg - 512 + 8 * fq, bb_ = row >> 13, pos_ = row & (SEQ_ - 1), key_ = pos_ & 63, k32_ = key_ & 31;
;                         unsigned char* p_ = ws + WS_V8T + ((((size_t)(bb_ * 8 + (c0_ >> 6)) * 128 + (pos_ >> 6)) * 64 + (c0_ & 63)) * 64) + 32 * ((k32_ >> 2) & 1) + 16 * (key_ >> 5) + (k32_ & 3) + 4 * (k32_ >> 3);
;                         const unsigned w0_ = pack4_fp8_x8(acc[ai][bj][m][0] * r), w1_ = pack4_fp8_x8(acc[ai][bj][m][1] * r);
;                         const int qi_ = fr & 3; unsigned char* pb_ = p_ - qi_;
;                         *(unsigned*)(pb_ + qi_ * 64) = quad_tr4(w0_, qi_); *(unsigned*)(pb_ + (4 + qi_) * 64) = quad_tr4(w1_, qi_);
;                     }
;                     if (f8qk && colg < 512) { u32x2 w8; w8.x = pack4_fp8_x8(acc[ai][bj][m][0] * r); w8.y = pack4_fp8_x8(acc[ai][bj][m][1] * r); *(u32x2*)(ws + WS_KN8 + (size_t)row * 512 + colg + 8 * fq) = w8; }
.LBB0_509:
	s_waitcnt lgkmcnt(0)
	v_pk_mul_f32 v[38:39], v[30:31], v[100:101] op_sel_hi:[1,0]
	v_add_u32_e32 v34, v101, v67
	v_mul_f32_e32 v38, 0x41000000, v38
	v_mul_f32_e32 v39, 0x41000000, v39
	v_med3_f32 v38, v38, s64, v250
	v_med3_f32 v39, v39, s64, v250
	v_ashrrev_i32_e32 v35, 31, v34
	v_cvt_pk_fp8_f32 v40, v38, v39
	v_lshlrev_b64 v[34:35], 13, v[34:35]
	v_pk_mul_f32 v[36:37], v[32:33], v[100:101] op_sel_hi:[1,0]
	v_pk_mul_f32 v[38:39], v[26:27], v[100:101] op_sel_hi:[1,0]
	v_and_or_b32 v34, v98, s87, v34
	v_mul_f32_e32 v36, 0x41000000, v36
	v_mul_f32_e32 v37, 0x41000000, v37
	v_mul_f32_e32 v38, 0x41000000, v38
	v_mul_f32_e32 v39, 0x41000000, v39
	v_or_b32_e32 v34, v34, v66
	v_med3_f32 v36, v36, s64, v250
	v_med3_f32 v37, v37, s64, v250
	v_med3_f32 v38, v38, s64, v250
	v_med3_f32 v39, v39, s64, v250
	v_lshlrev_b64 v[34:35], 6, v[34:35]
	v_cvt_pk_fp8_f32 v40, v36, v37 op_sel:[0,0,1]
	v_cvt_pk_fp8_f32 v41, v38, v39
	v_lshl_add_u64 v[34:35], s[20:21], 0, v[34:35]
	v_pk_mul_f32 v[36:37], v[28:29], v[100:101] op_sel_hi:[1,0]
	v_lshl_add_u64 v[34:35], v[34:35], 0, v[0:1]
	v_mov_b32_e32 v105, v1
	v_mul_f32_e32 v36, 0x41000000, v36
	v_mul_f32_e32 v37, 0x41000000, v37
	v_lshl_add_u64 v[34:35], v[34:35], 0, v[104:105]
	v_med3_f32 v36, v36, s64, v250
	v_med3_f32 v37, v37, s64, v250
	v_lshl_add_u64 v[34:35], v[34:35], 0, v[146:147]
	v_mov_b32_e32 v103, v1
	v_cvt_pk_fp8_f32 v41, v36, v37 op_sel:[0,0,1]
	v_mov_b32_dpp v36, v40 quad_perm:[1,0,3,2] row_mask:0xf bank_mask:0xf bound_ctrl:1
	v_lshl_add_u64 v[34:35], v[34:35], 0, v[102:103]
	v_perm_b32 v36, v36, v40, v161
	v_lshl_add_u64 v[34:35], v[34:35], 0, v[144:145]
	v_lshl_add_u64 v[34:35], v[34:35], 0, v[148:149]
	v_mov_b32_dpp v37, v36 quad_perm:[2,3,0,1] row_mask:0xf bank_mask:0xf bound_ctrl:1
	v_perm_b32 v36, v37, v36, v163
	global_store_dword v[34:35], v36, off
	s_nop 0
	v_mov_b32_dpp v36, v41 quad_perm:[1,0,3,2] row_mask:0xf bank_mask:0xf bound_ctrl:1
	v_perm_b32 v36, v36, v41, v161
	s_nop 1
	v_mov_b32_dpp v37, v36 quad_perm:[2,3,0,1] row_mask:0xf bank_mask:0xf bound_ctrl:1
	v_perm_b32 v36, v37, v36, v163
	global_store_dword v[34:35], v36, off offset:256
	s_and_b64 vcc, exec, s[6:7]
	s_cbranch_vccz .LBB0_526

; __device__ __forceinline__ u32x4 pack8(const f32x4 a, const f32x4 b) { u32x4 w; w.x = cvt_pk_bf16(a[0], a[1]); w.y = cvt_pk_bf16(a[2], a[3]); w.z = cvt_pk_bf16(b[0], b[1]); w.w = cvt_pk_bf16(b[2], b[3]); return w; }
;     __device__ __forceinline__ void operator()(const f32x4 (&acc)[2][2][4][2], const Unit& u, int wr, int wc, int fr_in, int fq_in) const {
;     ...
;         for (int bj = 0; bj < 2; ++bj) {
;             const int colg = u.pn * BM + bj * HALF + wc * 32; bf16_t* dst = colg < 512 ? kn + colg : v + (colg - 512);
; #pragma unroll
;             for (int ai = 0; ai < 2; ++ai)
; #pragma unroll
;                 for (int m = 0; m < 4; ++m) {
;                     const int row = row0 + ai * HALF + m * 16; const float r = t[ai * 64 + m * 16 + fr];
;                     if (!(f8qk && colg < 512) && !(f8pv && colg >= 512)) *(u32x4*)(dst + (size_t)row * 512 + 8 * fq) = pack8(acc[ai][bj][m][0] * r, acc[ai][bj][m][1] * r);
;                     if (f8pv && colg >= 512) {
;                         const int c0_ = colg - 512 + 8 * fq, bb_ = row >> 13, pos_ = row & (SEQ_ - 1), key_ = pos_ & 63, k32_ = key_ & 31;
;                         unsigned char* p_ = ws + WS_V8T + ((((size_t)(bb_ * 8 + (c0_ >> 6)) * 128 + (pos_ >> 6)) * 64 + (c0_ & 63)) * 64) + 32 * ((k32_ >> 2) & 1) + 16 * (key_ >> 5) + (k32_ & 3) + 4 * (k32_ >> 3);
;                         const unsigned w0_ = pack4_fp8_x8(acc[ai][bj][m][0] * r), w1_ = pack4_fp8_x8(acc[ai][bj][m][1] * r);
;                         const int qi_ = fr & 3; unsigned char* pb_ = p_ - qi_;
;                         *(unsigned*)(pb_ + qi_ * 64) = quad_tr4(w0_, qi_); *(unsigned*)(pb_ + (4 + qi_) * 64) = quad_tr4(w1_, qi_);
;                     }
;                     if (f8qk && colg < 512) { u32x2 w8; w8.x = pack4_fp8_x8(acc[ai][bj][m][0] * r); w8.y = pack4_fp8_x8(acc[ai][bj][m][1] * r); *(u32x2*)(ws + WS_KN8 + (size_t)row * 512 + colg + 8 * fq) = w8; }
.LBB0_511:
	s_waitcnt lgkmcnt(0)
	v_pk_mul_f32 v[30:31], v[22:23], v[92:93] op_sel_hi:[1,0]
	v_add_u32_e32 v26, v93, v67
	v_mul_f32_e32 v30, 0x41000000, v30
	v_mul_f32_e32 v31, 0x41000000, v31
	v_med3_f32 v30, v30, s64, v250
	v_med3_f32 v31, v31, s64, v250
	v_ashrrev_i32_e32 v27, 31, v26
	v_cvt_pk_fp8_f32 v32, v30, v31
	v_lshlrev_b64 v[26:27], 13, v[26:27]
	v_pk_mul_f32 v[28:29], v[24:25], v[92:93] op_sel_hi:[1,0]
	v_pk_mul_f32 v[30:31], v[18:19], v[92:93] op_sel_hi:[1,0]
	v_and_or_b32 v26, v90, s87, v26
	v_mul_f32_e32 v28, 0x41000000, v28
	v_mul_f32_e32 v29, 0x41000000, v29
	v_mul_f32_e32 v30, 0x41000000, v30
	v_mul_f32_e32 v31, 0x41000000, v31
	v_or_b32_e32 v26, v26, v66
	v_med3_f32 v28, v28, s64, v250
	v_med3_f32 v29, v29, s64, v250
	v_med3_f32 v30, v30, s64, v250
	v_med3_f32 v31, v31, s64, v250
	v_lshlrev_b64 v[26:27], 6, v[26:27]
	v_cvt_pk_fp8_f32 v32, v28, v29 op_sel:[0,0,1]
	v_cvt_pk_fp8_f32 v33, v30, v31
	v_lshl_add_u64 v[26:27], s[20:21], 0, v[26:27]
	v_pk_mul_f32 v[28:29], v[20:21], v[92:93] op_sel_hi:[1,0]
	v_lshl_add_u64 v[26:27], v[26:27], 0, v[0:1]
	v_mov_b32_e32 v97, v1
	v_mul_f32_e32 v28, 0x41000000, v28
	v_mul_f32_e32 v29, 0x41000000, v29
	v_lshl_add_u64 v[26:27], v[26:27], 0, v[96:97]
	v_med3_f32 v28, v28, s64, v250
	v_med3_f32 v29, v29, s64, v250
	v_lshl_add_u64 v[26:27], v[26:27], 0, v[146:147]
	v_mov_b32_e32 v95, v1
	v_cvt_pk_fp8_f32 v33, v28, v29 op_sel:[0,0,1]
	v_mov_b32_dpp v28, v32 quad_perm:[1,0,3,2] row_mask:0xf bank_mask:0xf bound_ctrl:1
	v_lshl_add_u64 v[26:27], v[26:27], 0, v[94:95]
	v_perm_b32 v28, v28, v32, v161
	v_lshl_add_u64 v[26:27], v[26:27], 0, v[144:145]
	v_lshl_add_u64 v[26:27], v[26:27], 0, v[148:149]
	v_mov_b32_dpp v29, v28 quad_perm:[2,3,0,1] row_mask:0xf bank_mask:0xf bound_ctrl:1
	v_perm_b32 v28, v29, v28, v163
	global_store_dword v[26:27], v28, off
	s_nop 0
	v_mov_b32_dpp v28, v33 quad_perm:[1,0,3,2] row_mask:0xf bank_mask:0xf bound_ctrl:1
	v_perm_b32 v28, v28, v33, v161
	s_nop 1
	v_mov_b32_dpp v29, v28 quad_perm:[2,3,0,1] row_mask:0xf bank_mask:0xf bound_ctrl:1
	v_perm_b32 v28, v29, v28, v163
	global_store_dword v[26:27], v28, off offset:256
	s_and_b64 vcc, exec, s[6:7]
	s_cbranch_vccz .LBB0_528

; __device__ __forceinline__ u32x4 pack8(const f32x4 a, const f32x4 b) { u32x4 w; w.x = cvt_pk_bf16(a[0], a[1]); w.y = cvt_pk_bf16(a[2], a[3]); w.z = cvt_pk_bf16(b[0], b[1]); w.w = cvt_pk_bf16(b[2], b[3]); return w; }
;     __device__ __forceinline__ void operator()(const f32x4 (&acc)[2][2][4][2], const Unit& u, int wr, int wc, int fr_in, int fq_in) const {
;     ...
;         for (int bj = 0; bj < 2; ++bj) {
;             const int colg = u.pn * BM + bj * HALF + wc * 32; bf16_t* dst = colg < 512 ? kn + colg : v + (colg - 512);
; #pragma unroll
;             for (int ai = 0; ai < 2; ++ai)
; #pragma unroll
;                 for (int m = 0; m < 4; ++m) {
;                     const int row = row0 + ai * HALF + m * 16; const float r = t[ai * 64 + m * 16 + fr];
;                     if (!(f8qk && colg < 512) && !(f8pv && colg >= 512)) *(u32x4*)(dst + (size_t)row * 512 + 8 * fq) = pack8(acc[ai][bj][m][0] * r, acc[ai][bj][m][1] * r);
;                     if (f8pv && colg >= 512) {
;                         const int c0_ = colg - 512 + 8 * fq, bb_ = row >> 13, pos_ = row & (SEQ_ - 1), key_ = pos_ & 63, k32_ = key_ & 31;
;                         unsigned char* p_ = ws + WS_V8T + ((((size_t)(bb_ * 8 + (c0_ >> 6)) * 128 + (pos_ >> 6)) * 64 + (c0_ & 63)) * 64) + 32 * ((k32_ >> 2) & 1) + 16 * (key_ >> 5) + (k32_ & 3) + 4 * (k32_ >> 3);
;                         const unsigned w0_ = pack4_fp8_x8(acc[ai][bj][m][0] * r), w1_ = pack4_fp8_x8(acc[ai][bj][m][1] * r);
;                         const int qi_ = fr & 3; unsigned char* pb_ = p_ - qi_;
;                         *(unsigned*)(pb_ + qi_ * 64) = quad_tr4(w0_, qi_); *(unsigned*)(pb_ + (4 + qi_) * 64) = quad_tr4(w1_, qi_);
;                     }
;                     if (f8qk && colg < 512) { u32x2 w8; w8.x = pack4_fp8_x8(acc[ai][bj][m][0] * r); w8.y = pack4_fp8_x8(acc[ai][bj][m][1] * r); *(u32x2*)(ws + WS_KN8 + (size_t)row * 512 + colg + 8 * fq) = w8; }
.LBB0_513:
	s_waitcnt lgkmcnt(0)
	v_pk_mul_f32 v[22:23], v[14:15], v[84:85] op_sel_hi:[1,0]
	v_add_u32_e32 v18, v85, v67
	v_mul_f32_e32 v22, 0x41000000, v22
	v_mul_f32_e32 v23, 0x41000000, v23
	v_med3_f32 v22, v22, s64, v250
	v_med3_f32 v23, v23, s64, v250
	v_ashrrev_i32_e32 v19, 31, v18
	v_cvt_pk_fp8_f32 v24, v22, v23
	v_lshlrev_b64 v[18:19], 13, v[18:19]
	v_pk_mul_f32 v[20:21], v[16:17], v[84:85] op_sel_hi:[1,0]
	v_pk_mul_f32 v[22:23], v[10:11], v[84:85] op_sel_hi:[1,0]
	v_and_or_b32 v18, v82, s87, v18
	v_mul_f32_e32 v20, 0x41000000, v20
	v_mul_f32_e32 v21, 0x41000000, v21
	v_mul_f32_e32 v22, 0x41000000, v22
	v_mul_f32_e32 v23, 0x41000000, v23
	v_or_b32_e32 v18, v18, v66
	v_med3_f32 v20, v20, s64, v250
	v_med3_f32 v21, v21, s64, v250
	v_med3_f32 v22, v22, s64, v250
	v_med3_f32 v23, v23, s64, v250
	v_lshlrev_b64 v[18:19], 6, v[18:19]
	v_cvt_pk_fp8_f32 v24, v20, v21 op_sel:[0,0,1]
	v_cvt_pk_fp8_f32 v25, v22, v23
	v_lshl_add_u64 v[18:19], s[20:21], 0, v[18:19]
	v_pk_mul_f32 v[20:21], v[12:13], v[84:85] op_sel_hi:[1,0]
	v_lshl_add_u64 v[18:19], v[18:19], 0, v[0:1]
	v_mov_b32_e32 v89, v1
	v_mul_f32_e32 v20, 0x41000000, v20
	v_mul_f32_e32 v21, 0x41000000, v21
	v_lshl_add_u64 v[18:19], v[18:19], 0, v[88:89]
	v_med3_f32 v20, v20, s64, v250
	v_med3_f32 v21, v21, s64, v250
	v_lshl_add_u64 v[18:19], v[18:19], 0, v[146:147]
	v_mov_b32_e32 v87, v1
	v_cvt_pk_fp8_f32 v25, v20, v21 op_sel:[0,0,1]
	v_mov_b32_dpp v20, v24 quad_perm:[1,0,3,2] row_mask:0xf bank_mask:0xf bound_ctrl:1
	v_lshl_add_u64 v[18:19], v[18:19], 0, v[86:87]
	v_perm_b32 v20, v20, v24, v161
	v_lshl_add_u64 v[18:19], v[18:19], 0, v[144:145]
	v_lshl_add_u64 v[18:19], v[18:19], 0, v[148:149]
	v_mov_b32_dpp v21, v20 quad_perm:[2,3,0,1] row_mask:0xf bank_mask:0xf bound_ctrl:1
	v_perm_b32 v20, v21, v20, v163
	global_store_dword v[18:19], v20, off
	s_nop 0
	v_mov_b32_dpp v20, v25 quad_perm:[1,0,3,2] row_mask:0xf bank_mask:0xf bound_ctrl:1
	v_perm_b32 v20, v20, v25, v161
	s_nop 1
	v_mov_b32_dpp v21, v20 quad_perm:[2,3,0,1] row_mask:0xf bank_mask:0xf bound_ctrl:1
	v_perm_b32 v20, v21, v20, v163
	global_store_dword v[18:19], v20, off offset:256
	s_and_b64 vcc, exec, s[6:7]
	s_cbranch_vccz .LBB0_530

; __device__ __forceinline__ u32x4 pack8(const f32x4 a, const f32x4 b) { u32x4 w; w.x = cvt_pk_bf16(a[0], a[1]); w.y = cvt_pk_bf16(a[2], a[3]); w.z = cvt_pk_bf16(b[0], b[1]); w.w = cvt_pk_bf16(b[2], b[3]); return w; }
;     __device__ __forceinline__ void operator()(const f32x4 (&acc)[2][2][4][2], const Unit& u, int wr, int wc, int fr_in, int fq_in) const {
;     ...
;         for (int bj = 0; bj < 2; ++bj) {
;             const int colg = u.pn * BM + bj * HALF + wc * 32; bf16_t* dst = colg < 512 ? kn + colg : v + (colg - 512);
; #pragma unroll
;             for (int ai = 0; ai < 2; ++ai)
; #pragma unroll
;                 for (int m = 0; m < 4; ++m) {
;                     const int row = row0 + ai * HALF + m * 16; const float r = t[ai * 64 + m * 16 + fr];
;                     if (!(f8qk && colg < 512) && !(f8pv && colg >= 512)) *(u32x4*)(dst + (size_t)row * 512 + 8 * fq) = pack8(acc[ai][bj][m][0] * r, acc[ai][bj][m][1] * r);
;                     if (f8pv && colg >= 512) {
;                         const int c0_ = colg - 512 + 8 * fq, bb_ = row >> 13, pos_ = row & (SEQ_ - 1), key_ = pos_ & 63, k32_ = key_ & 31;
;                         unsigned char* p_ = ws + WS_V8T + ((((size_t)(bb_ * 8 + (c0_ >> 6)) * 128 + (pos_ >> 6)) * 64 + (c0_ & 63)) * 64) + 32 * ((k32_ >> 2) & 1) + 16 * (key_ >> 5) + (k32_ & 3) + 4 * (k32_ >> 3);
;                         const unsigned w0_ = pack4_fp8_x8(acc[ai][bj][m][0] * r), w1_ = pack4_fp8_x8(acc[ai][bj][m][1] * r);
;                         const int qi_ = fr & 3; unsigned char* pb_ = p_ - qi_;
;                         *(unsigned*)(pb_ + qi_ * 64) = quad_tr4(w0_, qi_); *(unsigned*)(pb_ + (4 + qi_) * 64) = quad_tr4(w1_, qi_);
;                     }
;                     if (f8qk && colg < 512) { u32x2 w8; w8.x = pack4_fp8_x8(acc[ai][bj][m][0] * r); w8.y = pack4_fp8_x8(acc[ai][bj][m][1] * r); *(u32x2*)(ws + WS_KN8 + (size_t)row * 512 + colg + 8 * fq) = w8; }
.LBB0_515:
	v_add_u32_e32 v10, v77, v67
	v_ashrrev_i32_e32 v11, 31, v10
	v_lshlrev_b64 v[10:11], 13, v[10:11]
	v_and_or_b32 v10, v74, s87, v10
	v_or_b32_e32 v10, v10, v66
	v_lshlrev_b64 v[10:11], 6, v[10:11]
	v_lshl_add_u64 v[10:11], s[20:21], 0, v[10:11]
	s_waitcnt lgkmcnt(0)
	v_pk_mul_f32 v[14:15], v[6:7], v[76:77] op_sel_hi:[1,0]
	v_lshl_add_u64 v[10:11], v[10:11], 0, v[0:1]
	v_mul_f32_e32 v0, 0x41000000, v14
	v_mul_f32_e32 v14, 0x41000000, v15
	v_med3_f32 v0, v0, s64, v250
	v_med3_f32 v14, v14, s64, v250
	v_cvt_pk_fp8_f32 v16, v0, v14
	v_pk_mul_f32 v[12:13], v[8:9], v[76:77] op_sel_hi:[1,0]
	v_pk_mul_f32 v[14:15], v[2:3], v[76:77] op_sel_hi:[1,0]
	v_mul_f32_e32 v0, 0x41000000, v12
	v_mul_f32_e32 v12, 0x41000000, v13
	v_med3_f32 v0, v0, s64, v250
	v_med3_f32 v12, v12, s64, v250
	v_cvt_pk_fp8_f32 v16, v0, v12 op_sel:[0,0,1]
	v_mul_f32_e32 v0, 0x41000000, v14
	v_mul_f32_e32 v14, 0x41000000, v15
	v_med3_f32 v0, v0, s64, v250
	v_med3_f32 v14, v14, s64, v250
	v_cvt_pk_fp8_f32 v15, v0, v14
	v_pk_mul_f32 v[12:13], v[4:5], v[76:77] op_sel_hi:[1,0]
	v_mov_b32_e32 v81, v1
	v_mul_f32_e32 v0, 0x41000000, v12
	v_mul_f32_e32 v12, 0x41000000, v13
	v_lshl_add_u64 v[10:11], v[10:11], 0, v[80:81]
	v_med3_f32 v0, v0, s64, v250
	v_med3_f32 v12, v12, s64, v250
	v_lshl_add_u64 v[10:11], v[10:11], 0, v[146:147]
	v_mov_b32_e32 v79, v1
	v_cvt_pk_fp8_f32 v15, v0, v12 op_sel:[0,0,1]
	v_mov_b32_dpp v0, v16 quad_perm:[1,0,3,2] row_mask:0xf bank_mask:0xf bound_ctrl:1
	v_lshl_add_u64 v[10:11], v[10:11], 0, v[78:79]
	v_perm_b32 v0, v0, v16, v161
	v_lshl_add_u64 v[10:11], v[10:11], 0, v[144:145]
	v_lshl_add_u64 v[10:11], v[10:11], 0, v[148:149]
	v_mov_b32_dpp v12, v0 quad_perm:[2,3,0,1] row_mask:0xf bank_mask:0xf bound_ctrl:1
	v_perm_b32 v0, v12, v0, v163
	global_store_dword v[10:11], v0, off
	s_nop 0
	v_mov_b32_dpp v0, v15 quad_perm:[1,0,3,2] row_mask:0xf bank_mask:0xf bound_ctrl:1
	v_perm_b32 v0, v0, v15, v161
	s_nop 1
	v_mov_b32_dpp v12, v0 quad_perm:[2,3,0,1] row_mask:0xf bank_mask:0xf bound_ctrl:1
	v_perm_b32 v0, v12, v0, v163
	global_store_dword v[10:11], v0, off offset:256
	s_and_b64 vcc, exec, s[6:7]
	s_cbranch_vccz .LBB0_532

; __device__ __forceinline__ u32x4 pack8(const f32x4 a, const f32x4 b) { u32x4 w; w.x = cvt_pk_bf16(a[0], a[1]); w.y = cvt_pk_bf16(a[2], a[3]); w.z = cvt_pk_bf16(b[0], b[1]); w.w = cvt_pk_bf16(b[2], b[3]); return w; }
;     __device__ __forceinline__ void operator()(const f32x4 (&acc)[2][2][4][2], const Unit& u, int wr, int wc, int fr_in, int fq_in) const {
;     ...
;         for (int bj = 0; bj < 2; ++bj) {
;             const int colg = u.pn * BM + bj * HALF + wc * 32; bf16_t* dst = colg < 512 ? kn + colg : v + (colg - 512);
; #pragma unroll
;             for (int ai = 0; ai < 2; ++ai)
; #pragma unroll
;                 for (int m = 0; m < 4; ++m) {
;                     const int row = row0 + ai * HALF + m * 16; const float r = t[ai * 64 + m * 16 + fr];
;                     if (!(f8qk && colg < 512) && !(f8pv && colg >= 512)) *(u32x4*)(dst + (size_t)row * 512 + 8 * fq) = pack8(acc[ai][bj][m][0] * r, acc[ai][bj][m][1] * r);
;                     if (f8pv && colg >= 512) {
;                         const int c0_ = colg - 512 + 8 * fq, bb_ = row >> 13, pos_ = row & (SEQ_ - 1), key_ = pos_ & 63, k32_ = key_ & 31;
;                         unsigned char* p_ = ws + WS_V8T + ((((size_t)(bb_ * 8 + (c0_ >> 6)) * 128 + (pos_ >> 6)) * 64 + (c0_ & 63)) * 64) + 32 * ((k32_ >> 2) & 1) + 16 * (key_ >> 5) + (k32_ & 3) + 4 * (k32_ >> 3);
;                         const unsigned w0_ = pack4_fp8_x8(acc[ai][bj][m][0] * r), w1_ = pack4_fp8_x8(acc[ai][bj][m][1] * r);
;                         const int qi_ = fr & 3; unsigned char* pb_ = p_ - qi_;
;                         *(unsigned*)(pb_ + qi_ * 64) = quad_tr4(w0_, qi_); *(unsigned*)(pb_ + (4 + qi_) * 64) = quad_tr4(w1_, qi_);
;                     }
;                     if (f8qk && colg < 512) { u32x2 w8; w8.x = pack4_fp8_x8(acc[ai][bj][m][0] * r); w8.y = pack4_fp8_x8(acc[ai][bj][m][1] * r); *(u32x2*)(ws + WS_KN8 + (size_t)row * 512 + colg + 8 * fq) = w8; }
.LBB0_518:
	s_waitcnt lgkmcnt(0)
	v_pk_mul_f32 v[62:63], v[62:63], v[152:153] op_sel_hi:[1,0]
	v_pk_mul_f32 v[64:65], v[64:65], v[152:153] op_sel_hi:[1,0]
	v_mul_f32_e32 v62, 0x41000000, v62
	v_med3_f32 v68, v62, s64, v250
	v_mul_f32_e32 v62, 0x41000000, v63
	v_med3_f32 v63, v62, s64, v250
	v_cvt_pk_fp8_f32 v62, v68, v63
	v_mul_f32_e32 v63, 0x41000000, v64
	v_mul_f32_e32 v64, 0x41000000, v65
	v_pk_mul_f32 v[58:59], v[58:59], v[152:153] op_sel_hi:[1,0]
	v_med3_f32 v63, v63, s64, v250
	v_med3_f32 v64, v64, s64, v250
	v_mul_f32_e32 v58, 0x41000000, v58
	v_mul_f32_e32 v59, 0x41000000, v59
	v_cvt_pk_fp8_f32 v62, v63, v64 op_sel:[0,0,1]
	v_med3_f32 v58, v58, s64, v250
	v_med3_f32 v59, v59, s64, v250
	v_cvt_pk_fp8_f32 v63, v58, v59
	v_pk_mul_f32 v[60:61], v[60:61], v[152:153] op_sel_hi:[1,0]
	s_nop 0
	v_mul_f32_e32 v58, 0x41000000, v60
	v_mul_f32_e32 v59, 0x41000000, v61
	v_med3_f32 v58, v58, s64, v250
	v_med3_f32 v59, v59, s64, v250
	v_cvt_pk_fp8_f32 v63, v58, v59 op_sel:[0,0,1]
	v_lshlrev_b64 v[58:59], 9, v[150:151]
	v_lshl_add_u64 v[58:59], s[22:23], 0, v[58:59]
	v_lshl_add_u64 v[58:59], v[58:59], 0, s[28:29]
	v_lshl_add_u64 v[58:59], v[58:59], 0, v[142:143]
	global_store_dwordx2 v[58:59], v[62:63], off offset:128
	v_cndmask_b32_e64 v58, 0, 1, s[6:7]
	v_cmp_ne_u32_e64 s[4:5], 1, v58
	s_andn2_b64 vcc, exec, s[6:7]
	s_cbranch_vccz .LBB0_503

; __device__ __forceinline__ u32x4 pack8(const f32x4 a, const f32x4 b) { u32x4 w; w.x = cvt_pk_bf16(a[0], a[1]); w.y = cvt_pk_bf16(a[2], a[3]); w.z = cvt_pk_bf16(b[0], b[1]); w.w = cvt_pk_bf16(b[2], b[3]); return w; }
;     __device__ __forceinline__ void operator()(const f32x4 (&acc)[2][2][4][2], const Unit& u, int wr, int wc, int fr_in, int fq_in) const {
;     ...
;         for (int bj = 0; bj < 2; ++bj) {
;             const int colg = u.pn * BM + bj * HALF + wc * 32; bf16_t* dst = colg < 512 ? kn + colg : v + (colg - 512);
; #pragma unroll
;             for (int ai = 0; ai < 2; ++ai)
; #pragma unroll
;                 for (int m = 0; m < 4; ++m) {
;                     const int row = row0 + ai * HALF + m * 16; const float r = t[ai * 64 + m * 16 + fr];
;                     if (!(f8qk && colg < 512) && !(f8pv && colg >= 512)) *(u32x4*)(dst + (size_t)row * 512 + 8 * fq) = pack8(acc[ai][bj][m][0] * r, acc[ai][bj][m][1] * r);
;                     if (f8pv && colg >= 512) {
;                         const int c0_ = colg - 512 + 8 * fq, bb_ = row >> 13, pos_ = row & (SEQ_ - 1), key_ = pos_ & 63, k32_ = key_ & 31;
;                         unsigned char* p_ = ws + WS_V8T + ((((size_t)(bb_ * 8 + (c0_ >> 6)) * 128 + (pos_ >> 6)) * 64 + (c0_ & 63)) * 64) + 32 * ((k32_ >> 2) & 1) + 16 * (key_ >> 5) + (k32_ & 3) + 4 * (k32_ >> 3);
;                         const unsigned w0_ = pack4_fp8_x8(acc[ai][bj][m][0] * r), w1_ = pack4_fp8_x8(acc[ai][bj][m][1] * r);
;                         const int qi_ = fr & 3; unsigned char* pb_ = p_ - qi_;
;                         *(unsigned*)(pb_ + qi_ * 64) = quad_tr4(w0_, qi_); *(unsigned*)(pb_ + (4 + qi_) * 64) = quad_tr4(w1_, qi_);
;                     }
;                     if (f8qk && colg < 512) { u32x2 w8; w8.x = pack4_fp8_x8(acc[ai][bj][m][0] * r); w8.y = pack4_fp8_x8(acc[ai][bj][m][1] * r); *(u32x2*)(ws + WS_KN8 + (size_t)row * 512 + colg + 8 * fq) = w8; }
.LBB0_520:
	s_waitcnt lgkmcnt(0)
	v_pk_mul_f32 v[54:55], v[54:55], v[124:125] op_sel_hi:[1,0]
	v_pk_mul_f32 v[56:57], v[56:57], v[124:125] op_sel_hi:[1,0]
	v_mul_f32_e32 v54, 0x41000000, v54
	v_med3_f32 v58, v54, s64, v250
	v_mul_f32_e32 v54, 0x41000000, v55
	v_med3_f32 v55, v54, s64, v250
	v_cvt_pk_fp8_f32 v54, v58, v55
	v_mul_f32_e32 v55, 0x41000000, v56
	v_mul_f32_e32 v56, 0x41000000, v57
	v_pk_mul_f32 v[50:51], v[50:51], v[124:125] op_sel_hi:[1,0]
	v_med3_f32 v55, v55, s64, v250
	v_med3_f32 v56, v56, s64, v250
	v_mul_f32_e32 v50, 0x41000000, v50
	v_mul_f32_e32 v51, 0x41000000, v51
	v_cvt_pk_fp8_f32 v54, v55, v56 op_sel:[0,0,1]
	v_med3_f32 v50, v50, s64, v250
	v_med3_f32 v51, v51, s64, v250
	v_cvt_pk_fp8_f32 v55, v50, v51
	v_pk_mul_f32 v[52:53], v[52:53], v[124:125] op_sel_hi:[1,0]
	s_nop 0
	v_mul_f32_e32 v50, 0x41000000, v52
	v_mul_f32_e32 v51, 0x41000000, v53
	v_med3_f32 v50, v50, s64, v250
	v_med3_f32 v51, v51, s64, v250
	v_cvt_pk_fp8_f32 v55, v50, v51 op_sel:[0,0,1]
	v_lshlrev_b64 v[50:51], 9, v[122:123]
	v_lshl_add_u64 v[50:51], s[22:23], 0, v[50:51]
	v_lshl_add_u64 v[50:51], v[50:51], 0, s[28:29]
	v_lshl_add_u64 v[50:51], v[50:51], 0, v[142:143]
	global_store_dwordx2 v[50:51], v[54:55], off offset:128
	s_and_b64 vcc, exec, s[4:5]
	s_cbranch_vccz .LBB0_505

; __device__ __forceinline__ u32x4 pack8(const f32x4 a, const f32x4 b) { u32x4 w; w.x = cvt_pk_bf16(a[0], a[1]); w.y = cvt_pk_bf16(a[2], a[3]); w.z = cvt_pk_bf16(b[0], b[1]); w.w = cvt_pk_bf16(b[2], b[3]); return w; }
;     __device__ __forceinline__ void operator()(const f32x4 (&acc)[2][2][4][2], const Unit& u, int wr, int wc, int fr_in, int fq_in) const {
;     ...
;         for (int bj = 0; bj < 2; ++bj) {
;             const int colg = u.pn * BM + bj * HALF + wc * 32; bf16_t* dst = colg < 512 ? kn + colg : v + (colg - 512);
; #pragma unroll
;             for (int ai = 0; ai < 2; ++ai)
; #pragma unroll
;                 for (int m = 0; m < 4; ++m) {
;                     const int row = row0 + ai * HALF + m * 16; const float r = t[ai * 64 + m * 16 + fr];
;                     if (!(f8qk && colg < 512) && !(f8pv && colg >= 512)) *(u32x4*)(dst + (size_t)row * 512 + 8 * fq) = pack8(acc[ai][bj][m][0] * r, acc[ai][bj][m][1] * r);
;                     if (f8pv && colg >= 512) {
;                         const int c0_ = colg - 512 + 8 * fq, bb_ = row >> 13, pos_ = row & (SEQ_ - 1), key_ = pos_ & 63, k32_ = key_ & 31;
;                         unsigned char* p_ = ws + WS_V8T + ((((size_t)(bb_ * 8 + (c0_ >> 6)) * 128 + (pos_ >> 6)) * 64 + (c0_ & 63)) * 64) + 32 * ((k32_ >> 2) & 1) + 16 * (key_ >> 5) + (k32_ & 3) + 4 * (k32_ >> 3);
;                         const unsigned w0_ = pack4_fp8_x8(acc[ai][bj][m][0] * r), w1_ = pack4_fp8_x8(acc[ai][bj][m][1] * r);
;                         const int qi_ = fr & 3; unsigned char* pb_ = p_ - qi_;
;                         *(unsigned*)(pb_ + qi_ * 64) = quad_tr4(w0_, qi_); *(unsigned*)(pb_ + (4 + qi_) * 64) = quad_tr4(w1_, qi_);
;                     }
;                     if (f8qk && colg < 512) { u32x2 w8; w8.x = pack4_fp8_x8(acc[ai][bj][m][0] * r); w8.y = pack4_fp8_x8(acc[ai][bj][m][1] * r); *(u32x2*)(ws + WS_KN8 + (size_t)row * 512 + colg + 8 * fq) = w8; }
.LBB0_522:
	s_waitcnt lgkmcnt(0)
	v_pk_mul_f32 v[46:47], v[46:47], v[116:117] op_sel_hi:[1,0]
	v_pk_mul_f32 v[48:49], v[48:49], v[116:117] op_sel_hi:[1,0]
	v_mul_f32_e32 v46, 0x41000000, v46
	v_med3_f32 v50, v46, s64, v250
	v_mul_f32_e32 v46, 0x41000000, v47
	v_med3_f32 v47, v46, s64, v250
	v_cvt_pk_fp8_f32 v46, v50, v47
	v_mul_f32_e32 v47, 0x41000000, v48
	v_mul_f32_e32 v48, 0x41000000, v49
	v_pk_mul_f32 v[42:43], v[42:43], v[116:117] op_sel_hi:[1,0]
	v_med3_f32 v47, v47, s64, v250
	v_med3_f32 v48, v48, s64, v250
	v_mul_f32_e32 v42, 0x41000000, v42
	v_mul_f32_e32 v43, 0x41000000, v43
	v_cvt_pk_fp8_f32 v46, v47, v48 op_sel:[0,0,1]
	v_med3_f32 v42, v42, s64, v250
	v_med3_f32 v43, v43, s64, v250
	v_cvt_pk_fp8_f32 v47, v42, v43
	v_pk_mul_f32 v[44:45], v[44:45], v[116:117] op_sel_hi:[1,0]
	s_nop 0
	v_mul_f32_e32 v42, 0x41000000, v44
	v_mul_f32_e32 v43, 0x41000000, v45
	v_med3_f32 v42, v42, s64, v250
	v_med3_f32 v43, v43, s64, v250
	v_cvt_pk_fp8_f32 v47, v42, v43 op_sel:[0,0,1]
	v_lshlrev_b64 v[42:43], 9, v[114:115]
	v_lshl_add_u64 v[42:43], s[22:23], 0, v[42:43]
	v_lshl_add_u64 v[42:43], v[42:43], 0, s[28:29]
	v_lshl_add_u64 v[42:43], v[42:43], 0, v[142:143]
	global_store_dwordx2 v[42:43], v[46:47], off offset:128
	s_and_b64 vcc, exec, s[4:5]
	s_cbranch_vccz .LBB0_507

; __device__ __forceinline__ u32x4 pack8(const f32x4 a, const f32x4 b) { u32x4 w; w.x = cvt_pk_bf16(a[0], a[1]); w.y = cvt_pk_bf16(a[2], a[3]); w.z = cvt_pk_bf16(b[0], b[1]); w.w = cvt_pk_bf16(b[2], b[3]); return w; }
;     __device__ __forceinline__ void operator()(const f32x4 (&acc)[2][2][4][2], const Unit& u, int wr, int wc, int fr_in, int fq_in) const {
;     ...
;         for (int bj = 0; bj < 2; ++bj) {
;             const int colg = u.pn * BM + bj * HALF + wc * 32; bf16_t* dst = colg < 512 ? kn + colg : v + (colg - 512);
; #pragma unroll
;             for (int ai = 0; ai < 2; ++ai)
; #pragma unroll
;                 for (int m = 0; m < 4; ++m) {
;                     const int row = row0 + ai * HALF + m * 16; const float r = t[ai * 64 + m * 16 + fr];
;                     if (!(f8qk && colg < 512) && !(f8pv && colg >= 512)) *(u32x4*)(dst + (size_t)row * 512 + 8 * fq) = pack8(acc[ai][bj][m][0] * r, acc[ai][bj][m][1] * r);
;                     if (f8pv && colg >= 512) {
;                         const int c0_ = colg - 512 + 8 * fq, bb_ = row >> 13, pos_ = row & (SEQ_ - 1), key_ = pos_ & 63, k32_ = key_ & 31;
;                         unsigned char* p_ = ws + WS_V8T + ((((size_t)(bb_ * 8 + (c0_ >> 6)) * 128 + (pos_ >> 6)) * 64 + (c0_ & 63)) * 64) + 32 * ((k32_ >> 2) & 1) + 16 * (key_ >> 5) + (k32_ & 3) + 4 * (k32_ >> 3);
;                         const unsigned w0_ = pack4_fp8_x8(acc[ai][bj][m][0] * r), w1_ = pack4_fp8_x8(acc[ai][bj][m][1] * r);
;                         const int qi_ = fr & 3; unsigned char* pb_ = p_ - qi_;
;                         *(unsigned*)(pb_ + qi_ * 64) = quad_tr4(w0_, qi_); *(unsigned*)(pb_ + (4 + qi_) * 64) = quad_tr4(w1_, qi_);
;                     }
;                     if (f8qk && colg < 512) { u32x2 w8; w8.x = pack4_fp8_x8(acc[ai][bj][m][0] * r); w8.y = pack4_fp8_x8(acc[ai][bj][m][1] * r); *(u32x2*)(ws + WS_KN8 + (size_t)row * 512 + colg + 8 * fq) = w8; }
.LBB0_524:
	s_waitcnt lgkmcnt(0)
	v_pk_mul_f32 v[38:39], v[38:39], v[108:109] op_sel_hi:[1,0]
	v_pk_mul_f32 v[40:41], v[40:41], v[108:109] op_sel_hi:[1,0]
	v_mul_f32_e32 v38, 0x41000000, v38
	v_med3_f32 v42, v38, s64, v250
	v_mul_f32_e32 v38, 0x41000000, v39
	v_med3_f32 v39, v38, s64, v250
	v_cvt_pk_fp8_f32 v38, v42, v39
	v_mul_f32_e32 v39, 0x41000000, v40
	v_mul_f32_e32 v40, 0x41000000, v41
	v_pk_mul_f32 v[34:35], v[34:35], v[108:109] op_sel_hi:[1,0]
	v_med3_f32 v39, v39, s64, v250
	v_med3_f32 v40, v40, s64, v250
	v_mul_f32_e32 v34, 0x41000000, v34
	v_mul_f32_e32 v35, 0x41000000, v35
	v_cvt_pk_fp8_f32 v38, v39, v40 op_sel:[0,0,1]
	v_med3_f32 v34, v34, s64, v250
	v_med3_f32 v35, v35, s64, v250
	v_cvt_pk_fp8_f32 v39, v34, v35
	v_pk_mul_f32 v[36:37], v[36:37], v[108:109] op_sel_hi:[1,0]
	s_nop 0
	v_mul_f32_e32 v34, 0x41000000, v36
	v_mul_f32_e32 v35, 0x41000000, v37
	v_med3_f32 v34, v34, s64, v250
	v_med3_f32 v35, v35, s64, v250
	v_cvt_pk_fp8_f32 v39, v34, v35 op_sel:[0,0,1]
	v_lshlrev_b64 v[34:35], 9, v[106:107]
	v_lshl_add_u64 v[34:35], s[22:23], 0, v[34:35]
	v_lshl_add_u64 v[34:35], v[34:35], 0, s[28:29]
	v_lshl_add_u64 v[34:35], v[34:35], 0, v[142:143]
	global_store_dwordx2 v[34:35], v[38:39], off offset:128
	s_and_b64 vcc, exec, s[4:5]
	s_cbranch_vccz .LBB0_509

; __device__ __forceinline__ u32x4 pack8(const f32x4 a, const f32x4 b) { u32x4 w; w.x = cvt_pk_bf16(a[0], a[1]); w.y = cvt_pk_bf16(a[2], a[3]); w.z = cvt_pk_bf16(b[0], b[1]); w.w = cvt_pk_bf16(b[2], b[3]); return w; }
;     __device__ __forceinline__ void operator()(const f32x4 (&acc)[2][2][4][2], const Unit& u, int wr, int wc, int fr_in, int fq_in) const {
;     ...
;         for (int bj = 0; bj < 2; ++bj) {
;             const int colg = u.pn * BM + bj * HALF + wc * 32; bf16_t* dst = colg < 512 ? kn + colg : v + (colg - 512);
; #pragma unroll
;             for (int ai = 0; ai < 2; ++ai)
; #pragma unroll
;                 for (int m = 0; m < 4; ++m) {
;                     const int row = row0 + ai * HALF + m * 16; const float r = t[ai * 64 + m * 16 + fr];
;                     if (!(f8qk && colg < 512) && !(f8pv && colg >= 512)) *(u32x4*)(dst + (size_t)row * 512 + 8 * fq) = pack8(acc[ai][bj][m][0] * r, acc[ai][bj][m][1] * r);
;                     if (f8pv && colg >= 512) {
;                         const int c0_ = colg - 512 + 8 * fq, bb_ = row >> 13, pos_ = row & (SEQ_ - 1), key_ = pos_ & 63, k32_ = key_ & 31;
;                         unsigned char* p_ = ws + WS_V8T + ((((size_t)(bb_ * 8 + (c0_ >> 6)) * 128 + (pos_ >> 6)) * 64 + (c0_ & 63)) * 64) + 32 * ((k32_ >> 2) & 1) + 16 * (key_ >> 5) + (k32_ & 3) + 4 * (k32_ >> 3);
;                         const unsigned w0_ = pack4_fp8_x8(acc[ai][bj][m][0] * r), w1_ = pack4_fp8_x8(acc[ai][bj][m][1] * r);
;                         const int qi_ = fr & 3; unsigned char* pb_ = p_ - qi_;
;                         *(unsigned*)(pb_ + qi_ * 64) = quad_tr4(w0_, qi_); *(unsigned*)(pb_ + (4 + qi_) * 64) = quad_tr4(w1_, qi_);
;                     }
;                     if (f8qk && colg < 512) { u32x2 w8; w8.x = pack4_fp8_x8(acc[ai][bj][m][0] * r); w8.y = pack4_fp8_x8(acc[ai][bj][m][1] * r); *(u32x2*)(ws + WS_KN8 + (size_t)row * 512 + colg + 8 * fq) = w8; }
.LBB0_526:
	s_waitcnt lgkmcnt(0)
	v_pk_mul_f32 v[30:31], v[30:31], v[100:101] op_sel_hi:[1,0]
	v_pk_mul_f32 v[32:33], v[32:33], v[100:101] op_sel_hi:[1,0]
	v_mul_f32_e32 v30, 0x41000000, v30
	v_med3_f32 v34, v30, s64, v250
	v_mul_f32_e32 v30, 0x41000000, v31
	v_med3_f32 v31, v30, s64, v250
	v_cvt_pk_fp8_f32 v30, v34, v31
	v_mul_f32_e32 v31, 0x41000000, v32
	v_mul_f32_e32 v32, 0x41000000, v33
	v_pk_mul_f32 v[26:27], v[26:27], v[100:101] op_sel_hi:[1,0]
	v_med3_f32 v31, v31, s64, v250
	v_med3_f32 v32, v32, s64, v250
	v_mul_f32_e32 v26, 0x41000000, v26
	v_mul_f32_e32 v27, 0x41000000, v27
	v_cvt_pk_fp8_f32 v30, v31, v32 op_sel:[0,0,1]
	v_med3_f32 v26, v26, s64, v250
	v_med3_f32 v27, v27, s64, v250
	v_cvt_pk_fp8_f32 v31, v26, v27
	v_pk_mul_f32 v[28:29], v[28:29], v[100:101] op_sel_hi:[1,0]
	s_nop 0
	v_mul_f32_e32 v26, 0x41000000, v28
	v_mul_f32_e32 v27, 0x41000000, v29
	v_med3_f32 v26, v26, s64, v250
	v_med3_f32 v27, v27, s64, v250
	v_cvt_pk_fp8_f32 v31, v26, v27 op_sel:[0,0,1]
	v_lshlrev_b64 v[26:27], 9, v[98:99]
	v_lshl_add_u64 v[26:27], s[22:23], 0, v[26:27]
	v_lshl_add_u64 v[26:27], v[26:27], 0, s[28:29]
	v_lshl_add_u64 v[26:27], v[26:27], 0, v[142:143]
	global_store_dwordx2 v[26:27], v[30:31], off offset:128
	s_and_b64 vcc, exec, s[4:5]
	s_cbranch_vccz .LBB0_511

; __device__ __forceinline__ u32x4 pack8(const f32x4 a, const f32x4 b) { u32x4 w; w.x = cvt_pk_bf16(a[0], a[1]); w.y = cvt_pk_bf16(a[2], a[3]); w.z = cvt_pk_bf16(b[0], b[1]); w.w = cvt_pk_bf16(b[2], b[3]); return w; }
;     __device__ __forceinline__ void operator()(const f32x4 (&acc)[2][2][4][2], const Unit& u, int wr, int wc, int fr_in, int fq_in) const {
;     ...
;         for (int bj = 0; bj < 2; ++bj) {
;             const int colg = u.pn * BM + bj * HALF + wc * 32; bf16_t* dst = colg < 512 ? kn + colg : v + (colg - 512);
; #pragma unroll
;             for (int ai = 0; ai < 2; ++ai)
; #pragma unroll
;                 for (int m = 0; m < 4; ++m) {
;                     const int row = row0 + ai * HALF + m * 16; const float r = t[ai * 64 + m * 16 + fr];
;                     if (!(f8qk && colg < 512) && !(f8pv && colg >= 512)) *(u32x4*)(dst + (size_t)row * 512 + 8 * fq) = pack8(acc[ai][bj][m][0] * r, acc[ai][bj][m][1] * r);
;                     if (f8pv && colg >= 512) {
;                         const int c0_ = colg - 512 + 8 * fq, bb_ = row >> 13, pos_ = row & (SEQ_ - 1), key_ = pos_ & 63, k32_ = key_ & 31;
;                         unsigned char* p_ = ws + WS_V8T + ((((size_t)(bb_ * 8 + (c0_ >> 6)) * 128 + (pos_ >> 6)) * 64 + (c0_ & 63)) * 64) + 32 * ((k32_ >> 2) & 1) + 16 * (key_ >> 5) + (k32_ & 3) + 4 * (k32_ >> 3);
;                         const unsigned w0_ = pack4_fp8_x8(acc[ai][bj][m][0] * r), w1_ = pack4_fp8_x8(acc[ai][bj][m][1] * r);
;                         const int qi_ = fr & 3; unsigned char* pb_ = p_ - qi_;
;                         *(unsigned*)(pb_ + qi_ * 64) = quad_tr4(w0_, qi_); *(unsigned*)(pb_ + (4 + qi_) * 64) = quad_tr4(w1_, qi_);
;                     }
;                     if (f8qk && colg < 512) { u32x2 w8; w8.x = pack4_fp8_x8(acc[ai][bj][m][0] * r); w8.y = pack4_fp8_x8(acc[ai][bj][m][1] * r); *(u32x2*)(ws + WS_KN8 + (size_t)row * 512 + colg + 8 * fq) = w8; }
.LBB0_528:
	s_waitcnt lgkmcnt(0)
	v_pk_mul_f32 v[22:23], v[22:23], v[92:93] op_sel_hi:[1,0]
	v_pk_mul_f32 v[24:25], v[24:25], v[92:93] op_sel_hi:[1,0]
	v_mul_f32_e32 v22, 0x41000000, v22
	v_med3_f32 v26, v22, s64, v250
	v_mul_f32_e32 v22, 0x41000000, v23
	v_med3_f32 v23, v22, s64, v250
	v_cvt_pk_fp8_f32 v22, v26, v23
	v_mul_f32_e32 v23, 0x41000000, v24
	v_mul_f32_e32 v24, 0x41000000, v25
	v_pk_mul_f32 v[18:19], v[18:19], v[92:93] op_sel_hi:[1,0]
	v_med3_f32 v23, v23, s64, v250
	v_med3_f32 v24, v24, s64, v250
	v_mul_f32_e32 v18, 0x41000000, v18
	v_mul_f32_e32 v19, 0x41000000, v19
	v_cvt_pk_fp8_f32 v22, v23, v24 op_sel:[0,0,1]
	v_med3_f32 v18, v18, s64, v250
	v_med3_f32 v19, v19, s64, v250
	v_cvt_pk_fp8_f32 v23, v18, v19
	v_pk_mul_f32 v[20:21], v[20:21], v[92:93] op_sel_hi:[1,0]
	s_nop 0
	v_mul_f32_e32 v18, 0x41000000, v20
	v_mul_f32_e32 v19, 0x41000000, v21
	v_med3_f32 v18, v18, s64, v250
	v_med3_f32 v19, v19, s64, v250
	v_cvt_pk_fp8_f32 v23, v18, v19 op_sel:[0,0,1]
	v_lshlrev_b64 v[18:19], 9, v[90:91]
	v_lshl_add_u64 v[18:19], s[22:23], 0, v[18:19]
	v_lshl_add_u64 v[18:19], v[18:19], 0, s[28:29]
	v_lshl_add_u64 v[18:19], v[18:19], 0, v[142:143]
	global_store_dwordx2 v[18:19], v[22:23], off offset:128
	s_and_b64 vcc, exec, s[4:5]
	s_cbranch_vccz .LBB0_513

; __device__ __forceinline__ u32x4 pack8(const f32x4 a, const f32x4 b) { u32x4 w; w.x = cvt_pk_bf16(a[0], a[1]); w.y = cvt_pk_bf16(a[2], a[3]); w.z = cvt_pk_bf16(b[0], b[1]); w.w = cvt_pk_bf16(b[2], b[3]); return w; }
;     __device__ __forceinline__ void operator()(const f32x4 (&acc)[2][2][4][2], const Unit& u, int wr, int wc, int fr_in, int fq_in) const {
;     ...
;         for (int bj = 0; bj < 2; ++bj) {
;             const int colg = u.pn * BM + bj * HALF + wc * 32; bf16_t* dst = colg < 512 ? kn + colg : v + (colg - 512);
; #pragma unroll
;             for (int ai = 0; ai < 2; ++ai)
; #pragma unroll
;                 for (int m = 0; m < 4; ++m) {
;                     const int row = row0 + ai * HALF + m * 16; const float r = t[ai * 64 + m * 16 + fr];
;                     if (!(f8qk && colg < 512) && !(f8pv && colg >= 512)) *(u32x4*)(dst + (size_t)row * 512 + 8 * fq) = pack8(acc[ai][bj][m][0] * r, acc[ai][bj][m][1] * r);
;                     if (f8pv && colg >= 512) {
;                         const int c0_ = colg - 512 + 8 * fq, bb_ = row >> 13, pos_ = row & (SEQ_ - 1), key_ = pos_ & 63, k32_ = key_ & 31;
;                         unsigned char* p_ = ws + WS_V8T + ((((size_t)(bb_ * 8 + (c0_ >> 6)) * 128 + (pos_ >> 6)) * 64 + (c0_ & 63)) * 64) + 32 * ((k32_ >> 2) & 1) + 16 * (key_ >> 5) + (k32_ & 3) + 4 * (k32_ >> 3);
;                         const unsigned w0_ = pack4_fp8_x8(acc[ai][bj][m][0] * r), w1_ = pack4_fp8_x8(acc[ai][bj][m][1] * r);
;                         const int qi_ = fr & 3; unsigned char* pb_ = p_ - qi_;
;                         *(unsigned*)(pb_ + qi_ * 64) = quad_tr4(w0_, qi_); *(unsigned*)(pb_ + (4 + qi_) * 64) = quad_tr4(w1_, qi_);
;                     }
;                     if (f8qk && colg < 512) { u32x2 w8; w8.x = pack4_fp8_x8(acc[ai][bj][m][0] * r); w8.y = pack4_fp8_x8(acc[ai][bj][m][1] * r); *(u32x2*)(ws + WS_KN8 + (size_t)row * 512 + colg + 8 * fq) = w8; }
.LBB0_530:
	s_waitcnt lgkmcnt(0)
	v_pk_mul_f32 v[14:15], v[14:15], v[84:85] op_sel_hi:[1,0]
	v_pk_mul_f32 v[16:17], v[16:17], v[84:85] op_sel_hi:[1,0]
	v_mul_f32_e32 v14, 0x41000000, v14
	v_med3_f32 v18, v14, s64, v250
	v_mul_f32_e32 v14, 0x41000000, v15
	v_med3_f32 v15, v14, s64, v250
	v_cvt_pk_fp8_f32 v14, v18, v15
	v_mul_f32_e32 v15, 0x41000000, v16
	v_mul_f32_e32 v16, 0x41000000, v17
	v_pk_mul_f32 v[10:11], v[10:11], v[84:85] op_sel_hi:[1,0]
	v_med3_f32 v15, v15, s64, v250
	v_med3_f32 v16, v16, s64, v250
	v_mul_f32_e32 v10, 0x41000000, v10
	v_mul_f32_e32 v11, 0x41000000, v11
	v_cvt_pk_fp8_f32 v14, v15, v16 op_sel:[0,0,1]
	v_med3_f32 v10, v10, s64, v250
	v_med3_f32 v11, v11, s64, v250
	v_cvt_pk_fp8_f32 v15, v10, v11
	v_pk_mul_f32 v[12:13], v[12:13], v[84:85] op_sel_hi:[1,0]
	s_nop 0
	v_mul_f32_e32 v10, 0x41000000, v12
	v_mul_f32_e32 v11, 0x41000000, v13
	v_med3_f32 v10, v10, s64, v250
	v_med3_f32 v11, v11, s64, v250
	v_cvt_pk_fp8_f32 v15, v10, v11 op_sel:[0,0,1]
	v_lshlrev_b64 v[10:11], 9, v[82:83]
	v_lshl_add_u64 v[10:11], s[22:23], 0, v[10:11]
	v_lshl_add_u64 v[10:11], v[10:11], 0, s[28:29]
	v_lshl_add_u64 v[10:11], v[10:11], 0, v[142:143]
	global_store_dwordx2 v[10:11], v[14:15], off offset:128
	s_and_b64 vcc, exec, s[4:5]
	s_cbranch_vccz .LBB0_515

; __device__ __forceinline__ u32x4 pack8(const f32x4 a, const f32x4 b) { u32x4 w; w.x = cvt_pk_bf16(a[0], a[1]); w.y = cvt_pk_bf16(a[2], a[3]); w.z = cvt_pk_bf16(b[0], b[1]); w.w = cvt_pk_bf16(b[2], b[3]); return w; }
;     __device__ __forceinline__ void operator()(const f32x4 (&acc)[2][2][4][2], const Unit& u, int wr, int wc, int fr_in, int fq_in) const {
;     ...
;         for (int bj = 0; bj < 2; ++bj) {
;             const int colg = u.pn * BM + bj * HALF + wc * 32; bf16_t* dst = colg < 512 ? kn + colg : v + (colg - 512);
; #pragma unroll
;             for (int ai = 0; ai < 2; ++ai)
; #pragma unroll
;                 for (int m = 0; m < 4; ++m) {
;                     const int row = row0 + ai * HALF + m * 16; const float r = t[ai * 64 + m * 16 + fr];
;                     if (!(f8qk && colg < 512) && !(f8pv && colg >= 512)) *(u32x4*)(dst + (size_t)row * 512 + 8 * fq) = pack8(acc[ai][bj][m][0] * r, acc[ai][bj][m][1] * r);
;                     if (f8pv && colg >= 512) {
;                         const int c0_ = colg - 512 + 8 * fq, bb_ = row >> 13, pos_ = row & (SEQ_ - 1), key_ = pos_ & 63, k32_ = key_ & 31;
;                         unsigned char* p_ = ws + WS_V8T + ((((size_t)(bb_ * 8 + (c0_ >> 6)) * 128 + (pos_ >> 6)) * 64 + (c0_ & 63)) * 64) + 32 * ((k32_ >> 2) & 1) + 16 * (key_ >> 5) + (k32_ & 3) + 4 * (k32_ >> 3);
;                         const unsigned w0_ = pack4_fp8_x8(acc[ai][bj][m][0] * r), w1_ = pack4_fp8_x8(acc[ai][bj][m][1] * r);
;                         const int qi_ = fr & 3; unsigned char* pb_ = p_ - qi_;
;                         *(unsigned*)(pb_ + qi_ * 64) = quad_tr4(w0_, qi_); *(unsigned*)(pb_ + (4 + qi_) * 64) = quad_tr4(w1_, qi_);
;                     }
;                     if (f8qk && colg < 512) { u32x2 w8; w8.x = pack4_fp8_x8(acc[ai][bj][m][0] * r); w8.y = pack4_fp8_x8(acc[ai][bj][m][1] * r); *(u32x2*)(ws + WS_KN8 + (size_t)row * 512 + colg + 8 * fq) = w8; }
.LBB0_532:
	s_waitcnt lgkmcnt(0)
	v_pk_mul_f32 v[6:7], v[6:7], v[76:77] op_sel_hi:[1,0]
	v_pk_mul_f32 v[8:9], v[8:9], v[76:77] op_sel_hi:[1,0]
	v_mul_f32_e32 v0, 0x41000000, v6
	v_mul_f32_e32 v6, 0x41000000, v7
	v_med3_f32 v0, v0, s64, v250
	v_med3_f32 v7, v6, s64, v250
	v_cvt_pk_fp8_f32 v6, v0, v7
	v_mul_f32_e32 v0, 0x41000000, v8
	v_mul_f32_e32 v7, 0x41000000, v9
	v_med3_f32 v0, v0, s64, v250
	v_med3_f32 v7, v7, s64, v250
	v_pk_mul_f32 v[2:3], v[2:3], v[76:77] op_sel_hi:[1,0]
	v_cvt_pk_fp8_f32 v6, v0, v7 op_sel:[0,0,1]
	v_mul_f32_e32 v0, 0x41000000, v2
	v_mul_f32_e32 v2, 0x41000000, v3
	v_med3_f32 v0, v0, s64, v250
	v_med3_f32 v2, v2, s64, v250
	v_cvt_pk_fp8_f32 v7, v0, v2
	v_pk_mul_f32 v[4:5], v[4:5], v[76:77] op_sel_hi:[1,0]
	s_nop 0
	v_mul_f32_e32 v0, 0x41000000, v4
	v_mul_f32_e32 v2, 0x41000000, v5
	v_med3_f32 v0, v0, s64, v250
	v_med3_f32 v2, v2, s64, v250
	v_cvt_pk_fp8_f32 v7, v0, v2 op_sel:[0,0,1]
	v_lshlrev_b64 v[2:3], 9, v[74:75]
	v_lshl_add_u64 v[2:3], s[22:23], 0, v[2:3]
	v_lshl_add_u64 v[2:3], v[2:3], 0, s[28:29]
	v_lshl_add_u64 v[2:3], v[2:3], 0, v[142:143]
	global_store_dwordx2 v[2:3], v[6:7], off offset:128
	s_and_b64 vcc, exec, s[2:3]
	s_mov_b64 s[2:3], -1
	s_cbranch_vccnz .LBB0_452

; __device__ __forceinline__ u32x4 pack8(const f32x4 a, const f32x4 b) { u32x4 w; w.x = cvt_pk_bf16(a[0], a[1]); w.y = cvt_pk_bf16(a[2], a[3]); w.z = cvt_pk_bf16(b[0], b[1]); w.w = cvt_pk_bf16(b[2], b[3]); return w; }
; __device__ __forceinline__ float sumsq4(const f32x4 v) { return (v[0] * v[0] + v[1] * v[1]) + (v[2] * v[2] + v[3] * v[3]); }
; __device__ __forceinline__ float xor16_add(float v) { return v + __int_as_float(__builtin_amdgcn_ds_swizzle(__float_as_int(v), 0x401F)); }
; __device__ __forceinline__ float xor32_add(float v) { auto rr = __builtin_amdgcn_permlane32_swap(__float_as_uint(v), __float_as_uint(v), false, false); return __uint_as_float(rr[0]) + __uint_as_float(rr[1]); }
;     __device__ __forceinline__ void operator()(const f32x4 (&acc)[2][2][4][2], const Unit& u, int wr, int wc, int fr, int fq) const {
;     ...
;         const int row0 = u.pm * BM + wr * 64 + fr, col0 = u.pn * BM + wc * 32 + 8 * fq;
; #pragma unroll
;         for (int ai = 0; ai < 2; ++ai) {
;             u32x4 old[4][2];
; #pragma unroll
;             for (int m = 0; m < 4; ++m)
; #pragma unroll
;                 for (int bj = 0; bj < 2; ++bj) old[m][bj] = *(const u32x4*)(xb + (size_t)(row0 + ai * HALF + m * 16) * DM + col0 + bj * HALF);
; #pragma unroll
;             for (int m = 0; m < 4; ++m) {
;                 const int row = row0 + ai * HALF + m * 16; float ss = 0.f;
; #pragma unroll
;                 for (int bj = 0; bj < 2; ++bj) {
;                     const f32x4 v0 = bf2f_lo(old[m][bj], 0) + acc[ai][bj][m][0], v1 = bf2f_lo(old[m][bj], 1) + acc[ai][bj][m][1];
;                     ss += sumsq4(v0) + sumsq4(v1);
;                     *(u32x4*)(xb + (size_t)row * DM + col0 + bj * HALF) = pack8(v0, v1);
;                     { u32x2 w8; w8.x = pack4_fp8_x8(v0); w8.y = pack4_fp8_x8(v1); *(u32x2*)(xq + (size_t)row * DM + col0 + bj * HALF) = w8; }
;                 }
;                 ss = xor32_add(xor16_add(ss));
;                 if (fq == 0) ssx[(size_t)row * 16 + u.pn * 4 + wc] = ss;
; template <class Epi, class Sched, bool ALIGN_EPI = false, bool SP2 = false, bool F8 = false>
; __device__ __forceinline__ void gemm_phase(PG8_LAS unsigned char* lds, const Gemm g, const Sched& S, const Epi& E, const int tidb  ) {
;     ...
;         if constexpr (F8) asm volatile("s_nop 15\n\ts_nop 15" ::: "memory");
.LBB0_1045:
	v_lshl_add_u32 v32, s59, 8, v163
	v_lshl_or_b32 v2, s58, 8, v193
	v_ashrrev_i32_e32 v3, 31, v2
	v_ashrrev_i32_e32 v33, 31, v32
	v_lshl_add_u64 v[174:175], v[2:3], 1, s[20:21]
	v_lshl_add_u64 v[30:31], s[22:23], 0, v[2:3]
	v_lshlrev_b64 v[2:3], 11, v[32:33]
	s_nop 15
	s_nop 15
	v_lshl_add_u64 v[190:191], v[174:175], 0, v[2:3]
	global_load_dwordx4 v[204:207], v[190:191], off
	global_load_dwordx4 v[26:29], v[190:191], off offset:256
	v_or_b32_e32 v184, 16, v32
	v_ashrrev_i32_e32 v185, 31, v184
	v_or_b32_e32 v180, 32, v32
	v_lshlrev_b64 v[2:3], 11, v[184:185]
	v_ashrrev_i32_e32 v181, 31, v180
	v_or_b32_e32 v176, 48, v32
	v_lshl_add_u64 v[186:187], v[174:175], 0, v[2:3]
	v_lshlrev_b64 v[2:3], 11, v[180:181]
	v_ashrrev_i32_e32 v177, 31, v176
	v_lshl_add_u64 v[182:183], v[174:175], 0, v[2:3]
	v_lshlrev_b64 v[2:3], 11, v[176:177]
	v_lshl_add_u64 v[178:179], v[174:175], 0, v[2:3]
	global_load_dwordx4 v[22:25], v[186:187], off
	global_load_dwordx4 v[18:21], v[186:187], off offset:256
	global_load_dwordx4 v[14:17], v[182:183], off
	global_load_dwordx4 v[10:13], v[182:183], off offset:256
	global_load_dwordx4 v[6:9], v[178:179], off
	global_load_dwordx4 v[2:5], v[178:179], off offset:256
	v_lshlrev_b64 v[188:189], 10, v[32:33]
	v_lshl_add_u64 v[188:189], v[30:31], 0, v[188:189]
	s_lshl_b32 s24, s58, 2
	s_ashr_i32 s25, s24, 31
	s_lshl_b64 s[24:25], s[24:25], 2
	s_add_u32 s24, s49, s24
	s_addc_u32 s25, s50, s25
	s_waitcnt vmcnt(0)
	v_lshlrev_b32_e32 v196, 16, v204
	v_and_b32_e32 v197, 0xffff0000, v204
	v_lshlrev_b32_e32 v198, 16, v205
	v_and_b32_e32 v199, 0xffff0000, v205
	v_pk_add_f32 v[160:161], v[160:161], v[198:199]
	v_pk_add_f32 v[196:197], v[158:159], v[196:197]
	v_lshlrev_b32_e32 v158, 16, v206
	v_and_b32_e32 v159, 0xffff0000, v206
	v_lshlrev_b32_e32 v198, 16, v207
	v_and_b32_e32 v199, 0xffff0000, v207
	v_pk_add_f32 v[154:155], v[154:155], v[158:159]
	v_mul_f32_e32 v158, v197, v197
	v_mul_f32_e32 v159, v161, v161
	v_pk_add_f32 v[156:157], v[156:157], v[198:199]
	v_fmac_f32_e32 v158, v196, v196
	v_fmac_f32_e32 v159, v160, v160
	v_add_f32_e32 v158, v158, v159
	v_mul_f32_e32 v159, v155, v155
	v_mul_f32_e32 v195, v157, v157
	v_fmac_f32_e32 v159, v154, v154
	v_fmac_f32_e32 v195, v156, v156
	v_cvt_pk_bf16_f32 v204, v196, v197
	v_cvt_pk_bf16_f32 v205, v160, v161
	v_cvt_pk_bf16_f32 v206, v154, v155
	v_mul_f32_e32 v154, 0x41000000, v154
	v_mul_f32_e32 v155, 0x41000000, v155
	v_add_f32_e32 v159, v159, v195
	v_mul_f32_e32 v195, 0x41000000, v197
	v_med3_f32 v154, v154, s64, v250
	v_med3_f32 v155, v155, s64, v250
	v_cvt_pk_fp8_f32 v197, v154, v155
	v_add_f32_e32 v158, v158, v159
	v_mul_f32_e32 v159, 0x41000000, v196
	v_mul_f32_e32 v154, 0x41000000, v156
	v_mul_f32_e32 v155, 0x41000000, v157
	v_med3_f32 v159, v159, s64, v250
	v_med3_f32 v195, v195, s64, v250
	v_med3_f32 v154, v154, s64, v250
	v_med3_f32 v155, v155, s64, v250
	v_cvt_pk_fp8_f32 v196, v159, v195
	v_cvt_pk_fp8_f32 v197, v154, v155 op_sel:[0,0,1]
	v_lshlrev_b32_e32 v154, 16, v26
	v_and_b32_e32 v155, 0xffff0000, v26
	v_lshlrev_b32_e32 v26, 16, v27
	v_and_b32_e32 v27, 0xffff0000, v27
	v_pk_add_f32 v[26:27], v[152:153], v[26:27]
	v_pk_add_f32 v[150:151], v[150:151], v[154:155]
	v_lshlrev_b32_e32 v152, 16, v28
	v_and_b32_e32 v153, 0xffff0000, v28
	v_mul_f32_e32 v159, 0x41000000, v160
	v_mul_f32_e32 v160, 0x41000000, v161
	v_lshlrev_b32_e32 v28, 16, v29
	v_and_b32_e32 v29, 0xffff0000, v29
	v_pk_add_f32 v[152:153], v[146:147], v[152:153]
	v_mul_f32_e32 v146, v151, v151
	v_mul_f32_e32 v147, v27, v27
	v_med3_f32 v159, v159, s64, v250
	v_med3_f32 v160, v160, s64, v250
	v_pk_add_f32 v[28:29], v[148:149], v[28:29]
	v_fmac_f32_e32 v146, v150, v150
	v_fmac_f32_e32 v147, v26, v26
	v_cvt_pk_fp8_f32 v196, v159, v160 op_sel:[0,0,1]
	v_add_f32_e32 v146, v146, v147
	v_mul_f32_e32 v147, v153, v153
	v_mul_f32_e32 v148, v29, v29
	v_fmac_f32_e32 v147, v152, v152
	v_fmac_f32_e32 v148, v28, v28
	v_add_f32_e32 v147, v147, v148
	v_add_f32_e32 v146, v146, v147
	v_cvt_pk_bf16_f32 v207, v156, v157
	global_store_dwordx4 v[190:191], v[204:207], off
	global_store_dwordx2 v[188:189], v[196:197], off
	v_add_f32_e32 v154, v158, v146
	v_cvt_pk_bf16_f32 v146, v150, v151
	v_cvt_pk_bf16_f32 v147, v26, v27
	v_cvt_pk_bf16_f32 v148, v152, v153
	v_cvt_pk_bf16_f32 v149, v28, v29
	global_store_dwordx4 v[190:191], v[146:149], off offset:256
	v_mul_f32_e32 v26, 0x41000000, v26
	v_mul_f32_e32 v27, 0x41000000, v27
	v_mul_f32_e32 v146, 0x41000000, v150
	v_med3_f32 v147, v146, s64, v250
	v_mul_f32_e32 v146, 0x41000000, v151
	v_med3_f32 v148, v146, s64, v250
	v_cvt_pk_fp8_f32 v146, v147, v148
	v_med3_f32 v26, v26, s64, v250
	v_med3_f32 v27, v27, s64, v250
	v_cvt_pk_fp8_f32 v146, v26, v27 op_sel:[0,0,1]
	v_mul_f32_e32 v26, 0x41000000, v152
	v_mul_f32_e32 v27, 0x41000000, v153
	v_med3_f32 v26, v26, s64, v250
	v_med3_f32 v27, v27, s64, v250
	v_cvt_pk_fp8_f32 v147, v26, v27
	v_mul_f32_e32 v26, 0x41000000, v28
	v_mul_f32_e32 v27, 0x41000000, v29
	v_med3_f32 v26, v26, s64, v250
	v_med3_f32 v27, v27, s64, v250
	v_cvt_pk_fp8_f32 v147, v26, v27 op_sel:[0,0,1]
	ds_swizzle_b32 v26, v154 offset:swizzle(SWAP,16)
	global_store_dwordx2 v[188:189], v[146:147], off offset:128
	s_waitcnt lgkmcnt(0)
	v_add_f32_e32 v26, v154, v26
	v_mov_b32_e32 v27, v26
	s_nop 1
	v_permlane32_swap_b32_e32 v26, v27
	s_and_saveexec_b64 s[26:27], s[2:3]
	s_cbranch_execz .LBB0_1047
	v_lshlrev_b64 v[28:29], 6, v[32:33]
	v_lshl_add_u64 v[28:29], s[24:25], 0, v[28:29]
	v_add_f32_e32 v26, v26, v27
	global_store_dword v[28:29], v26, off
; __device__ __forceinline__ u32x4 pack8(const f32x4 a, const f32x4 b) { u32x4 w; w.x = cvt_pk_bf16(a[0], a[1]); w.y = cvt_pk_bf16(a[2], a[3]); w.z = cvt_pk_bf16(b[0], b[1]); w.w = cvt_pk_bf16(b[2], b[3]); return w; }
; __device__ __forceinline__ float sumsq4(const f32x4 v) { return (v[0] * v[0] + v[1] * v[1]) + (v[2] * v[2] + v[3] * v[3]); }
; __device__ __forceinline__ float xor16_add(float v) { return v + __int_as_float(__builtin_amdgcn_ds_swizzle(__float_as_int(v), 0x401F)); }
; __device__ __forceinline__ float xor32_add(float v) { auto rr = __builtin_amdgcn_permlane32_swap(__float_as_uint(v), __float_as_uint(v), false, false); return __uint_as_float(rr[0]) + __uint_as_float(rr[1]); }
; __device__ __forceinline__ f32x4 bf2f_lo(const u32x4 w, int h) { const unsigned a = h ? w.z : w.x, b = h ? w.w : w.y; return (f32x4){__uint_as_float(a << 16), __uint_as_float(a & 0xffff0000u), __uint_as_float(b << 16), __uint_as_float(b & 0xffff0000u)}; }
;     __device__ __forceinline__ void operator()(const f32x4 (&acc)[2][2][4][2], const Unit& u, int wr, int wc, int fr, int fq) const {
;     ...
;                 for (int bj = 0; bj < 2; ++bj) old[m][bj] = *(const u32x4*)(xb + (size_t)(row0 + ai * HALF + m * 16) * DM + col0 + bj * HALF);
; #pragma unroll
;             for (int m = 0; m < 4; ++m) {
;                 const int row = row0 + ai * HALF + m * 16; float ss = 0.f;
; #pragma unroll
;                 for (int bj = 0; bj < 2; ++bj) {
;                     const f32x4 v0 = bf2f_lo(old[m][bj], 0) + acc[ai][bj][m][0], v1 = bf2f_lo(old[m][bj], 1) + acc[ai][bj][m][1];
;                     ss += sumsq4(v0) + sumsq4(v1);
;                     *(u32x4*)(xb + (size_t)row * DM + col0 + bj * HALF) = pack8(v0, v1);
;                     { u32x2 w8; w8.x = pack4_fp8_x8(v0); w8.y = pack4_fp8_x8(v1); *(u32x2*)(xq + (size_t)row * DM + col0 + bj * HALF) = w8; }
;                 }
;                 ss = xor32_add(xor16_add(ss));
;                 if (fq == 0) ssx[(size_t)row * 16 + u.pn * 4 + wc] = ss;
;             }
.LBB0_1047:
	s_or_b64 exec, exec, s[26:27]
	v_lshlrev_b32_e32 v28, 16, v22
	v_and_b32_e32 v29, 0xffff0000, v22
	v_lshlrev_b32_e32 v22, 16, v23
	v_and_b32_e32 v23, 0xffff0000, v23
	v_pk_add_f32 v[144:145], v[144:145], v[22:23]
	v_pk_add_f32 v[28:29], v[142:143], v[28:29]
	v_lshlrev_b32_e32 v22, 16, v24
	v_and_b32_e32 v23, 0xffff0000, v24
	v_lshlrev_b32_e32 v24, 16, v25
	v_and_b32_e32 v25, 0xffff0000, v25
	v_pk_add_f32 v[140:141], v[140:141], v[24:25]
	v_pk_add_f32 v[24:25], v[138:139], v[22:23]
	v_mul_f32_e32 v22, v29, v29
	v_mul_f32_e32 v23, v145, v145
	v_fmac_f32_e32 v22, v28, v28
	v_fmac_f32_e32 v23, v144, v144
	v_add_f32_e32 v22, v22, v23
	v_mul_f32_e32 v23, v25, v25
	v_mul_f32_e32 v33, v141, v141
	v_fmac_f32_e32 v23, v24, v24
	v_fmac_f32_e32 v33, v140, v140
	v_add_f32_e32 v23, v23, v33
	v_add_f32_e32 v33, v22, v23
	v_cvt_pk_bf16_f32 v22, v28, v29
	v_mul_f32_e32 v28, 0x41000000, v28
	v_med3_f32 v138, v28, s64, v250
	v_mul_f32_e32 v28, 0x41000000, v29
	v_med3_f32 v29, v28, s64, v250
	v_cvt_pk_fp8_f32 v28, v138, v29
	v_mul_f32_e32 v29, 0x41000000, v144
	v_mul_f32_e32 v138, 0x41000000, v145
	v_med3_f32 v29, v29, s64, v250
	v_med3_f32 v138, v138, s64, v250
	v_cvt_pk_fp8_f32 v28, v29, v138 op_sel:[0,0,1]
	v_mul_f32_e32 v29, 0x41000000, v24
	v_med3_f32 v138, v29, s64, v250
	v_mul_f32_e32 v29, 0x41000000, v25
	v_med3_f32 v139, v29, s64, v250
	v_cvt_pk_fp8_f32 v29, v138, v139
	v_mul_f32_e32 v138, 0x41000000, v140
	v_mul_f32_e32 v139, 0x41000000, v141
	v_med3_f32 v138, v138, s64, v250
	v_med3_f32 v139, v139, s64, v250
	v_cvt_pk_fp8_f32 v29, v138, v139 op_sel:[0,0,1]
	v_lshlrev_b64 v[26:27], 10, v[184:185]
	v_cvt_pk_bf16_f32 v23, v144, v145
	v_cvt_pk_bf16_f32 v24, v24, v25
	v_cvt_pk_bf16_f32 v25, v140, v141
	v_lshl_add_u64 v[26:27], v[30:31], 0, v[26:27]
	global_store_dwordx4 v[186:187], v[22:25], off
	global_store_dwordx2 v[26:27], v[28:29], off
	s_nop 0
	v_lshlrev_b32_e32 v22, 16, v18
	v_and_b32_e32 v23, 0xffff0000, v18
	v_lshlrev_b32_e32 v18, 16, v19
	v_and_b32_e32 v19, 0xffff0000, v19
	v_pk_add_f32 v[24:25], v[136:137], v[18:19]
	v_pk_add_f32 v[22:23], v[134:135], v[22:23]
	v_lshlrev_b32_e32 v18, 16, v20
	v_and_b32_e32 v19, 0xffff0000, v20
	v_lshlrev_b32_e32 v20, 16, v21
	v_and_b32_e32 v21, 0xffff0000, v21
	v_pk_add_f32 v[28:29], v[132:133], v[20:21]
	v_pk_add_f32 v[20:21], v[130:131], v[18:19]
	v_mul_f32_e32 v18, v23, v23
	v_mul_f32_e32 v19, v25, v25
	v_fmac_f32_e32 v18, v22, v22
	v_fmac_f32_e32 v19, v24, v24
	v_add_f32_e32 v18, v18, v19
	v_mul_f32_e32 v19, v21, v21
	v_mul_f32_e32 v130, v29, v29
	v_fmac_f32_e32 v19, v20, v20
	v_fmac_f32_e32 v130, v28, v28
	v_add_f32_e32 v19, v19, v130
	v_add_f32_e32 v18, v18, v19
	v_add_f32_e32 v33, v33, v18
	v_cvt_pk_bf16_f32 v18, v22, v23
	v_mul_f32_e32 v22, 0x41000000, v22
	v_med3_f32 v130, v22, s64, v250
	v_mul_f32_e32 v22, 0x41000000, v23
	v_med3_f32 v23, v22, s64, v250
	v_cvt_pk_fp8_f32 v22, v130, v23
	v_cvt_pk_bf16_f32 v19, v24, v25
	v_mul_f32_e32 v23, 0x41000000, v24
	v_mul_f32_e32 v24, 0x41000000, v25
	v_med3_f32 v23, v23, s64, v250
	v_med3_f32 v24, v24, s64, v250
	v_cvt_pk_fp8_f32 v22, v23, v24 op_sel:[0,0,1]
	v_mul_f32_e32 v23, 0x41000000, v20
	v_med3_f32 v24, v23, s64, v250
	v_mul_f32_e32 v23, 0x41000000, v21
	v_med3_f32 v25, v23, s64, v250
	v_cvt_pk_fp8_f32 v23, v24, v25
	v_mul_f32_e32 v24, 0x41000000, v28
	v_mul_f32_e32 v25, 0x41000000, v29
	v_med3_f32 v24, v24, s64, v250
	v_med3_f32 v25, v25, s64, v250
	v_cvt_pk_fp8_f32 v23, v24, v25 op_sel:[0,0,1]
	ds_swizzle_b32 v24, v33 offset:swizzle(SWAP,16)
	v_cvt_pk_bf16_f32 v20, v20, v21
	v_cvt_pk_bf16_f32 v21, v28, v29
	global_store_dwordx4 v[186:187], v[18:21], off offset:256
	global_store_dwordx2 v[26:27], v[22:23], off offset:128
	s_waitcnt lgkmcnt(0)
	v_add_f32_e32 v18, v33, v24
	v_mov_b32_e32 v19, v18
	s_nop 1
	v_permlane32_swap_b32_e32 v18, v19
	s_and_saveexec_b64 s[26:27], s[2:3]
	s_cbranch_execz .LBB0_1049
	v_lshlrev_b64 v[20:21], 6, v[184:185]
	v_lshl_add_u64 v[20:21], s[24:25], 0, v[20:21]
	v_add_f32_e32 v18, v18, v19
	global_store_dword v[20:21], v18, off
.LBB0_1049:
	s_or_b64 exec, exec, s[26:27]
	v_lshlrev_b32_e32 v20, 16, v14
	v_and_b32_e32 v21, 0xffff0000, v14
	v_lshlrev_b32_e32 v14, 16, v15
	v_and_b32_e32 v15, 0xffff0000, v15
	v_pk_add_f32 v[22:23], v[128:129], v[14:15]
	v_pk_add_f32 v[20:21], v[126:127], v[20:21]
	v_lshlrev_b32_e32 v14, 16, v16
	v_and_b32_e32 v15, 0xffff0000, v16
	v_lshlrev_b32_e32 v16, 16, v17
	v_and_b32_e32 v17, 0xffff0000, v17
	v_pk_add_f32 v[24:25], v[124:125], v[16:17]
	v_pk_add_f32 v[16:17], v[122:123], v[14:15]
	v_mul_f32_e32 v14, v21, v21
	v_mul_f32_e32 v15, v23, v23
	v_fmac_f32_e32 v14, v20, v20
	v_fmac_f32_e32 v15, v22, v22
	v_add_f32_e32 v14, v14, v15
	v_mul_f32_e32 v15, v17, v17
	v_mul_f32_e32 v26, v25, v25
	v_fmac_f32_e32 v15, v16, v16
	v_fmac_f32_e32 v26, v24, v24
	v_add_f32_e32 v15, v15, v26
	v_add_f32_e32 v26, v14, v15
	v_cvt_pk_bf16_f32 v14, v20, v21
	v_mul_f32_e32 v20, 0x41000000, v20
	v_med3_f32 v27, v20, s64, v250
	v_mul_f32_e32 v20, 0x41000000, v21
	v_med3_f32 v21, v20, s64, v250
	v_cvt_pk_fp8_f32 v20, v27, v21
	v_cvt_pk_bf16_f32 v15, v22, v23
	v_mul_f32_e32 v21, 0x41000000, v22
	v_mul_f32_e32 v22, 0x41000000, v23
	v_med3_f32 v21, v21, s64, v250
	v_med3_f32 v22, v22, s64, v250
	v_cvt_pk_fp8_f32 v20, v21, v22 op_sel:[0,0,1]
	v_mul_f32_e32 v21, 0x41000000, v16
	v_med3_f32 v22, v21, s64, v250
	v_mul_f32_e32 v21, 0x41000000, v17
	v_med3_f32 v23, v21, s64, v250
	v_cvt_pk_fp8_f32 v21, v22, v23
	v_mul_f32_e32 v22, 0x41000000, v24
	v_mul_f32_e32 v23, 0x41000000, v25
	v_med3_f32 v22, v22, s64, v250
	v_med3_f32 v23, v23, s64, v250
	v_cvt_pk_fp8_f32 v21, v22, v23 op_sel:[0,0,1]
	v_lshlrev_b64 v[18:19], 10, v[180:181]
; __device__ __forceinline__ u32x4 pack8(const f32x4 a, const f32x4 b) { u32x4 w; w.x = cvt_pk_bf16(a[0], a[1]); w.y = cvt_pk_bf16(a[2], a[3]); w.z = cvt_pk_bf16(b[0], b[1]); w.w = cvt_pk_bf16(b[2], b[3]); return w; }
; __device__ __forceinline__ float sumsq4(const f32x4 v) { return (v[0] * v[0] + v[1] * v[1]) + (v[2] * v[2] + v[3] * v[3]); }
; __device__ __forceinline__ float xor16_add(float v) { return v + __int_as_float(__builtin_amdgcn_ds_swizzle(__float_as_int(v), 0x401F)); }
; __device__ __forceinline__ float xor32_add(float v) { auto rr = __builtin_amdgcn_permlane32_swap(__float_as_uint(v), __float_as_uint(v), false, false); return __uint_as_float(rr[0]) + __uint_as_float(rr[1]); }
; __device__ __forceinline__ f32x4 bf2f_lo(const u32x4 w, int h) { const unsigned a = h ? w.z : w.x, b = h ? w.w : w.y; return (f32x4){__uint_as_float(a << 16), __uint_as_float(a & 0xffff0000u), __uint_as_float(b << 16), __uint_as_float(b & 0xffff0000u)}; }
;     __device__ __forceinline__ void operator()(const f32x4 (&acc)[2][2][4][2], const Unit& u, int wr, int wc, int fr, int fq) const {
;     ...
;                 for (int bj = 0; bj < 2; ++bj) old[m][bj] = *(const u32x4*)(xb + (size_t)(row0 + ai * HALF + m * 16) * DM + col0 + bj * HALF);
; #pragma unroll
;             for (int m = 0; m < 4; ++m) {
;                 const int row = row0 + ai * HALF + m * 16; float ss = 0.f;
; #pragma unroll
;                 for (int bj = 0; bj < 2; ++bj) {
;                     const f32x4 v0 = bf2f_lo(old[m][bj], 0) + acc[ai][bj][m][0], v1 = bf2f_lo(old[m][bj], 1) + acc[ai][bj][m][1];
;                     ss += sumsq4(v0) + sumsq4(v1);
;                     *(u32x4*)(xb + (size_t)row * DM + col0 + bj * HALF) = pack8(v0, v1);
;                     { u32x2 w8; w8.x = pack4_fp8_x8(v0); w8.y = pack4_fp8_x8(v1); *(u32x2*)(xq + (size_t)row * DM + col0 + bj * HALF) = w8; }
;                 }
;                 ss = xor32_add(xor16_add(ss));
;                 if (fq == 0) ssx[(size_t)row * 16 + u.pn * 4 + wc] = ss;
;             }
	v_cvt_pk_bf16_f32 v16, v16, v17
	v_cvt_pk_bf16_f32 v17, v24, v25
	v_lshl_add_u64 v[18:19], v[30:31], 0, v[18:19]
	global_store_dwordx4 v[182:183], v[14:17], off
	global_store_dwordx2 v[18:19], v[20:21], off
	s_nop 0
	v_lshlrev_b32_e32 v14, 16, v10
	v_and_b32_e32 v15, 0xffff0000, v10
	v_lshlrev_b32_e32 v10, 16, v11
	v_and_b32_e32 v11, 0xffff0000, v11
	v_pk_add_f32 v[16:17], v[120:121], v[10:11]
	v_pk_add_f32 v[14:15], v[118:119], v[14:15]
	v_lshlrev_b32_e32 v10, 16, v12
	v_and_b32_e32 v11, 0xffff0000, v12
	v_lshlrev_b32_e32 v12, 16, v13
	v_and_b32_e32 v13, 0xffff0000, v13
	v_pk_add_f32 v[20:21], v[116:117], v[12:13]
	v_pk_add_f32 v[12:13], v[114:115], v[10:11]
	v_mul_f32_e32 v10, v15, v15
	v_mul_f32_e32 v11, v17, v17
	v_fmac_f32_e32 v10, v14, v14
	v_fmac_f32_e32 v11, v16, v16
	v_add_f32_e32 v10, v10, v11
	v_mul_f32_e32 v11, v13, v13
	v_mul_f32_e32 v22, v21, v21
	v_fmac_f32_e32 v11, v12, v12
	v_fmac_f32_e32 v22, v20, v20
	v_add_f32_e32 v11, v11, v22
	v_add_f32_e32 v10, v10, v11
	v_add_f32_e32 v22, v26, v10
	v_cvt_pk_bf16_f32 v10, v14, v15
	v_mul_f32_e32 v14, 0x41000000, v14
	v_med3_f32 v23, v14, s64, v250
	v_mul_f32_e32 v14, 0x41000000, v15
	v_med3_f32 v15, v14, s64, v250
	v_cvt_pk_fp8_f32 v14, v23, v15
	v_cvt_pk_bf16_f32 v11, v16, v17
	v_mul_f32_e32 v15, 0x41000000, v16
	v_mul_f32_e32 v16, 0x41000000, v17
	v_med3_f32 v15, v15, s64, v250
	v_med3_f32 v16, v16, s64, v250
	v_cvt_pk_fp8_f32 v14, v15, v16 op_sel:[0,0,1]
	v_mul_f32_e32 v15, 0x41000000, v12
	v_med3_f32 v16, v15, s64, v250
	v_mul_f32_e32 v15, 0x41000000, v13
	v_med3_f32 v17, v15, s64, v250
	v_cvt_pk_fp8_f32 v15, v16, v17
	v_mul_f32_e32 v16, 0x41000000, v20
	v_mul_f32_e32 v17, 0x41000000, v21
	v_med3_f32 v16, v16, s64, v250
	v_med3_f32 v17, v17, s64, v250
	v_cvt_pk_fp8_f32 v15, v16, v17 op_sel:[0,0,1]
	ds_swizzle_b32 v16, v22 offset:swizzle(SWAP,16)
	v_cvt_pk_bf16_f32 v12, v12, v13
	v_cvt_pk_bf16_f32 v13, v20, v21
	global_store_dwordx4 v[182:183], v[10:13], off offset:256
	global_store_dwordx2 v[18:19], v[14:15], off offset:128
	s_waitcnt lgkmcnt(0)
	v_add_f32_e32 v10, v22, v16
	v_mov_b32_e32 v11, v10
	s_nop 1
	v_permlane32_swap_b32_e32 v10, v11
	s_and_saveexec_b64 s[26:27], s[2:3]
	s_cbranch_execz .LBB0_1051
	v_lshlrev_b64 v[12:13], 6, v[180:181]
	v_lshl_add_u64 v[12:13], s[24:25], 0, v[12:13]
	v_add_f32_e32 v10, v10, v11
	global_store_dword v[12:13], v10, off
.LBB0_1051:
	s_or_b64 exec, exec, s[26:27]
	v_lshlrev_b32_e32 v12, 16, v6
	v_and_b32_e32 v13, 0xffff0000, v6
	v_lshlrev_b32_e32 v6, 16, v7
	v_and_b32_e32 v7, 0xffff0000, v7
	v_pk_add_f32 v[14:15], v[112:113], v[6:7]
	v_pk_add_f32 v[12:13], v[110:111], v[12:13]
	v_lshlrev_b32_e32 v6, 16, v8
	v_and_b32_e32 v7, 0xffff0000, v8
	v_lshlrev_b32_e32 v8, 16, v9
	v_and_b32_e32 v9, 0xffff0000, v9
	v_pk_add_f32 v[16:17], v[108:109], v[8:9]
	v_pk_add_f32 v[8:9], v[106:107], v[6:7]
	v_mul_f32_e32 v6, v13, v13
	v_mul_f32_e32 v7, v15, v15
	v_fmac_f32_e32 v6, v12, v12
	v_fmac_f32_e32 v7, v14, v14
	v_add_f32_e32 v6, v6, v7
	v_mul_f32_e32 v7, v9, v9
	v_mul_f32_e32 v18, v17, v17
	v_fmac_f32_e32 v7, v8, v8
	v_fmac_f32_e32 v18, v16, v16
	v_add_f32_e32 v7, v7, v18
	v_add_f32_e32 v18, v6, v7
	v_cvt_pk_bf16_f32 v6, v12, v13
	v_mul_f32_e32 v12, 0x41000000, v12
	v_med3_f32 v19, v12, s64, v250
	v_mul_f32_e32 v12, 0x41000000, v13
	v_med3_f32 v13, v12, s64, v250
	v_cvt_pk_fp8_f32 v12, v19, v13
	v_cvt_pk_bf16_f32 v7, v14, v15
	v_mul_f32_e32 v13, 0x41000000, v14
	v_mul_f32_e32 v14, 0x41000000, v15
	v_med3_f32 v13, v13, s64, v250
	v_med3_f32 v14, v14, s64, v250
	v_cvt_pk_fp8_f32 v12, v13, v14 op_sel:[0,0,1]
	v_mul_f32_e32 v13, 0x41000000, v8
	v_med3_f32 v14, v13, s64, v250
	v_mul_f32_e32 v13, 0x41000000, v9
	v_med3_f32 v15, v13, s64, v250
	v_cvt_pk_fp8_f32 v13, v14, v15
	v_mul_f32_e32 v14, 0x41000000, v16
	v_mul_f32_e32 v15, 0x41000000, v17
	v_med3_f32 v14, v14, s64, v250
	v_med3_f32 v15, v15, s64, v250
	v_cvt_pk_fp8_f32 v13, v14, v15 op_sel:[0,0,1]
	v_lshlrev_b64 v[10:11], 10, v[176:177]
	v_cvt_pk_bf16_f32 v8, v8, v9
	v_cvt_pk_bf16_f32 v9, v16, v17
	v_lshl_add_u64 v[10:11], v[30:31], 0, v[10:11]
	global_store_dwordx4 v[178:179], v[6:9], off
	global_store_dwordx2 v[10:11], v[12:13], off
	s_nop 0
	v_lshlrev_b32_e32 v6, 16, v2
	v_and_b32_e32 v7, 0xffff0000, v2
	v_lshlrev_b32_e32 v2, 16, v3
	v_and_b32_e32 v3, 0xffff0000, v3
	v_pk_add_f32 v[8:9], v[104:105], v[2:3]
	v_pk_add_f32 v[6:7], v[102:103], v[6:7]
	v_lshlrev_b32_e32 v2, 16, v4
	v_and_b32_e32 v3, 0xffff0000, v4
	v_lshlrev_b32_e32 v4, 16, v5
	v_and_b32_e32 v5, 0xffff0000, v5
	v_pk_add_f32 v[12:13], v[100:101], v[4:5]
	v_pk_add_f32 v[4:5], v[98:99], v[2:3]
	v_mul_f32_e32 v2, v7, v7
	v_mul_f32_e32 v3, v9, v9
	v_fmac_f32_e32 v2, v6, v6
	v_fmac_f32_e32 v3, v8, v8
	v_add_f32_e32 v2, v2, v3
	v_mul_f32_e32 v3, v5, v5
	v_mul_f32_e32 v14, v13, v13
	v_fmac_f32_e32 v3, v4, v4
	v_fmac_f32_e32 v14, v12, v12
	v_add_f32_e32 v3, v3, v14
	v_add_f32_e32 v2, v2, v3
	v_add_f32_e32 v14, v18, v2
	v_cvt_pk_bf16_f32 v2, v6, v7
	v_mul_f32_e32 v6, 0x41000000, v6
	v_med3_f32 v15, v6, s64, v250
	v_mul_f32_e32 v6, 0x41000000, v7
	v_med3_f32 v7, v6, s64, v250
	v_cvt_pk_fp8_f32 v6, v15, v7
	v_cvt_pk_bf16_f32 v3, v8, v9
	v_mul_f32_e32 v7, 0x41000000, v8
	v_mul_f32_e32 v8, 0x41000000, v9
	v_med3_f32 v7, v7, s64, v250
	v_med3_f32 v8, v8, s64, v250
	v_cvt_pk_fp8_f32 v6, v7, v8 op_sel:[0,0,1]
	v_mul_f32_e32 v7, 0x41000000, v4
	v_med3_f32 v8, v7, s64, v250
	v_mul_f32_e32 v7, 0x41000000, v5
	v_med3_f32 v9, v7, s64, v250
	v_cvt_pk_fp8_f32 v7, v8, v9
	v_mul_f32_e32 v8, 0x41000000, v12
	v_mul_f32_e32 v9, 0x41000000, v13
	v_med3_f32 v8, v8, s64, v250
	v_med3_f32 v9, v9, s64, v250
	v_cvt_pk_fp8_f32 v7, v8, v9 op_sel:[0,0,1]
	ds_swizzle_b32 v8, v14 offset:swizzle(SWAP,16)
	v_cvt_pk_bf16_f32 v4, v4, v5
	v_cvt_pk_bf16_f32 v5, v12, v13
	global_store_dwordx4 v[178:179], v[2:5], off offset:256
	global_store_dwordx2 v[10:11], v[6:7], off offset:128
	s_waitcnt lgkmcnt(0)
	v_add_f32_e32 v2, v14, v8
	v_mov_b32_e32 v3, v2
	s_nop 1
	v_permlane32_swap_b32_e32 v2, v3
	s_and_saveexec_b64 s[26:27], s[2:3]
	s_cbranch_execz .LBB0_1053
	v_lshlrev_b64 v[4:5], 6, v[176:177]
	v_lshl_add_u64 v[4:5], s[24:25], 0, v[4:5]
	v_add_f32_e32 v2, v2, v3
	global_store_dword v[4:5], v2, off
; __device__ __forceinline__ u32x4 pack8(const f32x4 a, const f32x4 b) { u32x4 w; w.x = cvt_pk_bf16(a[0], a[1]); w.y = cvt_pk_bf16(a[2], a[3]); w.z = cvt_pk_bf16(b[0], b[1]); w.w = cvt_pk_bf16(b[2], b[3]); return w; }
; __device__ __forceinline__ float sumsq4(const f32x4 v) { return (v[0] * v[0] + v[1] * v[1]) + (v[2] * v[2] + v[3] * v[3]); }
; __device__ __forceinline__ float xor16_add(float v) { return v + __int_as_float(__builtin_amdgcn_ds_swizzle(__float_as_int(v), 0x401F)); }
; __device__ __forceinline__ float xor32_add(float v) { auto rr = __builtin_amdgcn_permlane32_swap(__float_as_uint(v), __float_as_uint(v), false, false); return __uint_as_float(rr[0]) + __uint_as_float(rr[1]); }
; __device__ __forceinline__ f32x4 bf2f_lo(const u32x4 w, int h) { const unsigned a = h ? w.z : w.x, b = h ? w.w : w.y; return (f32x4){__uint_as_float(a << 16), __uint_as_float(a & 0xffff0000u), __uint_as_float(b << 16), __uint_as_float(b & 0xffff0000u)}; }
;     __device__ __forceinline__ void operator()(const f32x4 (&acc)[2][2][4][2], const Unit& u, int wr, int wc, int fr, int fq) const {
;     ...
;                 for (int bj = 0; bj < 2; ++bj) old[m][bj] = *(const u32x4*)(xb + (size_t)(row0 + ai * HALF + m * 16) * DM + col0 + bj * HALF);
; #pragma unroll
;             for (int m = 0; m < 4; ++m) {
;                 const int row = row0 + ai * HALF + m * 16; float ss = 0.f;
; #pragma unroll
;                 for (int bj = 0; bj < 2; ++bj) {
;                     const f32x4 v0 = bf2f_lo(old[m][bj], 0) + acc[ai][bj][m][0], v1 = bf2f_lo(old[m][bj], 1) + acc[ai][bj][m][1];
;                     ss += sumsq4(v0) + sumsq4(v1);
;                     *(u32x4*)(xb + (size_t)row * DM + col0 + bj * HALF) = pack8(v0, v1);
;                     { u32x2 w8; w8.x = pack4_fp8_x8(v0); w8.y = pack4_fp8_x8(v1); *(u32x2*)(xq + (size_t)row * DM + col0 + bj * HALF) = w8; }
;                 }
;                 ss = xor32_add(xor16_add(ss));
;                 if (fq == 0) ssx[(size_t)row * 16 + u.pn * 4 + wc] = ss;
;             }
.LBB0_1053:
	s_or_b64 exec, exec, s[26:27]
	v_add_u32_e32 v108, 0x80, v32
	v_ashrrev_i32_e32 v109, 31, v108
	v_lshlrev_b64 v[2:3], 11, v[108:109]
	v_lshl_add_u64 v[110:111], v[174:175], 0, v[2:3]
	global_load_dwordx4 v[114:117], v[110:111], off
	global_load_dwordx4 v[26:29], v[110:111], off offset:256
	v_add_u32_e32 v104, 0x90, v32
	v_ashrrev_i32_e32 v105, 31, v104
	v_add_u32_e32 v100, 0xa0, v32
	v_lshlrev_b64 v[2:3], 11, v[104:105]
	v_ashrrev_i32_e32 v101, 31, v100
	v_add_u32_e32 v32, 0xb0, v32
	v_lshl_add_u64 v[106:107], v[174:175], 0, v[2:3]
	v_lshlrev_b64 v[2:3], 11, v[100:101]
	v_ashrrev_i32_e32 v33, 31, v32
	v_lshl_add_u64 v[102:103], v[174:175], 0, v[2:3]
	v_lshlrev_b64 v[2:3], 11, v[32:33]
	v_lshl_add_u64 v[98:99], v[174:175], 0, v[2:3]
	global_load_dwordx4 v[22:25], v[106:107], off
	global_load_dwordx4 v[18:21], v[106:107], off offset:256
	global_load_dwordx4 v[14:17], v[102:103], off
	global_load_dwordx4 v[10:13], v[102:103], off offset:256
	global_load_dwordx4 v[6:9], v[98:99], off
	global_load_dwordx4 v[2:5], v[98:99], off offset:256
	v_lshlrev_b64 v[112:113], 10, v[108:109]
	v_lshl_add_u64 v[112:113], v[30:31], 0, v[112:113]
	s_waitcnt vmcnt(7)
	v_lshlrev_b32_e32 v118, 16, v114
	v_and_b32_e32 v119, 0xffff0000, v114
	v_lshlrev_b32_e32 v114, 16, v115
	v_and_b32_e32 v115, 0xffff0000, v115
	v_pk_add_f32 v[114:115], v[96:97], v[114:115]
	v_pk_add_f32 v[118:119], v[94:95], v[118:119]
	v_lshlrev_b32_e32 v94, 16, v116
	v_and_b32_e32 v95, 0xffff0000, v116
	v_lshlrev_b32_e32 v96, 16, v117
	v_and_b32_e32 v97, 0xffff0000, v117
	v_pk_add_f32 v[116:117], v[90:91], v[94:95]
	v_mul_f32_e32 v90, v119, v119
	v_mul_f32_e32 v91, v115, v115
	v_pk_add_f32 v[92:93], v[92:93], v[96:97]
	v_fmac_f32_e32 v90, v118, v118
	v_fmac_f32_e32 v91, v114, v114
	v_add_f32_e32 v90, v90, v91
	v_mul_f32_e32 v91, v117, v117
	v_mul_f32_e32 v94, v93, v93
	v_fmac_f32_e32 v91, v116, v116
	v_fmac_f32_e32 v94, v92, v92
	v_add_f32_e32 v91, v91, v94
	v_cvt_pk_bf16_f32 v94, v118, v119
	v_add_f32_e32 v90, v90, v91
	v_cvt_pk_bf16_f32 v95, v114, v115
	v_cvt_pk_bf16_f32 v96, v116, v117
	v_cvt_pk_bf16_f32 v97, v92, v93
	global_store_dwordx4 v[110:111], v[94:97], off
	v_mul_f32_e32 v91, 0x41000000, v118
	v_med3_f32 v91, v91, s64, v250
	v_mul_f32_e32 v94, 0x41000000, v119
	v_med3_f32 v95, v94, s64, v250
	v_cvt_pk_fp8_f32 v94, v91, v95
	v_mul_f32_e32 v91, 0x41000000, v114
	v_mul_f32_e32 v95, 0x41000000, v115
	v_med3_f32 v91, v91, s64, v250
	v_med3_f32 v95, v95, s64, v250
	v_cvt_pk_fp8_f32 v94, v91, v95 op_sel:[0,0,1]
	v_mul_f32_e32 v91, 0x41000000, v116
	v_mul_f32_e32 v95, 0x41000000, v117
	v_med3_f32 v91, v91, s64, v250
	v_med3_f32 v96, v95, s64, v250
	v_cvt_pk_fp8_f32 v95, v91, v96
	v_mul_f32_e32 v91, 0x41000000, v92
	v_mul_f32_e32 v92, 0x41000000, v93
	v_med3_f32 v91, v91, s64, v250
	v_med3_f32 v92, v92, s64, v250
	v_cvt_pk_fp8_f32 v95, v91, v92 op_sel:[0,0,1]
	s_waitcnt vmcnt(7)
	v_lshlrev_b32_e32 v92, 16, v26
	v_and_b32_e32 v93, 0xffff0000, v26
	v_lshlrev_b32_e32 v26, 16, v27
	v_and_b32_e32 v27, 0xffff0000, v27
	v_pk_add_f32 v[26:27], v[88:89], v[26:27]
	v_pk_add_f32 v[86:87], v[86:87], v[92:93]
	v_lshlrev_b32_e32 v88, 16, v28
	v_and_b32_e32 v89, 0xffff0000, v28
	v_lshlrev_b32_e32 v28, 16, v29
	v_and_b32_e32 v29, 0xffff0000, v29
	v_pk_add_f32 v[88:89], v[82:83], v[88:89]
	v_mul_f32_e32 v82, v87, v87
	v_mul_f32_e32 v83, v27, v27
	v_pk_add_f32 v[28:29], v[84:85], v[28:29]
	v_fmac_f32_e32 v82, v86, v86
	v_fmac_f32_e32 v83, v26, v26
	v_add_f32_e32 v82, v82, v83
	v_mul_f32_e32 v83, v89, v89
	v_mul_f32_e32 v84, v29, v29
	v_fmac_f32_e32 v83, v88, v88
	v_fmac_f32_e32 v84, v28, v28
	v_add_f32_e32 v83, v83, v84
	v_add_f32_e32 v82, v82, v83
	global_store_dwordx2 v[112:113], v[94:95], off
	v_add_f32_e32 v90, v90, v82
	v_cvt_pk_bf16_f32 v82, v86, v87
	v_cvt_pk_bf16_f32 v83, v26, v27
	v_cvt_pk_bf16_f32 v84, v88, v89
	v_cvt_pk_bf16_f32 v85, v28, v29
	global_store_dwordx4 v[110:111], v[82:85], off offset:256
	v_mul_f32_e32 v26, 0x41000000, v26
	v_mul_f32_e32 v27, 0x41000000, v27
	v_mul_f32_e32 v82, 0x41000000, v86
	v_med3_f32 v83, v82, s64, v250
	v_mul_f32_e32 v82, 0x41000000, v87
	v_med3_f32 v84, v82, s64, v250
	v_cvt_pk_fp8_f32 v82, v83, v84
	v_med3_f32 v26, v26, s64, v250
	v_med3_f32 v27, v27, s64, v250
	v_cvt_pk_fp8_f32 v82, v26, v27 op_sel:[0,0,1]
	v_mul_f32_e32 v26, 0x41000000, v88
	v_mul_f32_e32 v27, 0x41000000, v89
	v_med3_f32 v26, v26, s64, v250
	v_med3_f32 v27, v27, s64, v250
	v_cvt_pk_fp8_f32 v83, v26, v27
	v_mul_f32_e32 v26, 0x41000000, v28
	v_mul_f32_e32 v27, 0x41000000, v29
	v_med3_f32 v26, v26, s64, v250
	v_med3_f32 v27, v27, s64, v250
	v_cvt_pk_fp8_f32 v83, v26, v27 op_sel:[0,0,1]
	ds_swizzle_b32 v26, v90 offset:swizzle(SWAP,16)
	global_store_dwordx2 v[112:113], v[82:83], off offset:128
	s_waitcnt lgkmcnt(0)
	v_add_f32_e32 v26, v90, v26
	v_mov_b32_e32 v27, v26
	s_nop 1
	v_permlane32_swap_b32_e32 v26, v27
	s_and_saveexec_b64 s[26:27], s[2:3]
	s_cbranch_execz .LBB0_1055
	v_lshlrev_b64 v[28:29], 6, v[108:109]
	v_lshl_add_u64 v[28:29], s[24:25], 0, v[28:29]
	v_add_f32_e32 v26, v26, v27
	global_store_dword v[28:29], v26, off
; __device__ __forceinline__ u32x4 pack8(const f32x4 a, const f32x4 b) { u32x4 w; w.x = cvt_pk_bf16(a[0], a[1]); w.y = cvt_pk_bf16(a[2], a[3]); w.z = cvt_pk_bf16(b[0], b[1]); w.w = cvt_pk_bf16(b[2], b[3]); return w; }
; __device__ __forceinline__ float sumsq4(const f32x4 v) { return (v[0] * v[0] + v[1] * v[1]) + (v[2] * v[2] + v[3] * v[3]); }
; __device__ __forceinline__ float xor16_add(float v) { return v + __int_as_float(__builtin_amdgcn_ds_swizzle(__float_as_int(v), 0x401F)); }
; __device__ __forceinline__ float xor32_add(float v) { auto rr = __builtin_amdgcn_permlane32_swap(__float_as_uint(v), __float_as_uint(v), false, false); return __uint_as_float(rr[0]) + __uint_as_float(rr[1]); }
; __device__ __forceinline__ f32x4 bf2f_lo(const u32x4 w, int h) { const unsigned a = h ? w.z : w.x, b = h ? w.w : w.y; return (f32x4){__uint_as_float(a << 16), __uint_as_float(a & 0xffff0000u), __uint_as_float(b << 16), __uint_as_float(b & 0xffff0000u)}; }
;     __device__ __forceinline__ void operator()(const f32x4 (&acc)[2][2][4][2], const Unit& u, int wr, int wc, int fr, int fq) const {
;     ...
;                 for (int bj = 0; bj < 2; ++bj) old[m][bj] = *(const u32x4*)(xb + (size_t)(row0 + ai * HALF + m * 16) * DM + col0 + bj * HALF);
; #pragma unroll
;             for (int m = 0; m < 4; ++m) {
;                 const int row = row0 + ai * HALF + m * 16; float ss = 0.f;
; #pragma unroll
;                 for (int bj = 0; bj < 2; ++bj) {
;                     const f32x4 v0 = bf2f_lo(old[m][bj], 0) + acc[ai][bj][m][0], v1 = bf2f_lo(old[m][bj], 1) + acc[ai][bj][m][1];
;                     ss += sumsq4(v0) + sumsq4(v1);
;                     *(u32x4*)(xb + (size_t)row * DM + col0 + bj * HALF) = pack8(v0, v1);
;                     { u32x2 w8; w8.x = pack4_fp8_x8(v0); w8.y = pack4_fp8_x8(v1); *(u32x2*)(xq + (size_t)row * DM + col0 + bj * HALF) = w8; }
;                 }
;                 ss = xor32_add(xor16_add(ss));
;                 if (fq == 0) ssx[(size_t)row * 16 + u.pn * 4 + wc] = ss;
;             }
.LBB0_1055:
	s_or_b64 exec, exec, s[26:27]
	s_waitcnt vmcnt(9)
	v_lshlrev_b32_e32 v28, 16, v22
	v_and_b32_e32 v29, 0xffff0000, v22
	v_lshlrev_b32_e32 v22, 16, v23
	v_and_b32_e32 v23, 0xffff0000, v23
	v_pk_add_f32 v[80:81], v[80:81], v[22:23]
	v_pk_add_f32 v[28:29], v[78:79], v[28:29]
	v_lshlrev_b32_e32 v22, 16, v24
	v_and_b32_e32 v23, 0xffff0000, v24
	v_lshlrev_b32_e32 v24, 16, v25
	v_and_b32_e32 v25, 0xffff0000, v25
	v_pk_add_f32 v[76:77], v[76:77], v[24:25]
	v_pk_add_f32 v[24:25], v[74:75], v[22:23]
	v_mul_f32_e32 v22, v29, v29
	v_mul_f32_e32 v23, v81, v81
	v_fmac_f32_e32 v22, v28, v28
	v_fmac_f32_e32 v23, v80, v80
	v_add_f32_e32 v22, v22, v23
	v_mul_f32_e32 v23, v25, v25
	v_mul_f32_e32 v74, v77, v77
	v_fmac_f32_e32 v23, v24, v24
	v_fmac_f32_e32 v74, v76, v76
	v_add_f32_e32 v23, v23, v74
	v_add_f32_e32 v74, v22, v23
	v_cvt_pk_bf16_f32 v22, v28, v29
	v_mul_f32_e32 v28, 0x41000000, v28
	v_med3_f32 v75, v28, s64, v250
	v_mul_f32_e32 v28, 0x41000000, v29
	v_med3_f32 v29, v28, s64, v250
	v_cvt_pk_fp8_f32 v28, v75, v29
	v_mul_f32_e32 v29, 0x41000000, v80
	v_mul_f32_e32 v75, 0x41000000, v81
	v_med3_f32 v29, v29, s64, v250
	v_med3_f32 v75, v75, s64, v250
	v_cvt_pk_fp8_f32 v28, v29, v75 op_sel:[0,0,1]
	v_mul_f32_e32 v29, 0x41000000, v24
	v_med3_f32 v75, v29, s64, v250
	v_mul_f32_e32 v29, 0x41000000, v25
	v_med3_f32 v78, v29, s64, v250
	v_cvt_pk_fp8_f32 v29, v75, v78
	v_mul_f32_e32 v75, 0x41000000, v76
	v_mul_f32_e32 v78, 0x41000000, v77
	v_med3_f32 v75, v75, s64, v250
	v_med3_f32 v78, v78, s64, v250
	v_cvt_pk_fp8_f32 v29, v75, v78 op_sel:[0,0,1]
	v_lshlrev_b64 v[26:27], 10, v[104:105]
	v_cvt_pk_bf16_f32 v23, v80, v81
	v_cvt_pk_bf16_f32 v24, v24, v25
	v_cvt_pk_bf16_f32 v25, v76, v77
	v_lshl_add_u64 v[26:27], v[30:31], 0, v[26:27]
	global_store_dwordx4 v[106:107], v[22:25], off
	global_store_dwordx2 v[26:27], v[28:29], off
	s_waitcnt vmcnt(10)
	v_lshlrev_b32_e32 v22, 16, v18
	v_and_b32_e32 v23, 0xffff0000, v18
	v_lshlrev_b32_e32 v18, 16, v19
	v_and_b32_e32 v19, 0xffff0000, v19
	v_pk_add_f32 v[24:25], v[72:73], v[18:19]
	v_pk_add_f32 v[22:23], v[70:71], v[22:23]
	v_lshlrev_b32_e32 v18, 16, v20
	v_and_b32_e32 v19, 0xffff0000, v20
	v_lshlrev_b32_e32 v20, 16, v21
	v_and_b32_e32 v21, 0xffff0000, v21
	v_pk_add_f32 v[28:29], v[68:69], v[20:21]
	v_pk_add_f32 v[20:21], v[66:67], v[18:19]
	v_mul_f32_e32 v18, v23, v23
	v_mul_f32_e32 v19, v25, v25
	v_fmac_f32_e32 v18, v22, v22
	v_fmac_f32_e32 v19, v24, v24
	v_add_f32_e32 v18, v18, v19
	v_mul_f32_e32 v19, v21, v21
	v_mul_f32_e32 v66, v29, v29
	v_fmac_f32_e32 v19, v20, v20
	v_fmac_f32_e32 v66, v28, v28
	v_add_f32_e32 v19, v19, v66
	v_add_f32_e32 v18, v18, v19
	v_add_f32_e32 v66, v74, v18
	v_cvt_pk_bf16_f32 v18, v22, v23
	v_mul_f32_e32 v22, 0x41000000, v22
	v_med3_f32 v67, v22, s64, v250
	v_mul_f32_e32 v22, 0x41000000, v23
	v_med3_f32 v23, v22, s64, v250
	v_cvt_pk_fp8_f32 v22, v67, v23
	v_cvt_pk_bf16_f32 v19, v24, v25
	v_mul_f32_e32 v23, 0x41000000, v24
	v_mul_f32_e32 v24, 0x41000000, v25
	v_med3_f32 v23, v23, s64, v250
	v_med3_f32 v24, v24, s64, v250
	v_cvt_pk_fp8_f32 v22, v23, v24 op_sel:[0,0,1]
	v_mul_f32_e32 v23, 0x41000000, v20
	v_med3_f32 v24, v23, s64, v250
	v_mul_f32_e32 v23, 0x41000000, v21
	v_med3_f32 v25, v23, s64, v250
	v_cvt_pk_fp8_f32 v23, v24, v25
	v_mul_f32_e32 v24, 0x41000000, v28
	v_mul_f32_e32 v25, 0x41000000, v29
	v_med3_f32 v24, v24, s64, v250
	v_med3_f32 v25, v25, s64, v250
	v_cvt_pk_fp8_f32 v23, v24, v25 op_sel:[0,0,1]
	ds_swizzle_b32 v24, v66 offset:swizzle(SWAP,16)
	v_cvt_pk_bf16_f32 v20, v20, v21
	v_cvt_pk_bf16_f32 v21, v28, v29
	global_store_dwordx4 v[106:107], v[18:21], off offset:256
	global_store_dwordx2 v[26:27], v[22:23], off offset:128
	s_waitcnt lgkmcnt(0)
	v_add_f32_e32 v18, v66, v24
	v_mov_b32_e32 v19, v18
	s_nop 1
	v_permlane32_swap_b32_e32 v18, v19
	s_and_saveexec_b64 s[26:27], s[2:3]
	s_cbranch_execz .LBB0_1057
	v_lshlrev_b64 v[20:21], 6, v[104:105]
	v_lshl_add_u64 v[20:21], s[24:25], 0, v[20:21]
	v_add_f32_e32 v18, v18, v19
	global_store_dword v[20:21], v18, off
.LBB0_1057:
	s_or_b64 exec, exec, s[26:27]
	s_waitcnt vmcnt(11)
	v_lshlrev_b32_e32 v20, 16, v14
	v_and_b32_e32 v21, 0xffff0000, v14
	v_lshlrev_b32_e32 v14, 16, v15
	v_and_b32_e32 v15, 0xffff0000, v15
	v_pk_add_f32 v[22:23], v[64:65], v[14:15]
	v_pk_add_f32 v[20:21], v[62:63], v[20:21]
	v_lshlrev_b32_e32 v14, 16, v16
	v_and_b32_e32 v15, 0xffff0000, v16
	v_lshlrev_b32_e32 v16, 16, v17
	v_and_b32_e32 v17, 0xffff0000, v17
	v_pk_add_f32 v[24:25], v[60:61], v[16:17]
	v_pk_add_f32 v[16:17], v[58:59], v[14:15]
	v_mul_f32_e32 v14, v21, v21
	v_mul_f32_e32 v15, v23, v23
	v_fmac_f32_e32 v14, v20, v20
	v_fmac_f32_e32 v15, v22, v22
	v_add_f32_e32 v14, v14, v15
	v_mul_f32_e32 v15, v17, v17
	v_mul_f32_e32 v26, v25, v25
	v_fmac_f32_e32 v15, v16, v16
	v_fmac_f32_e32 v26, v24, v24
	v_add_f32_e32 v15, v15, v26
	v_add_f32_e32 v26, v14, v15
	v_cvt_pk_bf16_f32 v14, v20, v21
	v_mul_f32_e32 v20, 0x41000000, v20
	v_med3_f32 v27, v20, s64, v250
	v_mul_f32_e32 v20, 0x41000000, v21
	v_med3_f32 v21, v20, s64, v250
	v_cvt_pk_fp8_f32 v20, v27, v21
	v_cvt_pk_bf16_f32 v15, v22, v23
	v_mul_f32_e32 v21, 0x41000000, v22
	v_mul_f32_e32 v22, 0x41000000, v23
	v_med3_f32 v21, v21, s64, v250
	v_med3_f32 v22, v22, s64, v250
	v_cvt_pk_fp8_f32 v20, v21, v22 op_sel:[0,0,1]
	v_mul_f32_e32 v21, 0x41000000, v16
	v_med3_f32 v22, v21, s64, v250
	v_mul_f32_e32 v21, 0x41000000, v17
	v_med3_f32 v23, v21, s64, v250
	v_cvt_pk_fp8_f32 v21, v22, v23
	v_mul_f32_e32 v22, 0x41000000, v24
	v_mul_f32_e32 v23, 0x41000000, v25
	v_med3_f32 v22, v22, s64, v250
	v_med3_f32 v23, v23, s64, v250
	v_cvt_pk_fp8_f32 v21, v22, v23 op_sel:[0,0,1]
	v_lshlrev_b64 v[18:19], 10, v[100:101]
	v_cvt_pk_bf16_f32 v16, v16, v17
	v_cvt_pk_bf16_f32 v17, v24, v25
	v_lshl_add_u64 v[18:19], v[30:31], 0, v[18:19]
	global_store_dwordx4 v[102:103], v[14:17], off
	global_store_dwordx2 v[18:19], v[20:21], off
	s_waitcnt vmcnt(12)
; __device__ __forceinline__ u32x4 pack8(const f32x4 a, const f32x4 b) { u32x4 w; w.x = cvt_pk_bf16(a[0], a[1]); w.y = cvt_pk_bf16(a[2], a[3]); w.z = cvt_pk_bf16(b[0], b[1]); w.w = cvt_pk_bf16(b[2], b[3]); return w; }
; __device__ __forceinline__ float sumsq4(const f32x4 v) { return (v[0] * v[0] + v[1] * v[1]) + (v[2] * v[2] + v[3] * v[3]); }
; __device__ __forceinline__ float xor16_add(float v) { return v + __int_as_float(__builtin_amdgcn_ds_swizzle(__float_as_int(v), 0x401F)); }
; __device__ __forceinline__ float xor32_add(float v) { auto rr = __builtin_amdgcn_permlane32_swap(__float_as_uint(v), __float_as_uint(v), false, false); return __uint_as_float(rr[0]) + __uint_as_float(rr[1]); }
; __device__ __forceinline__ f32x4 bf2f_lo(const u32x4 w, int h) { const unsigned a = h ? w.z : w.x, b = h ? w.w : w.y; return (f32x4){__uint_as_float(a << 16), __uint_as_float(a & 0xffff0000u), __uint_as_float(b << 16), __uint_as_float(b & 0xffff0000u)}; }
;     __device__ __forceinline__ void operator()(const f32x4 (&acc)[2][2][4][2], const Unit& u, int wr, int wc, int fr, int fq) const {
;     ...
;                 for (int bj = 0; bj < 2; ++bj) old[m][bj] = *(const u32x4*)(xb + (size_t)(row0 + ai * HALF + m * 16) * DM + col0 + bj * HALF);
; #pragma unroll
;             for (int m = 0; m < 4; ++m) {
;                 const int row = row0 + ai * HALF + m * 16; float ss = 0.f;
; #pragma unroll
;                 for (int bj = 0; bj < 2; ++bj) {
;                     const f32x4 v0 = bf2f_lo(old[m][bj], 0) + acc[ai][bj][m][0], v1 = bf2f_lo(old[m][bj], 1) + acc[ai][bj][m][1];
;                     ss += sumsq4(v0) + sumsq4(v1);
;                     *(u32x4*)(xb + (size_t)row * DM + col0 + bj * HALF) = pack8(v0, v1);
;                     { u32x2 w8; w8.x = pack4_fp8_x8(v0); w8.y = pack4_fp8_x8(v1); *(u32x2*)(xq + (size_t)row * DM + col0 + bj * HALF) = w8; }
;                 }
;                 ss = xor32_add(xor16_add(ss));
;                 if (fq == 0) ssx[(size_t)row * 16 + u.pn * 4 + wc] = ss;
;             }
	v_lshlrev_b32_e32 v14, 16, v10
	v_and_b32_e32 v15, 0xffff0000, v10
	v_lshlrev_b32_e32 v10, 16, v11
	v_and_b32_e32 v11, 0xffff0000, v11
	v_pk_add_f32 v[16:17], v[56:57], v[10:11]
	v_pk_add_f32 v[14:15], v[54:55], v[14:15]
	v_lshlrev_b32_e32 v10, 16, v12
	v_and_b32_e32 v11, 0xffff0000, v12
	v_lshlrev_b32_e32 v12, 16, v13
	v_and_b32_e32 v13, 0xffff0000, v13
	v_pk_add_f32 v[20:21], v[52:53], v[12:13]
	v_pk_add_f32 v[12:13], v[50:51], v[10:11]
	v_mul_f32_e32 v10, v15, v15
	v_mul_f32_e32 v11, v17, v17
	v_fmac_f32_e32 v10, v14, v14
	v_fmac_f32_e32 v11, v16, v16
	v_add_f32_e32 v10, v10, v11
	v_mul_f32_e32 v11, v13, v13
	v_mul_f32_e32 v22, v21, v21
	v_fmac_f32_e32 v11, v12, v12
	v_fmac_f32_e32 v22, v20, v20
	v_add_f32_e32 v11, v11, v22
	v_add_f32_e32 v10, v10, v11
	v_add_f32_e32 v22, v26, v10
	v_cvt_pk_bf16_f32 v10, v14, v15
	v_mul_f32_e32 v14, 0x41000000, v14
	v_med3_f32 v23, v14, s64, v250
	v_mul_f32_e32 v14, 0x41000000, v15
	v_med3_f32 v15, v14, s64, v250
	v_cvt_pk_fp8_f32 v14, v23, v15
	v_cvt_pk_bf16_f32 v11, v16, v17
	v_mul_f32_e32 v15, 0x41000000, v16
	v_mul_f32_e32 v16, 0x41000000, v17
	v_med3_f32 v15, v15, s64, v250
	v_med3_f32 v16, v16, s64, v250
	v_cvt_pk_fp8_f32 v14, v15, v16 op_sel:[0,0,1]
	v_mul_f32_e32 v15, 0x41000000, v12
	v_med3_f32 v16, v15, s64, v250
	v_mul_f32_e32 v15, 0x41000000, v13
	v_med3_f32 v17, v15, s64, v250
	v_cvt_pk_fp8_f32 v15, v16, v17
	v_mul_f32_e32 v16, 0x41000000, v20
	v_mul_f32_e32 v17, 0x41000000, v21
	v_med3_f32 v16, v16, s64, v250
	v_med3_f32 v17, v17, s64, v250
	v_cvt_pk_fp8_f32 v15, v16, v17 op_sel:[0,0,1]
	ds_swizzle_b32 v16, v22 offset:swizzle(SWAP,16)
	v_cvt_pk_bf16_f32 v12, v12, v13
	v_cvt_pk_bf16_f32 v13, v20, v21
	global_store_dwordx4 v[102:103], v[10:13], off offset:256
	global_store_dwordx2 v[18:19], v[14:15], off offset:128
	s_waitcnt lgkmcnt(0)
	v_add_f32_e32 v10, v22, v16
	v_mov_b32_e32 v11, v10
	s_nop 1
	v_permlane32_swap_b32_e32 v10, v11
	s_and_saveexec_b64 s[26:27], s[2:3]
	s_cbranch_execz .LBB0_1059
	v_lshlrev_b64 v[12:13], 6, v[100:101]
	v_lshl_add_u64 v[12:13], s[24:25], 0, v[12:13]
	v_add_f32_e32 v10, v10, v11
	global_store_dword v[12:13], v10, off
.LBB0_1059:
	s_or_b64 exec, exec, s[26:27]
	s_waitcnt vmcnt(13)
	v_lshlrev_b32_e32 v12, 16, v6
	v_and_b32_e32 v13, 0xffff0000, v6
	v_lshlrev_b32_e32 v6, 16, v7
	v_and_b32_e32 v7, 0xffff0000, v7
	v_pk_add_f32 v[14:15], v[48:49], v[6:7]
	v_pk_add_f32 v[12:13], v[46:47], v[12:13]
	v_lshlrev_b32_e32 v6, 16, v8
	v_and_b32_e32 v7, 0xffff0000, v8
	v_lshlrev_b32_e32 v8, 16, v9
	v_and_b32_e32 v9, 0xffff0000, v9
	v_pk_add_f32 v[16:17], v[44:45], v[8:9]
	v_pk_add_f32 v[8:9], v[42:43], v[6:7]
	v_mul_f32_e32 v6, v13, v13
	v_mul_f32_e32 v7, v15, v15
	v_fmac_f32_e32 v6, v12, v12
	v_fmac_f32_e32 v7, v14, v14
	v_add_f32_e32 v6, v6, v7
	v_mul_f32_e32 v7, v9, v9
	v_mul_f32_e32 v18, v17, v17
	v_fmac_f32_e32 v7, v8, v8
	v_fmac_f32_e32 v18, v16, v16
	v_add_f32_e32 v7, v7, v18
	v_add_f32_e32 v18, v6, v7
	v_cvt_pk_bf16_f32 v6, v12, v13
	v_mul_f32_e32 v12, 0x41000000, v12
	v_med3_f32 v19, v12, s64, v250
	v_mul_f32_e32 v12, 0x41000000, v13
	v_med3_f32 v13, v12, s64, v250
	v_cvt_pk_fp8_f32 v12, v19, v13
	v_cvt_pk_bf16_f32 v7, v14, v15
	v_mul_f32_e32 v13, 0x41000000, v14
	v_mul_f32_e32 v14, 0x41000000, v15
	v_med3_f32 v13, v13, s64, v250
	v_med3_f32 v14, v14, s64, v250
	v_cvt_pk_fp8_f32 v12, v13, v14 op_sel:[0,0,1]
	v_mul_f32_e32 v13, 0x41000000, v8
	v_med3_f32 v14, v13, s64, v250
	v_mul_f32_e32 v13, 0x41000000, v9
	v_med3_f32 v15, v13, s64, v250
	v_cvt_pk_fp8_f32 v13, v14, v15
	v_mul_f32_e32 v14, 0x41000000, v16
	v_mul_f32_e32 v15, 0x41000000, v17
	v_med3_f32 v14, v14, s64, v250
	v_med3_f32 v15, v15, s64, v250
	v_cvt_pk_fp8_f32 v13, v14, v15 op_sel:[0,0,1]
	v_lshlrev_b64 v[10:11], 10, v[32:33]
	v_cvt_pk_bf16_f32 v8, v8, v9
	v_cvt_pk_bf16_f32 v9, v16, v17
	v_lshl_add_u64 v[10:11], v[30:31], 0, v[10:11]
	global_store_dwordx4 v[98:99], v[6:9], off
	global_store_dwordx2 v[10:11], v[12:13], off
	s_waitcnt vmcnt(14)
	v_lshlrev_b32_e32 v6, 16, v2
	v_and_b32_e32 v7, 0xffff0000, v2
	v_lshlrev_b32_e32 v2, 16, v3
	v_and_b32_e32 v3, 0xffff0000, v3
	v_pk_add_f32 v[8:9], v[40:41], v[2:3]
	v_pk_add_f32 v[6:7], v[38:39], v[6:7]
	v_lshlrev_b32_e32 v2, 16, v4
	v_and_b32_e32 v3, 0xffff0000, v4
	v_lshlrev_b32_e32 v4, 16, v5
	v_and_b32_e32 v5, 0xffff0000, v5
	v_pk_add_f32 v[12:13], v[36:37], v[4:5]
	v_pk_add_f32 v[4:5], v[34:35], v[2:3]
	v_mul_f32_e32 v2, v7, v7
	v_mul_f32_e32 v3, v9, v9
	v_fmac_f32_e32 v2, v6, v6
	v_fmac_f32_e32 v3, v8, v8
	v_add_f32_e32 v2, v2, v3
	v_mul_f32_e32 v3, v5, v5
	v_mul_f32_e32 v14, v13, v13
	v_fmac_f32_e32 v3, v4, v4
	v_fmac_f32_e32 v14, v12, v12
	v_add_f32_e32 v3, v3, v14
	v_add_f32_e32 v2, v2, v3
	v_add_f32_e32 v14, v18, v2
	v_cvt_pk_bf16_f32 v2, v6, v7
	v_mul_f32_e32 v6, 0x41000000, v6
	v_med3_f32 v15, v6, s64, v250
	v_mul_f32_e32 v6, 0x41000000, v7
	v_med3_f32 v7, v6, s64, v250
	v_cvt_pk_fp8_f32 v6, v15, v7
	v_cvt_pk_bf16_f32 v3, v8, v9
	v_mul_f32_e32 v7, 0x41000000, v8
	v_mul_f32_e32 v8, 0x41000000, v9
	v_med3_f32 v7, v7, s64, v250
	v_med3_f32 v8, v8, s64, v250
	v_cvt_pk_fp8_f32 v6, v7, v8 op_sel:[0,0,1]
	v_mul_f32_e32 v7, 0x41000000, v4
	v_med3_f32 v8, v7, s64, v250
	v_mul_f32_e32 v7, 0x41000000, v5
	v_med3_f32 v9, v7, s64, v250
	v_cvt_pk_fp8_f32 v7, v8, v9
	v_mul_f32_e32 v8, 0x41000000, v12
	v_mul_f32_e32 v9, 0x41000000, v13
	v_med3_f32 v8, v8, s64, v250
	v_med3_f32 v9, v9, s64, v250
	v_cvt_pk_fp8_f32 v7, v8, v9 op_sel:[0,0,1]
	ds_swizzle_b32 v8, v14 offset:swizzle(SWAP,16)
	v_cvt_pk_bf16_f32 v4, v4, v5
	v_cvt_pk_bf16_f32 v5, v12, v13
	global_store_dwordx4 v[98:99], v[2:5], off offset:256
	global_store_dwordx2 v[10:11], v[6:7], off offset:128
	s_waitcnt lgkmcnt(0)
	v_add_f32_e32 v2, v14, v8
	v_mov_b32_e32 v3, v2
	s_nop 1
	v_permlane32_swap_b32_e32 v2, v3
	s_and_saveexec_b64 s[26:27], s[2:3]
	s_cbranch_execz .LBB0_1061
	v_lshlrev_b64 v[4:5], 6, v[32:33]
	v_lshl_add_u64 v[4:5], s[24:25], 0, v[4:5]
	v_add_f32_e32 v2, v2, v3
	global_store_dword v[4:5], v2, off

; #define GAS __attribute__((address_space(1)))
; #define LAS __attribute__((address_space(3)))
; __device__ __forceinline__ void tr_item(const TrJob& J, int item, LAS float* scr, int lane) {
;     ...
;     for (int j = 0; j < 4; ++j) { const int n = (lane >> 3) + 8 * j; const LAS float* s = scr + (8 * c) * 33 + n;
;         if (J.f8) { int w0 = 0, w1 = 0;
;             w0 = __builtin_amdgcn_cvt_pk_fp8_f32(s[0 * 33] * g[0] * 64.0f, s[1 * 33] * g[1] * 64.0f, w0, false); w0 = __builtin_amdgcn_cvt_pk_fp8_f32(s[2 * 33] * g[2] * 64.0f, s[3 * 33] * g[3] * 64.0f, w0, true);
;             w1 = __builtin_amdgcn_cvt_pk_fp8_f32(s[4 * 33] * g[4] * 64.0f, s[5 * 33] * g[5] * 64.0f, w1, false); w1 = __builtin_amdgcn_cvt_pk_fp8_f32(s[6 * 33] * g[6] * 64.0f, s[7 * 33] * g[7] * 64.0f, w1, true);
;             v2u o; o.x = (unsigned)w0; o.y = (unsigned)w1; *(GAS v2u*)((unsigned char*)J.dst + (size_t)tr_dest_row(J.mode, n0, n) * J.K + k0 + 8 * c) = o; }
; __global__ void __launch_bounds__(NWAVES * 64, 2) hybrid_fwd(Params P) {
;     ...
;                 for (int g = (l == 1 ? L1_DONE : L3_DONE) + gw; g < MOE_ITEMS; g += NGW) { TrJob J; int it; moe_job(kp, ws, l, g, J, it); tr_item(J, it, scr, lane_p); }
.LBB0_1145:
	s_waitcnt lgkmcnt(3)
	v_mul_f32_e32 v10, v24, v10
	v_mul_f32_e32 v24, 0x42800000, v10
	v_mul_f32_e32 v10, v23, v11
	v_mul_f32_e32 v11, 0x42800000, v10
	s_waitcnt lgkmcnt(1)
	v_mul_f32_e32 v6, v28, v6
	v_mul_f32_e32 v7, v27, v7
	v_cvt_pk_fp8_f32 v10, v24, v11
	v_mul_f32_e32 v6, 0x42800000, v6
	v_mul_f32_e32 v7, 0x42800000, v7
	v_cvt_pk_fp8_f32 v11, v6, v7
	v_mul_f32_e32 v8, v26, v8
	v_mul_f32_e32 v9, v25, v9
	s_waitcnt lgkmcnt(0)
	v_mul_f32_e32 v2, v30, v2
	v_mul_f32_e32 v3, v29, v3
	v_mul_f32_e32 v8, 0x42800000, v8
	v_mul_f32_e32 v9, 0x42800000, v9
	v_mul_f32_e32 v2, 0x42800000, v2
	v_mul_f32_e32 v3, 0x42800000, v3
	v_cvt_pk_fp8_f32 v10, v8, v9 op_sel:[0,0,1]
	v_cvt_pk_fp8_f32 v11, v2, v3 op_sel:[0,0,1]
	v_mov_b64_e32 v[2:3], s[4:5]
	v_mad_i64_i32 v[2:3], s[2:3], s6, v31, v[2:3]
	v_lshl_add_u64 v[2:3], v[2:3], 0, s[8:9]
	v_lshl_add_u64 v[2:3], v[2:3], 0, v[4:5]
	global_store_dwordx2 v[2:3], v[10:11], off
	s_waitcnt lgkmcnt(0)
	s_add_i32 s1, s1, s0
	s_cmp_gt_i32 s1, 0xa7ff
	s_cbranch_scc1 .LBB0_1215

; #define GAS __attribute__((address_space(1)))
; #define LAS __attribute__((address_space(3)))
; __device__ __forceinline__ int tr_dest_row(int mode, int n0, int n) {
;     if (mode == TM_IN) { const int gb = n0 < 672 ? n0 : n0 + 96; return gb + (n0 == 640 ? rope_pos(n) : n); }
;     if (mode == TM_UQ) return n0 + ((((n0 >> 5) % 3) == 2) ? rope_pos(n) : n);
;     if (mode == TM_UKV) { const int h = n0 >> 7, j0 = n0 & 127; return (j0 < 64 ? h * 64 + j0 : 512 + h * 64 + (j0 - 64)) + n; }
;     if (mode == TM_W1) return (n0 >> 7) * 256 + (n0 & 127) + n;
;     if (mode == TM_W3) return (n0 >> 7) * 256 + 128 + (n0 & 127) + n;
; __device__ __forceinline__ void tr_item(const TrJob& J, int item, LAS float* scr, int lane) {
;     ...
;     for (int j = 0; j < 4; ++j) { const int n = (lane >> 3) + 8 * j; const LAS float* s = scr + (8 * c) * 33 + n;
;         if (J.f8) { int w0 = 0, w1 = 0;
;             w0 = __builtin_amdgcn_cvt_pk_fp8_f32(s[0 * 33] * g[0] * 64.0f, s[1 * 33] * g[1] * 64.0f, w0, false); w0 = __builtin_amdgcn_cvt_pk_fp8_f32(s[2 * 33] * g[2] * 64.0f, s[3 * 33] * g[3] * 64.0f, w0, true);
;             w1 = __builtin_amdgcn_cvt_pk_fp8_f32(s[4 * 33] * g[4] * 64.0f, s[5 * 33] * g[5] * 64.0f, w1, false); w1 = __builtin_amdgcn_cvt_pk_fp8_f32(s[6 * 33] * g[6] * 64.0f, s[7 * 33] * g[7] * 64.0f, w1, true);
;             v2u o; o.x = (unsigned)w0; o.y = (unsigned)w1; *(GAS v2u*)((unsigned char*)J.dst + (size_t)tr_dest_row(J.mode, n0, n) * J.K + k0 + 8 * c) = o; }
.LBB0_1182:
	s_waitcnt vmcnt(0) lgkmcnt(3)
	v_mul_f32_e32 v10, v24, v10
	v_mul_f32_e32 v32, 0x42800000, v10
	v_mul_f32_e32 v10, v23, v11
	v_mul_f32_e32 v11, 0x42800000, v10
	s_waitcnt lgkmcnt(1)
	v_mul_f32_e32 v6, v28, v6
	v_mul_f32_e32 v7, v27, v7
	v_cvt_pk_fp8_f32 v10, v32, v11
	v_mul_f32_e32 v6, 0x42800000, v6
	v_mul_f32_e32 v7, 0x42800000, v7
	v_cvt_pk_fp8_f32 v11, v6, v7
	v_mul_f32_e32 v8, v26, v8
	v_mul_f32_e32 v9, v25, v9
	s_waitcnt lgkmcnt(0)
	v_mul_f32_e32 v2, v30, v2
	v_mul_f32_e32 v3, v29, v3
	v_mul_f32_e32 v8, 0x42800000, v8
	v_mul_f32_e32 v9, 0x42800000, v9
	v_mul_f32_e32 v2, 0x42800000, v2
	v_mul_f32_e32 v3, 0x42800000, v3
	v_cvt_pk_fp8_f32 v10, v8, v9 op_sel:[0,0,1]
	v_cvt_pk_fp8_f32 v11, v2, v3 op_sel:[0,0,1]
	v_mov_b64_e32 v[2:3], s[4:5]
	s_ashr_i32 s9, s8, 31
	v_mad_i64_i32 v[2:3], s[12:13], s6, v31, v[2:3]
	v_lshl_add_u64 v[2:3], v[2:3], 0, s[8:9]
	v_lshl_add_u64 v[2:3], v[2:3], 0, v[4:5]
	global_store_dwordx2 v[2:3], v[10:11], off
	ds_read2_b32 v[10:11], v14 offset0:8 offset1:41
	ds_read2_b32 v[8:9], v14 offset0:74 offset1:107
	ds_read2_b32 v[6:7], v14 offset0:140 offset1:173
	ds_read2_b32 v[2:3], v14 offset0:206 offset1:239
	s_cmp_lt_i32 s21, 4
	s_mov_b64 s[12:13], -1
	s_cbranch_scc1 .LBB0_1188
	s_cmp_gt_i32 s21, 4
	s_cbranch_scc0 .LBB0_1185
	v_add_u32_e32 v31, s15, v16
	s_mov_b64 s[12:13], 0

; #define GAS __attribute__((address_space(1)))
; #define LAS __attribute__((address_space(3)))
; __device__ __forceinline__ int tr_dest_row(int mode, int n0, int n) {
;     if (mode == TM_IN) { const int gb = n0 < 672 ? n0 : n0 + 96; return gb + (n0 == 640 ? rope_pos(n) : n); }
;     if (mode == TM_UQ) return n0 + ((((n0 >> 5) % 3) == 2) ? rope_pos(n) : n);
;     if (mode == TM_UKV) { const int h = n0 >> 7, j0 = n0 & 127; return (j0 < 64 ? h * 64 + j0 : 512 + h * 64 + (j0 - 64)) + n; }
;     if (mode == TM_W1) return (n0 >> 7) * 256 + (n0 & 127) + n;
;     if (mode == TM_W3) return (n0 >> 7) * 256 + 128 + (n0 & 127) + n;
; __device__ __forceinline__ void tr_item(const TrJob& J, int item, LAS float* scr, int lane) {
;     ...
;     for (int j = 0; j < 4; ++j) { const int n = (lane >> 3) + 8 * j; const LAS float* s = scr + (8 * c) * 33 + n;
;         if (J.f8) { int w0 = 0, w1 = 0;
;             w0 = __builtin_amdgcn_cvt_pk_fp8_f32(s[0 * 33] * g[0] * 64.0f, s[1 * 33] * g[1] * 64.0f, w0, false); w0 = __builtin_amdgcn_cvt_pk_fp8_f32(s[2 * 33] * g[2] * 64.0f, s[3 * 33] * g[3] * 64.0f, w0, true);
;             w1 = __builtin_amdgcn_cvt_pk_fp8_f32(s[4 * 33] * g[4] * 64.0f, s[5 * 33] * g[5] * 64.0f, w1, false); w1 = __builtin_amdgcn_cvt_pk_fp8_f32(s[6 * 33] * g[6] * 64.0f, s[7 * 33] * g[7] * 64.0f, w1, true);
;             v2u o; o.x = (unsigned)w0; o.y = (unsigned)w1; *(GAS v2u*)((unsigned char*)J.dst + (size_t)tr_dest_row(J.mode, n0, n) * J.K + k0 + 8 * c) = o; }
.LBB0_1193:
	s_waitcnt lgkmcnt(3)
	v_mul_f32_e32 v10, v24, v10
	v_mul_f32_e32 v32, 0x42800000, v10
	v_mul_f32_e32 v10, v23, v11
	v_mul_f32_e32 v11, 0x42800000, v10
	s_waitcnt lgkmcnt(1)
	v_mul_f32_e32 v6, v28, v6
	v_mul_f32_e32 v7, v27, v7
	v_cvt_pk_fp8_f32 v10, v32, v11
	v_mul_f32_e32 v6, 0x42800000, v6
	v_mul_f32_e32 v7, 0x42800000, v7
	v_cvt_pk_fp8_f32 v11, v6, v7
	v_mul_f32_e32 v8, v26, v8
	v_mul_f32_e32 v9, v25, v9
	s_waitcnt lgkmcnt(0)
	v_mul_f32_e32 v2, v30, v2
	v_mul_f32_e32 v3, v29, v3
	v_mul_f32_e32 v8, 0x42800000, v8
	v_mul_f32_e32 v9, 0x42800000, v9
	v_mul_f32_e32 v2, 0x42800000, v2
	v_mul_f32_e32 v3, 0x42800000, v3
	v_cvt_pk_fp8_f32 v10, v8, v9 op_sel:[0,0,1]
	v_cvt_pk_fp8_f32 v11, v2, v3 op_sel:[0,0,1]
	v_mov_b64_e32 v[2:3], s[4:5]
	v_mad_i64_i32 v[2:3], s[12:13], s6, v31, v[2:3]
	v_lshl_add_u64 v[2:3], v[2:3], 0, s[8:9]
	v_lshl_add_u64 v[2:3], v[2:3], 0, v[4:5]
	global_store_dwordx2 v[2:3], v[10:11], off
	ds_read2_b32 v[10:11], v14 offset0:16 offset1:49
	ds_read2_b32 v[8:9], v14 offset0:82 offset1:115
	ds_read2_b32 v[6:7], v14 offset0:148 offset1:181
	ds_read2_b32 v[2:3], v14 offset0:214 offset1:247
	s_cmp_lt_i32 s21, 4
	s_mov_b64 s[12:13], -1
	s_cbranch_scc1 .LBB0_1199
	s_cmp_gt_i32 s21, 4
	s_cbranch_scc0 .LBB0_1196
	v_add_u32_e32 v31, s15, v18
	s_mov_b64 s[12:13], 0

; #define GAS __attribute__((address_space(1)))
; #define LAS __attribute__((address_space(3)))
; __device__ __forceinline__ int tr_dest_row(int mode, int n0, int n) {
;     if (mode == TM_IN) { const int gb = n0 < 672 ? n0 : n0 + 96; return gb + (n0 == 640 ? rope_pos(n) : n); }
;     if (mode == TM_UQ) return n0 + ((((n0 >> 5) % 3) == 2) ? rope_pos(n) : n);
;     if (mode == TM_UKV) { const int h = n0 >> 7, j0 = n0 & 127; return (j0 < 64 ? h * 64 + j0 : 512 + h * 64 + (j0 - 64)) + n; }
;     if (mode == TM_W1) return (n0 >> 7) * 256 + (n0 & 127) + n;
;     if (mode == TM_W3) return (n0 >> 7) * 256 + 128 + (n0 & 127) + n;
; __device__ __forceinline__ void tr_item(const TrJob& J, int item, LAS float* scr, int lane) {
;     ...
;     for (int j = 0; j < 4; ++j) { const int n = (lane >> 3) + 8 * j; const LAS float* s = scr + (8 * c) * 33 + n;
;         if (J.f8) { int w0 = 0, w1 = 0;
;             w0 = __builtin_amdgcn_cvt_pk_fp8_f32(s[0 * 33] * g[0] * 64.0f, s[1 * 33] * g[1] * 64.0f, w0, false); w0 = __builtin_amdgcn_cvt_pk_fp8_f32(s[2 * 33] * g[2] * 64.0f, s[3 * 33] * g[3] * 64.0f, w0, true);
;             w1 = __builtin_amdgcn_cvt_pk_fp8_f32(s[4 * 33] * g[4] * 64.0f, s[5 * 33] * g[5] * 64.0f, w1, false); w1 = __builtin_amdgcn_cvt_pk_fp8_f32(s[6 * 33] * g[6] * 64.0f, s[7 * 33] * g[7] * 64.0f, w1, true);
;             v2u o; o.x = (unsigned)w0; o.y = (unsigned)w1; *(GAS v2u*)((unsigned char*)J.dst + (size_t)tr_dest_row(J.mode, n0, n) * J.K + k0 + 8 * c) = o; }
.LBB0_1204:
	s_waitcnt lgkmcnt(3)
	v_mul_f32_e32 v10, v24, v10
	v_mul_f32_e32 v32, 0x42800000, v10
	v_mul_f32_e32 v10, v23, v11
	v_mul_f32_e32 v11, 0x42800000, v10
	s_waitcnt lgkmcnt(1)
	v_mul_f32_e32 v6, v28, v6
	v_mul_f32_e32 v7, v27, v7
	v_cvt_pk_fp8_f32 v10, v32, v11
	v_mul_f32_e32 v6, 0x42800000, v6
	v_mul_f32_e32 v7, 0x42800000, v7
	v_cvt_pk_fp8_f32 v11, v6, v7
	v_mul_f32_e32 v8, v26, v8
	v_mul_f32_e32 v9, v25, v9
	s_waitcnt lgkmcnt(0)
	v_mul_f32_e32 v2, v30, v2
	v_mul_f32_e32 v3, v29, v3
	v_mul_f32_e32 v8, 0x42800000, v8
	v_mul_f32_e32 v9, 0x42800000, v9
	v_mul_f32_e32 v2, 0x42800000, v2
	v_mul_f32_e32 v3, 0x42800000, v3
	v_cvt_pk_fp8_f32 v10, v8, v9 op_sel:[0,0,1]
	v_cvt_pk_fp8_f32 v11, v2, v3 op_sel:[0,0,1]
	v_mov_b64_e32 v[2:3], s[4:5]
	v_mad_i64_i32 v[2:3], s[12:13], s6, v31, v[2:3]
	v_lshl_add_u64 v[2:3], v[2:3], 0, s[8:9]
	v_lshl_add_u64 v[2:3], v[2:3], 0, v[4:5]
	global_store_dwordx2 v[2:3], v[10:11], off
	ds_read2_b32 v[10:11], v14 offset0:24 offset1:57
	ds_read2_b32 v[8:9], v14 offset0:90 offset1:123
	ds_read2_b32 v[6:7], v14 offset0:156 offset1:189
	ds_read2_b32 v[2:3], v14 offset0:222 offset1:255
	s_cmp_lt_i32 s21, 4
	s_mov_b64 s[12:13], -1
	s_cbranch_scc1 .LBB0_1210
	s_cmp_gt_i32 s21, 4
	s_cbranch_scc0 .LBB0_1207
	v_add_u32_e32 v31, s15, v20
	s_mov_b64 s[12:13], 0

; __device__ __forceinline__ u32x4 pack8(const f32x4 a, const f32x4 b) { u32x4 w; w.x = cvt_pk_bf16(a[0], a[1]); w.y = cvt_pk_bf16(a[2], a[3]); w.z = cvt_pk_bf16(b[0], b[1]); w.w = cvt_pk_bf16(b[2], b[3]); return w; }
;     __device__ __forceinline__ void operator()(const f32x4 (&acc)[2][2][4][2], const Unit& u, int wr, int wc, int fr, int fq) const {
;     ...
;             for (int m = 0; m < 4; ++m) { const int row = row0 + ai * HALF + m * 16; const float g = t[ai * HALF + wr * 64 + m * 16 + fr];
; #pragma unroll
;                 for (int bj = 0; bj < 2; ++bj) {
;                     if (f8y) { u32x2 w8; w8.x = pack4_fp8_x8(acc[ai][bj][m][0] * g); w8.y = pack4_fp8_x8(acc[ai][bj][m][1] * g); *(u32x2*)((unsigned char*)y + (size_t)row * DM + col0 + bj * HALF) = w8; }
;                     else *(u32x4*)(y + (size_t)row * DM + col0 + bj * HALF) = pack8(acc[ai][bj][m][0] * g, acc[ai][bj][m][1] * g); } }
.LBB0_1458:
	v_lshlrev_b64 v[130:131], 10, v[4:5]
	s_andn2_b64 vcc, exec, s[34:35]
	v_lshl_add_u64 v[130:131], v[2:3], 0, v[130:131]
	s_cbranch_vccnz .LBB0_1460
	v_mul_f32_e32 v0, 0x41000000, v156
	v_mul_f32_e32 v5, 0x41000000, v157
	v_med3_f32 v0, v0, s64, v250
	v_med3_f32 v5, v5, s64, v250
	v_cvt_pk_fp8_f32 v156, v0, v5
	v_mul_f32_e32 v0, 0x41000000, v136
	v_mul_f32_e32 v5, 0x41000000, v137
	v_med3_f32 v0, v0, s64, v250
	v_med3_f32 v5, v5, s64, v250
	v_cvt_pk_fp8_f32 v156, v0, v5 op_sel:[0,0,1]
	v_mul_f32_e32 v0, 0x41000000, v134
	v_mul_f32_e32 v5, 0x41000000, v135
	v_med3_f32 v0, v0, s64, v250
	v_med3_f32 v5, v5, s64, v250
	v_mov_b32_e32 v136, v8
	v_mov_b32_e32 v137, v8
	v_cvt_pk_fp8_f32 v157, v0, v5
	v_pk_mul_f32 v[132:133], v[132:133], v[136:137]
	s_nop 0
	v_mul_f32_e32 v0, 0x41000000, v132
	v_mul_f32_e32 v5, 0x41000000, v133
	v_med3_f32 v0, v0, s64, v250
	v_med3_f32 v5, v5, s64, v250
	v_cvt_pk_fp8_f32 v157, v0, v5 op_sel:[0,0,1]
	global_store_dwordx2 v[130:131], v[156:157], off

; __device__ __forceinline__ u32x4 pack8(const f32x4 a, const f32x4 b) { u32x4 w; w.x = cvt_pk_bf16(a[0], a[1]); w.y = cvt_pk_bf16(a[2], a[3]); w.z = cvt_pk_bf16(b[0], b[1]); w.w = cvt_pk_bf16(b[2], b[3]); return w; }
;     __device__ __forceinline__ void operator()(const f32x4 (&acc)[2][2][4][2], const Unit& u, int wr, int wc, int fr, int fq) const {
;     ...
;             for (int m = 0; m < 4; ++m) { const int row = row0 + ai * HALF + m * 16; const float g = t[ai * HALF + wr * 64 + m * 16 + fr];
; #pragma unroll
;                 for (int bj = 0; bj < 2; ++bj) {
;                     if (f8y) { u32x2 w8; w8.x = pack4_fp8_x8(acc[ai][bj][m][0] * g); w8.y = pack4_fp8_x8(acc[ai][bj][m][1] * g); *(u32x2*)((unsigned char*)y + (size_t)row * DM + col0 + bj * HALF) = w8; }
;                     else *(u32x4*)(y + (size_t)row * DM + col0 + bj * HALF) = pack8(acc[ai][bj][m][0] * g, acc[ai][bj][m][1] * g); } }
.LBB0_1462:
	s_andn2_b64 vcc, exec, s[34:35]
	s_cbranch_vccnz .LBB0_1464
	v_mul_f32_e32 v0, 0x41000000, v126
	v_mul_f32_e32 v5, 0x41000000, v127
	v_med3_f32 v0, v0, s64, v250
	v_med3_f32 v5, v5, s64, v250
	v_cvt_pk_fp8_f32 v126, v0, v5
	v_mul_f32_e32 v0, 0x41000000, v128
	v_mul_f32_e32 v5, 0x41000000, v129
	v_med3_f32 v0, v0, s64, v250
	v_med3_f32 v5, v5, s64, v250
	v_cvt_pk_fp8_f32 v126, v0, v5 op_sel:[0,0,1]
	v_mul_f32_e32 v0, 0x41000000, v122
	v_mul_f32_e32 v5, 0x41000000, v123
	v_med3_f32 v0, v0, s64, v250
	v_med3_f32 v5, v5, s64, v250
	v_mov_b32_e32 v9, v8
	v_cvt_pk_fp8_f32 v127, v0, v5
	v_pk_mul_f32 v[8:9], v[124:125], v[8:9]
	s_nop 0
	v_mul_f32_e32 v0, 0x41000000, v8
	v_mul_f32_e32 v5, 0x41000000, v9
	v_med3_f32 v0, v0, s64, v250
	v_med3_f32 v5, v5, s64, v250
	v_cvt_pk_fp8_f32 v127, v0, v5 op_sel:[0,0,1]
	global_store_dwordx2 v[130:131], v[126:127], off offset:128

; __device__ __forceinline__ u32x4 pack8(const f32x4 a, const f32x4 b) { u32x4 w; w.x = cvt_pk_bf16(a[0], a[1]); w.y = cvt_pk_bf16(a[2], a[3]); w.z = cvt_pk_bf16(b[0], b[1]); w.w = cvt_pk_bf16(b[2], b[3]); return w; }
;     __device__ __forceinline__ void operator()(const f32x4 (&acc)[2][2][4][2], const Unit& u, int wr, int wc, int fr, int fq) const {
;     ...
;             for (int m = 0; m < 4; ++m) { const int row = row0 + ai * HALF + m * 16; const float g = t[ai * HALF + wr * 64 + m * 16 + fr];
; #pragma unroll
;                 for (int bj = 0; bj < 2; ++bj) {
;                     if (f8y) { u32x2 w8; w8.x = pack4_fp8_x8(acc[ai][bj][m][0] * g); w8.y = pack4_fp8_x8(acc[ai][bj][m][1] * g); *(u32x2*)((unsigned char*)y + (size_t)row * DM + col0 + bj * HALF) = w8; }
;                     else *(u32x4*)(y + (size_t)row * DM + col0 + bj * HALF) = pack8(acc[ai][bj][m][0] * g, acc[ai][bj][m][1] * g); } }
.LBB0_1466:
	v_lshlrev_b64 v[114:115], 10, v[124:125]
	s_andn2_b64 vcc, exec, s[34:35]
	v_lshl_add_u64 v[114:115], v[2:3], 0, v[114:115]
	s_cbranch_vccnz .LBB0_1468
	v_mul_f32_e32 v0, 0x41000000, v126
	v_mul_f32_e32 v5, 0x41000000, v127
	v_med3_f32 v0, v0, s64, v250
	v_med3_f32 v5, v5, s64, v250
	v_cvt_pk_fp8_f32 v124, v0, v5
	v_mul_f32_e32 v0, 0x41000000, v120
	v_mul_f32_e32 v5, 0x41000000, v121
	v_med3_f32 v0, v0, s64, v250
	v_med3_f32 v5, v5, s64, v250
	v_cvt_pk_fp8_f32 v124, v0, v5 op_sel:[0,0,1]
	v_mul_f32_e32 v0, 0x41000000, v118
	v_mul_f32_e32 v5, 0x41000000, v119
	v_med3_f32 v0, v0, s64, v250
	v_med3_f32 v5, v5, s64, v250
	v_mov_b32_e32 v120, v8
	v_mov_b32_e32 v121, v8
	v_cvt_pk_fp8_f32 v125, v0, v5
	v_pk_mul_f32 v[116:117], v[116:117], v[120:121]
	s_nop 0
	v_mul_f32_e32 v0, 0x41000000, v116
	v_mul_f32_e32 v5, 0x41000000, v117
	v_med3_f32 v0, v0, s64, v250
	v_med3_f32 v5, v5, s64, v250
	v_cvt_pk_fp8_f32 v125, v0, v5 op_sel:[0,0,1]
	global_store_dwordx2 v[114:115], v[124:125], off

; __device__ __forceinline__ u32x4 pack8(const f32x4 a, const f32x4 b) { u32x4 w; w.x = cvt_pk_bf16(a[0], a[1]); w.y = cvt_pk_bf16(a[2], a[3]); w.z = cvt_pk_bf16(b[0], b[1]); w.w = cvt_pk_bf16(b[2], b[3]); return w; }
;     __device__ __forceinline__ void operator()(const f32x4 (&acc)[2][2][4][2], const Unit& u, int wr, int wc, int fr, int fq) const {
;     ...
;             for (int m = 0; m < 4; ++m) { const int row = row0 + ai * HALF + m * 16; const float g = t[ai * HALF + wr * 64 + m * 16 + fr];
; #pragma unroll
;                 for (int bj = 0; bj < 2; ++bj) {
;                     if (f8y) { u32x2 w8; w8.x = pack4_fp8_x8(acc[ai][bj][m][0] * g); w8.y = pack4_fp8_x8(acc[ai][bj][m][1] * g); *(u32x2*)((unsigned char*)y + (size_t)row * DM + col0 + bj * HALF) = w8; }
;                     else *(u32x4*)(y + (size_t)row * DM + col0 + bj * HALF) = pack8(acc[ai][bj][m][0] * g, acc[ai][bj][m][1] * g); } }
.LBB0_1470:
	s_andn2_b64 vcc, exec, s[34:35]
	s_cbranch_vccnz .LBB0_1472
	v_mul_f32_e32 v0, 0x41000000, v110
	v_mul_f32_e32 v5, 0x41000000, v111
	v_med3_f32 v0, v0, s64, v250
	v_med3_f32 v5, v5, s64, v250
	v_cvt_pk_fp8_f32 v110, v0, v5
	v_mul_f32_e32 v0, 0x41000000, v112
	v_mul_f32_e32 v5, 0x41000000, v113
	v_med3_f32 v0, v0, s64, v250
	v_med3_f32 v5, v5, s64, v250
	v_cvt_pk_fp8_f32 v110, v0, v5 op_sel:[0,0,1]
	v_mul_f32_e32 v0, 0x41000000, v106
	v_mul_f32_e32 v5, 0x41000000, v107
	v_med3_f32 v0, v0, s64, v250
	v_med3_f32 v5, v5, s64, v250
	v_mov_b32_e32 v9, v8
	v_cvt_pk_fp8_f32 v111, v0, v5
	v_pk_mul_f32 v[8:9], v[108:109], v[8:9]
	s_nop 0
	v_mul_f32_e32 v0, 0x41000000, v8
	v_mul_f32_e32 v5, 0x41000000, v9
	v_med3_f32 v0, v0, s64, v250
	v_med3_f32 v5, v5, s64, v250
	v_cvt_pk_fp8_f32 v111, v0, v5 op_sel:[0,0,1]
	global_store_dwordx2 v[114:115], v[110:111], off offset:128

; __device__ __forceinline__ u32x4 pack8(const f32x4 a, const f32x4 b) { u32x4 w; w.x = cvt_pk_bf16(a[0], a[1]); w.y = cvt_pk_bf16(a[2], a[3]); w.z = cvt_pk_bf16(b[0], b[1]); w.w = cvt_pk_bf16(b[2], b[3]); return w; }
;     __device__ __forceinline__ void operator()(const f32x4 (&acc)[2][2][4][2], const Unit& u, int wr, int wc, int fr, int fq) const {
;     ...
;             for (int m = 0; m < 4; ++m) { const int row = row0 + ai * HALF + m * 16; const float g = t[ai * HALF + wr * 64 + m * 16 + fr];
; #pragma unroll
;                 for (int bj = 0; bj < 2; ++bj) {
;                     if (f8y) { u32x2 w8; w8.x = pack4_fp8_x8(acc[ai][bj][m][0] * g); w8.y = pack4_fp8_x8(acc[ai][bj][m][1] * g); *(u32x2*)((unsigned char*)y + (size_t)row * DM + col0 + bj * HALF) = w8; }
;                     else *(u32x4*)(y + (size_t)row * DM + col0 + bj * HALF) = pack8(acc[ai][bj][m][0] * g, acc[ai][bj][m][1] * g); } }
.LBB0_1474:
	v_lshlrev_b64 v[98:99], 10, v[108:109]
	s_andn2_b64 vcc, exec, s[34:35]
	v_lshl_add_u64 v[98:99], v[2:3], 0, v[98:99]
	s_cbranch_vccnz .LBB0_1476
	v_mul_f32_e32 v0, 0x41000000, v110
	v_mul_f32_e32 v5, 0x41000000, v111
	v_med3_f32 v0, v0, s64, v250
	v_med3_f32 v5, v5, s64, v250
	v_cvt_pk_fp8_f32 v108, v0, v5
	v_mul_f32_e32 v0, 0x41000000, v104
	v_mul_f32_e32 v5, 0x41000000, v105
	v_med3_f32 v0, v0, s64, v250
	v_med3_f32 v5, v5, s64, v250
	v_cvt_pk_fp8_f32 v108, v0, v5 op_sel:[0,0,1]
	v_mul_f32_e32 v0, 0x41000000, v102
	v_mul_f32_e32 v5, 0x41000000, v103
	v_med3_f32 v0, v0, s64, v250
	v_med3_f32 v5, v5, s64, v250
	v_mov_b32_e32 v104, v8
	v_mov_b32_e32 v105, v8
	v_cvt_pk_fp8_f32 v109, v0, v5
	v_pk_mul_f32 v[100:101], v[100:101], v[104:105]
	s_nop 0
	v_mul_f32_e32 v0, 0x41000000, v100
	v_mul_f32_e32 v5, 0x41000000, v101
	v_med3_f32 v0, v0, s64, v250
	v_med3_f32 v5, v5, s64, v250
	v_cvt_pk_fp8_f32 v109, v0, v5 op_sel:[0,0,1]
	global_store_dwordx2 v[98:99], v[108:109], off

; __device__ __forceinline__ u32x4 pack8(const f32x4 a, const f32x4 b) { u32x4 w; w.x = cvt_pk_bf16(a[0], a[1]); w.y = cvt_pk_bf16(a[2], a[3]); w.z = cvt_pk_bf16(b[0], b[1]); w.w = cvt_pk_bf16(b[2], b[3]); return w; }
;     __device__ __forceinline__ void operator()(const f32x4 (&acc)[2][2][4][2], const Unit& u, int wr, int wc, int fr, int fq) const {
;     ...
;             for (int m = 0; m < 4; ++m) { const int row = row0 + ai * HALF + m * 16; const float g = t[ai * HALF + wr * 64 + m * 16 + fr];
; #pragma unroll
;                 for (int bj = 0; bj < 2; ++bj) {
;                     if (f8y) { u32x2 w8; w8.x = pack4_fp8_x8(acc[ai][bj][m][0] * g); w8.y = pack4_fp8_x8(acc[ai][bj][m][1] * g); *(u32x2*)((unsigned char*)y + (size_t)row * DM + col0 + bj * HALF) = w8; }
;                     else *(u32x4*)(y + (size_t)row * DM + col0 + bj * HALF) = pack8(acc[ai][bj][m][0] * g, acc[ai][bj][m][1] * g); } }
.LBB0_1478:
	s_andn2_b64 vcc, exec, s[34:35]
	s_cbranch_vccnz .LBB0_1480
	v_mul_f32_e32 v0, 0x41000000, v94
	v_mul_f32_e32 v5, 0x41000000, v95
	v_med3_f32 v0, v0, s64, v250
	v_med3_f32 v5, v5, s64, v250
	v_cvt_pk_fp8_f32 v94, v0, v5
	v_mul_f32_e32 v0, 0x41000000, v96
	v_mul_f32_e32 v5, 0x41000000, v97
	v_med3_f32 v0, v0, s64, v250
	v_med3_f32 v5, v5, s64, v250
	v_cvt_pk_fp8_f32 v94, v0, v5 op_sel:[0,0,1]
	v_mul_f32_e32 v0, 0x41000000, v90
	v_mul_f32_e32 v5, 0x41000000, v91
	v_med3_f32 v0, v0, s64, v250
	v_med3_f32 v5, v5, s64, v250
	v_mov_b32_e32 v9, v8
	v_cvt_pk_fp8_f32 v95, v0, v5
	v_pk_mul_f32 v[8:9], v[92:93], v[8:9]
	s_nop 0
	v_mul_f32_e32 v0, 0x41000000, v8
	v_mul_f32_e32 v5, 0x41000000, v9
	v_med3_f32 v0, v0, s64, v250
	v_med3_f32 v5, v5, s64, v250
	v_cvt_pk_fp8_f32 v95, v0, v5 op_sel:[0,0,1]
	global_store_dwordx2 v[98:99], v[94:95], off offset:128

; __device__ __forceinline__ u32x4 pack8(const f32x4 a, const f32x4 b) { u32x4 w; w.x = cvt_pk_bf16(a[0], a[1]); w.y = cvt_pk_bf16(a[2], a[3]); w.z = cvt_pk_bf16(b[0], b[1]); w.w = cvt_pk_bf16(b[2], b[3]); return w; }
;     __device__ __forceinline__ void operator()(const f32x4 (&acc)[2][2][4][2], const Unit& u, int wr, int wc, int fr, int fq) const {
;     ...
;             for (int m = 0; m < 4; ++m) { const int row = row0 + ai * HALF + m * 16; const float g = t[ai * HALF + wr * 64 + m * 16 + fr];
; #pragma unroll
;                 for (int bj = 0; bj < 2; ++bj) {
;                     if (f8y) { u32x2 w8; w8.x = pack4_fp8_x8(acc[ai][bj][m][0] * g); w8.y = pack4_fp8_x8(acc[ai][bj][m][1] * g); *(u32x2*)((unsigned char*)y + (size_t)row * DM + col0 + bj * HALF) = w8; }
;                     else *(u32x4*)(y + (size_t)row * DM + col0 + bj * HALF) = pack8(acc[ai][bj][m][0] * g, acc[ai][bj][m][1] * g); } }
.LBB0_1482:
	v_lshlrev_b64 v[82:83], 10, v[92:93]
	s_andn2_b64 vcc, exec, s[34:35]
	v_lshl_add_u64 v[82:83], v[2:3], 0, v[82:83]
	s_cbranch_vccnz .LBB0_1484
	v_mul_f32_e32 v0, 0x41000000, v94
	v_mul_f32_e32 v5, 0x41000000, v95
	v_med3_f32 v0, v0, s64, v250
	v_med3_f32 v5, v5, s64, v250
	v_cvt_pk_fp8_f32 v92, v0, v5
	v_mul_f32_e32 v0, 0x41000000, v88
	v_mul_f32_e32 v5, 0x41000000, v89
	v_med3_f32 v0, v0, s64, v250
	v_med3_f32 v5, v5, s64, v250
	v_cvt_pk_fp8_f32 v92, v0, v5 op_sel:[0,0,1]
	v_mul_f32_e32 v0, 0x41000000, v86
	v_mul_f32_e32 v5, 0x41000000, v87
	v_med3_f32 v0, v0, s64, v250
	v_med3_f32 v5, v5, s64, v250
	v_mov_b32_e32 v88, v8
	v_mov_b32_e32 v89, v8
	v_cvt_pk_fp8_f32 v93, v0, v5
	v_pk_mul_f32 v[84:85], v[84:85], v[88:89]
	s_nop 0
	v_mul_f32_e32 v0, 0x41000000, v84
	v_mul_f32_e32 v5, 0x41000000, v85
	v_med3_f32 v0, v0, s64, v250
	v_med3_f32 v5, v5, s64, v250
	v_cvt_pk_fp8_f32 v93, v0, v5 op_sel:[0,0,1]
	global_store_dwordx2 v[82:83], v[92:93], off

; __device__ __forceinline__ u32x4 pack8(const f32x4 a, const f32x4 b) { u32x4 w; w.x = cvt_pk_bf16(a[0], a[1]); w.y = cvt_pk_bf16(a[2], a[3]); w.z = cvt_pk_bf16(b[0], b[1]); w.w = cvt_pk_bf16(b[2], b[3]); return w; }
;     __device__ __forceinline__ void operator()(const f32x4 (&acc)[2][2][4][2], const Unit& u, int wr, int wc, int fr, int fq) const {
;     ...
;             for (int m = 0; m < 4; ++m) { const int row = row0 + ai * HALF + m * 16; const float g = t[ai * HALF + wr * 64 + m * 16 + fr];
; #pragma unroll
;                 for (int bj = 0; bj < 2; ++bj) {
;                     if (f8y) { u32x2 w8; w8.x = pack4_fp8_x8(acc[ai][bj][m][0] * g); w8.y = pack4_fp8_x8(acc[ai][bj][m][1] * g); *(u32x2*)((unsigned char*)y + (size_t)row * DM + col0 + bj * HALF) = w8; }
;                     else *(u32x4*)(y + (size_t)row * DM + col0 + bj * HALF) = pack8(acc[ai][bj][m][0] * g, acc[ai][bj][m][1] * g); } }
.LBB0_1486:
	s_andn2_b64 vcc, exec, s[34:35]
	s_cbranch_vccnz .LBB0_1488
	v_mul_f32_e32 v0, 0x41000000, v78
	v_mul_f32_e32 v5, 0x41000000, v79
	v_med3_f32 v0, v0, s64, v250
	v_med3_f32 v5, v5, s64, v250
	v_cvt_pk_fp8_f32 v78, v0, v5
	v_mul_f32_e32 v0, 0x41000000, v80
	v_mul_f32_e32 v5, 0x41000000, v81
	v_med3_f32 v0, v0, s64, v250
	v_med3_f32 v5, v5, s64, v250
	v_cvt_pk_fp8_f32 v78, v0, v5 op_sel:[0,0,1]
	v_mul_f32_e32 v0, 0x41000000, v70
	v_mul_f32_e32 v5, 0x41000000, v71
	v_med3_f32 v0, v0, s64, v250
	v_med3_f32 v5, v5, s64, v250
	v_mov_b32_e32 v9, v8
	v_cvt_pk_fp8_f32 v79, v0, v5
	v_pk_mul_f32 v[8:9], v[72:73], v[8:9]
	s_nop 0
	v_mul_f32_e32 v0, 0x41000000, v8
	v_mul_f32_e32 v5, 0x41000000, v9
	v_med3_f32 v0, v0, s64, v250
	v_med3_f32 v5, v5, s64, v250
	v_cvt_pk_fp8_f32 v79, v0, v5 op_sel:[0,0,1]
	global_store_dwordx2 v[82:83], v[78:79], off offset:128

; __device__ __forceinline__ u32x4 pack8(const f32x4 a, const f32x4 b) { u32x4 w; w.x = cvt_pk_bf16(a[0], a[1]); w.y = cvt_pk_bf16(a[2], a[3]); w.z = cvt_pk_bf16(b[0], b[1]); w.w = cvt_pk_bf16(b[2], b[3]); return w; }
;     __device__ __forceinline__ void operator()(const f32x4 (&acc)[2][2][4][2], const Unit& u, int wr, int wc, int fr, int fq) const {
;     ...
;             for (int m = 0; m < 4; ++m) { const int row = row0 + ai * HALF + m * 16; const float g = t[ai * HALF + wr * 64 + m * 16 + fr];
; #pragma unroll
;                 for (int bj = 0; bj < 2; ++bj) {
;                     if (f8y) { u32x2 w8; w8.x = pack4_fp8_x8(acc[ai][bj][m][0] * g); w8.y = pack4_fp8_x8(acc[ai][bj][m][1] * g); *(u32x2*)((unsigned char*)y + (size_t)row * DM + col0 + bj * HALF) = w8; }
;                     else *(u32x4*)(y + (size_t)row * DM + col0 + bj * HALF) = pack8(acc[ai][bj][m][0] * g, acc[ai][bj][m][1] * g); } }
.LBB0_1490:
	v_lshlrev_b64 v[66:67], 10, v[78:79]
	s_andn2_b64 vcc, exec, s[34:35]
	v_lshl_add_u64 v[66:67], v[2:3], 0, v[66:67]
	s_cbranch_vccnz .LBB0_1492
	v_mul_f32_e32 v0, 0x41000000, v74
	v_mul_f32_e32 v5, 0x41000000, v75
	v_med3_f32 v0, v0, s64, v250
	v_med3_f32 v5, v5, s64, v250
	v_cvt_pk_fp8_f32 v74, v0, v5
	v_mul_f32_e32 v0, 0x41000000, v76
	v_mul_f32_e32 v5, 0x41000000, v77
	v_med3_f32 v0, v0, s64, v250
	v_med3_f32 v5, v5, s64, v250
	v_cvt_pk_fp8_f32 v74, v0, v5 op_sel:[0,0,1]
	v_mul_f32_e32 v0, 0x41000000, v72
	v_mul_f32_e32 v5, 0x41000000, v73
	v_med3_f32 v0, v0, s64, v250
	v_med3_f32 v5, v5, s64, v250
	v_mov_b32_e32 v76, v8
	v_mov_b32_e32 v77, v8
	v_cvt_pk_fp8_f32 v75, v0, v5
	v_pk_mul_f32 v[68:69], v[68:69], v[76:77]
	s_nop 0
	v_mul_f32_e32 v0, 0x41000000, v68
	v_mul_f32_e32 v5, 0x41000000, v69
	v_med3_f32 v0, v0, s64, v250
	v_med3_f32 v5, v5, s64, v250
	v_cvt_pk_fp8_f32 v75, v0, v5 op_sel:[0,0,1]
	global_store_dwordx2 v[66:67], v[74:75], off

; __device__ __forceinline__ u32x4 pack8(const f32x4 a, const f32x4 b) { u32x4 w; w.x = cvt_pk_bf16(a[0], a[1]); w.y = cvt_pk_bf16(a[2], a[3]); w.z = cvt_pk_bf16(b[0], b[1]); w.w = cvt_pk_bf16(b[2], b[3]); return w; }
;     __device__ __forceinline__ void operator()(const f32x4 (&acc)[2][2][4][2], const Unit& u, int wr, int wc, int fr, int fq) const {
;     ...
;             for (int m = 0; m < 4; ++m) { const int row = row0 + ai * HALF + m * 16; const float g = t[ai * HALF + wr * 64 + m * 16 + fr];
; #pragma unroll
;                 for (int bj = 0; bj < 2; ++bj) {
;                     if (f8y) { u32x2 w8; w8.x = pack4_fp8_x8(acc[ai][bj][m][0] * g); w8.y = pack4_fp8_x8(acc[ai][bj][m][1] * g); *(u32x2*)((unsigned char*)y + (size_t)row * DM + col0 + bj * HALF) = w8; }
;                     else *(u32x4*)(y + (size_t)row * DM + col0 + bj * HALF) = pack8(acc[ai][bj][m][0] * g, acc[ai][bj][m][1] * g); } }
.LBB0_1494:
	s_andn2_b64 vcc, exec, s[34:35]
	s_cbranch_vccnz .LBB0_1496
	v_mul_f32_e32 v0, 0x41000000, v62
	v_mul_f32_e32 v5, 0x41000000, v63
	v_med3_f32 v0, v0, s64, v250
	v_med3_f32 v5, v5, s64, v250
	v_cvt_pk_fp8_f32 v62, v0, v5
	v_mul_f32_e32 v0, 0x41000000, v64
	v_mul_f32_e32 v5, 0x41000000, v65
	v_med3_f32 v0, v0, s64, v250
	v_med3_f32 v5, v5, s64, v250
	v_cvt_pk_fp8_f32 v62, v0, v5 op_sel:[0,0,1]
	v_mul_f32_e32 v0, 0x41000000, v58
	v_mul_f32_e32 v5, 0x41000000, v59
	v_med3_f32 v0, v0, s64, v250
	v_med3_f32 v5, v5, s64, v250
	v_mov_b32_e32 v9, v8
	v_cvt_pk_fp8_f32 v63, v0, v5
	v_pk_mul_f32 v[8:9], v[60:61], v[8:9]
	s_nop 0
	v_mul_f32_e32 v0, 0x41000000, v8
	v_mul_f32_e32 v5, 0x41000000, v9
	v_med3_f32 v0, v0, s64, v250
	v_med3_f32 v5, v5, s64, v250
	v_cvt_pk_fp8_f32 v63, v0, v5 op_sel:[0,0,1]
	global_store_dwordx2 v[66:67], v[62:63], off offset:128

; __device__ __forceinline__ u32x4 pack8(const f32x4 a, const f32x4 b) { u32x4 w; w.x = cvt_pk_bf16(a[0], a[1]); w.y = cvt_pk_bf16(a[2], a[3]); w.z = cvt_pk_bf16(b[0], b[1]); w.w = cvt_pk_bf16(b[2], b[3]); return w; }
;     __device__ __forceinline__ void operator()(const f32x4 (&acc)[2][2][4][2], const Unit& u, int wr, int wc, int fr, int fq) const {
;     ...
;             for (int m = 0; m < 4; ++m) { const int row = row0 + ai * HALF + m * 16; const float g = t[ai * HALF + wr * 64 + m * 16 + fr];
; #pragma unroll
;                 for (int bj = 0; bj < 2; ++bj) {
;                     if (f8y) { u32x2 w8; w8.x = pack4_fp8_x8(acc[ai][bj][m][0] * g); w8.y = pack4_fp8_x8(acc[ai][bj][m][1] * g); *(u32x2*)((unsigned char*)y + (size_t)row * DM + col0 + bj * HALF) = w8; }
;                     else *(u32x4*)(y + (size_t)row * DM + col0 + bj * HALF) = pack8(acc[ai][bj][m][0] * g, acc[ai][bj][m][1] * g); } }
.LBB0_1498:
	v_lshlrev_b64 v[50:51], 10, v[60:61]
	s_andn2_b64 vcc, exec, s[34:35]
	v_lshl_add_u64 v[50:51], v[2:3], 0, v[50:51]
	s_cbranch_vccnz .LBB0_1500
	v_mul_f32_e32 v0, 0x41000000, v62
	v_mul_f32_e32 v5, 0x41000000, v63
	v_med3_f32 v0, v0, s64, v250
	v_med3_f32 v5, v5, s64, v250
	v_cvt_pk_fp8_f32 v60, v0, v5
	v_mul_f32_e32 v0, 0x41000000, v56
	v_mul_f32_e32 v5, 0x41000000, v57
	v_med3_f32 v0, v0, s64, v250
	v_med3_f32 v5, v5, s64, v250
	v_cvt_pk_fp8_f32 v60, v0, v5 op_sel:[0,0,1]
	v_mul_f32_e32 v0, 0x41000000, v54
	v_mul_f32_e32 v5, 0x41000000, v55
	v_med3_f32 v0, v0, s64, v250
	v_med3_f32 v5, v5, s64, v250
	v_mov_b32_e32 v56, v8
	v_mov_b32_e32 v57, v8
	v_cvt_pk_fp8_f32 v61, v0, v5
	v_pk_mul_f32 v[52:53], v[52:53], v[56:57]
	s_nop 0
	v_mul_f32_e32 v0, 0x41000000, v52
	v_mul_f32_e32 v5, 0x41000000, v53
	v_med3_f32 v0, v0, s64, v250
	v_med3_f32 v5, v5, s64, v250
	v_cvt_pk_fp8_f32 v61, v0, v5 op_sel:[0,0,1]
	global_store_dwordx2 v[50:51], v[60:61], off

; __device__ __forceinline__ u32x4 pack8(const f32x4 a, const f32x4 b) { u32x4 w; w.x = cvt_pk_bf16(a[0], a[1]); w.y = cvt_pk_bf16(a[2], a[3]); w.z = cvt_pk_bf16(b[0], b[1]); w.w = cvt_pk_bf16(b[2], b[3]); return w; }
;     __device__ __forceinline__ void operator()(const f32x4 (&acc)[2][2][4][2], const Unit& u, int wr, int wc, int fr, int fq) const {
;     ...
;             for (int m = 0; m < 4; ++m) { const int row = row0 + ai * HALF + m * 16; const float g = t[ai * HALF + wr * 64 + m * 16 + fr];
; #pragma unroll
;                 for (int bj = 0; bj < 2; ++bj) {
;                     if (f8y) { u32x2 w8; w8.x = pack4_fp8_x8(acc[ai][bj][m][0] * g); w8.y = pack4_fp8_x8(acc[ai][bj][m][1] * g); *(u32x2*)((unsigned char*)y + (size_t)row * DM + col0 + bj * HALF) = w8; }
;                     else *(u32x4*)(y + (size_t)row * DM + col0 + bj * HALF) = pack8(acc[ai][bj][m][0] * g, acc[ai][bj][m][1] * g); } }
.LBB0_1502:
	s_andn2_b64 vcc, exec, s[34:35]
	s_cbranch_vccnz .LBB0_1504
	v_mul_f32_e32 v0, 0x41000000, v46
	v_mul_f32_e32 v5, 0x41000000, v47
	v_med3_f32 v0, v0, s64, v250
	v_med3_f32 v5, v5, s64, v250
	v_cvt_pk_fp8_f32 v46, v0, v5
	v_mul_f32_e32 v0, 0x41000000, v48
	v_mul_f32_e32 v5, 0x41000000, v49
	v_med3_f32 v0, v0, s64, v250
	v_med3_f32 v5, v5, s64, v250
	v_cvt_pk_fp8_f32 v46, v0, v5 op_sel:[0,0,1]
	v_mul_f32_e32 v0, 0x41000000, v42
	v_mul_f32_e32 v5, 0x41000000, v43
	v_med3_f32 v0, v0, s64, v250
	v_med3_f32 v5, v5, s64, v250
	v_mov_b32_e32 v9, v8
	v_cvt_pk_fp8_f32 v47, v0, v5
	v_pk_mul_f32 v[8:9], v[44:45], v[8:9]
	s_nop 0
	v_mul_f32_e32 v0, 0x41000000, v8
	v_mul_f32_e32 v5, 0x41000000, v9
	v_med3_f32 v0, v0, s64, v250
	v_med3_f32 v5, v5, s64, v250
	v_cvt_pk_fp8_f32 v47, v0, v5 op_sel:[0,0,1]
	global_store_dwordx2 v[50:51], v[46:47], off offset:128

; __device__ __forceinline__ u32x4 pack8(const f32x4 a, const f32x4 b) { u32x4 w; w.x = cvt_pk_bf16(a[0], a[1]); w.y = cvt_pk_bf16(a[2], a[3]); w.z = cvt_pk_bf16(b[0], b[1]); w.w = cvt_pk_bf16(b[2], b[3]); return w; }
;     __device__ __forceinline__ void operator()(const f32x4 (&acc)[2][2][4][2], const Unit& u, int wr, int wc, int fr, int fq) const {
;     ...
;             for (int m = 0; m < 4; ++m) { const int row = row0 + ai * HALF + m * 16; const float g = t[ai * HALF + wr * 64 + m * 16 + fr];
; #pragma unroll
;                 for (int bj = 0; bj < 2; ++bj) {
;                     if (f8y) { u32x2 w8; w8.x = pack4_fp8_x8(acc[ai][bj][m][0] * g); w8.y = pack4_fp8_x8(acc[ai][bj][m][1] * g); *(u32x2*)((unsigned char*)y + (size_t)row * DM + col0 + bj * HALF) = w8; }
;                     else *(u32x4*)(y + (size_t)row * DM + col0 + bj * HALF) = pack8(acc[ai][bj][m][0] * g, acc[ai][bj][m][1] * g); } }
.LBB0_1506:
	v_lshlrev_b64 v[34:35], 10, v[44:45]
	s_andn2_b64 vcc, exec, s[34:35]
	v_lshl_add_u64 v[34:35], v[2:3], 0, v[34:35]
	s_cbranch_vccnz .LBB0_1508
	v_mul_f32_e32 v0, 0x41000000, v46
	v_mul_f32_e32 v5, 0x41000000, v47
	v_med3_f32 v0, v0, s64, v250
	v_med3_f32 v5, v5, s64, v250
	v_cvt_pk_fp8_f32 v44, v0, v5
	v_mul_f32_e32 v0, 0x41000000, v40
	v_mul_f32_e32 v5, 0x41000000, v41
	v_med3_f32 v0, v0, s64, v250
	v_med3_f32 v5, v5, s64, v250
	v_cvt_pk_fp8_f32 v44, v0, v5 op_sel:[0,0,1]
	v_mul_f32_e32 v0, 0x41000000, v38
	v_mul_f32_e32 v5, 0x41000000, v39
	v_med3_f32 v0, v0, s64, v250
	v_med3_f32 v5, v5, s64, v250
	v_mov_b32_e32 v40, v8
	v_mov_b32_e32 v41, v8
	v_cvt_pk_fp8_f32 v45, v0, v5
	v_pk_mul_f32 v[36:37], v[36:37], v[40:41]
	s_nop 0
	v_mul_f32_e32 v0, 0x41000000, v36
	v_mul_f32_e32 v5, 0x41000000, v37
	v_med3_f32 v0, v0, s64, v250
	v_med3_f32 v5, v5, s64, v250
	v_cvt_pk_fp8_f32 v45, v0, v5 op_sel:[0,0,1]
	global_store_dwordx2 v[34:35], v[44:45], off

; __device__ __forceinline__ u32x4 pack8(const f32x4 a, const f32x4 b) { u32x4 w; w.x = cvt_pk_bf16(a[0], a[1]); w.y = cvt_pk_bf16(a[2], a[3]); w.z = cvt_pk_bf16(b[0], b[1]); w.w = cvt_pk_bf16(b[2], b[3]); return w; }
;     __device__ __forceinline__ void operator()(const f32x4 (&acc)[2][2][4][2], const Unit& u, int wr, int wc, int fr, int fq) const {
;     ...
;             for (int m = 0; m < 4; ++m) { const int row = row0 + ai * HALF + m * 16; const float g = t[ai * HALF + wr * 64 + m * 16 + fr];
; #pragma unroll
;                 for (int bj = 0; bj < 2; ++bj) {
;                     if (f8y) { u32x2 w8; w8.x = pack4_fp8_x8(acc[ai][bj][m][0] * g); w8.y = pack4_fp8_x8(acc[ai][bj][m][1] * g); *(u32x2*)((unsigned char*)y + (size_t)row * DM + col0 + bj * HALF) = w8; }
;                     else *(u32x4*)(y + (size_t)row * DM + col0 + bj * HALF) = pack8(acc[ai][bj][m][0] * g, acc[ai][bj][m][1] * g); } }
.LBB0_1510:
	s_andn2_b64 vcc, exec, s[34:35]
	s_cbranch_vccnz .LBB0_1512
	v_mul_f32_e32 v0, 0x41000000, v30
	v_mul_f32_e32 v5, 0x41000000, v31
	v_med3_f32 v0, v0, s64, v250
	v_med3_f32 v5, v5, s64, v250
	v_cvt_pk_fp8_f32 v30, v0, v5
	v_mul_f32_e32 v0, 0x41000000, v32
	v_mul_f32_e32 v5, 0x41000000, v33
	v_med3_f32 v0, v0, s64, v250
	v_med3_f32 v5, v5, s64, v250
	v_cvt_pk_fp8_f32 v30, v0, v5 op_sel:[0,0,1]
	v_mul_f32_e32 v0, 0x41000000, v26
	v_mul_f32_e32 v5, 0x41000000, v27
	v_med3_f32 v0, v0, s64, v250
	v_med3_f32 v5, v5, s64, v250
	v_mov_b32_e32 v9, v8
	v_cvt_pk_fp8_f32 v31, v0, v5
	v_pk_mul_f32 v[8:9], v[28:29], v[8:9]
	s_nop 0
	v_mul_f32_e32 v0, 0x41000000, v8
	v_mul_f32_e32 v5, 0x41000000, v9
	v_med3_f32 v0, v0, s64, v250
	v_med3_f32 v5, v5, s64, v250
	v_cvt_pk_fp8_f32 v31, v0, v5 op_sel:[0,0,1]
	global_store_dwordx2 v[34:35], v[30:31], off offset:128

; __device__ __forceinline__ u32x4 pack8(const f32x4 a, const f32x4 b) { u32x4 w; w.x = cvt_pk_bf16(a[0], a[1]); w.y = cvt_pk_bf16(a[2], a[3]); w.z = cvt_pk_bf16(b[0], b[1]); w.w = cvt_pk_bf16(b[2], b[3]); return w; }
;     __device__ __forceinline__ void operator()(const f32x4 (&acc)[2][2][4][2], const Unit& u, int wr, int wc, int fr, int fq) const {
;     ...
;             for (int m = 0; m < 4; ++m) { const int row = row0 + ai * HALF + m * 16; const float g = t[ai * HALF + wr * 64 + m * 16 + fr];
; #pragma unroll
;                 for (int bj = 0; bj < 2; ++bj) {
;                     if (f8y) { u32x2 w8; w8.x = pack4_fp8_x8(acc[ai][bj][m][0] * g); w8.y = pack4_fp8_x8(acc[ai][bj][m][1] * g); *(u32x2*)((unsigned char*)y + (size_t)row * DM + col0 + bj * HALF) = w8; }
;                     else *(u32x4*)(y + (size_t)row * DM + col0 + bj * HALF) = pack8(acc[ai][bj][m][0] * g, acc[ai][bj][m][1] * g); } }
.LBB0_1514:
	v_lshlrev_b64 v[18:19], 10, v[26:27]
	s_andn2_b64 vcc, exec, s[34:35]
	v_lshl_add_u64 v[2:3], v[2:3], 0, v[18:19]
	s_cbranch_vccnz .LBB0_1516
	v_mul_f32_e32 v0, 0x41000000, v22
	v_mul_f32_e32 v18, 0x41000000, v23
	v_med3_f32 v0, v0, s64, v250
	v_med3_f32 v19, v18, s64, v250
	v_cvt_pk_fp8_f32 v18, v0, v19
	v_mul_f32_e32 v0, 0x41000000, v24
	v_mul_f32_e32 v19, 0x41000000, v25
	v_med3_f32 v0, v0, s64, v250
	v_med3_f32 v19, v19, s64, v250
	v_cvt_pk_fp8_f32 v18, v0, v19 op_sel:[0,0,1]
	v_mul_f32_e32 v0, 0x41000000, v6
	v_mul_f32_e32 v6, 0x41000000, v7
	v_med3_f32 v0, v0, s64, v250
	v_med3_f32 v6, v6, s64, v250
	v_mov_b32_e32 v22, v8
	v_mov_b32_e32 v23, v8
	v_cvt_pk_fp8_f32 v19, v0, v6
	v_pk_mul_f32 v[20:21], v[20:21], v[22:23]
	s_nop 0
	v_mul_f32_e32 v0, 0x41000000, v20
	v_mul_f32_e32 v6, 0x41000000, v21
	v_med3_f32 v0, v0, s64, v250
	v_med3_f32 v6, v6, s64, v250
	v_cvt_pk_fp8_f32 v19, v0, v6 op_sel:[0,0,1]
	global_store_dwordx2 v[2:3], v[18:19], off

; __device__ __forceinline__ u32x4 pack8(const f32x4 a, const f32x4 b) { u32x4 w; w.x = cvt_pk_bf16(a[0], a[1]); w.y = cvt_pk_bf16(a[2], a[3]); w.z = cvt_pk_bf16(b[0], b[1]); w.w = cvt_pk_bf16(b[2], b[3]); return w; }
;     __device__ __forceinline__ void operator()(const f32x4 (&acc)[2][2][4][2], const Unit& u, int wr, int wc, int fr, int fq) const {
;     ...
;             for (int m = 0; m < 4; ++m) { const int row = row0 + ai * HALF + m * 16; const float g = t[ai * HALF + wr * 64 + m * 16 + fr];
; #pragma unroll
;                 for (int bj = 0; bj < 2; ++bj) {
;                     if (f8y) { u32x2 w8; w8.x = pack4_fp8_x8(acc[ai][bj][m][0] * g); w8.y = pack4_fp8_x8(acc[ai][bj][m][1] * g); *(u32x2*)((unsigned char*)y + (size_t)row * DM + col0 + bj * HALF) = w8; }
;                     else *(u32x4*)(y + (size_t)row * DM + col0 + bj * HALF) = pack8(acc[ai][bj][m][0] * g, acc[ai][bj][m][1] * g); } }
.LBB0_1520:
	v_mul_f32_e32 v0, 0x41000000, v14
	v_mul_f32_e32 v4, 0x41000000, v15
	v_med3_f32 v0, v0, s64, v250
	v_med3_f32 v5, v4, s64, v250
	v_cvt_pk_fp8_f32 v4, v0, v5
	v_mul_f32_e32 v0, 0x41000000, v16
	v_mul_f32_e32 v5, 0x41000000, v17
	v_med3_f32 v0, v0, s64, v250
	v_med3_f32 v5, v5, s64, v250
	v_cvt_pk_fp8_f32 v4, v0, v5 op_sel:[0,0,1]
	v_mul_f32_e32 v0, 0x41000000, v6
	v_mul_f32_e32 v5, 0x41000000, v7
	v_med3_f32 v0, v0, s64, v250
	v_med3_f32 v6, v5, s64, v250
	v_mov_b32_e32 v9, v8
	v_cvt_pk_fp8_f32 v5, v0, v6
	v_pk_mul_f32 v[8:9], v[12:13], v[8:9]
	s_nop 0
	v_mul_f32_e32 v0, 0x41000000, v8
	v_mul_f32_e32 v6, 0x41000000, v9
	v_med3_f32 v0, v0, s64, v250
	v_med3_f32 v6, v6, s64, v250
	v_cvt_pk_fp8_f32 v5, v0, v6 op_sel:[0,0,1]
	global_store_dwordx2 v[2:3], v[4:5], off offset:128
	s_and_b64 vcc, exec, s[4:5]
	s_mov_b64 s[4:5], -1
	s_cbranch_vccnz .LBB0_1438

; #define LDS_WAIT() asm volatile("s_waitcnt lgkmcnt(0)" ::: "memory")
; __device__ __forceinline__ void tr_item(const TrJob& J, int item, LAS float* scr, int lane) {
;     const int nblk = J.N / 32, kb = item / nblk, nb = item % nblk, k0 = 64 * kb, n0 = 32 * nb;
;     float wv[32];
; #pragma unroll
;     for (int i = 0; i < 32; ++i) wv[i] = __builtin_nontemporal_load(J.W + (size_t)(k0 + 2 * i + (lane >> 5)) * J.N + n0 + (lane & 31));
; #pragma unroll
;     for (int i = 0; i < 32; ++i) scr[(2 * i + (lane >> 5)) * 33 + (lane & 31)] = wv[i];
;     LDS_WAIT(); asm volatile("" ::: "memory");
; __device__ __forceinline__ void moe_job(const KP* kp, unsigned char* ws, int l, int g, TrJob& J, int& it) {
;     const int mj = l >> 1, j = g / IT_FF; it = g % IT_FF;
;     unsigned char* WM13 = ws + WS_WM; unsigned char* WM2 = WM13 + (size_t)NEXP * 2 * FF_ * D_ * 2; const int eb = f8_layer(l) ? 1 : 2;
;     if (j < 2 * NEXP) { const int e = j >> 1;
;         if ((j & 1) == 0) J = TrJob{kp->in[14] + (size_t)(mj * NEXP + e) * D_ * FF_, D_, FF_, (bf16*)(WM13 + (size_t)e * 2 * FF_ * D_ * eb), kp->in[9] + l * D_, TM_W1, (int)f8_layer(l)};
;         else J = TrJob{kp->in[15] + (size_t)(mj * NEXP + e) * D_ * FF_, D_, FF_, (bf16*)(WM13 + (size_t)e * 2 * FF_ * D_ * eb), kp->in[9] + l * D_, TM_W3, (int)f8_layer(l)};
.LBB0_1528:
	s_mul_hi_i32 s4, s12, 0x92492493
	s_add_i32 s4, s4, s12
	s_lshr_b32 s5, s4, 31
	s_ashr_i32 s4, s4, 10
	s_add_i32 s4, s4, s5
	s_mul_i32 s5, s4, 0xfffff900
	s_add_i32 s10, s12, s5
	s_ashr_i32 s5, s4, 1
	s_and_b32 s15, s4, 1
	s_add_i32 s6, s5, 8
	s_mul_hi_i32 s7, s5, 0x700000
	s_mul_i32 s5, s5, 0x700000
	s_add_u32 s4, s1, s5
	s_addc_u32 s5, s13, s7
	s_cmp_eq_u32 s15, 0
	s_mul_hi_i32 s11, s6, 0xe00000
	s_mul_i32 s16, s6, 0xe00000
	s_cselect_b32 s6, s28, 0x78
	s_add_u32 s6, s8, s6
	s_addc_u32 s7, s9, 0
	s_load_dwordx2 s[6:7], s[6:7], 0x0
	s_waitcnt lgkmcnt(0)
	s_add_u32 s18, s6, s16
	s_mul_i32 s6, s10, 0x4925
	s_addc_u32 s19, s7, s11
	s_lshr_b32 s7, s6, 31
	s_ashr_i32 s6, s6, 21
	s_add_i32 s6, s6, s7
	s_sext_i32_i16 s11, s6
	s_mulk_i32 s6, 0x70
	s_sub_i32 s6, s10, s6
	s_sext_i32_i16 s7, s6
	s_lshl_b32 s10, s7, 5
	s_lshl_b32 s6, s11, 6
	s_ashr_i32 s11, s10, 31
	s_lshl_b64 s[16:17], s[10:11], 2
	s_add_u32 s16, s18, s16
	s_addc_u32 s17, s19, s17
	v_add_u32_e32 v40, s6, v14
	v_lshl_add_u64 v[36:37], s[16:17], 0, v[0:1]
	v_mad_i64_i32 v[2:3], s[16:17], v40, s33, v[36:37]
	global_load_dword v41, v[2:3], off nt
	v_add_u32_e32 v2, 2, v40
	v_mad_i64_i32 v[2:3], s[16:17], v2, s33, v[36:37]
	global_load_dword v42, v[2:3], off nt
	v_add_u32_e32 v2, 4, v40
	v_mad_i64_i32 v[2:3], s[16:17], v2, s33, v[36:37]
	global_load_dword v43, v[2:3], off nt
	v_add_u32_e32 v2, 6, v40
	v_mad_i64_i32 v[2:3], s[16:17], v2, s33, v[36:37]
	global_load_dword v44, v[2:3], off nt
	v_add_u32_e32 v2, 8, v40
	v_mad_i64_i32 v[2:3], s[16:17], v2, s33, v[36:37]
	global_load_dword v2, v[2:3], off nt
	v_add_u32_e32 v3, 10, v40
	v_mad_i64_i32 v[4:5], s[16:17], v3, s33, v[36:37]
	v_add_u32_e32 v3, 12, v40
	v_mad_i64_i32 v[6:7], s[16:17], v3, s33, v[36:37]
	v_add_u32_e32 v3, 14, v40
	global_load_dword v5, v[4:5], off nt
	v_add_u32_e32 v8, 34, v40
	global_load_dword v9, v[6:7], off nt
	v_mad_i64_i32 v[6:7], s[16:17], v3, s33, v[36:37]
	v_add_u32_e32 v3, 16, v40
	global_load_dword v23, v[6:7], off nt
	v_mad_i64_i32 v[6:7], s[16:17], v3, s33, v[36:37]
	v_add_u32_e32 v4, 18, v40
	global_load_dword v3, v[6:7], off nt
	v_mad_i64_i32 v[6:7], s[16:17], v4, s33, v[36:37]
	v_add_u32_e32 v4, 20, v40
	v_mad_i64_i32 v[12:13], s[16:17], v4, s33, v[36:37]
	v_add_u32_e32 v4, 22, v40
	global_load_dword v7, v[6:7], off nt
	v_add_u32_e32 v28, 58, v40
	global_load_dword v18, v[12:13], off nt
	v_mad_i64_i32 v[12:13], s[16:17], v4, s33, v[36:37]
	v_add_u32_e32 v4, 24, v40
	global_load_dword v26, v[12:13], off nt
	v_mad_i64_i32 v[12:13], s[16:17], v4, s33, v[36:37]
	v_add_u32_e32 v6, 26, v40
	global_load_dword v4, v[12:13], off nt
	v_mad_i64_i32 v[12:13], s[16:17], v6, s33, v[36:37]
	v_add_u32_e32 v6, 28, v40
	v_mad_i64_i32 v[20:21], s[16:17], v6, s33, v[36:37]
	v_add_u32_e32 v6, 30, v40
	v_mad_i64_i32 v[24:25], s[16:17], v6, s33, v[36:37]
	v_add_u32_e32 v6, 32, v40
	global_load_dword v12, v[12:13], off nt
	s_lshl_b32 s7, s7, 6
	global_load_dword v21, v[20:21], off nt
	s_and_b32 s7, s7, 0xffffff00
	global_load_dword v29, v[24:25], off nt
	v_mad_i64_i32 v[24:25], s[16:17], v6, s33, v[36:37]
	global_load_dword v6, v[24:25], off nt
	v_mad_i64_i32 v[24:25], s[16:17], v8, s33, v[36:37]
	v_add_u32_e32 v8, 36, v40
	global_load_dword v19, v[24:25], off nt
	v_mad_i64_i32 v[24:25], s[16:17], v8, s33, v[36:37]
	v_add_u32_e32 v8, 38, v40
	v_mad_i64_i32 v[30:31], s[16:17], v8, s33, v[36:37]
	v_add_u32_e32 v8, 40, v40
	v_mad_i64_i32 v[32:33], s[16:17], v8, s33, v[36:37]
	v_add_u32_e32 v13, 42, v40
	global_load_dword v24, v[24:25], off nt
	v_add_u32_e32 v20, 50, v40
	global_load_dword v31, v[30:31], off nt
	s_and_b32 s10, s10, 0x60
	global_load_dword v8, v[32:33], off nt
	v_mad_i64_i32 v[32:33], s[16:17], v13, s33, v[36:37]
	v_add_u32_e32 v13, 44, v40
	global_load_dword v22, v[32:33], off nt
	v_mad_i64_i32 v[32:33], s[16:17], v13, s33, v[36:37]
	v_add_u32_e32 v13, 46, v40
	global_load_dword v27, v[32:33], off nt
	v_mad_i64_i32 v[32:33], s[16:17], v13, s33, v[36:37]
	v_add_u32_e32 v13, 48, v40
	v_mad_i64_i32 v[34:35], s[16:17], v13, s33, v[36:37]
	global_load_dword v33, v[32:33], off nt
	s_or_b32 s10, s7, s10
	global_load_dword v13, v[34:35], off nt
	v_mad_i64_i32 v[34:35], s[16:17], v20, s33, v[36:37]
	v_add_u32_e32 v20, 52, v40
	global_load_dword v25, v[34:35], off nt
	v_mad_i64_i32 v[34:35], s[16:17], v20, s33, v[36:37]
	v_add_u32_e32 v20, 54, v40
	global_load_dword v30, v[34:35], off nt
	v_mad_i64_i32 v[34:35], s[16:17], v20, s33, v[36:37]
	v_add_u32_e32 v20, 56, v40
	v_mad_i64_i32 v[38:39], s[16:17], v20, s33, v[36:37]
	global_load_dword v34, v[34:35], off nt
	v_add_u32_e32 v32, 60, v40
	global_load_dword v20, v[38:39], off nt
	v_mad_i64_i32 v[38:39], s[16:17], v28, s33, v[36:37]
	v_add_u32_e32 v35, 62, v40
	global_load_dword v28, v[38:39], off nt
	v_mad_i64_i32 v[38:39], s[16:17], v32, s33, v[36:37]
	v_mad_i64_i32 v[36:37], s[16:17], v35, s33, v[36:37]
	global_load_dword v32, v[38:39], off nt
	global_load_dword v35, v[36:37], off nt
	v_add_u32_e32 v36, 0x400, v17
	s_waitcnt vmcnt(0)
	ds_write2_b32 v17, v41, v42 offset1:66
	ds_write2_b32 v17, v43, v44 offset0:132 offset1:198
	ds_write2_b32 v36, v2, v5 offset0:8 offset1:74
	ds_write2_b32 v36, v9, v23 offset0:140 offset1:206
	v_add_u32_e32 v2, 0x800, v17
	ds_write2_b32 v2, v3, v7 offset0:16 offset1:82
	ds_write2_b32 v2, v18, v26 offset0:148 offset1:214
	v_add_u32_e32 v2, 0xc00, v17
	ds_write2_b32 v2, v4, v12 offset0:24 offset1:90
	ds_write2_b32 v2, v21, v29 offset0:156 offset1:222
	v_add_u32_e32 v2, 0x1000, v17
	ds_write2_b32 v2, v6, v19 offset0:32 offset1:98
	ds_write2_b32 v2, v24, v31 offset0:164 offset1:230
	v_add_u32_e32 v2, 0x1400, v17
	ds_write2_b32 v2, v8, v22 offset0:40 offset1:106
	ds_write2_b32 v2, v27, v33 offset0:172 offset1:238
	v_add_u32_e32 v2, 0x1800, v17
	ds_write2_b32 v2, v13, v25 offset0:48 offset1:114
	ds_write2_b32 v2, v30, v34 offset0:180 offset1:246
	v_add_u32_e32 v2, 0x1c00, v17
	ds_write2_b32 v2, v20, v28 offset0:56 offset1:122
	ds_write2_b32 v2, v32, v35 offset0:188 offset1:254
	v_or_b32_e32 v2, s6, v10
	s_waitcnt lgkmcnt(0)
; #define GAS __attribute__((address_space(1)))
; #define LAS __attribute__((address_space(3)))
; __device__ __forceinline__ void tr_item(const TrJob& J, int item, LAS float* scr, int lane) {
;     ...
;     const int c = lane & 7; float g[8];
; #pragma unroll
;     for (int e = 0; e < 8; ++e) g[e] = J.gain ? J.gain[k0 + 8 * c + e] : 1.f;
; #pragma unroll
;     for (int j = 0; j < 4; ++j) { const int n = (lane >> 3) + 8 * j; const LAS float* s = scr + (8 * c) * 33 + n;
;         if (J.f8) { int w0 = 0, w1 = 0;
;             w0 = __builtin_amdgcn_cvt_pk_fp8_f32(s[0 * 33] * g[0] * 64.0f, s[1 * 33] * g[1] * 64.0f, w0, false); w0 = __builtin_amdgcn_cvt_pk_fp8_f32(s[2 * 33] * g[2] * 64.0f, s[3 * 33] * g[3] * 64.0f, w0, true);
;             w1 = __builtin_amdgcn_cvt_pk_fp8_f32(s[4 * 33] * g[4] * 64.0f, s[5 * 33] * g[5] * 64.0f, w1, false); w1 = __builtin_amdgcn_cvt_pk_fp8_f32(s[6 * 33] * g[6] * 64.0f, s[7 * 33] * g[7] * 64.0f, w1, true);
;             v2u o; o.x = (unsigned)w0; o.y = (unsigned)w1; *(GAS v2u*)((unsigned char*)J.dst + (size_t)tr_dest_row(J.mode, n0, n) * J.K + k0 + 8 * c) = o; }
	v_ashrrev_i32_e32 v3, 31, v2
	v_lshl_add_u64 v[6:7], v[2:3], 2, s[2:3]
	global_load_dwordx4 v[2:5], v[6:7], off offset:16
	s_nop 0
	global_load_dwordx4 v[6:9], v[6:7], off
	ds_read2_b32 v[18:19], v16 offset1:8
	ds_read2_b32 v[20:21], v16 offset0:33 offset1:41
	ds_read2_b32 v[24:25], v16 offset0:66 offset1:74
	ds_read2_b32 v[26:27], v16 offset0:99 offset1:107
	ds_read2_b32 v[28:29], v16 offset0:132 offset1:140
	ds_read2_b32 v[30:31], v16 offset0:165 offset1:173
	ds_read2_b32 v[32:33], v16 offset0:198 offset1:206
	ds_read2_b32 v[34:35], v16 offset0:231 offset1:239
	s_lshl_b32 s11, s15, 7
	s_or_b32 s10, s10, s11
	s_ashr_i32 s7, s6, 31
	s_add_i32 s12, s12, s14
	s_cmpk_lt_i32 s12, 0x3e80
	s_waitcnt vmcnt(0) lgkmcnt(7)
	v_mul_f32_e32 v12, v6, v18
	s_waitcnt lgkmcnt(6)
	v_mul_f32_e32 v13, v7, v20
	v_mul_f32_e32 v12, 0x42800000, v12
	v_mul_f32_e32 v13, 0x42800000, v13
	v_cvt_pk_fp8_f32 v22, v12, v13
	s_waitcnt lgkmcnt(5)
	v_mul_f32_e32 v12, v8, v24
	s_waitcnt lgkmcnt(4)
	v_mul_f32_e32 v13, v9, v26
	v_mul_f32_e32 v12, 0x42800000, v12
	v_mul_f32_e32 v13, 0x42800000, v13
	v_cvt_pk_fp8_f32 v22, v12, v13 op_sel:[0,0,1]
	s_waitcnt lgkmcnt(3)
	v_mul_f32_e32 v12, v2, v28
	s_waitcnt lgkmcnt(2)
	v_mul_f32_e32 v13, v3, v30
	v_mul_f32_e32 v12, 0x42800000, v12
	v_mul_f32_e32 v13, 0x42800000, v13
	v_cvt_pk_fp8_f32 v23, v12, v13
	s_waitcnt lgkmcnt(1)
	v_mul_f32_e32 v12, v4, v32
	s_waitcnt lgkmcnt(0)
	v_mul_f32_e32 v13, v5, v34
	v_mul_f32_e32 v12, 0x42800000, v12
	v_mul_f32_e32 v13, 0x42800000, v13
	v_cvt_pk_fp8_f32 v23, v12, v13 op_sel:[0,0,1]
	v_add_u32_e32 v12, s10, v15
	v_ashrrev_i32_e32 v13, 31, v12
	v_lshlrev_b64 v[36:37], 10, v[12:13]
	v_mul_f32_e32 v13, v6, v19
	v_mul_f32_e32 v18, v7, v21
	v_mul_f32_e32 v13, 0x42800000, v13
	v_mul_f32_e32 v19, 0x42800000, v18
	v_cvt_pk_fp8_f32 v18, v13, v19
	v_mul_f32_e32 v13, v8, v25
	v_mul_f32_e32 v19, v9, v27
	v_mul_f32_e32 v13, 0x42800000, v13
	v_mul_f32_e32 v19, 0x42800000, v19
	v_cvt_pk_fp8_f32 v18, v13, v19 op_sel:[0,0,1]
	v_mul_f32_e32 v13, v2, v29
	v_mul_f32_e32 v19, v3, v31
	v_mul_f32_e32 v13, 0x42800000, v13
	v_mul_f32_e32 v20, 0x42800000, v19
	v_cvt_pk_fp8_f32 v19, v13, v20
	v_mul_f32_e32 v13, v4, v33
	v_mul_f32_e32 v20, v5, v35
	v_mul_f32_e32 v13, 0x42800000, v13
	v_mul_f32_e32 v20, 0x42800000, v20
	v_cvt_pk_fp8_f32 v19, v13, v20 op_sel:[0,0,1]
	v_add_u32_e32 v20, 8, v12
	v_ashrrev_i32_e32 v21, 31, v20
	v_lshlrev_b64 v[20:21], 10, v[20:21]
	v_lshl_add_u64 v[20:21], s[4:5], 0, v[20:21]
	v_lshl_add_u64 v[20:21], v[20:21], 0, s[6:7]
	v_lshl_add_u64 v[20:21], v[20:21], 0, v[10:11]
	global_store_dwordx2 v[20:21], v[18:19], off
	ds_read2_b32 v[18:19], v16 offset0:16 offset1:24
	ds_read2_b32 v[20:21], v16 offset0:49 offset1:57
	v_lshl_add_u64 v[36:37], s[4:5], 0, v[36:37]
	v_lshl_add_u64 v[36:37], v[36:37], 0, s[6:7]
	ds_read2_b32 v[24:25], v16 offset0:82 offset1:90
	ds_read2_b32 v[26:27], v16 offset0:115 offset1:123
	v_lshl_add_u64 v[36:37], v[36:37], 0, v[10:11]
	s_waitcnt lgkmcnt(3)
	v_mul_f32_e32 v13, v6, v18
	s_waitcnt lgkmcnt(2)
	v_mul_f32_e32 v18, v7, v20
	global_store_dwordx2 v[36:37], v[22:23], off
	v_mul_f32_e32 v13, 0x42800000, v13
	v_mul_f32_e32 v18, 0x42800000, v18
	ds_read2_b32 v[28:29], v16 offset0:148 offset1:156
	ds_read2_b32 v[30:31], v16 offset0:181 offset1:189
	v_cvt_pk_fp8_f32 v22, v13, v18
	s_waitcnt lgkmcnt(3)
	v_mul_f32_e32 v13, v8, v24
	s_waitcnt lgkmcnt(2)
	v_mul_f32_e32 v18, v9, v26
	v_mul_f32_e32 v13, 0x42800000, v13
	v_mul_f32_e32 v18, 0x42800000, v18
	ds_read2_b32 v[32:33], v16 offset0:214 offset1:222
	ds_read2_b32 v[34:35], v16 offset0:247 offset1:255
	v_cvt_pk_fp8_f32 v22, v13, v18 op_sel:[0,0,1]
	s_waitcnt lgkmcnt(3)
	v_mul_f32_e32 v13, v2, v28
	s_waitcnt lgkmcnt(2)
	v_mul_f32_e32 v18, v3, v30
	v_mul_f32_e32 v13, 0x42800000, v13
	v_mul_f32_e32 v18, 0x42800000, v18
	v_cvt_pk_fp8_f32 v23, v13, v18
	s_waitcnt lgkmcnt(1)
	v_mul_f32_e32 v13, v4, v32
	s_waitcnt lgkmcnt(0)
	v_mul_f32_e32 v18, v5, v34
	v_mul_f32_e32 v13, 0x42800000, v13
	v_mul_f32_e32 v18, 0x42800000, v18
	v_mul_f32_e32 v6, v6, v19
	v_cvt_pk_fp8_f32 v23, v13, v18 op_sel:[0,0,1]
	v_mul_f32_e32 v13, 0x42800000, v6
	v_mul_f32_e32 v6, v7, v21
	v_mul_f32_e32 v7, 0x42800000, v6
	v_cvt_pk_fp8_f32 v6, v13, v7
	v_mul_f32_e32 v7, v8, v25
	v_mul_f32_e32 v8, v9, v27
	v_mul_f32_e32 v7, 0x42800000, v7
	v_mul_f32_e32 v8, 0x42800000, v8
	v_mul_f32_e32 v2, v2, v29
	v_mul_f32_e32 v3, v3, v31
	v_cvt_pk_fp8_f32 v6, v7, v8 op_sel:[0,0,1]
	v_mul_f32_e32 v2, 0x42800000, v2
	v_mul_f32_e32 v3, 0x42800000, v3
	v_cvt_pk_fp8_f32 v7, v2, v3
	v_mul_f32_e32 v2, v4, v33
	v_mul_f32_e32 v3, v5, v35
	v_mul_f32_e32 v2, 0x42800000, v2
	v_mul_f32_e32 v3, 0x42800000, v3
	v_add_u32_e32 v36, 16, v12
	v_cvt_pk_fp8_f32 v7, v2, v3 op_sel:[0,0,1]
	v_add_u32_e32 v2, 24, v12
	v_ashrrev_i32_e32 v37, 31, v36
	v_ashrrev_i32_e32 v3, 31, v2
	v_lshlrev_b64 v[36:37], 10, v[36:37]
	v_lshlrev_b64 v[2:3], 10, v[2:3]
	v_lshl_add_u64 v[36:37], s[4:5], 0, v[36:37]
	v_lshl_add_u64 v[2:3], s[4:5], 0, v[2:3]
	v_lshl_add_u64 v[36:37], v[36:37], 0, s[6:7]
	v_lshl_add_u64 v[2:3], v[2:3], 0, s[6:7]
	v_lshl_add_u64 v[36:37], v[36:37], 0, v[10:11]
	v_lshl_add_u64 v[2:3], v[2:3], 0, v[10:11]
	global_store_dwordx2 v[36:37], v[22:23], off
	global_store_dwordx2 v[2:3], v[6:7], off
	s_waitcnt lgkmcnt(0)
	s_cbranch_scc1 .LBB0_1528

; #define GAS __attribute__((address_space(1)))
; template <bool INIT, bool FINAL>
; __device__ __forceinline__ void row_pass(const float* xin, float* xout, bf16* xb, float* ssx, const bf16* Y, const int* pos, const float* gfin, int gw, int NGW, int lane, unsigned char* xq = nullptr  ) {
;     ...
;                 for (int j = 0; j < 4; ++j) { const v2u c = xw[u][j], a = aw[u][j], b = bw[u][j];
;                     if (Y8) { typedef float f2_ __attribute__((ext_vector_type(2)));
;                         const f2_ a01 = __builtin_amdgcn_cvt_pk_f32_fp8((int)a.x, false), a23 = __builtin_amdgcn_cvt_pk_f32_fp8((int)a.x, true), b01 = __builtin_amdgcn_cvt_pk_f32_fp8((int)b.x, false), b23 = __builtin_amdgcn_cvt_pk_f32_fp8((int)b.x, true);
;                         v[u][j].x = __uint_as_float(c.x << 16) + (a01[0] + b01[0]) * 0.125f; v[u][j].y = __uint_as_float(c.x & 0xffff0000u) + (a01[1] + b01[1]) * 0.125f;
;                         v[u][j].z = __uint_as_float(c.y << 16) + (a23[0] + b23[0]) * 0.125f; v[u][j].w = __uint_as_float(c.y & 0xffff0000u) + (a23[1] + b23[1]) * 0.125f; }
;                     else {
;                     v[u][j].x = __uint_as_float(c.x << 16) + (__uint_as_float(a.x << 16) + __uint_as_float(b.x << 16)); v[u][j].y = __uint_as_float(c.x & 0xffff0000u) + (__uint_as_float(a.x & 0xffff0000u) + __uint_as_float(b.x & 0xffff0000u));
;                     v[u][j].z = __uint_as_float(c.y << 16) + (__uint_as_float(a.y << 16) + __uint_as_float(b.y << 16)); v[u][j].w = __uint_as_float(c.y & 0xffff0000u) + (__uint_as_float(a.y & 0xffff0000u) + __uint_as_float(b.y & 0xffff0000u)); } }
;         }
; #pragma unroll
;         for (int u = 0; u < U; ++u) { const int t = t0 + u * NGW; if (t < T_) {
;             float ss = 0.f;
; #pragma unroll
;             for (int j = 0; j < 4; ++j) ss += (v[u][j].x * v[u][j].x + v[u][j].y * v[u][j].y) + (v[u][j].z * v[u][j].z + v[u][j].w * v[u][j].w);
;             ss = wave_sum(ss);
;             if (FINAL) {
;                 GAS f32x4* xo = (GAS f32x4*)(xout + (size_t)t * D_) + lane;
;                 const float rs = 1.0f / sqrtf(ss * (1.0f / D_) + EPS_);
; #pragma unroll
;                 for (int j = 0; j < 4; ++j) { const f32x4 g = ((const GAS f32x4*)gfin)[lane + 64 * j]; xo[64 * j] = v[u][j] * rs * g; }
;             } else {
;                 GAS v2u* bo = (GAS v2u*)(xb + (size_t)t * D_) + lane;
; #pragma unroll
.LBB0_1595:
	s_mov_b64 s[12:13], 0xfb00000
	v_lshl_add_u64 v[118:119], v[96:97], 0, s[12:13]
	s_mov_b64 s[12:13], 0xfb00200
	v_lshl_add_u64 v[120:121], v[96:97], 0, s[12:13]
	s_mov_b64 s[12:13], 0xfb00400
	v_lshl_add_u64 v[122:123], v[96:97], 0, s[12:13]
	s_mov_b64 s[12:13], 0xfb00600
	s_waitcnt vmcnt(7)
	v_lshlrev_b32_e32 v125, 16, v109
	v_lshlrev_b32_e32 v124, 16, v108
	s_waitcnt vmcnt(3)
	v_lshlrev_b32_e32 v127, 16, v117
	v_lshlrev_b32_e32 v126, 16, v116
	v_and_b32_e32 v109, 0xffff0000, v109
	v_and_b32_e32 v108, 0xffff0000, v108
	v_and_b32_e32 v117, 0xffff0000, v117
	v_and_b32_e32 v116, 0xffff0000, v116
	v_lshl_add_u64 v[98:99], v[96:97], 0, s[12:13]
	v_lshlrev_b32_e32 v97, 16, v103
	v_lshlrev_b32_e32 v96, 16, v102
	v_and_b32_e32 v103, 0xffff0000, v103
	v_and_b32_e32 v102, 0xffff0000, v102
	v_pk_add_f32 v[108:109], v[108:109], v[116:117]
	v_pk_add_f32 v[124:125], v[124:125], v[126:127]
	v_pk_add_f32 v[102:103], v[108:109], v[102:103]
	v_pk_add_f32 v[96:97], v[124:125], v[96:97]
	v_pk_mul_f32 v[108:109], v[102:103], v[102:103]
	v_and_b32_sdwa v0, v97, v252 dst_sel:DWORD dst_unused:UNUSED_PAD src0_sel:WORD_1 src1_sel:DWORD
	v_pk_fma_f32 v[116:117], v[96:97], v[96:97], v[108:109]
	v_and_b32_sdwa v108, v103, v252 dst_sel:DWORD dst_unused:UNUSED_PAD src0_sel:WORD_1 src1_sel:DWORD
	v_and_b32_sdwa v109, v102, v252 dst_sel:DWORD dst_unused:UNUSED_PAD src0_sel:WORD_1 src1_sel:DWORD
	v_and_b32_sdwa v7, v96, v252 dst_sel:DWORD dst_unused:UNUSED_PAD src0_sel:WORD_1 src1_sel:DWORD
	v_add3_u32 v108, v103, v108, s90
	v_add3_u32 v109, v102, v109, s90
	v_add3_u32 v7, v96, v7, s90
	v_add3_u32 v0, v97, v0, s90
	v_and_b32_e32 v108, 0xffff0000, v108
	v_and_b32_e32 v124, 0xffff0000, v109
	v_or_b32_sdwa v109, v108, v0 dst_sel:DWORD dst_unused:UNUSED_PAD src0_sel:DWORD src1_sel:WORD_1
	v_or_b32_sdwa v108, v124, v7 dst_sel:DWORD dst_unused:UNUSED_PAD src0_sel:DWORD src1_sel:WORD_1
	global_store_dwordx2 v[118:119], v[108:109], off
	v_lshlrev_b32_e32 v119, 16, v113
	v_lshlrev_b32_e32 v118, 16, v112
	s_waitcnt vmcnt(3)
	v_lshlrev_b32_e32 v125, 16, v115
	v_lshlrev_b32_e32 v124, 16, v114
	v_and_b32_e32 v113, 0xffff0000, v113
	v_and_b32_e32 v112, 0xffff0000, v112
	v_and_b32_e32 v115, 0xffff0000, v115
	v_and_b32_e32 v114, 0xffff0000, v114
	v_lshlrev_b32_e32 v109, 16, v111
	v_lshlrev_b32_e32 v108, 16, v110
	v_and_b32_e32 v111, 0xffff0000, v111
	v_and_b32_e32 v110, 0xffff0000, v110
	v_pk_add_f32 v[112:113], v[112:113], v[114:115]
	v_pk_add_f32 v[118:119], v[118:119], v[124:125]
	v_pk_add_f32 v[110:111], v[112:113], v[110:111]
	v_pk_add_f32 v[108:109], v[118:119], v[108:109]
	v_pk_mul_f32 v[112:113], v[110:111], v[110:111]
	v_and_b32_sdwa v0, v109, v252 dst_sel:DWORD dst_unused:UNUSED_PAD src0_sel:WORD_1 src1_sel:DWORD
	v_pk_fma_f32 v[114:115], v[108:109], v[108:109], v[112:113]
	v_and_b32_sdwa v112, v111, v252 dst_sel:DWORD dst_unused:UNUSED_PAD src0_sel:WORD_1 src1_sel:DWORD
	v_and_b32_sdwa v113, v110, v252 dst_sel:DWORD dst_unused:UNUSED_PAD src0_sel:WORD_1 src1_sel:DWORD
	v_and_b32_sdwa v7, v108, v252 dst_sel:DWORD dst_unused:UNUSED_PAD src0_sel:WORD_1 src1_sel:DWORD
	v_add3_u32 v112, v111, v112, s90
	v_add3_u32 v113, v110, v113, s90
	v_add3_u32 v7, v108, v7, s90
	v_add3_u32 v0, v109, v0, s90
	v_and_b32_e32 v112, 0xffff0000, v112
	v_and_b32_e32 v118, 0xffff0000, v113
	v_or_b32_sdwa v113, v112, v0 dst_sel:DWORD dst_unused:UNUSED_PAD src0_sel:DWORD src1_sel:WORD_1
	v_or_b32_sdwa v112, v118, v7 dst_sel:DWORD dst_unused:UNUSED_PAD src0_sel:DWORD src1_sel:WORD_1
	global_store_dwordx2 v[120:121], v[112:113], off
	v_lshlrev_b32_e32 v119, 16, v105
	v_lshlrev_b32_e32 v118, 16, v104
	s_waitcnt vmcnt(3)
	v_lshlrev_b32_e32 v121, 16, v107
	v_lshlrev_b32_e32 v120, 16, v106
	v_and_b32_e32 v105, 0xffff0000, v105
	v_and_b32_e32 v104, 0xffff0000, v104
	v_and_b32_e32 v107, 0xffff0000, v107
	v_and_b32_e32 v106, 0xffff0000, v106
	v_lshlrev_b32_e32 v113, 16, v101
	v_lshlrev_b32_e32 v112, 16, v100
	v_and_b32_e32 v101, 0xffff0000, v101
	v_and_b32_e32 v100, 0xffff0000, v100
	v_pk_add_f32 v[104:105], v[104:105], v[106:107]
	v_pk_add_f32 v[118:119], v[118:119], v[120:121]
	v_pk_add_f32 v[100:101], v[104:105], v[100:101]
	v_pk_add_f32 v[112:113], v[118:119], v[112:113]
	v_pk_mul_f32 v[104:105], v[100:101], v[100:101]
	v_and_b32_sdwa v0, v113, v252 dst_sel:DWORD dst_unused:UNUSED_PAD src0_sel:WORD_1 src1_sel:DWORD
	v_pk_fma_f32 v[106:107], v[112:113], v[112:113], v[104:105]
	v_and_b32_sdwa v104, v101, v252 dst_sel:DWORD dst_unused:UNUSED_PAD src0_sel:WORD_1 src1_sel:DWORD
	v_and_b32_sdwa v105, v100, v252 dst_sel:DWORD dst_unused:UNUSED_PAD src0_sel:WORD_1 src1_sel:DWORD
	v_and_b32_sdwa v7, v112, v252 dst_sel:DWORD dst_unused:UNUSED_PAD src0_sel:WORD_1 src1_sel:DWORD
	v_add3_u32 v104, v101, v104, s90
	v_add3_u32 v105, v100, v105, s90
	v_add3_u32 v7, v112, v7, s90
	v_add3_u32 v0, v113, v0, s90
	v_and_b32_e32 v104, 0xffff0000, v104
	v_and_b32_e32 v118, 0xffff0000, v105
	v_or_b32_sdwa v105, v104, v0 dst_sel:DWORD dst_unused:UNUSED_PAD src0_sel:DWORD src1_sel:WORD_1
	v_or_b32_sdwa v104, v118, v7 dst_sel:DWORD dst_unused:UNUSED_PAD src0_sel:DWORD src1_sel:WORD_1
	v_lshlrev_b32_e32 v119, 16, v93
	v_lshlrev_b32_e32 v118, 16, v92
	s_waitcnt vmcnt(2)
; #define GAS __attribute__((address_space(1)))
; __device__ __forceinline__ unsigned pk2(float lo, float hi) { return f2bf(lo) | (f2bf(hi) << 16); }
; template <bool INIT, bool FINAL>
; __device__ __forceinline__ void row_pass(const float* xin, float* xout, bf16* xb, float* ssx, const bf16* Y, const int* pos, const float* gfin, int gw, int NGW, int lane, unsigned char* xq = nullptr  ) {
;     ...
;         for (int u = 0; u < U; ++u) { const int t = t0 + u * NGW; if (t < T_) {
;             float ss = 0.f;
; #pragma unroll
;             for (int j = 0; j < 4; ++j) ss += (v[u][j].x * v[u][j].x + v[u][j].y * v[u][j].y) + (v[u][j].z * v[u][j].z + v[u][j].w * v[u][j].w);
;             ss = wave_sum(ss);
;             if (FINAL) {
;                 GAS f32x4* xo = (GAS f32x4*)(xout + (size_t)t * D_) + lane;
;                 const float rs = 1.0f / sqrtf(ss * (1.0f / D_) + EPS_);
; #pragma unroll
;                 for (int j = 0; j < 4; ++j) { const f32x4 g = ((const GAS f32x4*)gfin)[lane + 64 * j]; xo[64 * j] = v[u][j] * rs * g; }
;             } else {
;                 GAS v2u* bo = (GAS v2u*)(xb + (size_t)t * D_) + lane;
; #pragma unroll
;                 for (int j = 0; j < 4; ++j) { v2u w; w.x = pk2(v[u][j].x, v[u][j].y); w.y = pk2(v[u][j].z, v[u][j].w); bo[64 * j] = w; }
;                 if (xq) { GAS unsigned* qo = (GAS unsigned*)(xq + (size_t)t * D_) + lane;
; #pragma unroll
;                     for (int j = 0; j < 4; ++j) { int w = 0;
;                         w = __builtin_amdgcn_cvt_pk_fp8_f32(__builtin_amdgcn_fmed3f(v[u][j].x * 8.0f, -448.f, 448.f), __builtin_amdgcn_fmed3f(v[u][j].y * 8.0f, -448.f, 448.f), w, false);
;                         w = __builtin_amdgcn_cvt_pk_fp8_f32(__builtin_amdgcn_fmed3f(v[u][j].z * 8.0f, -448.f, 448.f), __builtin_amdgcn_fmed3f(v[u][j].w * 8.0f, -448.f, 448.f), w, true); qo[64 * j] = (unsigned)w; } }
;                 if (lane < 16) ssx[(size_t)t * 16 + lane] = lane == 0 ? ss : 0.f;
	v_lshlrev_b32_e32 v121, 16, v95
	v_lshlrev_b32_e32 v120, 16, v94
	v_and_b32_e32 v93, 0xffff0000, v93
	v_and_b32_e32 v92, 0xffff0000, v92
	v_and_b32_e32 v95, 0xffff0000, v95
	v_and_b32_e32 v94, 0xffff0000, v94
	global_store_dwordx2 v[122:123], v[104:105], off
	v_lshlrev_b32_e32 v105, 16, v91
	v_lshlrev_b32_e32 v104, 16, v90
	v_and_b32_e32 v91, 0xffff0000, v91
	v_and_b32_e32 v90, 0xffff0000, v90
	v_pk_add_f32 v[92:93], v[92:93], v[94:95]
	v_pk_add_f32 v[118:119], v[118:119], v[120:121]
	v_pk_add_f32 v[90:91], v[92:93], v[90:91]
	v_pk_add_f32 v[104:105], v[118:119], v[104:105]
	v_pk_mul_f32 v[92:93], v[90:91], v[90:91]
	v_add_f32_e32 v0, v114, v115
	v_add_f32_e32 v7, v116, v117
	v_pk_fma_f32 v[92:93], v[104:105], v[104:105], v[92:93]
	v_add_f32_e32 v0, v7, v0
	v_add_f32_e32 v7, v106, v107
	v_add_f32_e32 v0, v0, v7
	v_add_f32_e32 v7, v92, v93
	v_add_f32_e32 v0, v0, v7
	ds_swizzle_b32 v7, v0 offset:swizzle(SWAP,1)
	v_and_b32_sdwa v93, v104, v252 dst_sel:DWORD dst_unused:UNUSED_PAD src0_sel:WORD_1 src1_sel:DWORD
	v_add3_u32 v94, v104, v93, s90
	v_and_b32_sdwa v93, v91, v252 dst_sel:DWORD dst_unused:UNUSED_PAD src0_sel:WORD_1 src1_sel:DWORD
	v_and_b32_sdwa v95, v90, v252 dst_sel:DWORD dst_unused:UNUSED_PAD src0_sel:WORD_1 src1_sel:DWORD
	s_waitcnt lgkmcnt(0)
	v_add_f32_e32 v0, v0, v7
	ds_swizzle_b32 v7, v0 offset:swizzle(SWAP,2)
	v_and_b32_sdwa v92, v105, v252 dst_sel:DWORD dst_unused:UNUSED_PAD src0_sel:WORD_1 src1_sel:DWORD
	v_add3_u32 v93, v91, v93, s90
	v_add3_u32 v95, v90, v95, s90
	v_add3_u32 v92, v105, v92, s90
	s_waitcnt lgkmcnt(0)
	v_add_f32_e32 v0, v0, v7
	ds_swizzle_b32 v7, v0 offset:swizzle(SWAP,4)
	v_and_b32_e32 v93, 0xffff0000, v93
	v_and_b32_e32 v95, 0xffff0000, v95
	v_or_b32_sdwa v93, v93, v92 dst_sel:DWORD dst_unused:UNUSED_PAD src0_sel:DWORD src1_sel:WORD_1
	v_or_b32_sdwa v92, v95, v94 dst_sel:DWORD dst_unused:UNUSED_PAD src0_sel:DWORD src1_sel:WORD_1
	s_waitcnt lgkmcnt(0)
	v_add_f32_e32 v0, v0, v7
	ds_swizzle_b32 v7, v0 offset:swizzle(SWAP,8)
	global_store_dwordx2 v[98:99], v[92:93], off
	v_cndmask_b32_e64 v92, 0, 1, s[26:27]
	v_cmp_ne_u32_e64 s[12:13], 1, v92
	s_andn2_b64 vcc, exec, s[26:27]
	s_waitcnt lgkmcnt(0)
	v_add_f32_e32 v0, v0, v7
	ds_swizzle_b32 v7, v0 offset:swizzle(SWAP,16)
	s_waitcnt lgkmcnt(0)
	v_add_f32_e32 v0, v0, v7
	v_mov_b32_e32 v7, v0
	s_nop 1
	v_permlane32_swap_b32_e32 v0, v7
	s_cbranch_vccnz .LBB0_1597
	v_mul_f32_e32 v94, 0x41000000, v96
	v_mul_f32_e32 v95, 0x41000000, v102
	v_med3_f32 v94, v94, s64, v250
	v_med3_f32 v95, v95, s64, v250
	v_cvt_pk_fp8_f32 v96, v94, v95
	v_mul_f32_e32 v94, 0x41000000, v97
	v_mul_f32_e32 v95, 0x41000000, v103
	v_med3_f32 v94, v94, s64, v250
	v_med3_f32 v95, v95, s64, v250
	v_cvt_pk_fp8_f32 v96, v94, v95 op_sel:[0,0,1]
	v_mul_f32_e32 v94, 0x41000000, v108
	v_mul_f32_e32 v95, 0x41000000, v110
	v_med3_f32 v94, v94, s64, v250
	v_med3_f32 v95, v95, s64, v250
	v_cvt_pk_fp8_f32 v97, v94, v95
	v_mul_f32_e32 v94, 0x41000000, v109
	v_mul_f32_e32 v95, 0x41000000, v111
	v_med3_f32 v94, v94, s64, v250
	v_med3_f32 v95, v95, s64, v250
	v_cvt_pk_fp8_f32 v97, v94, v95 op_sel:[0,0,1]
	v_mul_f32_e32 v94, 0x41000000, v112
	v_mul_f32_e32 v95, 0x41000000, v100
	v_med3_f32 v94, v94, s64, v250
	v_med3_f32 v95, v95, s64, v250
	v_cvt_pk_fp8_f32 v98, v94, v95
	v_mul_f32_e32 v94, 0x41000000, v113
	v_mul_f32_e32 v95, 0x41000000, v101
	v_med3_f32 v94, v94, s64, v250
	v_med3_f32 v95, v95, s64, v250
	v_cvt_pk_fp8_f32 v98, v94, v95 op_sel:[0,0,1]
	v_mul_f32_e32 v94, 0x41000000, v104
	v_mul_f32_e32 v90, 0x41000000, v90
	v_med3_f32 v94, v94, s64, v250
	v_med3_f32 v90, v90, s64, v250
	v_cvt_pk_fp8_f32 v95, v94, v90
	v_lshl_add_u64 v[92:93], s[24:25], 0, v[12:13]
	s_mov_b32 s46, 0x8b00000
	v_mul_f32_e32 v90, 0x41000000, v105
	v_mul_f32_e32 v91, 0x41000000, v91
	v_add_co_u32_e32 v92, vcc, s46, v92
	v_med3_f32 v90, v90, s64, v250
	v_med3_f32 v91, v91, s64, v250
	v_addc_co_u32_e32 v93, vcc, 0, v93, vcc
	v_cvt_pk_fp8_f32 v95, v90, v91 op_sel:[0,0,1]
	global_store_dword v[92:93], v96, off
	global_store_dword v[92:93], v97, off offset:256
	global_store_dword v[92:93], v98, off offset:512
	global_store_dword v[92:93], v95, off offset:768

; template <bool INIT, bool FINAL>
; __device__ __forceinline__ void row_pass(const float* xin, float* xout, bf16* xb, float* ssx, const bf16* Y, const int* pos, const float* gfin, int gw, int NGW, int lane, unsigned char* xq = nullptr  ) {
;     ...
;                 for (int j = 0; j < 4; ++j) { const v2u c = xw[u][j], a = aw[u][j], b = bw[u][j];
;                     if (Y8) { typedef float f2_ __attribute__((ext_vector_type(2)));
;                         const f2_ a01 = __builtin_amdgcn_cvt_pk_f32_fp8((int)a.x, false), a23 = __builtin_amdgcn_cvt_pk_f32_fp8((int)a.x, true), b01 = __builtin_amdgcn_cvt_pk_f32_fp8((int)b.x, false), b23 = __builtin_amdgcn_cvt_pk_f32_fp8((int)b.x, true);
;                         v[u][j].x = __uint_as_float(c.x << 16) + (a01[0] + b01[0]) * 0.125f; v[u][j].y = __uint_as_float(c.x & 0xffff0000u) + (a01[1] + b01[1]) * 0.125f;
;                         v[u][j].z = __uint_as_float(c.y << 16) + (a23[0] + b23[0]) * 0.125f; v[u][j].w = __uint_as_float(c.y & 0xffff0000u) + (a23[1] + b23[1]) * 0.125f; }
;                     else {
;                     v[u][j].x = __uint_as_float(c.x << 16) + (__uint_as_float(a.x << 16) + __uint_as_float(b.x << 16)); v[u][j].y = __uint_as_float(c.x & 0xffff0000u) + (__uint_as_float(a.x & 0xffff0000u) + __uint_as_float(b.x & 0xffff0000u));
;                     v[u][j].z = __uint_as_float(c.y << 16) + (__uint_as_float(a.y << 16) + __uint_as_float(b.y << 16)); v[u][j].w = __uint_as_float(c.y & 0xffff0000u) + (__uint_as_float(a.y & 0xffff0000u) + __uint_as_float(b.y & 0xffff0000u)); } }
;         }
; #pragma unroll
;         for (int u = 0; u < U; ++u) { const int t = t0 + u * NGW; if (t < T_) {
;             float ss = 0.f;
; #pragma unroll
;             for (int j = 0; j < 4; ++j) ss += (v[u][j].x * v[u][j].x + v[u][j].y * v[u][j].y) + (v[u][j].z * v[u][j].z + v[u][j].w * v[u][j].w);
;             ss = wave_sum(ss);
.LBB0_1600:
	v_lshlrev_b32_e32 v93, 16, v57
	v_lshlrev_b32_e32 v92, 16, v56
	v_lshlrev_b32_e32 v95, 16, v81
	v_lshlrev_b32_e32 v94, 16, v80
	v_and_b32_e32 v97, 0xffff0000, v57
	v_and_b32_e32 v96, 0xffff0000, v56
	v_and_b32_e32 v99, 0xffff0000, v81
	v_and_b32_e32 v98, 0xffff0000, v80
	v_lshlrev_b32_e32 v91, 16, v23
	v_lshlrev_b32_e32 v90, 16, v22
	v_pk_add_f32 v[92:93], v[92:93], v[94:95]
	v_and_b32_e32 v95, 0xffff0000, v23
	v_and_b32_e32 v94, 0xffff0000, v22
	v_pk_add_f32 v[96:97], v[96:97], v[98:99]
	v_pk_add_f32 v[92:93], v[92:93], v[90:91]
	v_pk_add_f32 v[90:91], v[96:97], v[94:95]
	v_lshlrev_b32_e32 v97, 16, v55
	v_lshlrev_b32_e32 v96, 16, v54
	v_lshlrev_b32_e32 v99, 16, v79
	v_lshlrev_b32_e32 v98, 16, v78
	v_and_b32_e32 v101, 0xffff0000, v55
	v_and_b32_e32 v100, 0xffff0000, v54
	v_and_b32_e32 v103, 0xffff0000, v79
	v_and_b32_e32 v102, 0xffff0000, v78
	v_lshlrev_b32_e32 v95, 16, v27
	v_lshlrev_b32_e32 v94, 16, v26
	v_pk_add_f32 v[96:97], v[96:97], v[98:99]
	v_and_b32_e32 v99, 0xffff0000, v27
	v_and_b32_e32 v98, 0xffff0000, v26
	v_pk_add_f32 v[100:101], v[100:101], v[102:103]
	v_pk_add_f32 v[96:97], v[96:97], v[94:95]
	v_pk_add_f32 v[94:95], v[100:101], v[98:99]
	v_lshlrev_b32_e32 v101, 16, v53
	v_lshlrev_b32_e32 v100, 16, v52
	v_lshlrev_b32_e32 v103, 16, v77
	v_lshlrev_b32_e32 v102, 16, v76
	v_and_b32_e32 v105, 0xffff0000, v53
	v_and_b32_e32 v104, 0xffff0000, v52
	v_and_b32_e32 v107, 0xffff0000, v77
	v_and_b32_e32 v106, 0xffff0000, v76
	v_lshlrev_b32_e32 v99, 16, v33
	v_lshlrev_b32_e32 v98, 16, v32
	v_pk_add_f32 v[100:101], v[100:101], v[102:103]
	v_and_b32_e32 v103, 0xffff0000, v33
	v_and_b32_e32 v102, 0xffff0000, v32
	v_pk_add_f32 v[104:105], v[104:105], v[106:107]
	v_pk_add_f32 v[100:101], v[100:101], v[98:99]
	v_pk_add_f32 v[98:99], v[104:105], v[102:103]
	v_lshlrev_b32_e32 v105, 16, v51
	v_lshlrev_b32_e32 v104, 16, v50
	v_lshlrev_b32_e32 v107, 16, v75
	v_lshlrev_b32_e32 v106, 16, v74
	v_and_b32_e32 v109, 0xffff0000, v51
	v_and_b32_e32 v108, 0xffff0000, v50
	v_and_b32_e32 v111, 0xffff0000, v75
	v_and_b32_e32 v110, 0xffff0000, v74
	v_lshlrev_b32_e32 v103, 16, v37
	v_lshlrev_b32_e32 v102, 16, v36
	v_pk_add_f32 v[104:105], v[104:105], v[106:107]
	v_and_b32_e32 v107, 0xffff0000, v37
	v_and_b32_e32 v106, 0xffff0000, v36
	v_pk_add_f32 v[108:109], v[108:109], v[110:111]
	v_pk_add_f32 v[104:105], v[104:105], v[102:103]
	v_pk_add_f32 v[102:103], v[108:109], v[106:107]
	v_pk_mul_f32 v[106:107], v[90:91], v[90:91]
	v_pk_mul_f32 v[108:109], v[94:95], v[94:95]
	v_pk_fma_f32 v[106:107], v[92:93], v[92:93], v[106:107]
	v_pk_fma_f32 v[108:109], v[96:97], v[96:97], v[108:109]
	v_pk_mul_f32 v[110:111], v[98:99], v[98:99]
	v_pk_mul_f32 v[112:113], v[102:103], v[102:103]
	v_pk_fma_f32 v[110:111], v[100:101], v[100:101], v[110:111]
	v_add_f32_e32 v0, v106, v107
	v_add_f32_e32 v7, v108, v109
	v_pk_fma_f32 v[112:113], v[104:105], v[104:105], v[112:113]
	v_add_f32_e32 v0, v7, v0
	v_add_f32_e32 v7, v110, v111
	v_add_f32_e32 v0, v7, v0
	v_add_f32_e32 v7, v112, v113
	v_add_f32_e32 v0, v7, v0
	ds_swizzle_b32 v7, v0 offset:swizzle(SWAP,1)
	v_and_b32_sdwa v109, v92, v252 dst_sel:DWORD dst_unused:UNUSED_PAD src0_sel:WORD_1 src1_sel:DWORD
	v_add3_u32 v110, v92, v109, s90
	v_and_b32_sdwa v109, v91, v252 dst_sel:DWORD dst_unused:UNUSED_PAD src0_sel:WORD_1 src1_sel:DWORD
	v_and_b32_sdwa v111, v90, v252 dst_sel:DWORD dst_unused:UNUSED_PAD src0_sel:WORD_1 src1_sel:DWORD
	s_waitcnt lgkmcnt(0)
	v_add_f32_e32 v0, v0, v7
	ds_swizzle_b32 v7, v0 offset:swizzle(SWAP,2)
	s_ashr_i32 s59, s58, 31
	v_and_b32_sdwa v108, v93, v252 dst_sel:DWORD dst_unused:UNUSED_PAD src0_sel:WORD_1 src1_sel:DWORD
	v_add3_u32 v109, v91, v109, s90
	v_add3_u32 v111, v90, v111, s90
	s_waitcnt lgkmcnt(0)
	v_add_f32_e32 v0, v0, v7
	ds_swizzle_b32 v7, v0 offset:swizzle(SWAP,4)
	s_lshl_b64 s[10:11], s[58:59], 11
	v_add3_u32 v108, v93, v108, s90
	v_and_b32_e32 v109, 0xffff0000, v109
	v_and_b32_e32 v111, 0xffff0000, v111
	v_lshl_add_u64 v[106:107], v[4:5], 0, s[10:11]
	v_or_b32_sdwa v109, v109, v108 dst_sel:DWORD dst_unused:UNUSED_PAD src0_sel:DWORD src1_sel:WORD_1
	v_or_b32_sdwa v108, v111, v110 dst_sel:DWORD dst_unused:UNUSED_PAD src0_sel:DWORD src1_sel:WORD_1
	s_waitcnt lgkmcnt(0)
; #define GAS __attribute__((address_space(1)))
; __device__ __forceinline__ unsigned pk2(float lo, float hi) { return f2bf(lo) | (f2bf(hi) << 16); }
; template <bool INIT, bool FINAL>
; __device__ __forceinline__ void row_pass(const float* xin, float* xout, bf16* xb, float* ssx, const bf16* Y, const int* pos, const float* gfin, int gw, int NGW, int lane, unsigned char* xq = nullptr  ) {
;     ...
;             ss = wave_sum(ss);
;             if (FINAL) {
;                 GAS f32x4* xo = (GAS f32x4*)(xout + (size_t)t * D_) + lane;
;                 const float rs = 1.0f / sqrtf(ss * (1.0f / D_) + EPS_);
; #pragma unroll
;                 for (int j = 0; j < 4; ++j) { const f32x4 g = ((const GAS f32x4*)gfin)[lane + 64 * j]; xo[64 * j] = v[u][j] * rs * g; }
;             } else {
;                 GAS v2u* bo = (GAS v2u*)(xb + (size_t)t * D_) + lane;
; #pragma unroll
;                 for (int j = 0; j < 4; ++j) { v2u w; w.x = pk2(v[u][j].x, v[u][j].y); w.y = pk2(v[u][j].z, v[u][j].w); bo[64 * j] = w; }
;                 if (xq) { GAS unsigned* qo = (GAS unsigned*)(xq + (size_t)t * D_) + lane;
; #pragma unroll
;                     for (int j = 0; j < 4; ++j) { int w = 0;
;                         w = __builtin_amdgcn_cvt_pk_fp8_f32(__builtin_amdgcn_fmed3f(v[u][j].x * 8.0f, -448.f, 448.f), __builtin_amdgcn_fmed3f(v[u][j].y * 8.0f, -448.f, 448.f), w, false);
;                         w = __builtin_amdgcn_cvt_pk_fp8_f32(__builtin_amdgcn_fmed3f(v[u][j].z * 8.0f, -448.f, 448.f), __builtin_amdgcn_fmed3f(v[u][j].w * 8.0f, -448.f, 448.f), w, true); qo[64 * j] = (unsigned)w; } }
;                 if (lane < 16) ssx[(size_t)t * 16 + lane] = lane == 0 ? ss : 0.f;
	v_add_f32_e32 v0, v0, v7
	global_store_dwordx2 v[106:107], v[108:109], off
	v_and_b32_sdwa v109, v96, v252 dst_sel:DWORD dst_unused:UNUSED_PAD src0_sel:WORD_1 src1_sel:DWORD
	ds_swizzle_b32 v7, v0 offset:swizzle(SWAP,8)
	v_add3_u32 v110, v96, v109, s90
	v_and_b32_sdwa v109, v95, v252 dst_sel:DWORD dst_unused:UNUSED_PAD src0_sel:WORD_1 src1_sel:DWORD
	v_and_b32_sdwa v111, v94, v252 dst_sel:DWORD dst_unused:UNUSED_PAD src0_sel:WORD_1 src1_sel:DWORD
	v_and_b32_sdwa v108, v97, v252 dst_sel:DWORD dst_unused:UNUSED_PAD src0_sel:WORD_1 src1_sel:DWORD
	v_add3_u32 v109, v95, v109, s90
	v_add3_u32 v111, v94, v111, s90
	v_add3_u32 v108, v97, v108, s90
	v_and_b32_e32 v109, 0xffff0000, v109
	v_and_b32_e32 v111, 0xffff0000, v111
	v_or_b32_sdwa v109, v109, v108 dst_sel:DWORD dst_unused:UNUSED_PAD src0_sel:DWORD src1_sel:WORD_1
	v_or_b32_sdwa v108, v111, v110 dst_sel:DWORD dst_unused:UNUSED_PAD src0_sel:DWORD src1_sel:WORD_1
	global_store_dwordx2 v[106:107], v[108:109], off offset:512
	v_and_b32_sdwa v109, v100, v252 dst_sel:DWORD dst_unused:UNUSED_PAD src0_sel:WORD_1 src1_sel:DWORD
	s_waitcnt lgkmcnt(0)
	v_add_f32_e32 v0, v0, v7
	v_add3_u32 v110, v100, v109, s90
	v_and_b32_sdwa v109, v99, v252 dst_sel:DWORD dst_unused:UNUSED_PAD src0_sel:WORD_1 src1_sel:DWORD
	v_and_b32_sdwa v111, v98, v252 dst_sel:DWORD dst_unused:UNUSED_PAD src0_sel:WORD_1 src1_sel:DWORD
	ds_swizzle_b32 v7, v0 offset:swizzle(SWAP,16)
	v_and_b32_sdwa v108, v101, v252 dst_sel:DWORD dst_unused:UNUSED_PAD src0_sel:WORD_1 src1_sel:DWORD
	v_add3_u32 v109, v99, v109, s90
	v_add3_u32 v111, v98, v111, s90
	v_add3_u32 v108, v101, v108, s90
	v_and_b32_e32 v109, 0xffff0000, v109
	v_and_b32_e32 v111, 0xffff0000, v111
	v_or_b32_sdwa v109, v109, v108 dst_sel:DWORD dst_unused:UNUSED_PAD src0_sel:DWORD src1_sel:WORD_1
	v_or_b32_sdwa v108, v111, v110 dst_sel:DWORD dst_unused:UNUSED_PAD src0_sel:DWORD src1_sel:WORD_1
	global_store_dwordx2 v[106:107], v[108:109], off offset:1024
	v_and_b32_sdwa v109, v104, v252 dst_sel:DWORD dst_unused:UNUSED_PAD src0_sel:WORD_1 src1_sel:DWORD
	v_add3_u32 v110, v104, v109, s90
	v_and_b32_sdwa v109, v103, v252 dst_sel:DWORD dst_unused:UNUSED_PAD src0_sel:WORD_1 src1_sel:DWORD
	v_and_b32_sdwa v111, v102, v252 dst_sel:DWORD dst_unused:UNUSED_PAD src0_sel:WORD_1 src1_sel:DWORD
	s_waitcnt lgkmcnt(0)
	v_add_f32_e32 v0, v0, v7
	v_and_b32_sdwa v108, v105, v252 dst_sel:DWORD dst_unused:UNUSED_PAD src0_sel:WORD_1 src1_sel:DWORD
	v_add3_u32 v109, v103, v109, s90
	v_add3_u32 v111, v102, v111, s90
	v_mov_b32_e32 v7, v0
	v_add3_u32 v108, v105, v108, s90
	v_and_b32_e32 v109, 0xffff0000, v109
	v_and_b32_e32 v111, 0xffff0000, v111
	v_permlane32_swap_b32_e32 v0, v7
	v_or_b32_sdwa v109, v109, v108 dst_sel:DWORD dst_unused:UNUSED_PAD src0_sel:DWORD src1_sel:WORD_1
	v_or_b32_sdwa v108, v111, v110 dst_sel:DWORD dst_unused:UNUSED_PAD src0_sel:DWORD src1_sel:WORD_1
	s_and_b64 vcc, exec, s[12:13]
	global_store_dwordx2 v[106:107], v[108:109], off offset:1536
	s_cbranch_vccnz .LBB0_1602
	v_mul_f32_e32 v92, 0x41000000, v92
	v_mul_f32_e32 v90, 0x41000000, v90
	v_med3_f32 v92, v92, s64, v250
	v_med3_f32 v90, v90, s64, v250
	v_cvt_pk_fp8_f32 v108, v92, v90
	v_mul_f32_e32 v90, 0x41000000, v93
	v_mul_f32_e32 v91, 0x41000000, v91
	v_med3_f32 v90, v90, s64, v250
	v_med3_f32 v91, v91, s64, v250
	v_cvt_pk_fp8_f32 v108, v90, v91 op_sel:[0,0,1]
	v_mul_f32_e32 v90, 0x41000000, v96
	v_mul_f32_e32 v91, 0x41000000, v94
	v_med3_f32 v90, v90, s64, v250
	v_med3_f32 v91, v91, s64, v250
	v_cvt_pk_fp8_f32 v92, v90, v91
	v_mul_f32_e32 v90, 0x41000000, v97
	v_mul_f32_e32 v91, 0x41000000, v95
	v_med3_f32 v90, v90, s64, v250
	v_med3_f32 v91, v91, s64, v250
	v_cvt_pk_fp8_f32 v92, v90, v91 op_sel:[0,0,1]
	v_mul_f32_e32 v90, 0x41000000, v100
	v_mul_f32_e32 v91, 0x41000000, v98
	v_med3_f32 v90, v90, s64, v250
	v_med3_f32 v91, v91, s64, v250
	v_cvt_pk_fp8_f32 v93, v90, v91
	v_mul_f32_e32 v90, 0x41000000, v101
	v_mul_f32_e32 v91, 0x41000000, v99
	v_med3_f32 v90, v90, s64, v250
	v_med3_f32 v91, v91, s64, v250
	v_cvt_pk_fp8_f32 v93, v90, v91 op_sel:[0,0,1]
	v_mul_f32_e32 v90, 0x41000000, v104
	v_mul_f32_e32 v91, 0x41000000, v102
	v_med3_f32 v90, v90, s64, v250
	v_med3_f32 v91, v91, s64, v250
	v_cvt_pk_fp8_f32 v94, v90, v91
	v_mul_f32_e32 v90, 0x41000000, v105
	v_mul_f32_e32 v91, 0x41000000, v103
	s_lshl_b64 s[10:11], s[58:59], 10
	v_med3_f32 v90, v90, s64, v250
	v_med3_f32 v91, v91, s64, v250
	v_lshl_add_u64 v[106:107], v[10:11], 0, s[10:11]
	v_cvt_pk_fp8_f32 v94, v90, v91 op_sel:[0,0,1]
	global_store_dword v[106:107], v108, off
	global_store_dword v[106:107], v92, off offset:256
	global_store_dword v[106:107], v93, off offset:512
	global_store_dword v[106:107], v94, off offset:768

; template <bool INIT, bool FINAL>
; __device__ __forceinline__ void row_pass(const float* xin, float* xout, bf16* xb, float* ssx, const bf16* Y, const int* pos, const float* gfin, int gw, int NGW, int lane, unsigned char* xq = nullptr  ) {
;     ...
;                 for (int j = 0; j < 4; ++j) { const v2u c = xw[u][j], a = aw[u][j], b = bw[u][j];
;                     if (Y8) { typedef float f2_ __attribute__((ext_vector_type(2)));
;                         const f2_ a01 = __builtin_amdgcn_cvt_pk_f32_fp8((int)a.x, false), a23 = __builtin_amdgcn_cvt_pk_f32_fp8((int)a.x, true), b01 = __builtin_amdgcn_cvt_pk_f32_fp8((int)b.x, false), b23 = __builtin_amdgcn_cvt_pk_f32_fp8((int)b.x, true);
;                         v[u][j].x = __uint_as_float(c.x << 16) + (a01[0] + b01[0]) * 0.125f; v[u][j].y = __uint_as_float(c.x & 0xffff0000u) + (a01[1] + b01[1]) * 0.125f;
;                         v[u][j].z = __uint_as_float(c.y << 16) + (a23[0] + b23[0]) * 0.125f; v[u][j].w = __uint_as_float(c.y & 0xffff0000u) + (a23[1] + b23[1]) * 0.125f; }
;                     else {
;                     v[u][j].x = __uint_as_float(c.x << 16) + (__uint_as_float(a.x << 16) + __uint_as_float(b.x << 16)); v[u][j].y = __uint_as_float(c.x & 0xffff0000u) + (__uint_as_float(a.x & 0xffff0000u) + __uint_as_float(b.x & 0xffff0000u));
;                     v[u][j].z = __uint_as_float(c.y << 16) + (__uint_as_float(a.y << 16) + __uint_as_float(b.y << 16)); v[u][j].w = __uint_as_float(c.y & 0xffff0000u) + (__uint_as_float(a.y & 0xffff0000u) + __uint_as_float(b.y & 0xffff0000u)); } }
;         }
; #pragma unroll
;         for (int u = 0; u < U; ++u) { const int t = t0 + u * NGW; if (t < T_) {
;             float ss = 0.f;
; #pragma unroll
;             for (int j = 0; j < 4; ++j) ss += (v[u][j].x * v[u][j].x + v[u][j].y * v[u][j].y) + (v[u][j].z * v[u][j].z + v[u][j].w * v[u][j].w);
;             ss = wave_sum(ss);
.LBB0_1608:
	v_lshlrev_b32_e32 v93, 16, v65
	v_lshlrev_b32_e32 v92, 16, v64
	v_lshlrev_b32_e32 v95, 16, v89
	v_lshlrev_b32_e32 v94, 16, v88
	v_and_b32_e32 v97, 0xffff0000, v65
	v_and_b32_e32 v96, 0xffff0000, v64
	v_and_b32_e32 v99, 0xffff0000, v89
	v_and_b32_e32 v98, 0xffff0000, v88
	v_lshlrev_b32_e32 v91, 16, v31
	v_lshlrev_b32_e32 v90, 16, v30
	v_pk_add_f32 v[92:93], v[92:93], v[94:95]
	v_and_b32_e32 v95, 0xffff0000, v31
	v_and_b32_e32 v94, 0xffff0000, v30
	v_pk_add_f32 v[96:97], v[96:97], v[98:99]
	v_pk_add_f32 v[92:93], v[92:93], v[90:91]
	v_pk_add_f32 v[90:91], v[96:97], v[94:95]
	v_lshlrev_b32_e32 v97, 16, v63
	v_lshlrev_b32_e32 v96, 16, v62
	v_lshlrev_b32_e32 v99, 16, v87
	v_lshlrev_b32_e32 v98, 16, v86
	v_and_b32_e32 v101, 0xffff0000, v63
	v_and_b32_e32 v100, 0xffff0000, v62
	v_and_b32_e32 v103, 0xffff0000, v87
	v_and_b32_e32 v102, 0xffff0000, v86
	v_lshlrev_b32_e32 v95, 16, v35
	v_lshlrev_b32_e32 v94, 16, v34
	v_pk_add_f32 v[96:97], v[96:97], v[98:99]
	v_and_b32_e32 v99, 0xffff0000, v35
	v_and_b32_e32 v98, 0xffff0000, v34
	v_pk_add_f32 v[100:101], v[100:101], v[102:103]
	v_pk_add_f32 v[96:97], v[96:97], v[94:95]
	v_pk_add_f32 v[94:95], v[100:101], v[98:99]
	v_lshlrev_b32_e32 v101, 16, v61
	v_lshlrev_b32_e32 v100, 16, v60
	v_lshlrev_b32_e32 v103, 16, v85
	v_lshlrev_b32_e32 v102, 16, v84
	v_and_b32_e32 v105, 0xffff0000, v61
	v_and_b32_e32 v104, 0xffff0000, v60
	v_and_b32_e32 v107, 0xffff0000, v85
	v_and_b32_e32 v106, 0xffff0000, v84
	v_lshlrev_b32_e32 v99, 16, v39
	v_lshlrev_b32_e32 v98, 16, v38
	v_pk_add_f32 v[100:101], v[100:101], v[102:103]
	v_and_b32_e32 v103, 0xffff0000, v39
	v_and_b32_e32 v102, 0xffff0000, v38
	v_pk_add_f32 v[104:105], v[104:105], v[106:107]
	v_pk_add_f32 v[100:101], v[100:101], v[98:99]
	v_pk_add_f32 v[98:99], v[104:105], v[102:103]
	v_lshlrev_b32_e32 v105, 16, v59
	v_lshlrev_b32_e32 v104, 16, v58
	v_lshlrev_b32_e32 v107, 16, v83
	v_lshlrev_b32_e32 v106, 16, v82
	v_and_b32_e32 v109, 0xffff0000, v59
	v_and_b32_e32 v108, 0xffff0000, v58
	v_and_b32_e32 v111, 0xffff0000, v83
	v_and_b32_e32 v110, 0xffff0000, v82
	v_lshlrev_b32_e32 v103, 16, v41
	v_lshlrev_b32_e32 v102, 16, v40
	v_pk_add_f32 v[104:105], v[104:105], v[106:107]
	v_and_b32_e32 v107, 0xffff0000, v41
	v_and_b32_e32 v106, 0xffff0000, v40
	v_pk_add_f32 v[108:109], v[108:109], v[110:111]
	v_pk_add_f32 v[104:105], v[104:105], v[102:103]
	v_pk_add_f32 v[102:103], v[108:109], v[106:107]
	v_pk_mul_f32 v[106:107], v[90:91], v[90:91]
	v_pk_mul_f32 v[108:109], v[94:95], v[94:95]
	v_pk_fma_f32 v[106:107], v[92:93], v[92:93], v[106:107]
	v_pk_fma_f32 v[108:109], v[96:97], v[96:97], v[108:109]
	v_pk_mul_f32 v[110:111], v[98:99], v[98:99]
	v_pk_mul_f32 v[112:113], v[102:103], v[102:103]
	v_pk_fma_f32 v[110:111], v[100:101], v[100:101], v[110:111]
	v_add_f32_e32 v0, v106, v107
	v_add_f32_e32 v7, v108, v109
	v_pk_fma_f32 v[112:113], v[104:105], v[104:105], v[112:113]
	v_add_f32_e32 v0, v7, v0
	v_add_f32_e32 v7, v110, v111
	v_add_f32_e32 v0, v7, v0
	v_add_f32_e32 v7, v112, v113
	v_add_f32_e32 v0, v7, v0
	ds_swizzle_b32 v7, v0 offset:swizzle(SWAP,1)
	v_and_b32_sdwa v109, v92, v252 dst_sel:DWORD dst_unused:UNUSED_PAD src0_sel:WORD_1 src1_sel:DWORD
	v_add3_u32 v110, v92, v109, s90
	v_and_b32_sdwa v109, v91, v252 dst_sel:DWORD dst_unused:UNUSED_PAD src0_sel:WORD_1 src1_sel:DWORD
	v_and_b32_sdwa v111, v90, v252 dst_sel:DWORD dst_unused:UNUSED_PAD src0_sel:WORD_1 src1_sel:DWORD
	s_waitcnt lgkmcnt(0)
	v_add_f32_e32 v0, v0, v7
	ds_swizzle_b32 v7, v0 offset:swizzle(SWAP,2)
	s_ashr_i32 s61, s60, 31
	v_and_b32_sdwa v108, v93, v252 dst_sel:DWORD dst_unused:UNUSED_PAD src0_sel:WORD_1 src1_sel:DWORD
	v_add3_u32 v109, v91, v109, s90
	v_add3_u32 v111, v90, v111, s90
	s_waitcnt lgkmcnt(0)
	v_add_f32_e32 v0, v0, v7
	ds_swizzle_b32 v7, v0 offset:swizzle(SWAP,4)
	s_lshl_b64 s[14:15], s[60:61], 11
	v_add3_u32 v108, v93, v108, s90
	v_and_b32_e32 v109, 0xffff0000, v109
	v_and_b32_e32 v111, 0xffff0000, v111
	v_lshl_add_u64 v[106:107], v[4:5], 0, s[14:15]
	v_or_b32_sdwa v109, v109, v108 dst_sel:DWORD dst_unused:UNUSED_PAD src0_sel:DWORD src1_sel:WORD_1
	v_or_b32_sdwa v108, v111, v110 dst_sel:DWORD dst_unused:UNUSED_PAD src0_sel:DWORD src1_sel:WORD_1
	s_waitcnt lgkmcnt(0)
; #define GAS __attribute__((address_space(1)))
; __device__ __forceinline__ unsigned pk2(float lo, float hi) { return f2bf(lo) | (f2bf(hi) << 16); }
; template <bool INIT, bool FINAL>
; __device__ __forceinline__ void row_pass(const float* xin, float* xout, bf16* xb, float* ssx, const bf16* Y, const int* pos, const float* gfin, int gw, int NGW, int lane, unsigned char* xq = nullptr  ) {
;     ...
;             ss = wave_sum(ss);
;             if (FINAL) {
;                 GAS f32x4* xo = (GAS f32x4*)(xout + (size_t)t * D_) + lane;
;                 const float rs = 1.0f / sqrtf(ss * (1.0f / D_) + EPS_);
; #pragma unroll
;                 for (int j = 0; j < 4; ++j) { const f32x4 g = ((const GAS f32x4*)gfin)[lane + 64 * j]; xo[64 * j] = v[u][j] * rs * g; }
;             } else {
;                 GAS v2u* bo = (GAS v2u*)(xb + (size_t)t * D_) + lane;
; #pragma unroll
;                 for (int j = 0; j < 4; ++j) { v2u w; w.x = pk2(v[u][j].x, v[u][j].y); w.y = pk2(v[u][j].z, v[u][j].w); bo[64 * j] = w; }
;                 if (xq) { GAS unsigned* qo = (GAS unsigned*)(xq + (size_t)t * D_) + lane;
; #pragma unroll
;                     for (int j = 0; j < 4; ++j) { int w = 0;
;                         w = __builtin_amdgcn_cvt_pk_fp8_f32(__builtin_amdgcn_fmed3f(v[u][j].x * 8.0f, -448.f, 448.f), __builtin_amdgcn_fmed3f(v[u][j].y * 8.0f, -448.f, 448.f), w, false);
;                         w = __builtin_amdgcn_cvt_pk_fp8_f32(__builtin_amdgcn_fmed3f(v[u][j].z * 8.0f, -448.f, 448.f), __builtin_amdgcn_fmed3f(v[u][j].w * 8.0f, -448.f, 448.f), w, true); qo[64 * j] = (unsigned)w; } }
;                 if (lane < 16) ssx[(size_t)t * 16 + lane] = lane == 0 ? ss : 0.f;
	v_add_f32_e32 v0, v0, v7
	global_store_dwordx2 v[106:107], v[108:109], off
	v_and_b32_sdwa v109, v96, v252 dst_sel:DWORD dst_unused:UNUSED_PAD src0_sel:WORD_1 src1_sel:DWORD
	ds_swizzle_b32 v7, v0 offset:swizzle(SWAP,8)
	v_add3_u32 v110, v96, v109, s90
	v_and_b32_sdwa v109, v95, v252 dst_sel:DWORD dst_unused:UNUSED_PAD src0_sel:WORD_1 src1_sel:DWORD
	v_and_b32_sdwa v111, v94, v252 dst_sel:DWORD dst_unused:UNUSED_PAD src0_sel:WORD_1 src1_sel:DWORD
	v_and_b32_sdwa v108, v97, v252 dst_sel:DWORD dst_unused:UNUSED_PAD src0_sel:WORD_1 src1_sel:DWORD
	v_add3_u32 v109, v95, v109, s90
	v_add3_u32 v111, v94, v111, s90
	v_add3_u32 v108, v97, v108, s90
	v_and_b32_e32 v109, 0xffff0000, v109
	v_and_b32_e32 v111, 0xffff0000, v111
	v_or_b32_sdwa v109, v109, v108 dst_sel:DWORD dst_unused:UNUSED_PAD src0_sel:DWORD src1_sel:WORD_1
	v_or_b32_sdwa v108, v111, v110 dst_sel:DWORD dst_unused:UNUSED_PAD src0_sel:DWORD src1_sel:WORD_1
	global_store_dwordx2 v[106:107], v[108:109], off offset:512
	v_and_b32_sdwa v109, v100, v252 dst_sel:DWORD dst_unused:UNUSED_PAD src0_sel:WORD_1 src1_sel:DWORD
	s_waitcnt lgkmcnt(0)
	v_add_f32_e32 v0, v0, v7
	v_add3_u32 v110, v100, v109, s90
	v_and_b32_sdwa v109, v99, v252 dst_sel:DWORD dst_unused:UNUSED_PAD src0_sel:WORD_1 src1_sel:DWORD
	v_and_b32_sdwa v111, v98, v252 dst_sel:DWORD dst_unused:UNUSED_PAD src0_sel:WORD_1 src1_sel:DWORD
	ds_swizzle_b32 v7, v0 offset:swizzle(SWAP,16)
	v_and_b32_sdwa v108, v101, v252 dst_sel:DWORD dst_unused:UNUSED_PAD src0_sel:WORD_1 src1_sel:DWORD
	v_add3_u32 v109, v99, v109, s90
	v_add3_u32 v111, v98, v111, s90
	v_add3_u32 v108, v101, v108, s90
	v_and_b32_e32 v109, 0xffff0000, v109
	v_and_b32_e32 v111, 0xffff0000, v111
	v_or_b32_sdwa v109, v109, v108 dst_sel:DWORD dst_unused:UNUSED_PAD src0_sel:DWORD src1_sel:WORD_1
	v_or_b32_sdwa v108, v111, v110 dst_sel:DWORD dst_unused:UNUSED_PAD src0_sel:DWORD src1_sel:WORD_1
	global_store_dwordx2 v[106:107], v[108:109], off offset:1024
	v_and_b32_sdwa v109, v104, v252 dst_sel:DWORD dst_unused:UNUSED_PAD src0_sel:WORD_1 src1_sel:DWORD
	v_add3_u32 v110, v104, v109, s90
	v_and_b32_sdwa v109, v103, v252 dst_sel:DWORD dst_unused:UNUSED_PAD src0_sel:WORD_1 src1_sel:DWORD
	v_and_b32_sdwa v111, v102, v252 dst_sel:DWORD dst_unused:UNUSED_PAD src0_sel:WORD_1 src1_sel:DWORD
	s_waitcnt lgkmcnt(0)
	v_add_f32_e32 v0, v0, v7
	v_and_b32_sdwa v108, v105, v252 dst_sel:DWORD dst_unused:UNUSED_PAD src0_sel:WORD_1 src1_sel:DWORD
	v_add3_u32 v109, v103, v109, s90
	v_add3_u32 v111, v102, v111, s90
	v_mov_b32_e32 v7, v0
	v_add3_u32 v108, v105, v108, s90
	v_and_b32_e32 v109, 0xffff0000, v109
	v_and_b32_e32 v111, 0xffff0000, v111
	v_permlane32_swap_b32_e32 v0, v7
	v_or_b32_sdwa v109, v109, v108 dst_sel:DWORD dst_unused:UNUSED_PAD src0_sel:DWORD src1_sel:WORD_1
	v_or_b32_sdwa v108, v111, v110 dst_sel:DWORD dst_unused:UNUSED_PAD src0_sel:DWORD src1_sel:WORD_1
	s_and_b64 vcc, exec, s[12:13]
	global_store_dwordx2 v[106:107], v[108:109], off offset:1536
	s_cbranch_vccnz .LBB0_1610
	v_mul_f32_e32 v92, 0x41000000, v92
	v_mul_f32_e32 v90, 0x41000000, v90
	v_med3_f32 v92, v92, s64, v250
	v_med3_f32 v90, v90, s64, v250
	v_cvt_pk_fp8_f32 v108, v92, v90
	v_mul_f32_e32 v90, 0x41000000, v93
	v_mul_f32_e32 v91, 0x41000000, v91
	v_med3_f32 v90, v90, s64, v250
	v_med3_f32 v91, v91, s64, v250
	v_cvt_pk_fp8_f32 v108, v90, v91 op_sel:[0,0,1]
	v_mul_f32_e32 v90, 0x41000000, v96
	v_mul_f32_e32 v91, 0x41000000, v94
	v_med3_f32 v90, v90, s64, v250
	v_med3_f32 v91, v91, s64, v250
	v_cvt_pk_fp8_f32 v92, v90, v91
	v_mul_f32_e32 v90, 0x41000000, v97
	v_mul_f32_e32 v91, 0x41000000, v95
	v_med3_f32 v90, v90, s64, v250
	v_med3_f32 v91, v91, s64, v250
	v_cvt_pk_fp8_f32 v92, v90, v91 op_sel:[0,0,1]
	v_mul_f32_e32 v90, 0x41000000, v100
	v_mul_f32_e32 v91, 0x41000000, v98
	v_med3_f32 v90, v90, s64, v250
	v_med3_f32 v91, v91, s64, v250
	v_cvt_pk_fp8_f32 v93, v90, v91
	v_mul_f32_e32 v90, 0x41000000, v101
	v_mul_f32_e32 v91, 0x41000000, v99
	v_med3_f32 v90, v90, s64, v250
	v_med3_f32 v91, v91, s64, v250
	v_cvt_pk_fp8_f32 v93, v90, v91 op_sel:[0,0,1]
	v_mul_f32_e32 v90, 0x41000000, v104
	v_mul_f32_e32 v91, 0x41000000, v102
	v_med3_f32 v90, v90, s64, v250
	v_med3_f32 v91, v91, s64, v250
	v_cvt_pk_fp8_f32 v94, v90, v91
	v_mul_f32_e32 v90, 0x41000000, v105
	v_mul_f32_e32 v91, 0x41000000, v103
	s_lshl_b64 s[14:15], s[60:61], 10
	v_med3_f32 v90, v90, s64, v250
	v_med3_f32 v91, v91, s64, v250
	v_lshl_add_u64 v[106:107], v[10:11], 0, s[14:15]
	v_cvt_pk_fp8_f32 v94, v90, v91 op_sel:[0,0,1]
	global_store_dword v[106:107], v108, off
	global_store_dword v[106:107], v92, off offset:256
	global_store_dword v[106:107], v93, off offset:512
	global_store_dword v[106:107], v94, off offset:768

; template <bool INIT, bool FINAL>
; __device__ __forceinline__ void row_pass(const float* xin, float* xout, bf16* xb, float* ssx, const bf16* Y, const int* pos, const float* gfin, int gw, int NGW, int lane, unsigned char* xq = nullptr  ) {
;     ...
;                 for (int j = 0; j < 4; ++j) { const v2u c = xw[u][j], a = aw[u][j], b = bw[u][j];
;                     if (Y8) { typedef float f2_ __attribute__((ext_vector_type(2)));
;                         const f2_ a01 = __builtin_amdgcn_cvt_pk_f32_fp8((int)a.x, false), a23 = __builtin_amdgcn_cvt_pk_f32_fp8((int)a.x, true), b01 = __builtin_amdgcn_cvt_pk_f32_fp8((int)b.x, false), b23 = __builtin_amdgcn_cvt_pk_f32_fp8((int)b.x, true);
;                         v[u][j].x = __uint_as_float(c.x << 16) + (a01[0] + b01[0]) * 0.125f; v[u][j].y = __uint_as_float(c.x & 0xffff0000u) + (a01[1] + b01[1]) * 0.125f;
;                         v[u][j].z = __uint_as_float(c.y << 16) + (a23[0] + b23[0]) * 0.125f; v[u][j].w = __uint_as_float(c.y & 0xffff0000u) + (a23[1] + b23[1]) * 0.125f; }
;                     else {
;                     v[u][j].x = __uint_as_float(c.x << 16) + (__uint_as_float(a.x << 16) + __uint_as_float(b.x << 16)); v[u][j].y = __uint_as_float(c.x & 0xffff0000u) + (__uint_as_float(a.x & 0xffff0000u) + __uint_as_float(b.x & 0xffff0000u));
;                     v[u][j].z = __uint_as_float(c.y << 16) + (__uint_as_float(a.y << 16) + __uint_as_float(b.y << 16)); v[u][j].w = __uint_as_float(c.y & 0xffff0000u) + (__uint_as_float(a.y & 0xffff0000u) + __uint_as_float(b.y & 0xffff0000u)); } }
;         }
; #pragma unroll
;         for (int u = 0; u < U; ++u) { const int t = t0 + u * NGW; if (t < T_) {
;             float ss = 0.f;
; #pragma unroll
;             for (int j = 0; j < 4; ++j) ss += (v[u][j].x * v[u][j].x + v[u][j].y * v[u][j].y) + (v[u][j].z * v[u][j].z + v[u][j].w * v[u][j].w);
;             ss = wave_sum(ss);
.LBB0_1614:
	v_lshlrev_b32_e32 v93, 16, v49
	v_lshlrev_b32_e32 v92, 16, v48
	v_lshlrev_b32_e32 v95, 16, v73
	v_lshlrev_b32_e32 v94, 16, v72
	v_and_b32_e32 v97, 0xffff0000, v49
	v_and_b32_e32 v96, 0xffff0000, v48
	v_and_b32_e32 v99, 0xffff0000, v73
	v_and_b32_e32 v98, 0xffff0000, v72
	v_lshlrev_b32_e32 v91, 16, v19
	v_lshlrev_b32_e32 v90, 16, v18
	v_pk_add_f32 v[92:93], v[92:93], v[94:95]
	v_and_b32_e32 v95, 0xffff0000, v19
	v_and_b32_e32 v94, 0xffff0000, v18
	v_pk_add_f32 v[96:97], v[96:97], v[98:99]
	v_pk_add_f32 v[92:93], v[92:93], v[90:91]
	v_pk_add_f32 v[90:91], v[96:97], v[94:95]
	v_lshlrev_b32_e32 v97, 16, v47
	v_lshlrev_b32_e32 v96, 16, v46
	v_lshlrev_b32_e32 v99, 16, v71
	v_lshlrev_b32_e32 v98, 16, v70
	v_and_b32_e32 v101, 0xffff0000, v47
	v_and_b32_e32 v100, 0xffff0000, v46
	v_and_b32_e32 v103, 0xffff0000, v71
	v_and_b32_e32 v102, 0xffff0000, v70
	v_lshlrev_b32_e32 v95, 16, v21
	v_lshlrev_b32_e32 v94, 16, v20
	v_pk_add_f32 v[96:97], v[96:97], v[98:99]
	v_and_b32_e32 v99, 0xffff0000, v21
	v_and_b32_e32 v98, 0xffff0000, v20
	v_pk_add_f32 v[100:101], v[100:101], v[102:103]
	v_pk_add_f32 v[96:97], v[96:97], v[94:95]
	v_pk_add_f32 v[94:95], v[100:101], v[98:99]
	v_lshlrev_b32_e32 v101, 16, v45
	v_lshlrev_b32_e32 v100, 16, v44
	v_lshlrev_b32_e32 v103, 16, v69
	v_lshlrev_b32_e32 v102, 16, v68
	v_and_b32_e32 v105, 0xffff0000, v45
	v_and_b32_e32 v104, 0xffff0000, v44
	v_and_b32_e32 v107, 0xffff0000, v69
	v_and_b32_e32 v106, 0xffff0000, v68
	v_lshlrev_b32_e32 v99, 16, v25
	v_lshlrev_b32_e32 v98, 16, v24
	v_pk_add_f32 v[100:101], v[100:101], v[102:103]
	v_and_b32_e32 v103, 0xffff0000, v25
	v_and_b32_e32 v102, 0xffff0000, v24
	v_pk_add_f32 v[104:105], v[104:105], v[106:107]
	v_pk_add_f32 v[100:101], v[100:101], v[98:99]
	v_pk_add_f32 v[98:99], v[104:105], v[102:103]
	v_lshlrev_b32_e32 v105, 16, v43
	v_lshlrev_b32_e32 v104, 16, v42
	v_lshlrev_b32_e32 v107, 16, v67
	v_lshlrev_b32_e32 v106, 16, v66
	v_and_b32_e32 v109, 0xffff0000, v43
	v_and_b32_e32 v108, 0xffff0000, v42
	v_and_b32_e32 v111, 0xffff0000, v67
	v_and_b32_e32 v110, 0xffff0000, v66
	v_lshlrev_b32_e32 v103, 16, v29
	v_lshlrev_b32_e32 v102, 16, v28
	v_pk_add_f32 v[104:105], v[104:105], v[106:107]
	v_and_b32_e32 v107, 0xffff0000, v29
	v_and_b32_e32 v106, 0xffff0000, v28
	v_pk_add_f32 v[108:109], v[108:109], v[110:111]
	v_pk_add_f32 v[104:105], v[104:105], v[102:103]
	v_pk_add_f32 v[102:103], v[108:109], v[106:107]
	v_pk_mul_f32 v[106:107], v[90:91], v[90:91]
	v_pk_mul_f32 v[108:109], v[94:95], v[94:95]
	v_pk_fma_f32 v[106:107], v[92:93], v[92:93], v[106:107]
	v_pk_fma_f32 v[108:109], v[96:97], v[96:97], v[108:109]
	v_pk_mul_f32 v[110:111], v[98:99], v[98:99]
	v_pk_mul_f32 v[112:113], v[102:103], v[102:103]
	v_pk_fma_f32 v[110:111], v[100:101], v[100:101], v[110:111]
	v_add_f32_e32 v0, v106, v107
	v_add_f32_e32 v7, v108, v109
	v_pk_fma_f32 v[112:113], v[104:105], v[104:105], v[112:113]
	v_add_f32_e32 v0, v7, v0
	v_add_f32_e32 v7, v110, v111
	v_add_f32_e32 v0, v7, v0
	v_add_f32_e32 v7, v112, v113
	v_add_f32_e32 v0, v7, v0
	ds_swizzle_b32 v7, v0 offset:swizzle(SWAP,1)
	v_and_b32_sdwa v109, v92, v252 dst_sel:DWORD dst_unused:UNUSED_PAD src0_sel:WORD_1 src1_sel:DWORD
	v_add3_u32 v110, v92, v109, s90
	v_and_b32_sdwa v109, v91, v252 dst_sel:DWORD dst_unused:UNUSED_PAD src0_sel:WORD_1 src1_sel:DWORD
	v_and_b32_sdwa v111, v90, v252 dst_sel:DWORD dst_unused:UNUSED_PAD src0_sel:WORD_1 src1_sel:DWORD
	s_waitcnt lgkmcnt(0)
	v_add_f32_e32 v0, v0, v7
	ds_swizzle_b32 v7, v0 offset:swizzle(SWAP,2)
	s_ashr_i32 s57, s56, 31
	v_and_b32_sdwa v108, v93, v252 dst_sel:DWORD dst_unused:UNUSED_PAD src0_sel:WORD_1 src1_sel:DWORD
	v_add3_u32 v109, v91, v109, s90
	v_add3_u32 v111, v90, v111, s90
	s_waitcnt lgkmcnt(0)
	v_add_f32_e32 v0, v0, v7
	ds_swizzle_b32 v7, v0 offset:swizzle(SWAP,4)
	s_lshl_b64 s[8:9], s[56:57], 11
	v_add3_u32 v108, v93, v108, s90
	v_and_b32_e32 v109, 0xffff0000, v109
	v_and_b32_e32 v111, 0xffff0000, v111
	v_lshl_add_u64 v[106:107], v[4:5], 0, s[8:9]
	v_or_b32_sdwa v109, v109, v108 dst_sel:DWORD dst_unused:UNUSED_PAD src0_sel:DWORD src1_sel:WORD_1
	v_or_b32_sdwa v108, v111, v110 dst_sel:DWORD dst_unused:UNUSED_PAD src0_sel:DWORD src1_sel:WORD_1
	s_waitcnt lgkmcnt(0)
; #define GAS __attribute__((address_space(1)))
; __device__ __forceinline__ unsigned pk2(float lo, float hi) { return f2bf(lo) | (f2bf(hi) << 16); }
; template <bool INIT, bool FINAL>
; __device__ __forceinline__ void row_pass(const float* xin, float* xout, bf16* xb, float* ssx, const bf16* Y, const int* pos, const float* gfin, int gw, int NGW, int lane, unsigned char* xq = nullptr  ) {
;     ...
;             ss = wave_sum(ss);
;             if (FINAL) {
;                 GAS f32x4* xo = (GAS f32x4*)(xout + (size_t)t * D_) + lane;
;                 const float rs = 1.0f / sqrtf(ss * (1.0f / D_) + EPS_);
; #pragma unroll
;                 for (int j = 0; j < 4; ++j) { const f32x4 g = ((const GAS f32x4*)gfin)[lane + 64 * j]; xo[64 * j] = v[u][j] * rs * g; }
;             } else {
;                 GAS v2u* bo = (GAS v2u*)(xb + (size_t)t * D_) + lane;
; #pragma unroll
;                 for (int j = 0; j < 4; ++j) { v2u w; w.x = pk2(v[u][j].x, v[u][j].y); w.y = pk2(v[u][j].z, v[u][j].w); bo[64 * j] = w; }
;                 if (xq) { GAS unsigned* qo = (GAS unsigned*)(xq + (size_t)t * D_) + lane;
; #pragma unroll
;                     for (int j = 0; j < 4; ++j) { int w = 0;
;                         w = __builtin_amdgcn_cvt_pk_fp8_f32(__builtin_amdgcn_fmed3f(v[u][j].x * 8.0f, -448.f, 448.f), __builtin_amdgcn_fmed3f(v[u][j].y * 8.0f, -448.f, 448.f), w, false);
;                         w = __builtin_amdgcn_cvt_pk_fp8_f32(__builtin_amdgcn_fmed3f(v[u][j].z * 8.0f, -448.f, 448.f), __builtin_amdgcn_fmed3f(v[u][j].w * 8.0f, -448.f, 448.f), w, true); qo[64 * j] = (unsigned)w; } }
;                 if (lane < 16) ssx[(size_t)t * 16 + lane] = lane == 0 ? ss : 0.f;
	v_add_f32_e32 v0, v0, v7
	global_store_dwordx2 v[106:107], v[108:109], off
	v_and_b32_sdwa v109, v96, v252 dst_sel:DWORD dst_unused:UNUSED_PAD src0_sel:WORD_1 src1_sel:DWORD
	ds_swizzle_b32 v7, v0 offset:swizzle(SWAP,8)
	v_add3_u32 v110, v96, v109, s90
	v_and_b32_sdwa v109, v95, v252 dst_sel:DWORD dst_unused:UNUSED_PAD src0_sel:WORD_1 src1_sel:DWORD
	v_and_b32_sdwa v111, v94, v252 dst_sel:DWORD dst_unused:UNUSED_PAD src0_sel:WORD_1 src1_sel:DWORD
	v_and_b32_sdwa v108, v97, v252 dst_sel:DWORD dst_unused:UNUSED_PAD src0_sel:WORD_1 src1_sel:DWORD
	v_add3_u32 v109, v95, v109, s90
	v_add3_u32 v111, v94, v111, s90
	v_add3_u32 v108, v97, v108, s90
	v_and_b32_e32 v109, 0xffff0000, v109
	v_and_b32_e32 v111, 0xffff0000, v111
	v_or_b32_sdwa v109, v109, v108 dst_sel:DWORD dst_unused:UNUSED_PAD src0_sel:DWORD src1_sel:WORD_1
	v_or_b32_sdwa v108, v111, v110 dst_sel:DWORD dst_unused:UNUSED_PAD src0_sel:DWORD src1_sel:WORD_1
	global_store_dwordx2 v[106:107], v[108:109], off offset:512
	v_and_b32_sdwa v109, v100, v252 dst_sel:DWORD dst_unused:UNUSED_PAD src0_sel:WORD_1 src1_sel:DWORD
	s_waitcnt lgkmcnt(0)
	v_add_f32_e32 v0, v0, v7
	v_add3_u32 v110, v100, v109, s90
	v_and_b32_sdwa v109, v99, v252 dst_sel:DWORD dst_unused:UNUSED_PAD src0_sel:WORD_1 src1_sel:DWORD
	v_and_b32_sdwa v111, v98, v252 dst_sel:DWORD dst_unused:UNUSED_PAD src0_sel:WORD_1 src1_sel:DWORD
	ds_swizzle_b32 v7, v0 offset:swizzle(SWAP,16)
	v_and_b32_sdwa v108, v101, v252 dst_sel:DWORD dst_unused:UNUSED_PAD src0_sel:WORD_1 src1_sel:DWORD
	v_add3_u32 v109, v99, v109, s90
	v_add3_u32 v111, v98, v111, s90
	v_add3_u32 v108, v101, v108, s90
	v_and_b32_e32 v109, 0xffff0000, v109
	v_and_b32_e32 v111, 0xffff0000, v111
	v_or_b32_sdwa v109, v109, v108 dst_sel:DWORD dst_unused:UNUSED_PAD src0_sel:DWORD src1_sel:WORD_1
	v_or_b32_sdwa v108, v111, v110 dst_sel:DWORD dst_unused:UNUSED_PAD src0_sel:DWORD src1_sel:WORD_1
	global_store_dwordx2 v[106:107], v[108:109], off offset:1024
	v_and_b32_sdwa v109, v104, v252 dst_sel:DWORD dst_unused:UNUSED_PAD src0_sel:WORD_1 src1_sel:DWORD
	v_add3_u32 v110, v104, v109, s90
	v_and_b32_sdwa v109, v103, v252 dst_sel:DWORD dst_unused:UNUSED_PAD src0_sel:WORD_1 src1_sel:DWORD
	v_and_b32_sdwa v111, v102, v252 dst_sel:DWORD dst_unused:UNUSED_PAD src0_sel:WORD_1 src1_sel:DWORD
	s_waitcnt lgkmcnt(0)
	v_add_f32_e32 v0, v0, v7
	v_and_b32_sdwa v108, v105, v252 dst_sel:DWORD dst_unused:UNUSED_PAD src0_sel:WORD_1 src1_sel:DWORD
	v_add3_u32 v109, v103, v109, s90
	v_add3_u32 v111, v102, v111, s90
	v_mov_b32_e32 v7, v0
	v_add3_u32 v108, v105, v108, s90
	v_and_b32_e32 v109, 0xffff0000, v109
	v_and_b32_e32 v111, 0xffff0000, v111
	v_permlane32_swap_b32_e32 v0, v7
	v_or_b32_sdwa v109, v109, v108 dst_sel:DWORD dst_unused:UNUSED_PAD src0_sel:DWORD src1_sel:WORD_1
	v_or_b32_sdwa v108, v111, v110 dst_sel:DWORD dst_unused:UNUSED_PAD src0_sel:DWORD src1_sel:WORD_1
	s_and_b64 vcc, exec, s[12:13]
	global_store_dwordx2 v[106:107], v[108:109], off offset:1536
	s_cbranch_vccnz .LBB0_1616
	v_mul_f32_e32 v92, 0x41000000, v92
	v_mul_f32_e32 v90, 0x41000000, v90
	v_med3_f32 v92, v92, s64, v250
	v_med3_f32 v90, v90, s64, v250
	v_cvt_pk_fp8_f32 v108, v92, v90
	v_mul_f32_e32 v90, 0x41000000, v93
	v_mul_f32_e32 v91, 0x41000000, v91
	v_med3_f32 v90, v90, s64, v250
	v_med3_f32 v91, v91, s64, v250
	v_cvt_pk_fp8_f32 v108, v90, v91 op_sel:[0,0,1]
	v_mul_f32_e32 v90, 0x41000000, v96
	v_mul_f32_e32 v91, 0x41000000, v94
	v_med3_f32 v90, v90, s64, v250
	v_med3_f32 v91, v91, s64, v250
	v_cvt_pk_fp8_f32 v92, v90, v91
	v_mul_f32_e32 v90, 0x41000000, v97
	v_mul_f32_e32 v91, 0x41000000, v95
	v_med3_f32 v90, v90, s64, v250
	v_med3_f32 v91, v91, s64, v250
	v_cvt_pk_fp8_f32 v92, v90, v91 op_sel:[0,0,1]
	v_mul_f32_e32 v90, 0x41000000, v100
	v_mul_f32_e32 v91, 0x41000000, v98
	v_med3_f32 v90, v90, s64, v250
	v_med3_f32 v91, v91, s64, v250
	v_cvt_pk_fp8_f32 v93, v90, v91
	v_mul_f32_e32 v90, 0x41000000, v101
	v_mul_f32_e32 v91, 0x41000000, v99
	v_med3_f32 v90, v90, s64, v250
	v_med3_f32 v91, v91, s64, v250
	v_cvt_pk_fp8_f32 v93, v90, v91 op_sel:[0,0,1]
	v_mul_f32_e32 v90, 0x41000000, v104
	v_mul_f32_e32 v91, 0x41000000, v102
	v_med3_f32 v90, v90, s64, v250
	v_med3_f32 v91, v91, s64, v250
	v_cvt_pk_fp8_f32 v94, v90, v91
	v_mul_f32_e32 v90, 0x41000000, v105
	v_mul_f32_e32 v91, 0x41000000, v103
	s_lshl_b64 s[8:9], s[56:57], 10
	v_med3_f32 v90, v90, s64, v250
	v_med3_f32 v91, v91, s64, v250
	v_lshl_add_u64 v[106:107], v[10:11], 0, s[8:9]
	v_cvt_pk_fp8_f32 v94, v90, v91 op_sel:[0,0,1]
	global_store_dword v[106:107], v108, off
	global_store_dword v[106:107], v92, off offset:256
	global_store_dword v[106:107], v93, off offset:512
	global_store_dword v[106:107], v94, off offset:768

; __device__ __forceinline__ u32x4 pack8(const f32x4 a, const f32x4 b) { u32x4 w; w.x = cvt_pk_bf16(a[0], a[1]); w.y = cvt_pk_bf16(a[2], a[3]); w.z = cvt_pk_bf16(b[0], b[1]); w.w = cvt_pk_bf16(b[2], b[3]); return w; }
; __device__ __forceinline__ float sumsq4(const f32x4 v) { return (v[0] * v[0] + v[1] * v[1]) + (v[2] * v[2] + v[3] * v[3]); }
; __device__ __forceinline__ float xor16_add(float v) { return v + __int_as_float(__builtin_amdgcn_ds_swizzle(__float_as_int(v), 0x401F)); }
; __device__ __forceinline__ float xor32_add(float v) { auto rr = __builtin_amdgcn_permlane32_swap(__float_as_uint(v), __float_as_uint(v), false, false); return __uint_as_float(rr[0]) + __uint_as_float(rr[1]); }
; __device__ __forceinline__ f32x4 bf2f_lo(const u32x4 w, int h) { const unsigned a = h ? w.z : w.x, b = h ? w.w : w.y; return (f32x4){__uint_as_float(a << 16), __uint_as_float(a & 0xffff0000u), __uint_as_float(b << 16), __uint_as_float(b & 0xffff0000u)}; }
;     __device__ __forceinline__ void operator()(const f32x4 (&acc)[2][2][4][2], const Unit& u, int wr, int wc, int fr, int fq) const {
;     ...
;                 for (int bj = 0; bj < 2; ++bj) old[m][bj] = *(const u32x4*)(xb + (size_t)(row0 + ai * HALF + m * 16) * DM + col0 + bj * HALF);
; #pragma unroll
;             for (int m = 0; m < 4; ++m) {
;                 const int row = row0 + ai * HALF + m * 16; float ss = 0.f;
; #pragma unroll
;                 for (int bj = 0; bj < 2; ++bj) {
;                     const f32x4 v0 = bf2f_lo(old[m][bj], 0) + acc[ai][bj][m][0], v1 = bf2f_lo(old[m][bj], 1) + acc[ai][bj][m][1];
;                     ss += sumsq4(v0) + sumsq4(v1);
;                     *(u32x4*)(xb + (size_t)row * DM + col0 + bj * HALF) = pack8(v0, v1);
;                     { u32x2 w8; w8.x = pack4_fp8_x8(v0); w8.y = pack4_fp8_x8(v1); *(u32x2*)(xq + (size_t)row * DM + col0 + bj * HALF) = w8; }
;                 }
;                 ss = xor32_add(xor16_add(ss));
;                 if (fq == 0) ssx[(size_t)row * 16 + u.pn * 4 + wc] = ss;
.LBB0_1811:
	v_lshl_add_u32 v172, s61, 8, v163
	v_lshl_or_b32 v122, s60, 8, v193
	v_ashrrev_i32_e32 v123, 31, v122
	v_ashrrev_i32_e32 v173, 31, v172
	v_lshl_add_u64 v[174:175], v[122:123], 1, s[22:23]
	v_lshl_add_u64 v[170:171], s[24:25], 0, v[122:123]
	v_lshlrev_b64 v[122:123], 11, v[172:173]
	v_lshl_add_u64 v[190:191], v[174:175], 0, v[122:123]
	global_load_dwordx4 v[204:207], v[190:191], off
	global_load_dwordx4 v[154:157], v[190:191], off offset:256
	v_or_b32_e32 v184, 16, v172
	v_ashrrev_i32_e32 v185, 31, v184
	v_or_b32_e32 v180, 32, v172
	v_lshlrev_b64 v[122:123], 11, v[184:185]
	v_ashrrev_i32_e32 v181, 31, v180
	v_or_b32_e32 v176, 48, v172
	v_lshl_add_u64 v[186:187], v[174:175], 0, v[122:123]
	v_lshlrev_b64 v[122:123], 11, v[180:181]
	v_ashrrev_i32_e32 v177, 31, v176
	v_lshl_add_u64 v[182:183], v[174:175], 0, v[122:123]
	v_lshlrev_b64 v[122:123], 11, v[176:177]
	v_lshl_add_u64 v[178:179], v[174:175], 0, v[122:123]
	global_load_dwordx4 v[150:153], v[186:187], off
	global_load_dwordx4 v[146:149], v[186:187], off offset:256
	global_load_dwordx4 v[142:145], v[182:183], off
	global_load_dwordx4 v[138:141], v[182:183], off offset:256
	global_load_dwordx4 v[126:129], v[178:179], off
	global_load_dwordx4 v[122:125], v[178:179], off offset:256
	v_lshlrev_b64 v[188:189], 10, v[172:173]
	v_lshl_add_u64 v[188:189], v[170:171], 0, v[188:189]
	s_lshl_b32 s28, s60, 2
	s_ashr_i32 s29, s28, 31
	s_lshl_b64 s[28:29], s[28:29], 2
	s_add_u32 s28, s49, s28
	s_addc_u32 s29, s50, s29
	s_waitcnt vmcnt(0)
	v_lshlrev_b32_e32 v196, 16, v204
	v_and_b32_e32 v197, 0xffff0000, v204
	v_lshlrev_b32_e32 v198, 16, v205
	v_and_b32_e32 v199, 0xffff0000, v205
	v_pk_add_f32 v[136:137], v[136:137], v[198:199]
	v_pk_add_f32 v[196:197], v[134:135], v[196:197]
	v_lshlrev_b32_e32 v134, 16, v206
	v_and_b32_e32 v135, 0xffff0000, v206
	v_lshlrev_b32_e32 v198, 16, v207
	v_and_b32_e32 v199, 0xffff0000, v207
	v_pk_add_f32 v[130:131], v[130:131], v[134:135]
	v_mul_f32_e32 v134, v197, v197
	v_mul_f32_e32 v135, v137, v137
	v_pk_add_f32 v[132:133], v[132:133], v[198:199]
	v_fmac_f32_e32 v134, v196, v196
	v_fmac_f32_e32 v135, v136, v136
	v_add_f32_e32 v134, v134, v135
	v_mul_f32_e32 v135, v131, v131
	v_mul_f32_e32 v195, v133, v133
	v_fmac_f32_e32 v135, v130, v130
	v_fmac_f32_e32 v195, v132, v132
	v_cvt_pk_bf16_f32 v204, v196, v197
	v_cvt_pk_bf16_f32 v205, v136, v137
	v_cvt_pk_bf16_f32 v206, v130, v131
	v_mul_f32_e32 v130, 0x41000000, v130
	v_mul_f32_e32 v131, 0x41000000, v131
	v_add_f32_e32 v135, v135, v195
	v_mul_f32_e32 v195, 0x41000000, v197
	v_med3_f32 v130, v130, s64, v250
	v_med3_f32 v131, v131, s64, v250
	v_cvt_pk_fp8_f32 v197, v130, v131
	v_add_f32_e32 v134, v134, v135
	v_mul_f32_e32 v135, 0x41000000, v196
	v_mul_f32_e32 v130, 0x41000000, v132
	v_mul_f32_e32 v131, 0x41000000, v133
	v_med3_f32 v135, v135, s64, v250
	v_med3_f32 v195, v195, s64, v250
	v_med3_f32 v130, v130, s64, v250
	v_med3_f32 v131, v131, s64, v250
	v_cvt_pk_bf16_f32 v207, v132, v133
	v_cvt_pk_fp8_f32 v196, v135, v195
	v_cvt_pk_fp8_f32 v197, v130, v131 op_sel:[0,0,1]
	v_lshlrev_b32_e32 v130, 16, v154
	v_and_b32_e32 v131, 0xffff0000, v154
	v_lshlrev_b32_e32 v132, 16, v155
	v_and_b32_e32 v133, 0xffff0000, v155
	v_pk_add_f32 v[120:121], v[120:121], v[132:133]
	v_pk_add_f32 v[118:119], v[118:119], v[130:131]
	v_lshlrev_b32_e32 v130, 16, v156
	v_and_b32_e32 v131, 0xffff0000, v156
	v_mul_f32_e32 v135, 0x41000000, v136
	v_mul_f32_e32 v136, 0x41000000, v137
	v_lshlrev_b32_e32 v132, 16, v157
	v_and_b32_e32 v133, 0xffff0000, v157
	v_pk_add_f32 v[130:131], v[114:115], v[130:131]
	v_mul_f32_e32 v114, v119, v119
	v_mul_f32_e32 v115, v121, v121
	v_med3_f32 v135, v135, s64, v250
	v_med3_f32 v136, v136, s64, v250
	v_pk_add_f32 v[132:133], v[116:117], v[132:133]
	v_fmac_f32_e32 v114, v118, v118
	v_fmac_f32_e32 v115, v120, v120
	v_cvt_pk_fp8_f32 v196, v135, v136 op_sel:[0,0,1]
	v_add_f32_e32 v114, v114, v115
	v_mul_f32_e32 v115, v131, v131
	v_mul_f32_e32 v116, v133, v133
	v_fmac_f32_e32 v115, v130, v130
	v_fmac_f32_e32 v116, v132, v132
	v_add_f32_e32 v115, v115, v116
	v_add_f32_e32 v114, v114, v115
	global_store_dwordx4 v[190:191], v[204:207], off
	global_store_dwordx2 v[188:189], v[196:197], off
	v_add_f32_e32 v134, v134, v114
	v_cvt_pk_bf16_f32 v114, v118, v119
	v_cvt_pk_bf16_f32 v115, v120, v121
	v_cvt_pk_bf16_f32 v116, v130, v131
	v_cvt_pk_bf16_f32 v117, v132, v133
	global_store_dwordx4 v[190:191], v[114:117], off offset:256
	s_nop 1
	v_mul_f32_e32 v114, 0x41000000, v118
	v_med3_f32 v115, v114, s64, v250
	v_mul_f32_e32 v114, 0x41000000, v119
	v_med3_f32 v116, v114, s64, v250
	v_cvt_pk_fp8_f32 v114, v115, v116
	v_mul_f32_e32 v115, 0x41000000, v120
	v_mul_f32_e32 v116, 0x41000000, v121
	v_med3_f32 v115, v115, s64, v250
	v_med3_f32 v116, v116, s64, v250
	v_cvt_pk_fp8_f32 v114, v115, v116 op_sel:[0,0,1]
	v_mul_f32_e32 v115, 0x41000000, v130
	v_med3_f32 v116, v115, s64, v250
	v_mul_f32_e32 v115, 0x41000000, v131
	v_med3_f32 v117, v115, s64, v250
	v_cvt_pk_fp8_f32 v115, v116, v117
	v_mul_f32_e32 v116, 0x41000000, v132
	v_mul_f32_e32 v117, 0x41000000, v133
	v_med3_f32 v116, v116, s64, v250
	v_med3_f32 v117, v117, s64, v250
	v_cvt_pk_fp8_f32 v115, v116, v117 op_sel:[0,0,1]
	global_store_dwordx2 v[188:189], v[114:115], off offset:128
	ds_swizzle_b32 v114, v134 offset:swizzle(SWAP,16)
	s_waitcnt lgkmcnt(0)
	v_add_f32_e32 v114, v134, v114
	v_mov_b32_e32 v115, v114
	s_nop 1
	v_permlane32_swap_b32_e32 v114, v115
	s_and_saveexec_b64 s[30:31], s[2:3]
	s_cbranch_execz .LBB0_1813
	v_lshlrev_b64 v[116:117], 6, v[172:173]
	v_lshl_add_u64 v[116:117], s[28:29], 0, v[116:117]
	v_add_f32_e32 v114, v114, v115
	global_store_dword v[116:117], v114, off
; __device__ __forceinline__ u32x4 pack8(const f32x4 a, const f32x4 b) { u32x4 w; w.x = cvt_pk_bf16(a[0], a[1]); w.y = cvt_pk_bf16(a[2], a[3]); w.z = cvt_pk_bf16(b[0], b[1]); w.w = cvt_pk_bf16(b[2], b[3]); return w; }
; __device__ __forceinline__ float sumsq4(const f32x4 v) { return (v[0] * v[0] + v[1] * v[1]) + (v[2] * v[2] + v[3] * v[3]); }
; __device__ __forceinline__ float xor16_add(float v) { return v + __int_as_float(__builtin_amdgcn_ds_swizzle(__float_as_int(v), 0x401F)); }
; __device__ __forceinline__ float xor32_add(float v) { auto rr = __builtin_amdgcn_permlane32_swap(__float_as_uint(v), __float_as_uint(v), false, false); return __uint_as_float(rr[0]) + __uint_as_float(rr[1]); }
; __device__ __forceinline__ f32x4 bf2f_lo(const u32x4 w, int h) { const unsigned a = h ? w.z : w.x, b = h ? w.w : w.y; return (f32x4){__uint_as_float(a << 16), __uint_as_float(a & 0xffff0000u), __uint_as_float(b << 16), __uint_as_float(b & 0xffff0000u)}; }
;     __device__ __forceinline__ void operator()(const f32x4 (&acc)[2][2][4][2], const Unit& u, int wr, int wc, int fr, int fq) const {
;     ...
;             for (int m = 0; m < 4; ++m) {
;                 const int row = row0 + ai * HALF + m * 16; float ss = 0.f;
; #pragma unroll
;                 for (int bj = 0; bj < 2; ++bj) {
;                     const f32x4 v0 = bf2f_lo(old[m][bj], 0) + acc[ai][bj][m][0], v1 = bf2f_lo(old[m][bj], 1) + acc[ai][bj][m][1];
;                     ss += sumsq4(v0) + sumsq4(v1);
;                     *(u32x4*)(xb + (size_t)row * DM + col0 + bj * HALF) = pack8(v0, v1);
;                     { u32x2 w8; w8.x = pack4_fp8_x8(v0); w8.y = pack4_fp8_x8(v1); *(u32x2*)(xq + (size_t)row * DM + col0 + bj * HALF) = w8; }
;                 }
;                 ss = xor32_add(xor16_add(ss));
;                 if (fq == 0) ssx[(size_t)row * 16 + u.pn * 4 + wc] = ss;
.LBB0_1813:
	s_or_b64 exec, exec, s[30:31]
	v_lshlrev_b32_e32 v116, 16, v150
	v_and_b32_e32 v117, 0xffff0000, v150
	v_lshlrev_b32_e32 v118, 16, v151
	v_and_b32_e32 v119, 0xffff0000, v151
	v_pk_add_f32 v[112:113], v[112:113], v[118:119]
	v_pk_add_f32 v[110:111], v[110:111], v[116:117]
	v_lshlrev_b32_e32 v116, 16, v152
	v_and_b32_e32 v117, 0xffff0000, v152
	v_lshlrev_b32_e32 v118, 16, v153
	v_and_b32_e32 v119, 0xffff0000, v153
	v_pk_add_f32 v[118:119], v[108:109], v[118:119]
	v_pk_add_f32 v[108:109], v[106:107], v[116:117]
	v_mul_f32_e32 v106, v111, v111
	v_mul_f32_e32 v107, v113, v113
	v_fmac_f32_e32 v106, v110, v110
	v_fmac_f32_e32 v107, v112, v112
	v_add_f32_e32 v106, v106, v107
	v_mul_f32_e32 v107, v109, v109
	v_mul_f32_e32 v116, v119, v119
	v_fmac_f32_e32 v107, v108, v108
	v_fmac_f32_e32 v116, v118, v118
	v_add_f32_e32 v107, v107, v116
	v_add_f32_e32 v116, v106, v107
	v_cvt_pk_bf16_f32 v106, v110, v111
	v_mul_f32_e32 v110, 0x41000000, v110
	v_med3_f32 v117, v110, s64, v250
	v_mul_f32_e32 v110, 0x41000000, v111
	v_med3_f32 v111, v110, s64, v250
	v_cvt_pk_fp8_f32 v110, v117, v111
	v_cvt_pk_bf16_f32 v107, v112, v113
	v_mul_f32_e32 v111, 0x41000000, v112
	v_mul_f32_e32 v112, 0x41000000, v113
	v_med3_f32 v111, v111, s64, v250
	v_med3_f32 v112, v112, s64, v250
	v_cvt_pk_fp8_f32 v110, v111, v112 op_sel:[0,0,1]
	v_mul_f32_e32 v111, 0x41000000, v108
	v_med3_f32 v112, v111, s64, v250
	v_mul_f32_e32 v111, 0x41000000, v109
	v_med3_f32 v113, v111, s64, v250
	v_cvt_pk_fp8_f32 v111, v112, v113
	v_mul_f32_e32 v112, 0x41000000, v118
	v_mul_f32_e32 v113, 0x41000000, v119
	v_med3_f32 v112, v112, s64, v250
	v_med3_f32 v113, v113, s64, v250
	v_cvt_pk_fp8_f32 v111, v112, v113 op_sel:[0,0,1]
	v_lshlrev_b64 v[114:115], 10, v[184:185]
	v_cvt_pk_bf16_f32 v108, v108, v109
	v_cvt_pk_bf16_f32 v109, v118, v119
	v_lshl_add_u64 v[114:115], v[170:171], 0, v[114:115]
	global_store_dwordx4 v[186:187], v[106:109], off
	global_store_dwordx2 v[114:115], v[110:111], off
	s_nop 0
	v_lshlrev_b32_e32 v106, 16, v146
	v_and_b32_e32 v107, 0xffff0000, v146
	v_lshlrev_b32_e32 v108, 16, v147
	v_and_b32_e32 v109, 0xffff0000, v147
	v_pk_add_f32 v[104:105], v[104:105], v[108:109]
	v_pk_add_f32 v[102:103], v[102:103], v[106:107]
	v_lshlrev_b32_e32 v106, 16, v148
	v_and_b32_e32 v107, 0xffff0000, v148
	v_lshlrev_b32_e32 v108, 16, v149
	v_and_b32_e32 v109, 0xffff0000, v149
	v_pk_add_f32 v[108:109], v[100:101], v[108:109]
	v_pk_add_f32 v[100:101], v[98:99], v[106:107]
	v_mul_f32_e32 v98, v103, v103
	v_mul_f32_e32 v99, v105, v105
	v_fmac_f32_e32 v98, v102, v102
	v_fmac_f32_e32 v99, v104, v104
	v_add_f32_e32 v98, v98, v99
	v_mul_f32_e32 v99, v101, v101
	v_mul_f32_e32 v106, v109, v109
	v_fmac_f32_e32 v99, v100, v100
	v_fmac_f32_e32 v106, v108, v108
	v_add_f32_e32 v99, v99, v106
	v_add_f32_e32 v98, v98, v99
	v_add_f32_e32 v106, v116, v98
	v_cvt_pk_bf16_f32 v98, v102, v103
	v_mul_f32_e32 v102, 0x41000000, v102
	v_med3_f32 v107, v102, s64, v250
	v_mul_f32_e32 v102, 0x41000000, v103
	v_med3_f32 v103, v102, s64, v250
	v_cvt_pk_fp8_f32 v102, v107, v103
	v_cvt_pk_bf16_f32 v99, v104, v105
	v_mul_f32_e32 v103, 0x41000000, v104
	v_mul_f32_e32 v104, 0x41000000, v105
	v_med3_f32 v103, v103, s64, v250
	v_med3_f32 v104, v104, s64, v250
	v_cvt_pk_fp8_f32 v102, v103, v104 op_sel:[0,0,1]
	v_mul_f32_e32 v103, 0x41000000, v100
	v_med3_f32 v104, v103, s64, v250
	v_mul_f32_e32 v103, 0x41000000, v101
	v_med3_f32 v105, v103, s64, v250
	v_cvt_pk_fp8_f32 v103, v104, v105
	v_mul_f32_e32 v104, 0x41000000, v108
	v_mul_f32_e32 v105, 0x41000000, v109
	v_med3_f32 v104, v104, s64, v250
	v_med3_f32 v105, v105, s64, v250
	v_cvt_pk_fp8_f32 v103, v104, v105 op_sel:[0,0,1]
	ds_swizzle_b32 v104, v106 offset:swizzle(SWAP,16)
	v_cvt_pk_bf16_f32 v100, v100, v101
	v_cvt_pk_bf16_f32 v101, v108, v109
	global_store_dwordx4 v[186:187], v[98:101], off offset:256
	global_store_dwordx2 v[114:115], v[102:103], off offset:128
	s_waitcnt lgkmcnt(0)
	v_add_f32_e32 v98, v106, v104
	v_mov_b32_e32 v99, v98
	s_nop 1
	v_permlane32_swap_b32_e32 v98, v99
	s_and_saveexec_b64 s[30:31], s[2:3]
	s_cbranch_execz .LBB0_1815
	v_lshlrev_b64 v[100:101], 6, v[184:185]
	v_lshl_add_u64 v[100:101], s[28:29], 0, v[100:101]
	v_add_f32_e32 v98, v98, v99
	global_store_dword v[100:101], v98, off
; __device__ __forceinline__ u32x4 pack8(const f32x4 a, const f32x4 b) { u32x4 w; w.x = cvt_pk_bf16(a[0], a[1]); w.y = cvt_pk_bf16(a[2], a[3]); w.z = cvt_pk_bf16(b[0], b[1]); w.w = cvt_pk_bf16(b[2], b[3]); return w; }
; __device__ __forceinline__ float sumsq4(const f32x4 v) { return (v[0] * v[0] + v[1] * v[1]) + (v[2] * v[2] + v[3] * v[3]); }
; __device__ __forceinline__ float xor16_add(float v) { return v + __int_as_float(__builtin_amdgcn_ds_swizzle(__float_as_int(v), 0x401F)); }
; __device__ __forceinline__ float xor32_add(float v) { auto rr = __builtin_amdgcn_permlane32_swap(__float_as_uint(v), __float_as_uint(v), false, false); return __uint_as_float(rr[0]) + __uint_as_float(rr[1]); }
; __device__ __forceinline__ f32x4 bf2f_lo(const u32x4 w, int h) { const unsigned a = h ? w.z : w.x, b = h ? w.w : w.y; return (f32x4){__uint_as_float(a << 16), __uint_as_float(a & 0xffff0000u), __uint_as_float(b << 16), __uint_as_float(b & 0xffff0000u)}; }
;     __device__ __forceinline__ void operator()(const f32x4 (&acc)[2][2][4][2], const Unit& u, int wr, int wc, int fr, int fq) const {
;     ...
;             for (int m = 0; m < 4; ++m) {
;                 const int row = row0 + ai * HALF + m * 16; float ss = 0.f;
; #pragma unroll
;                 for (int bj = 0; bj < 2; ++bj) {
;                     const f32x4 v0 = bf2f_lo(old[m][bj], 0) + acc[ai][bj][m][0], v1 = bf2f_lo(old[m][bj], 1) + acc[ai][bj][m][1];
;                     ss += sumsq4(v0) + sumsq4(v1);
;                     *(u32x4*)(xb + (size_t)row * DM + col0 + bj * HALF) = pack8(v0, v1);
;                     { u32x2 w8; w8.x = pack4_fp8_x8(v0); w8.y = pack4_fp8_x8(v1); *(u32x2*)(xq + (size_t)row * DM + col0 + bj * HALF) = w8; }
;                 }
;                 ss = xor32_add(xor16_add(ss));
;                 if (fq == 0) ssx[(size_t)row * 16 + u.pn * 4 + wc] = ss;
.LBB0_1815:
	s_or_b64 exec, exec, s[30:31]
	v_lshlrev_b32_e32 v100, 16, v142
	v_and_b32_e32 v101, 0xffff0000, v142
	v_lshlrev_b32_e32 v102, 16, v143
	v_and_b32_e32 v103, 0xffff0000, v143
	v_pk_add_f32 v[96:97], v[96:97], v[102:103]
	v_pk_add_f32 v[94:95], v[94:95], v[100:101]
	v_lshlrev_b32_e32 v100, 16, v144
	v_and_b32_e32 v101, 0xffff0000, v144
	v_lshlrev_b32_e32 v102, 16, v145
	v_and_b32_e32 v103, 0xffff0000, v145
	v_pk_add_f32 v[102:103], v[92:93], v[102:103]
	v_pk_add_f32 v[92:93], v[90:91], v[100:101]
	v_mul_f32_e32 v90, v95, v95
	v_mul_f32_e32 v91, v97, v97
	v_fmac_f32_e32 v90, v94, v94
	v_fmac_f32_e32 v91, v96, v96
	v_add_f32_e32 v90, v90, v91
	v_mul_f32_e32 v91, v93, v93
	v_mul_f32_e32 v100, v103, v103
	v_fmac_f32_e32 v91, v92, v92
	v_fmac_f32_e32 v100, v102, v102
	v_add_f32_e32 v91, v91, v100
	v_add_f32_e32 v100, v90, v91
	v_cvt_pk_bf16_f32 v90, v94, v95
	v_mul_f32_e32 v94, 0x41000000, v94
	v_med3_f32 v101, v94, s64, v250
	v_mul_f32_e32 v94, 0x41000000, v95
	v_med3_f32 v95, v94, s64, v250
	v_cvt_pk_fp8_f32 v94, v101, v95
	v_cvt_pk_bf16_f32 v91, v96, v97
	v_mul_f32_e32 v95, 0x41000000, v96
	v_mul_f32_e32 v96, 0x41000000, v97
	v_med3_f32 v95, v95, s64, v250
	v_med3_f32 v96, v96, s64, v250
	v_cvt_pk_fp8_f32 v94, v95, v96 op_sel:[0,0,1]
	v_mul_f32_e32 v95, 0x41000000, v92
	v_med3_f32 v96, v95, s64, v250
	v_mul_f32_e32 v95, 0x41000000, v93
	v_med3_f32 v97, v95, s64, v250
	v_cvt_pk_fp8_f32 v95, v96, v97
	v_mul_f32_e32 v96, 0x41000000, v102
	v_mul_f32_e32 v97, 0x41000000, v103
	v_med3_f32 v96, v96, s64, v250
	v_med3_f32 v97, v97, s64, v250
	v_cvt_pk_fp8_f32 v95, v96, v97 op_sel:[0,0,1]
	v_lshlrev_b64 v[98:99], 10, v[180:181]
	v_cvt_pk_bf16_f32 v92, v92, v93
	v_cvt_pk_bf16_f32 v93, v102, v103
	v_lshl_add_u64 v[98:99], v[170:171], 0, v[98:99]
	global_store_dwordx4 v[182:183], v[90:93], off
	global_store_dwordx2 v[98:99], v[94:95], off
	s_nop 0
	v_lshlrev_b32_e32 v90, 16, v138
	v_and_b32_e32 v91, 0xffff0000, v138
	v_lshlrev_b32_e32 v92, 16, v139
	v_and_b32_e32 v93, 0xffff0000, v139
	v_pk_add_f32 v[88:89], v[88:89], v[92:93]
	v_pk_add_f32 v[86:87], v[86:87], v[90:91]
	v_lshlrev_b32_e32 v90, 16, v140
	v_and_b32_e32 v91, 0xffff0000, v140
	v_lshlrev_b32_e32 v92, 16, v141
	v_and_b32_e32 v93, 0xffff0000, v141
	v_pk_add_f32 v[92:93], v[84:85], v[92:93]
	v_pk_add_f32 v[84:85], v[82:83], v[90:91]
	v_mul_f32_e32 v82, v87, v87
	v_mul_f32_e32 v83, v89, v89
	v_fmac_f32_e32 v82, v86, v86
	v_fmac_f32_e32 v83, v88, v88
	v_add_f32_e32 v82, v82, v83
	v_mul_f32_e32 v83, v85, v85
	v_mul_f32_e32 v90, v93, v93
	v_fmac_f32_e32 v83, v84, v84
	v_fmac_f32_e32 v90, v92, v92
	v_add_f32_e32 v83, v83, v90
	v_add_f32_e32 v82, v82, v83
	v_add_f32_e32 v90, v100, v82
	v_cvt_pk_bf16_f32 v82, v86, v87
	v_mul_f32_e32 v86, 0x41000000, v86
	v_med3_f32 v91, v86, s64, v250
	v_mul_f32_e32 v86, 0x41000000, v87
	v_med3_f32 v87, v86, s64, v250
	v_cvt_pk_fp8_f32 v86, v91, v87
	v_cvt_pk_bf16_f32 v83, v88, v89
	v_mul_f32_e32 v87, 0x41000000, v88
	v_mul_f32_e32 v88, 0x41000000, v89
	v_med3_f32 v87, v87, s64, v250
	v_med3_f32 v88, v88, s64, v250
	v_cvt_pk_fp8_f32 v86, v87, v88 op_sel:[0,0,1]
	v_mul_f32_e32 v87, 0x41000000, v84
	v_med3_f32 v88, v87, s64, v250
	v_mul_f32_e32 v87, 0x41000000, v85
	v_med3_f32 v89, v87, s64, v250
	v_cvt_pk_fp8_f32 v87, v88, v89
	v_mul_f32_e32 v88, 0x41000000, v92
	v_mul_f32_e32 v89, 0x41000000, v93
	v_med3_f32 v88, v88, s64, v250
	v_med3_f32 v89, v89, s64, v250
	v_cvt_pk_fp8_f32 v87, v88, v89 op_sel:[0,0,1]
	ds_swizzle_b32 v88, v90 offset:swizzle(SWAP,16)
	v_cvt_pk_bf16_f32 v84, v84, v85
	v_cvt_pk_bf16_f32 v85, v92, v93
	global_store_dwordx4 v[182:183], v[82:85], off offset:256
	global_store_dwordx2 v[98:99], v[86:87], off offset:128
	s_waitcnt lgkmcnt(0)
	v_add_f32_e32 v82, v90, v88
	v_mov_b32_e32 v83, v82
	s_nop 1
	v_permlane32_swap_b32_e32 v82, v83
	s_and_saveexec_b64 s[30:31], s[2:3]
	s_cbranch_execz .LBB0_1817
	v_lshlrev_b64 v[84:85], 6, v[180:181]
	v_lshl_add_u64 v[84:85], s[28:29], 0, v[84:85]
	v_add_f32_e32 v82, v82, v83
	global_store_dword v[84:85], v82, off
.LBB0_1817:
	s_or_b64 exec, exec, s[30:31]
	v_lshlrev_b32_e32 v84, 16, v126
	v_and_b32_e32 v85, 0xffff0000, v126
	v_lshlrev_b32_e32 v86, 16, v127
	v_and_b32_e32 v87, 0xffff0000, v127
	v_pk_add_f32 v[80:81], v[80:81], v[86:87]
	v_pk_add_f32 v[78:79], v[78:79], v[84:85]
	v_lshlrev_b32_e32 v84, 16, v128
	v_and_b32_e32 v85, 0xffff0000, v128
	v_lshlrev_b32_e32 v86, 16, v129
	v_and_b32_e32 v87, 0xffff0000, v129
	v_pk_add_f32 v[86:87], v[76:77], v[86:87]
	v_pk_add_f32 v[76:77], v[74:75], v[84:85]
	v_mul_f32_e32 v74, v79, v79
	v_mul_f32_e32 v75, v81, v81
	v_fmac_f32_e32 v74, v78, v78
	v_fmac_f32_e32 v75, v80, v80
	v_add_f32_e32 v74, v74, v75
	v_mul_f32_e32 v75, v77, v77
	v_mul_f32_e32 v84, v87, v87
	v_fmac_f32_e32 v75, v76, v76
	v_fmac_f32_e32 v84, v86, v86
	v_add_f32_e32 v75, v75, v84
	v_add_f32_e32 v84, v74, v75
	v_cvt_pk_bf16_f32 v74, v78, v79
	v_mul_f32_e32 v78, 0x41000000, v78
	v_med3_f32 v85, v78, s64, v250
	v_mul_f32_e32 v78, 0x41000000, v79
	v_med3_f32 v79, v78, s64, v250
	v_cvt_pk_fp8_f32 v78, v85, v79
	v_cvt_pk_bf16_f32 v75, v80, v81
	v_mul_f32_e32 v79, 0x41000000, v80
	v_mul_f32_e32 v80, 0x41000000, v81
	v_med3_f32 v79, v79, s64, v250
	v_med3_f32 v80, v80, s64, v250
	v_cvt_pk_fp8_f32 v78, v79, v80 op_sel:[0,0,1]
	v_mul_f32_e32 v79, 0x41000000, v76
	v_med3_f32 v80, v79, s64, v250
	v_mul_f32_e32 v79, 0x41000000, v77
	v_med3_f32 v81, v79, s64, v250
	v_cvt_pk_fp8_f32 v79, v80, v81
	v_mul_f32_e32 v80, 0x41000000, v86
	v_mul_f32_e32 v81, 0x41000000, v87
	v_med3_f32 v80, v80, s64, v250
	v_med3_f32 v81, v81, s64, v250
	v_cvt_pk_fp8_f32 v79, v80, v81 op_sel:[0,0,1]
	v_lshlrev_b64 v[82:83], 10, v[176:177]
; __device__ __forceinline__ u32x4 pack8(const f32x4 a, const f32x4 b) { u32x4 w; w.x = cvt_pk_bf16(a[0], a[1]); w.y = cvt_pk_bf16(a[2], a[3]); w.z = cvt_pk_bf16(b[0], b[1]); w.w = cvt_pk_bf16(b[2], b[3]); return w; }
; __device__ __forceinline__ float sumsq4(const f32x4 v) { return (v[0] * v[0] + v[1] * v[1]) + (v[2] * v[2] + v[3] * v[3]); }
; __device__ __forceinline__ float xor16_add(float v) { return v + __int_as_float(__builtin_amdgcn_ds_swizzle(__float_as_int(v), 0x401F)); }
; __device__ __forceinline__ float xor32_add(float v) { auto rr = __builtin_amdgcn_permlane32_swap(__float_as_uint(v), __float_as_uint(v), false, false); return __uint_as_float(rr[0]) + __uint_as_float(rr[1]); }
; __device__ __forceinline__ f32x4 bf2f_lo(const u32x4 w, int h) { const unsigned a = h ? w.z : w.x, b = h ? w.w : w.y; return (f32x4){__uint_as_float(a << 16), __uint_as_float(a & 0xffff0000u), __uint_as_float(b << 16), __uint_as_float(b & 0xffff0000u)}; }
;     __device__ __forceinline__ void operator()(const f32x4 (&acc)[2][2][4][2], const Unit& u, int wr, int wc, int fr, int fq) const {
;     ...
;             for (int m = 0; m < 4; ++m) {
;                 const int row = row0 + ai * HALF + m * 16; float ss = 0.f;
; #pragma unroll
;                 for (int bj = 0; bj < 2; ++bj) {
;                     const f32x4 v0 = bf2f_lo(old[m][bj], 0) + acc[ai][bj][m][0], v1 = bf2f_lo(old[m][bj], 1) + acc[ai][bj][m][1];
;                     ss += sumsq4(v0) + sumsq4(v1);
;                     *(u32x4*)(xb + (size_t)row * DM + col0 + bj * HALF) = pack8(v0, v1);
;                     { u32x2 w8; w8.x = pack4_fp8_x8(v0); w8.y = pack4_fp8_x8(v1); *(u32x2*)(xq + (size_t)row * DM + col0 + bj * HALF) = w8; }
;                 }
;                 ss = xor32_add(xor16_add(ss));
;                 if (fq == 0) ssx[(size_t)row * 16 + u.pn * 4 + wc] = ss;
	v_cvt_pk_bf16_f32 v76, v76, v77
	v_cvt_pk_bf16_f32 v77, v86, v87
	v_lshl_add_u64 v[82:83], v[170:171], 0, v[82:83]
	global_store_dwordx4 v[178:179], v[74:77], off
	global_store_dwordx2 v[82:83], v[78:79], off
	s_nop 0
	v_lshlrev_b32_e32 v74, 16, v122
	v_and_b32_e32 v75, 0xffff0000, v122
	v_lshlrev_b32_e32 v76, 16, v123
	v_and_b32_e32 v77, 0xffff0000, v123
	v_pk_add_f32 v[72:73], v[72:73], v[76:77]
	v_pk_add_f32 v[70:71], v[70:71], v[74:75]
	v_lshlrev_b32_e32 v74, 16, v124
	v_and_b32_e32 v75, 0xffff0000, v124
	v_lshlrev_b32_e32 v76, 16, v125
	v_and_b32_e32 v77, 0xffff0000, v125
	v_pk_add_f32 v[76:77], v[68:69], v[76:77]
	v_pk_add_f32 v[68:69], v[66:67], v[74:75]
	v_mul_f32_e32 v66, v71, v71
	v_mul_f32_e32 v67, v73, v73
	v_fmac_f32_e32 v66, v70, v70
	v_fmac_f32_e32 v67, v72, v72
	v_add_f32_e32 v66, v66, v67
	v_mul_f32_e32 v67, v69, v69
	v_mul_f32_e32 v74, v77, v77
	v_fmac_f32_e32 v67, v68, v68
	v_fmac_f32_e32 v74, v76, v76
	v_add_f32_e32 v67, v67, v74
	v_add_f32_e32 v66, v66, v67
	v_add_f32_e32 v74, v84, v66
	v_cvt_pk_bf16_f32 v66, v70, v71
	v_mul_f32_e32 v70, 0x41000000, v70
	v_med3_f32 v75, v70, s64, v250
	v_mul_f32_e32 v70, 0x41000000, v71
	v_med3_f32 v71, v70, s64, v250
	v_cvt_pk_fp8_f32 v70, v75, v71
	v_cvt_pk_bf16_f32 v67, v72, v73
	v_mul_f32_e32 v71, 0x41000000, v72
	v_mul_f32_e32 v72, 0x41000000, v73
	v_med3_f32 v71, v71, s64, v250
	v_med3_f32 v72, v72, s64, v250
	v_cvt_pk_fp8_f32 v70, v71, v72 op_sel:[0,0,1]
	v_mul_f32_e32 v71, 0x41000000, v68
	v_med3_f32 v72, v71, s64, v250
	v_mul_f32_e32 v71, 0x41000000, v69
	v_med3_f32 v73, v71, s64, v250
	v_cvt_pk_fp8_f32 v71, v72, v73
	v_mul_f32_e32 v72, 0x41000000, v76
	v_mul_f32_e32 v73, 0x41000000, v77
	v_med3_f32 v72, v72, s64, v250
	v_med3_f32 v73, v73, s64, v250
	v_cvt_pk_fp8_f32 v71, v72, v73 op_sel:[0,0,1]
	ds_swizzle_b32 v72, v74 offset:swizzle(SWAP,16)
	v_cvt_pk_bf16_f32 v68, v68, v69
	v_cvt_pk_bf16_f32 v69, v76, v77
	global_store_dwordx4 v[178:179], v[66:69], off offset:256
	global_store_dwordx2 v[82:83], v[70:71], off offset:128
	s_waitcnt lgkmcnt(0)
	v_add_f32_e32 v66, v74, v72
	v_mov_b32_e32 v67, v66
	s_nop 1
	v_permlane32_swap_b32_e32 v66, v67
	s_and_saveexec_b64 s[30:31], s[2:3]
	s_cbranch_execz .LBB0_1819
	v_lshlrev_b64 v[68:69], 6, v[176:177]
	v_lshl_add_u64 v[68:69], s[28:29], 0, v[68:69]
	v_add_f32_e32 v66, v66, v67
	global_store_dword v[68:69], v66, off
.LBB0_1819:
	s_or_b64 exec, exec, s[30:31]
	v_add_u32_e32 v106, 0x80, v172
	v_ashrrev_i32_e32 v107, 31, v106
	v_lshlrev_b64 v[66:67], 11, v[106:107]
	v_lshl_add_u64 v[108:109], v[174:175], 0, v[66:67]
	global_load_dwordx4 v[112:115], v[108:109], off
	global_load_dwordx4 v[90:93], v[108:109], off offset:256
	v_add_u32_e32 v102, 0x90, v172
	v_ashrrev_i32_e32 v103, 31, v102
	v_add_u32_e32 v98, 0xa0, v172
	v_lshlrev_b64 v[66:67], 11, v[102:103]
	v_ashrrev_i32_e32 v99, 31, v98
	v_add_u32_e32 v94, 0xb0, v172
	v_lshl_add_u64 v[104:105], v[174:175], 0, v[66:67]
	v_lshlrev_b64 v[66:67], 11, v[98:99]
	v_ashrrev_i32_e32 v95, 31, v94
	v_lshl_add_u64 v[100:101], v[174:175], 0, v[66:67]
	v_lshlrev_b64 v[66:67], 11, v[94:95]
	v_lshl_add_u64 v[96:97], v[174:175], 0, v[66:67]
	global_load_dwordx4 v[86:89], v[104:105], off
	global_load_dwordx4 v[82:85], v[104:105], off offset:256
	global_load_dwordx4 v[78:81], v[100:101], off
	global_load_dwordx4 v[74:77], v[100:101], off offset:256
	global_load_dwordx4 v[70:73], v[96:97], off
	global_load_dwordx4 v[66:69], v[96:97], off offset:256
	v_lshlrev_b64 v[110:111], 10, v[106:107]
	v_lshl_add_u64 v[110:111], v[170:171], 0, v[110:111]
	s_waitcnt vmcnt(7)
	v_lshlrev_b32_e32 v116, 16, v112
	v_and_b32_e32 v117, 0xffff0000, v112
	v_lshlrev_b32_e32 v112, 16, v113
	v_and_b32_e32 v113, 0xffff0000, v113
	v_pk_add_f32 v[112:113], v[64:65], v[112:113]
	v_pk_add_f32 v[116:117], v[62:63], v[116:117]
	v_lshlrev_b32_e32 v62, 16, v114
	v_and_b32_e32 v63, 0xffff0000, v114
	v_lshlrev_b32_e32 v64, 16, v115
	v_and_b32_e32 v65, 0xffff0000, v115
	v_pk_add_f32 v[114:115], v[58:59], v[62:63]
	v_mul_f32_e32 v58, v117, v117
	v_mul_f32_e32 v59, v113, v113
	v_pk_add_f32 v[60:61], v[60:61], v[64:65]
	v_fmac_f32_e32 v58, v116, v116
	v_fmac_f32_e32 v59, v112, v112
	v_add_f32_e32 v58, v58, v59
	v_mul_f32_e32 v59, v115, v115
	v_mul_f32_e32 v62, v61, v61
	v_fmac_f32_e32 v59, v114, v114
	v_fmac_f32_e32 v62, v60, v60
	v_add_f32_e32 v59, v59, v62
	v_cvt_pk_bf16_f32 v62, v116, v117
	v_add_f32_e32 v58, v58, v59
	v_cvt_pk_bf16_f32 v63, v112, v113
	v_cvt_pk_bf16_f32 v64, v114, v115
	v_cvt_pk_bf16_f32 v65, v60, v61
	global_store_dwordx4 v[108:109], v[62:65], off
	v_mul_f32_e32 v59, 0x41000000, v116
	v_med3_f32 v59, v59, s64, v250
	v_mul_f32_e32 v62, 0x41000000, v117
	v_med3_f32 v63, v62, s64, v250
	v_cvt_pk_fp8_f32 v62, v59, v63
	v_mul_f32_e32 v59, 0x41000000, v112
	v_mul_f32_e32 v63, 0x41000000, v113
	v_med3_f32 v59, v59, s64, v250
	v_med3_f32 v63, v63, s64, v250
	v_cvt_pk_fp8_f32 v62, v59, v63 op_sel:[0,0,1]
	v_mul_f32_e32 v59, 0x41000000, v114
	v_mul_f32_e32 v63, 0x41000000, v115
	v_med3_f32 v59, v59, s64, v250
	v_med3_f32 v64, v63, s64, v250
	v_cvt_pk_fp8_f32 v63, v59, v64
	v_mul_f32_e32 v59, 0x41000000, v60
	v_mul_f32_e32 v60, 0x41000000, v61
	v_med3_f32 v59, v59, s64, v250
	v_med3_f32 v60, v60, s64, v250
	v_cvt_pk_fp8_f32 v63, v59, v60 op_sel:[0,0,1]
	s_waitcnt vmcnt(7)
; __device__ __forceinline__ u32x4 pack8(const f32x4 a, const f32x4 b) { u32x4 w; w.x = cvt_pk_bf16(a[0], a[1]); w.y = cvt_pk_bf16(a[2], a[3]); w.z = cvt_pk_bf16(b[0], b[1]); w.w = cvt_pk_bf16(b[2], b[3]); return w; }
; __device__ __forceinline__ float sumsq4(const f32x4 v) { return (v[0] * v[0] + v[1] * v[1]) + (v[2] * v[2] + v[3] * v[3]); }
; __device__ __forceinline__ float xor16_add(float v) { return v + __int_as_float(__builtin_amdgcn_ds_swizzle(__float_as_int(v), 0x401F)); }
; __device__ __forceinline__ float xor32_add(float v) { auto rr = __builtin_amdgcn_permlane32_swap(__float_as_uint(v), __float_as_uint(v), false, false); return __uint_as_float(rr[0]) + __uint_as_float(rr[1]); }
; __device__ __forceinline__ f32x4 bf2f_lo(const u32x4 w, int h) { const unsigned a = h ? w.z : w.x, b = h ? w.w : w.y; return (f32x4){__uint_as_float(a << 16), __uint_as_float(a & 0xffff0000u), __uint_as_float(b << 16), __uint_as_float(b & 0xffff0000u)}; }
;     __device__ __forceinline__ void operator()(const f32x4 (&acc)[2][2][4][2], const Unit& u, int wr, int wc, int fr, int fq) const {
;     ...
;             for (int m = 0; m < 4; ++m) {
;                 const int row = row0 + ai * HALF + m * 16; float ss = 0.f;
; #pragma unroll
;                 for (int bj = 0; bj < 2; ++bj) {
;                     const f32x4 v0 = bf2f_lo(old[m][bj], 0) + acc[ai][bj][m][0], v1 = bf2f_lo(old[m][bj], 1) + acc[ai][bj][m][1];
;                     ss += sumsq4(v0) + sumsq4(v1);
;                     *(u32x4*)(xb + (size_t)row * DM + col0 + bj * HALF) = pack8(v0, v1);
;                     { u32x2 w8; w8.x = pack4_fp8_x8(v0); w8.y = pack4_fp8_x8(v1); *(u32x2*)(xq + (size_t)row * DM + col0 + bj * HALF) = w8; }
;                 }
;                 ss = xor32_add(xor16_add(ss));
;                 if (fq == 0) ssx[(size_t)row * 16 + u.pn * 4 + wc] = ss;
	v_lshlrev_b32_e32 v60, 16, v90
	v_and_b32_e32 v61, 0xffff0000, v90
	v_pk_add_f32 v[54:55], v[54:55], v[60:61]
	global_store_dwordx2 v[110:111], v[62:63], off
	v_lshlrev_b32_e32 v62, 16, v91
	v_and_b32_e32 v63, 0xffff0000, v91
	v_pk_add_f32 v[56:57], v[56:57], v[62:63]
	v_lshlrev_b32_e32 v60, 16, v92
	v_and_b32_e32 v61, 0xffff0000, v92
	v_lshlrev_b32_e32 v62, 16, v93
	v_and_b32_e32 v63, 0xffff0000, v93
	v_pk_add_f32 v[60:61], v[50:51], v[60:61]
	v_mul_f32_e32 v50, v55, v55
	v_mul_f32_e32 v51, v57, v57
	v_pk_add_f32 v[62:63], v[52:53], v[62:63]
	v_fmac_f32_e32 v50, v54, v54
	v_fmac_f32_e32 v51, v56, v56
	v_add_f32_e32 v50, v50, v51
	v_mul_f32_e32 v51, v61, v61
	v_mul_f32_e32 v52, v63, v63
	v_fmac_f32_e32 v51, v60, v60
	v_fmac_f32_e32 v52, v62, v62
	v_add_f32_e32 v51, v51, v52
	v_add_f32_e32 v50, v50, v51
	v_add_f32_e32 v58, v58, v50
	v_cvt_pk_bf16_f32 v50, v54, v55
	v_cvt_pk_bf16_f32 v51, v56, v57
	v_cvt_pk_bf16_f32 v52, v60, v61
	v_cvt_pk_bf16_f32 v53, v62, v63
	global_store_dwordx4 v[108:109], v[50:53], off offset:256
	s_nop 1
	v_mul_f32_e32 v50, 0x41000000, v54
	v_med3_f32 v51, v50, s64, v250
	v_mul_f32_e32 v50, 0x41000000, v55
	v_med3_f32 v52, v50, s64, v250
	v_cvt_pk_fp8_f32 v50, v51, v52
	v_mul_f32_e32 v51, 0x41000000, v56
	v_mul_f32_e32 v52, 0x41000000, v57
	v_med3_f32 v51, v51, s64, v250
	v_med3_f32 v52, v52, s64, v250
	v_cvt_pk_fp8_f32 v50, v51, v52 op_sel:[0,0,1]
	v_mul_f32_e32 v51, 0x41000000, v60
	v_med3_f32 v52, v51, s64, v250
	v_mul_f32_e32 v51, 0x41000000, v61
	v_med3_f32 v53, v51, s64, v250
	v_cvt_pk_fp8_f32 v51, v52, v53
	v_mul_f32_e32 v52, 0x41000000, v62
	v_mul_f32_e32 v53, 0x41000000, v63
	v_med3_f32 v52, v52, s64, v250
	v_med3_f32 v53, v53, s64, v250
	v_cvt_pk_fp8_f32 v51, v52, v53 op_sel:[0,0,1]
	global_store_dwordx2 v[110:111], v[50:51], off offset:128
	ds_swizzle_b32 v50, v58 offset:swizzle(SWAP,16)
	s_waitcnt lgkmcnt(0)
	v_add_f32_e32 v50, v58, v50
	v_mov_b32_e32 v51, v50
	s_nop 1
	v_permlane32_swap_b32_e32 v50, v51
	s_and_saveexec_b64 s[30:31], s[2:3]
	s_cbranch_execz .LBB0_1821
	v_lshlrev_b64 v[52:53], 6, v[106:107]
	v_lshl_add_u64 v[52:53], s[28:29], 0, v[52:53]
	v_add_f32_e32 v50, v50, v51
	global_store_dword v[52:53], v50, off
.LBB0_1821:
	s_or_b64 exec, exec, s[30:31]
	s_waitcnt vmcnt(9)
	v_lshlrev_b32_e32 v52, 16, v86
	v_and_b32_e32 v53, 0xffff0000, v86
	v_lshlrev_b32_e32 v54, 16, v87
	v_and_b32_e32 v55, 0xffff0000, v87
	v_pk_add_f32 v[48:49], v[48:49], v[54:55]
	v_pk_add_f32 v[46:47], v[46:47], v[52:53]
	v_lshlrev_b32_e32 v52, 16, v88
	v_and_b32_e32 v53, 0xffff0000, v88
	v_lshlrev_b32_e32 v54, 16, v89
	v_and_b32_e32 v55, 0xffff0000, v89
	v_pk_add_f32 v[54:55], v[44:45], v[54:55]
	v_pk_add_f32 v[44:45], v[42:43], v[52:53]
	v_mul_f32_e32 v42, v47, v47
	v_mul_f32_e32 v43, v49, v49
	v_fmac_f32_e32 v42, v46, v46
	v_fmac_f32_e32 v43, v48, v48
	v_add_f32_e32 v42, v42, v43
	v_mul_f32_e32 v43, v45, v45
	v_mul_f32_e32 v52, v55, v55
	v_fmac_f32_e32 v43, v44, v44
	v_fmac_f32_e32 v52, v54, v54
	v_add_f32_e32 v43, v43, v52
	v_add_f32_e32 v52, v42, v43
	v_cvt_pk_bf16_f32 v42, v46, v47
	v_mul_f32_e32 v46, 0x41000000, v46
	v_med3_f32 v53, v46, s64, v250
	v_mul_f32_e32 v46, 0x41000000, v47
	v_med3_f32 v47, v46, s64, v250
	v_cvt_pk_fp8_f32 v46, v53, v47
	v_cvt_pk_bf16_f32 v43, v48, v49
	v_mul_f32_e32 v47, 0x41000000, v48
	v_mul_f32_e32 v48, 0x41000000, v49
	v_med3_f32 v47, v47, s64, v250
	v_med3_f32 v48, v48, s64, v250
	v_cvt_pk_fp8_f32 v46, v47, v48 op_sel:[0,0,1]
	v_mul_f32_e32 v47, 0x41000000, v44
	v_med3_f32 v48, v47, s64, v250
	v_mul_f32_e32 v47, 0x41000000, v45
	v_med3_f32 v49, v47, s64, v250
	v_cvt_pk_fp8_f32 v47, v48, v49
	v_mul_f32_e32 v48, 0x41000000, v54
	v_mul_f32_e32 v49, 0x41000000, v55
	v_med3_f32 v48, v48, s64, v250
	v_med3_f32 v49, v49, s64, v250
	v_cvt_pk_fp8_f32 v47, v48, v49 op_sel:[0,0,1]
	v_lshlrev_b64 v[50:51], 10, v[102:103]
	v_cvt_pk_bf16_f32 v44, v44, v45
	v_cvt_pk_bf16_f32 v45, v54, v55
	v_lshl_add_u64 v[50:51], v[170:171], 0, v[50:51]
	global_store_dwordx4 v[104:105], v[42:45], off
	global_store_dwordx2 v[50:51], v[46:47], off
	s_waitcnt vmcnt(10)
	v_lshlrev_b32_e32 v42, 16, v82
	v_and_b32_e32 v43, 0xffff0000, v82
	v_lshlrev_b32_e32 v44, 16, v83
	v_and_b32_e32 v45, 0xffff0000, v83
	v_pk_add_f32 v[40:41], v[40:41], v[44:45]
	v_pk_add_f32 v[38:39], v[38:39], v[42:43]
	v_lshlrev_b32_e32 v42, 16, v84
	v_and_b32_e32 v43, 0xffff0000, v84
	v_lshlrev_b32_e32 v44, 16, v85
	v_and_b32_e32 v45, 0xffff0000, v85
	v_pk_add_f32 v[44:45], v[36:37], v[44:45]
	v_pk_add_f32 v[36:37], v[34:35], v[42:43]
	v_mul_f32_e32 v34, v39, v39
	v_mul_f32_e32 v35, v41, v41
	v_fmac_f32_e32 v34, v38, v38
	v_fmac_f32_e32 v35, v40, v40
	v_add_f32_e32 v34, v34, v35
	v_mul_f32_e32 v35, v37, v37
	v_mul_f32_e32 v42, v45, v45
	v_fmac_f32_e32 v35, v36, v36
	v_fmac_f32_e32 v42, v44, v44
	v_add_f32_e32 v35, v35, v42
	v_add_f32_e32 v34, v34, v35
	v_add_f32_e32 v42, v52, v34
	v_cvt_pk_bf16_f32 v34, v38, v39
	v_mul_f32_e32 v38, 0x41000000, v38
	v_med3_f32 v43, v38, s64, v250
	v_mul_f32_e32 v38, 0x41000000, v39
	v_med3_f32 v39, v38, s64, v250
	v_cvt_pk_fp8_f32 v38, v43, v39
	v_cvt_pk_bf16_f32 v35, v40, v41
	v_mul_f32_e32 v39, 0x41000000, v40
	v_mul_f32_e32 v40, 0x41000000, v41
	v_med3_f32 v39, v39, s64, v250
	v_med3_f32 v40, v40, s64, v250
	v_cvt_pk_fp8_f32 v38, v39, v40 op_sel:[0,0,1]
	v_mul_f32_e32 v39, 0x41000000, v36
	v_med3_f32 v40, v39, s64, v250
	v_mul_f32_e32 v39, 0x41000000, v37
	v_med3_f32 v41, v39, s64, v250
	v_cvt_pk_fp8_f32 v39, v40, v41
	v_mul_f32_e32 v40, 0x41000000, v44
	v_mul_f32_e32 v41, 0x41000000, v45
	v_med3_f32 v40, v40, s64, v250
	v_med3_f32 v41, v41, s64, v250
	v_cvt_pk_fp8_f32 v39, v40, v41 op_sel:[0,0,1]
	ds_swizzle_b32 v40, v42 offset:swizzle(SWAP,16)
	v_cvt_pk_bf16_f32 v36, v36, v37
	v_cvt_pk_bf16_f32 v37, v44, v45
	global_store_dwordx4 v[104:105], v[34:37], off offset:256
	global_store_dwordx2 v[50:51], v[38:39], off offset:128
	s_waitcnt lgkmcnt(0)
	v_add_f32_e32 v34, v42, v40
	v_mov_b32_e32 v35, v34
	s_nop 1
	v_permlane32_swap_b32_e32 v34, v35
	s_and_saveexec_b64 s[30:31], s[2:3]
	s_cbranch_execz .LBB0_1823
	v_lshlrev_b64 v[36:37], 6, v[102:103]
	v_lshl_add_u64 v[36:37], s[28:29], 0, v[36:37]
	v_add_f32_e32 v34, v34, v35
	global_store_dword v[36:37], v34, off
; __device__ __forceinline__ u32x4 pack8(const f32x4 a, const f32x4 b) { u32x4 w; w.x = cvt_pk_bf16(a[0], a[1]); w.y = cvt_pk_bf16(a[2], a[3]); w.z = cvt_pk_bf16(b[0], b[1]); w.w = cvt_pk_bf16(b[2], b[3]); return w; }
; __device__ __forceinline__ float sumsq4(const f32x4 v) { return (v[0] * v[0] + v[1] * v[1]) + (v[2] * v[2] + v[3] * v[3]); }
; __device__ __forceinline__ float xor16_add(float v) { return v + __int_as_float(__builtin_amdgcn_ds_swizzle(__float_as_int(v), 0x401F)); }
; __device__ __forceinline__ float xor32_add(float v) { auto rr = __builtin_amdgcn_permlane32_swap(__float_as_uint(v), __float_as_uint(v), false, false); return __uint_as_float(rr[0]) + __uint_as_float(rr[1]); }
; __device__ __forceinline__ f32x4 bf2f_lo(const u32x4 w, int h) { const unsigned a = h ? w.z : w.x, b = h ? w.w : w.y; return (f32x4){__uint_as_float(a << 16), __uint_as_float(a & 0xffff0000u), __uint_as_float(b << 16), __uint_as_float(b & 0xffff0000u)}; }
;     __device__ __forceinline__ void operator()(const f32x4 (&acc)[2][2][4][2], const Unit& u, int wr, int wc, int fr, int fq) const {
;     ...
;             for (int m = 0; m < 4; ++m) {
;                 const int row = row0 + ai * HALF + m * 16; float ss = 0.f;
; #pragma unroll
;                 for (int bj = 0; bj < 2; ++bj) {
;                     const f32x4 v0 = bf2f_lo(old[m][bj], 0) + acc[ai][bj][m][0], v1 = bf2f_lo(old[m][bj], 1) + acc[ai][bj][m][1];
;                     ss += sumsq4(v0) + sumsq4(v1);
;                     *(u32x4*)(xb + (size_t)row * DM + col0 + bj * HALF) = pack8(v0, v1);
;                     { u32x2 w8; w8.x = pack4_fp8_x8(v0); w8.y = pack4_fp8_x8(v1); *(u32x2*)(xq + (size_t)row * DM + col0 + bj * HALF) = w8; }
;                 }
;                 ss = xor32_add(xor16_add(ss));
;                 if (fq == 0) ssx[(size_t)row * 16 + u.pn * 4 + wc] = ss;
.LBB0_1823:
	s_or_b64 exec, exec, s[30:31]
	s_waitcnt vmcnt(11)
	v_lshlrev_b32_e32 v36, 16, v78
	v_and_b32_e32 v37, 0xffff0000, v78
	v_lshlrev_b32_e32 v38, 16, v79
	v_and_b32_e32 v39, 0xffff0000, v79
	v_pk_add_f32 v[32:33], v[32:33], v[38:39]
	v_pk_add_f32 v[30:31], v[30:31], v[36:37]
	v_lshlrev_b32_e32 v36, 16, v80
	v_and_b32_e32 v37, 0xffff0000, v80
	v_lshlrev_b32_e32 v38, 16, v81
	v_and_b32_e32 v39, 0xffff0000, v81
	v_pk_add_f32 v[38:39], v[28:29], v[38:39]
	v_pk_add_f32 v[28:29], v[26:27], v[36:37]
	v_mul_f32_e32 v26, v31, v31
	v_mul_f32_e32 v27, v33, v33
	v_fmac_f32_e32 v26, v30, v30
	v_fmac_f32_e32 v27, v32, v32
	v_add_f32_e32 v26, v26, v27
	v_mul_f32_e32 v27, v29, v29
	v_mul_f32_e32 v36, v39, v39
	v_fmac_f32_e32 v27, v28, v28
	v_fmac_f32_e32 v36, v38, v38
	v_add_f32_e32 v27, v27, v36
	v_add_f32_e32 v36, v26, v27
	v_cvt_pk_bf16_f32 v26, v30, v31
	v_mul_f32_e32 v30, 0x41000000, v30
	v_med3_f32 v37, v30, s64, v250
	v_mul_f32_e32 v30, 0x41000000, v31
	v_med3_f32 v31, v30, s64, v250
	v_cvt_pk_fp8_f32 v30, v37, v31
	v_cvt_pk_bf16_f32 v27, v32, v33
	v_mul_f32_e32 v31, 0x41000000, v32
	v_mul_f32_e32 v32, 0x41000000, v33
	v_med3_f32 v31, v31, s64, v250
	v_med3_f32 v32, v32, s64, v250
	v_cvt_pk_fp8_f32 v30, v31, v32 op_sel:[0,0,1]
	v_mul_f32_e32 v31, 0x41000000, v28
	v_med3_f32 v32, v31, s64, v250
	v_mul_f32_e32 v31, 0x41000000, v29
	v_med3_f32 v33, v31, s64, v250
	v_cvt_pk_fp8_f32 v31, v32, v33
	v_mul_f32_e32 v32, 0x41000000, v38
	v_mul_f32_e32 v33, 0x41000000, v39
	v_med3_f32 v32, v32, s64, v250
	v_med3_f32 v33, v33, s64, v250
	v_cvt_pk_fp8_f32 v31, v32, v33 op_sel:[0,0,1]
	v_lshlrev_b64 v[34:35], 10, v[98:99]
	v_cvt_pk_bf16_f32 v28, v28, v29
	v_cvt_pk_bf16_f32 v29, v38, v39
	v_lshl_add_u64 v[34:35], v[170:171], 0, v[34:35]
	global_store_dwordx4 v[100:101], v[26:29], off
	global_store_dwordx2 v[34:35], v[30:31], off
	s_waitcnt vmcnt(12)
	v_lshlrev_b32_e32 v26, 16, v74
	v_and_b32_e32 v27, 0xffff0000, v74
	v_lshlrev_b32_e32 v28, 16, v75
	v_and_b32_e32 v29, 0xffff0000, v75
	v_pk_add_f32 v[24:25], v[24:25], v[28:29]
	v_pk_add_f32 v[22:23], v[22:23], v[26:27]
	v_lshlrev_b32_e32 v26, 16, v76
	v_and_b32_e32 v27, 0xffff0000, v76
	v_lshlrev_b32_e32 v28, 16, v77
	v_and_b32_e32 v29, 0xffff0000, v77
	v_pk_add_f32 v[28:29], v[20:21], v[28:29]
	v_pk_add_f32 v[20:21], v[18:19], v[26:27]
	v_mul_f32_e32 v18, v23, v23
	v_mul_f32_e32 v19, v25, v25
	v_fmac_f32_e32 v18, v22, v22
	v_fmac_f32_e32 v19, v24, v24
	v_add_f32_e32 v18, v18, v19
	v_mul_f32_e32 v19, v21, v21
	v_mul_f32_e32 v26, v29, v29
	v_fmac_f32_e32 v19, v20, v20
	v_fmac_f32_e32 v26, v28, v28
	v_add_f32_e32 v19, v19, v26
	v_add_f32_e32 v18, v18, v19
	v_add_f32_e32 v26, v36, v18
	v_cvt_pk_bf16_f32 v18, v22, v23
	v_mul_f32_e32 v22, 0x41000000, v22
	v_med3_f32 v27, v22, s64, v250
	v_mul_f32_e32 v22, 0x41000000, v23
	v_med3_f32 v23, v22, s64, v250
	v_cvt_pk_fp8_f32 v22, v27, v23
	v_cvt_pk_bf16_f32 v19, v24, v25
	v_mul_f32_e32 v23, 0x41000000, v24
	v_mul_f32_e32 v24, 0x41000000, v25
	v_med3_f32 v23, v23, s64, v250
	v_med3_f32 v24, v24, s64, v250
	v_cvt_pk_fp8_f32 v22, v23, v24 op_sel:[0,0,1]
	v_mul_f32_e32 v23, 0x41000000, v20
	v_med3_f32 v24, v23, s64, v250
	v_mul_f32_e32 v23, 0x41000000, v21
	v_med3_f32 v25, v23, s64, v250
	v_cvt_pk_fp8_f32 v23, v24, v25
	v_mul_f32_e32 v24, 0x41000000, v28
	v_mul_f32_e32 v25, 0x41000000, v29
	v_med3_f32 v24, v24, s64, v250
	v_med3_f32 v25, v25, s64, v250
	v_cvt_pk_fp8_f32 v23, v24, v25 op_sel:[0,0,1]
	ds_swizzle_b32 v24, v26 offset:swizzle(SWAP,16)
	v_cvt_pk_bf16_f32 v20, v20, v21
	v_cvt_pk_bf16_f32 v21, v28, v29
	global_store_dwordx4 v[100:101], v[18:21], off offset:256
	global_store_dwordx2 v[34:35], v[22:23], off offset:128
	s_waitcnt lgkmcnt(0)
	v_add_f32_e32 v18, v26, v24
	v_mov_b32_e32 v19, v18
	s_nop 1
	v_permlane32_swap_b32_e32 v18, v19
	s_and_saveexec_b64 s[30:31], s[2:3]
	s_cbranch_execz .LBB0_1825
	v_lshlrev_b64 v[20:21], 6, v[98:99]
	v_lshl_add_u64 v[20:21], s[28:29], 0, v[20:21]
	v_add_f32_e32 v18, v18, v19
	global_store_dword v[20:21], v18, off
; __device__ __forceinline__ u32x4 pack8(const f32x4 a, const f32x4 b) { u32x4 w; w.x = cvt_pk_bf16(a[0], a[1]); w.y = cvt_pk_bf16(a[2], a[3]); w.z = cvt_pk_bf16(b[0], b[1]); w.w = cvt_pk_bf16(b[2], b[3]); return w; }
; __device__ __forceinline__ float sumsq4(const f32x4 v) { return (v[0] * v[0] + v[1] * v[1]) + (v[2] * v[2] + v[3] * v[3]); }
; __device__ __forceinline__ float xor16_add(float v) { return v + __int_as_float(__builtin_amdgcn_ds_swizzle(__float_as_int(v), 0x401F)); }
; __device__ __forceinline__ float xor32_add(float v) { auto rr = __builtin_amdgcn_permlane32_swap(__float_as_uint(v), __float_as_uint(v), false, false); return __uint_as_float(rr[0]) + __uint_as_float(rr[1]); }
; __device__ __forceinline__ f32x4 bf2f_lo(const u32x4 w, int h) { const unsigned a = h ? w.z : w.x, b = h ? w.w : w.y; return (f32x4){__uint_as_float(a << 16), __uint_as_float(a & 0xffff0000u), __uint_as_float(b << 16), __uint_as_float(b & 0xffff0000u)}; }
;     __device__ __forceinline__ void operator()(const f32x4 (&acc)[2][2][4][2], const Unit& u, int wr, int wc, int fr, int fq) const {
;     ...
;             for (int m = 0; m < 4; ++m) {
;                 const int row = row0 + ai * HALF + m * 16; float ss = 0.f;
; #pragma unroll
;                 for (int bj = 0; bj < 2; ++bj) {
;                     const f32x4 v0 = bf2f_lo(old[m][bj], 0) + acc[ai][bj][m][0], v1 = bf2f_lo(old[m][bj], 1) + acc[ai][bj][m][1];
;                     ss += sumsq4(v0) + sumsq4(v1);
;                     *(u32x4*)(xb + (size_t)row * DM + col0 + bj * HALF) = pack8(v0, v1);
;                     { u32x2 w8; w8.x = pack4_fp8_x8(v0); w8.y = pack4_fp8_x8(v1); *(u32x2*)(xq + (size_t)row * DM + col0 + bj * HALF) = w8; }
;                 }
;                 ss = xor32_add(xor16_add(ss));
;                 if (fq == 0) ssx[(size_t)row * 16 + u.pn * 4 + wc] = ss;
.LBB0_1825:
	s_or_b64 exec, exec, s[30:31]
	s_waitcnt vmcnt(13)
	v_lshlrev_b32_e32 v20, 16, v70
	v_and_b32_e32 v21, 0xffff0000, v70
	v_lshlrev_b32_e32 v22, 16, v71
	v_and_b32_e32 v23, 0xffff0000, v71
	v_pk_add_f32 v[16:17], v[16:17], v[22:23]
	v_pk_add_f32 v[14:15], v[14:15], v[20:21]
	v_lshlrev_b32_e32 v20, 16, v72
	v_and_b32_e32 v21, 0xffff0000, v72
	v_lshlrev_b32_e32 v22, 16, v73
	v_and_b32_e32 v23, 0xffff0000, v73
	v_pk_add_f32 v[22:23], v[12:13], v[22:23]
	v_pk_add_f32 v[12:13], v[10:11], v[20:21]
	v_mul_f32_e32 v10, v15, v15
	v_mul_f32_e32 v11, v17, v17
	v_fmac_f32_e32 v10, v14, v14
	v_fmac_f32_e32 v11, v16, v16
	v_add_f32_e32 v10, v10, v11
	v_mul_f32_e32 v11, v13, v13
	v_mul_f32_e32 v20, v23, v23
	v_fmac_f32_e32 v11, v12, v12
	v_fmac_f32_e32 v20, v22, v22
	v_add_f32_e32 v11, v11, v20
	v_add_f32_e32 v20, v10, v11
	v_cvt_pk_bf16_f32 v10, v14, v15
	v_mul_f32_e32 v14, 0x41000000, v14
	v_med3_f32 v21, v14, s64, v250
	v_mul_f32_e32 v14, 0x41000000, v15
	v_med3_f32 v15, v14, s64, v250
	v_cvt_pk_fp8_f32 v14, v21, v15
	v_cvt_pk_bf16_f32 v11, v16, v17
	v_mul_f32_e32 v15, 0x41000000, v16
	v_mul_f32_e32 v16, 0x41000000, v17
	v_med3_f32 v15, v15, s64, v250
	v_med3_f32 v16, v16, s64, v250
	v_cvt_pk_fp8_f32 v14, v15, v16 op_sel:[0,0,1]
	v_mul_f32_e32 v15, 0x41000000, v12
	v_med3_f32 v16, v15, s64, v250
	v_mul_f32_e32 v15, 0x41000000, v13
	v_med3_f32 v17, v15, s64, v250
	v_cvt_pk_fp8_f32 v15, v16, v17
	v_mul_f32_e32 v16, 0x41000000, v22
	v_mul_f32_e32 v17, 0x41000000, v23
	v_med3_f32 v16, v16, s64, v250
	v_med3_f32 v17, v17, s64, v250
	v_cvt_pk_fp8_f32 v15, v16, v17 op_sel:[0,0,1]
	v_lshlrev_b64 v[18:19], 10, v[94:95]
	v_cvt_pk_bf16_f32 v12, v12, v13
	v_cvt_pk_bf16_f32 v13, v22, v23
	v_lshl_add_u64 v[18:19], v[170:171], 0, v[18:19]
	global_store_dwordx4 v[96:97], v[10:13], off
	global_store_dwordx2 v[18:19], v[14:15], off
	s_waitcnt vmcnt(14)
	v_lshlrev_b32_e32 v10, 16, v66
	v_and_b32_e32 v11, 0xffff0000, v66
	v_lshlrev_b32_e32 v12, 16, v67
	v_and_b32_e32 v13, 0xffff0000, v67
	v_pk_add_f32 v[8:9], v[8:9], v[12:13]
	v_pk_add_f32 v[6:7], v[6:7], v[10:11]
	v_lshlrev_b32_e32 v10, 16, v68
	v_and_b32_e32 v11, 0xffff0000, v68
	v_lshlrev_b32_e32 v12, 16, v69
	v_and_b32_e32 v13, 0xffff0000, v69
	v_pk_add_f32 v[12:13], v[4:5], v[12:13]
	v_pk_add_f32 v[4:5], v[2:3], v[10:11]
	v_mul_f32_e32 v2, v7, v7
	v_mul_f32_e32 v3, v9, v9
	v_fmac_f32_e32 v2, v6, v6
	v_fmac_f32_e32 v3, v8, v8
	v_add_f32_e32 v2, v2, v3
	v_mul_f32_e32 v3, v5, v5
	v_mul_f32_e32 v10, v13, v13
	v_fmac_f32_e32 v3, v4, v4
	v_fmac_f32_e32 v10, v12, v12
	v_add_f32_e32 v3, v3, v10
	v_add_f32_e32 v2, v2, v3
	v_add_f32_e32 v10, v20, v2
	v_cvt_pk_bf16_f32 v2, v6, v7
	v_mul_f32_e32 v6, 0x41000000, v6
	v_med3_f32 v11, v6, s64, v250
	v_mul_f32_e32 v6, 0x41000000, v7
	v_med3_f32 v7, v6, s64, v250
	v_cvt_pk_fp8_f32 v6, v11, v7
	v_cvt_pk_bf16_f32 v3, v8, v9
	v_mul_f32_e32 v7, 0x41000000, v8
	v_mul_f32_e32 v8, 0x41000000, v9
	v_med3_f32 v7, v7, s64, v250
	v_med3_f32 v8, v8, s64, v250
	v_cvt_pk_fp8_f32 v6, v7, v8 op_sel:[0,0,1]
	v_mul_f32_e32 v7, 0x41000000, v4
	v_med3_f32 v8, v7, s64, v250
	v_mul_f32_e32 v7, 0x41000000, v5
	v_med3_f32 v9, v7, s64, v250
	v_cvt_pk_fp8_f32 v7, v8, v9
	v_mul_f32_e32 v8, 0x41000000, v12
	v_mul_f32_e32 v9, 0x41000000, v13
	v_med3_f32 v8, v8, s64, v250
	v_med3_f32 v9, v9, s64, v250
	v_cvt_pk_fp8_f32 v7, v8, v9 op_sel:[0,0,1]
	ds_swizzle_b32 v8, v10 offset:swizzle(SWAP,16)
	v_cvt_pk_bf16_f32 v4, v4, v5
	v_cvt_pk_bf16_f32 v5, v12, v13
	global_store_dwordx4 v[96:97], v[2:5], off offset:256
	global_store_dwordx2 v[18:19], v[6:7], off offset:128
	s_waitcnt lgkmcnt(0)
	v_add_f32_e32 v2, v10, v8
	v_mov_b32_e32 v3, v2
	s_nop 1
	v_permlane32_swap_b32_e32 v2, v3
	s_and_saveexec_b64 s[30:31], s[2:3]
	s_cbranch_execz .LBB0_1827
	v_lshlrev_b64 v[4:5], 6, v[94:95]
	v_lshl_add_u64 v[4:5], s[28:29], 0, v[4:5]
	v_add_f32_e32 v2, v2, v3
	global_store_dword v[4:5], v2, off

; __device__ __forceinline__ u32x4 pack8(const f32x4 a, const f32x4 b) { u32x4 w; w.x = cvt_pk_bf16(a[0], a[1]); w.y = cvt_pk_bf16(a[2], a[3]); w.z = cvt_pk_bf16(b[0], b[1]); w.w = cvt_pk_bf16(b[2], b[3]); return w; }
; __device__ __forceinline__ float sumsq4(const f32x4 v) { return (v[0] * v[0] + v[1] * v[1]) + (v[2] * v[2] + v[3] * v[3]); }
; __device__ __forceinline__ float xor16_add(float v) { return v + __int_as_float(__builtin_amdgcn_ds_swizzle(__float_as_int(v), 0x401F)); }
; __device__ __forceinline__ float xor32_add(float v) { auto rr = __builtin_amdgcn_permlane32_swap(__float_as_uint(v), __float_as_uint(v), false, false); return __uint_as_float(rr[0]) + __uint_as_float(rr[1]); }
; __device__ __forceinline__ f32x4 bf2f_lo(const u32x4 w, int h) { const unsigned a = h ? w.z : w.x, b = h ? w.w : w.y; return (f32x4){__uint_as_float(a << 16), __uint_as_float(a & 0xffff0000u), __uint_as_float(b << 16), __uint_as_float(b & 0xffff0000u)}; }
;     __device__ __forceinline__ void operator()(const f32x4 (&acc)[2][2][4][2], const Unit& u, int wr, int wc, int fr, int fq) const {
;     ...
;                 for (int bj = 0; bj < 2; ++bj) old[m][bj] = *(const u32x4*)(xb + (size_t)(row0 + ai * HALF + m * 16) * DM + col0 + bj * HALF);
; #pragma unroll
;             for (int m = 0; m < 4; ++m) {
;                 const int row = row0 + ai * HALF + m * 16; float ss = 0.f;
; #pragma unroll
;                 for (int bj = 0; bj < 2; ++bj) {
;                     const f32x4 v0 = bf2f_lo(old[m][bj], 0) + acc[ai][bj][m][0], v1 = bf2f_lo(old[m][bj], 1) + acc[ai][bj][m][1];
;                     ss += sumsq4(v0) + sumsq4(v1);
;                     *(u32x4*)(xb + (size_t)row * DM + col0 + bj * HALF) = pack8(v0, v1);
;                     { u32x2 w8; w8.x = pack4_fp8_x8(v0); w8.y = pack4_fp8_x8(v1); *(u32x2*)(xq + (size_t)row * DM + col0 + bj * HALF) = w8; }
;                 }
;                 ss = xor32_add(xor16_add(ss));
;                 if (fq == 0) ssx[(size_t)row * 16 + u.pn * 4 + wc] = ss;
.LBB0_1861:
	v_lshl_add_u32 v32, s61, 8, v163
	v_lshl_or_b32 v2, s60, 8, v193
	v_ashrrev_i32_e32 v3, 31, v2
	v_ashrrev_i32_e32 v33, 31, v32
	v_lshl_add_u64 v[174:175], v[2:3], 1, s[22:23]
	v_lshl_add_u64 v[30:31], s[24:25], 0, v[2:3]
	v_lshlrev_b64 v[2:3], 11, v[32:33]
	s_nop 15
	s_nop 15
	v_lshl_add_u64 v[190:191], v[174:175], 0, v[2:3]
	global_load_dwordx4 v[204:207], v[190:191], off
	global_load_dwordx4 v[26:29], v[190:191], off offset:256
	v_or_b32_e32 v184, 16, v32
	v_ashrrev_i32_e32 v185, 31, v184
	v_or_b32_e32 v180, 32, v32
	v_lshlrev_b64 v[2:3], 11, v[184:185]
	v_ashrrev_i32_e32 v181, 31, v180
	v_or_b32_e32 v176, 48, v32
	v_lshl_add_u64 v[186:187], v[174:175], 0, v[2:3]
	v_lshlrev_b64 v[2:3], 11, v[180:181]
	v_ashrrev_i32_e32 v177, 31, v176
	v_lshl_add_u64 v[182:183], v[174:175], 0, v[2:3]
	v_lshlrev_b64 v[2:3], 11, v[176:177]
	v_lshl_add_u64 v[178:179], v[174:175], 0, v[2:3]
	global_load_dwordx4 v[22:25], v[186:187], off
	global_load_dwordx4 v[18:21], v[186:187], off offset:256
	global_load_dwordx4 v[14:17], v[182:183], off
	global_load_dwordx4 v[10:13], v[182:183], off offset:256
	global_load_dwordx4 v[6:9], v[178:179], off
	global_load_dwordx4 v[2:5], v[178:179], off offset:256
	v_lshlrev_b64 v[188:189], 10, v[32:33]
	v_lshl_add_u64 v[188:189], v[30:31], 0, v[188:189]
	s_lshl_b32 s26, s60, 2
	s_ashr_i32 s27, s26, 31
	s_lshl_b64 s[26:27], s[26:27], 2
	s_add_u32 s26, s49, s26
	s_addc_u32 s27, s50, s27
	s_waitcnt vmcnt(0)
	v_lshlrev_b32_e32 v196, 16, v204
	v_and_b32_e32 v197, 0xffff0000, v204
	v_lshlrev_b32_e32 v198, 16, v205
	v_and_b32_e32 v199, 0xffff0000, v205
	v_pk_add_f32 v[160:161], v[160:161], v[198:199]
	v_pk_add_f32 v[196:197], v[158:159], v[196:197]
	v_lshlrev_b32_e32 v158, 16, v206
	v_and_b32_e32 v159, 0xffff0000, v206
	v_lshlrev_b32_e32 v198, 16, v207
	v_and_b32_e32 v199, 0xffff0000, v207
	v_pk_add_f32 v[154:155], v[154:155], v[158:159]
	v_mul_f32_e32 v158, v197, v197
	v_mul_f32_e32 v159, v161, v161
	v_pk_add_f32 v[156:157], v[156:157], v[198:199]
	v_fmac_f32_e32 v158, v196, v196
	v_fmac_f32_e32 v159, v160, v160
	v_add_f32_e32 v158, v158, v159
	v_mul_f32_e32 v159, v155, v155
	v_mul_f32_e32 v195, v157, v157
	v_fmac_f32_e32 v159, v154, v154
	v_fmac_f32_e32 v195, v156, v156
	v_cvt_pk_bf16_f32 v204, v196, v197
	v_cvt_pk_bf16_f32 v205, v160, v161
	v_cvt_pk_bf16_f32 v206, v154, v155
	v_mul_f32_e32 v154, 0x41000000, v154
	v_mul_f32_e32 v155, 0x41000000, v155
	v_add_f32_e32 v159, v159, v195
	v_mul_f32_e32 v195, 0x41000000, v197
	v_med3_f32 v154, v154, s64, v250
	v_med3_f32 v155, v155, s64, v250
	v_cvt_pk_fp8_f32 v197, v154, v155
	v_add_f32_e32 v158, v158, v159
	v_mul_f32_e32 v159, 0x41000000, v196
	v_mul_f32_e32 v154, 0x41000000, v156
	v_mul_f32_e32 v155, 0x41000000, v157
	v_med3_f32 v159, v159, s64, v250
	v_med3_f32 v195, v195, s64, v250
	v_med3_f32 v154, v154, s64, v250
	v_med3_f32 v155, v155, s64, v250
	v_cvt_pk_fp8_f32 v196, v159, v195
	v_cvt_pk_fp8_f32 v197, v154, v155 op_sel:[0,0,1]
	v_lshlrev_b32_e32 v154, 16, v26
	v_and_b32_e32 v155, 0xffff0000, v26
	v_lshlrev_b32_e32 v26, 16, v27
	v_and_b32_e32 v27, 0xffff0000, v27
	v_pk_add_f32 v[26:27], v[152:153], v[26:27]
	v_pk_add_f32 v[150:151], v[150:151], v[154:155]
	v_lshlrev_b32_e32 v152, 16, v28
	v_and_b32_e32 v153, 0xffff0000, v28
	v_mul_f32_e32 v159, 0x41000000, v160
	v_mul_f32_e32 v160, 0x41000000, v161
	v_lshlrev_b32_e32 v28, 16, v29
	v_and_b32_e32 v29, 0xffff0000, v29
	v_pk_add_f32 v[152:153], v[146:147], v[152:153]
	v_mul_f32_e32 v146, v151, v151
	v_mul_f32_e32 v147, v27, v27
	v_med3_f32 v159, v159, s64, v250
	v_med3_f32 v160, v160, s64, v250
	v_pk_add_f32 v[28:29], v[148:149], v[28:29]
	v_fmac_f32_e32 v146, v150, v150
	v_fmac_f32_e32 v147, v26, v26
	v_cvt_pk_fp8_f32 v196, v159, v160 op_sel:[0,0,1]
	v_add_f32_e32 v146, v146, v147
	v_mul_f32_e32 v147, v153, v153
	v_mul_f32_e32 v148, v29, v29
	v_fmac_f32_e32 v147, v152, v152
	v_fmac_f32_e32 v148, v28, v28
	v_add_f32_e32 v147, v147, v148
	v_add_f32_e32 v146, v146, v147
	v_cvt_pk_bf16_f32 v207, v156, v157
	global_store_dwordx4 v[190:191], v[204:207], off
	global_store_dwordx2 v[188:189], v[196:197], off
	v_add_f32_e32 v154, v158, v146
	v_cvt_pk_bf16_f32 v146, v150, v151
	v_cvt_pk_bf16_f32 v147, v26, v27
	v_cvt_pk_bf16_f32 v148, v152, v153
	v_cvt_pk_bf16_f32 v149, v28, v29
	global_store_dwordx4 v[190:191], v[146:149], off offset:256
	v_mul_f32_e32 v26, 0x41000000, v26
	v_mul_f32_e32 v27, 0x41000000, v27
	v_mul_f32_e32 v146, 0x41000000, v150
	v_med3_f32 v147, v146, s64, v250
	v_mul_f32_e32 v146, 0x41000000, v151
	v_med3_f32 v148, v146, s64, v250
	v_cvt_pk_fp8_f32 v146, v147, v148
	v_med3_f32 v26, v26, s64, v250
	v_med3_f32 v27, v27, s64, v250
	v_cvt_pk_fp8_f32 v146, v26, v27 op_sel:[0,0,1]
	v_mul_f32_e32 v26, 0x41000000, v152
	v_mul_f32_e32 v27, 0x41000000, v153
	v_med3_f32 v26, v26, s64, v250
	v_med3_f32 v27, v27, s64, v250
	v_cvt_pk_fp8_f32 v147, v26, v27
	v_mul_f32_e32 v26, 0x41000000, v28
	v_mul_f32_e32 v27, 0x41000000, v29
	v_med3_f32 v26, v26, s64, v250
	v_med3_f32 v27, v27, s64, v250
	v_cvt_pk_fp8_f32 v147, v26, v27 op_sel:[0,0,1]
	ds_swizzle_b32 v26, v154 offset:swizzle(SWAP,16)
	global_store_dwordx2 v[188:189], v[146:147], off offset:128
	s_waitcnt lgkmcnt(0)
	v_add_f32_e32 v26, v154, v26
	v_mov_b32_e32 v27, v26
	s_nop 1
	v_permlane32_swap_b32_e32 v26, v27
	s_and_saveexec_b64 s[28:29], s[2:3]
	s_cbranch_execz .LBB0_1863
	v_lshlrev_b64 v[28:29], 6, v[32:33]
	v_lshl_add_u64 v[28:29], s[26:27], 0, v[28:29]
	v_add_f32_e32 v26, v26, v27
	global_store_dword v[28:29], v26, off
; __device__ __forceinline__ u32x4 pack8(const f32x4 a, const f32x4 b) { u32x4 w; w.x = cvt_pk_bf16(a[0], a[1]); w.y = cvt_pk_bf16(a[2], a[3]); w.z = cvt_pk_bf16(b[0], b[1]); w.w = cvt_pk_bf16(b[2], b[3]); return w; }
; __device__ __forceinline__ float sumsq4(const f32x4 v) { return (v[0] * v[0] + v[1] * v[1]) + (v[2] * v[2] + v[3] * v[3]); }
; __device__ __forceinline__ float xor16_add(float v) { return v + __int_as_float(__builtin_amdgcn_ds_swizzle(__float_as_int(v), 0x401F)); }
; __device__ __forceinline__ float xor32_add(float v) { auto rr = __builtin_amdgcn_permlane32_swap(__float_as_uint(v), __float_as_uint(v), false, false); return __uint_as_float(rr[0]) + __uint_as_float(rr[1]); }
; __device__ __forceinline__ f32x4 bf2f_lo(const u32x4 w, int h) { const unsigned a = h ? w.z : w.x, b = h ? w.w : w.y; return (f32x4){__uint_as_float(a << 16), __uint_as_float(a & 0xffff0000u), __uint_as_float(b << 16), __uint_as_float(b & 0xffff0000u)}; }
;     __device__ __forceinline__ void operator()(const f32x4 (&acc)[2][2][4][2], const Unit& u, int wr, int wc, int fr, int fq) const {
;     ...
;             for (int m = 0; m < 4; ++m) {
;                 const int row = row0 + ai * HALF + m * 16; float ss = 0.f;
; #pragma unroll
;                 for (int bj = 0; bj < 2; ++bj) {
;                     const f32x4 v0 = bf2f_lo(old[m][bj], 0) + acc[ai][bj][m][0], v1 = bf2f_lo(old[m][bj], 1) + acc[ai][bj][m][1];
;                     ss += sumsq4(v0) + sumsq4(v1);
;                     *(u32x4*)(xb + (size_t)row * DM + col0 + bj * HALF) = pack8(v0, v1);
;                     { u32x2 w8; w8.x = pack4_fp8_x8(v0); w8.y = pack4_fp8_x8(v1); *(u32x2*)(xq + (size_t)row * DM + col0 + bj * HALF) = w8; }
;                 }
;                 ss = xor32_add(xor16_add(ss));
;                 if (fq == 0) ssx[(size_t)row * 16 + u.pn * 4 + wc] = ss;
.LBB0_1863:
	s_or_b64 exec, exec, s[28:29]
	v_lshlrev_b32_e32 v28, 16, v22
	v_and_b32_e32 v29, 0xffff0000, v22
	v_lshlrev_b32_e32 v22, 16, v23
	v_and_b32_e32 v23, 0xffff0000, v23
	v_pk_add_f32 v[144:145], v[144:145], v[22:23]
	v_pk_add_f32 v[28:29], v[142:143], v[28:29]
	v_lshlrev_b32_e32 v22, 16, v24
	v_and_b32_e32 v23, 0xffff0000, v24
	v_lshlrev_b32_e32 v24, 16, v25
	v_and_b32_e32 v25, 0xffff0000, v25
	v_pk_add_f32 v[140:141], v[140:141], v[24:25]
	v_pk_add_f32 v[24:25], v[138:139], v[22:23]
	v_mul_f32_e32 v22, v29, v29
	v_mul_f32_e32 v23, v145, v145
	v_fmac_f32_e32 v22, v28, v28
	v_fmac_f32_e32 v23, v144, v144
	v_add_f32_e32 v22, v22, v23
	v_mul_f32_e32 v23, v25, v25
	v_mul_f32_e32 v33, v141, v141
	v_fmac_f32_e32 v23, v24, v24
	v_fmac_f32_e32 v33, v140, v140
	v_add_f32_e32 v23, v23, v33
	v_add_f32_e32 v33, v22, v23
	v_cvt_pk_bf16_f32 v22, v28, v29
	v_mul_f32_e32 v28, 0x41000000, v28
	v_med3_f32 v138, v28, s64, v250
	v_mul_f32_e32 v28, 0x41000000, v29
	v_med3_f32 v29, v28, s64, v250
	v_cvt_pk_fp8_f32 v28, v138, v29
	v_mul_f32_e32 v29, 0x41000000, v144
	v_mul_f32_e32 v138, 0x41000000, v145
	v_med3_f32 v29, v29, s64, v250
	v_med3_f32 v138, v138, s64, v250
	v_cvt_pk_fp8_f32 v28, v29, v138 op_sel:[0,0,1]
	v_mul_f32_e32 v29, 0x41000000, v24
	v_med3_f32 v138, v29, s64, v250
	v_mul_f32_e32 v29, 0x41000000, v25
	v_med3_f32 v139, v29, s64, v250
	v_cvt_pk_fp8_f32 v29, v138, v139
	v_mul_f32_e32 v138, 0x41000000, v140
	v_mul_f32_e32 v139, 0x41000000, v141
	v_med3_f32 v138, v138, s64, v250
	v_med3_f32 v139, v139, s64, v250
	v_cvt_pk_fp8_f32 v29, v138, v139 op_sel:[0,0,1]
	v_lshlrev_b64 v[26:27], 10, v[184:185]
	v_cvt_pk_bf16_f32 v23, v144, v145
	v_cvt_pk_bf16_f32 v24, v24, v25
	v_cvt_pk_bf16_f32 v25, v140, v141
	v_lshl_add_u64 v[26:27], v[30:31], 0, v[26:27]
	global_store_dwordx4 v[186:187], v[22:25], off
	global_store_dwordx2 v[26:27], v[28:29], off
	s_nop 0
	v_lshlrev_b32_e32 v22, 16, v18
	v_and_b32_e32 v23, 0xffff0000, v18
	v_lshlrev_b32_e32 v18, 16, v19
	v_and_b32_e32 v19, 0xffff0000, v19
	v_pk_add_f32 v[24:25], v[136:137], v[18:19]
	v_pk_add_f32 v[22:23], v[134:135], v[22:23]
	v_lshlrev_b32_e32 v18, 16, v20
	v_and_b32_e32 v19, 0xffff0000, v20
	v_lshlrev_b32_e32 v20, 16, v21
	v_and_b32_e32 v21, 0xffff0000, v21
	v_pk_add_f32 v[28:29], v[132:133], v[20:21]
	v_pk_add_f32 v[20:21], v[130:131], v[18:19]
	v_mul_f32_e32 v18, v23, v23
	v_mul_f32_e32 v19, v25, v25
	v_fmac_f32_e32 v18, v22, v22
	v_fmac_f32_e32 v19, v24, v24
	v_add_f32_e32 v18, v18, v19
	v_mul_f32_e32 v19, v21, v21
	v_mul_f32_e32 v130, v29, v29
	v_fmac_f32_e32 v19, v20, v20
	v_fmac_f32_e32 v130, v28, v28
	v_add_f32_e32 v19, v19, v130
	v_add_f32_e32 v18, v18, v19
	v_add_f32_e32 v33, v33, v18
	v_cvt_pk_bf16_f32 v18, v22, v23
	v_mul_f32_e32 v22, 0x41000000, v22
	v_med3_f32 v130, v22, s64, v250
	v_mul_f32_e32 v22, 0x41000000, v23
	v_med3_f32 v23, v22, s64, v250
	v_cvt_pk_fp8_f32 v22, v130, v23
	v_cvt_pk_bf16_f32 v19, v24, v25
	v_mul_f32_e32 v23, 0x41000000, v24
	v_mul_f32_e32 v24, 0x41000000, v25
	v_med3_f32 v23, v23, s64, v250
	v_med3_f32 v24, v24, s64, v250
	v_cvt_pk_fp8_f32 v22, v23, v24 op_sel:[0,0,1]
	v_mul_f32_e32 v23, 0x41000000, v20
	v_med3_f32 v24, v23, s64, v250
	v_mul_f32_e32 v23, 0x41000000, v21
	v_med3_f32 v25, v23, s64, v250
	v_cvt_pk_fp8_f32 v23, v24, v25
	v_mul_f32_e32 v24, 0x41000000, v28
	v_mul_f32_e32 v25, 0x41000000, v29
	v_med3_f32 v24, v24, s64, v250
	v_med3_f32 v25, v25, s64, v250
	v_cvt_pk_fp8_f32 v23, v24, v25 op_sel:[0,0,1]
	ds_swizzle_b32 v24, v33 offset:swizzle(SWAP,16)
	v_cvt_pk_bf16_f32 v20, v20, v21
	v_cvt_pk_bf16_f32 v21, v28, v29
	global_store_dwordx4 v[186:187], v[18:21], off offset:256
	global_store_dwordx2 v[26:27], v[22:23], off offset:128
	s_waitcnt lgkmcnt(0)
	v_add_f32_e32 v18, v33, v24
	v_mov_b32_e32 v19, v18
	s_nop 1
	v_permlane32_swap_b32_e32 v18, v19
	s_and_saveexec_b64 s[28:29], s[2:3]
	s_cbranch_execz .LBB0_1865
	v_lshlrev_b64 v[20:21], 6, v[184:185]
	v_lshl_add_u64 v[20:21], s[26:27], 0, v[20:21]
	v_add_f32_e32 v18, v18, v19
	global_store_dword v[20:21], v18, off
.LBB0_1865:
	s_or_b64 exec, exec, s[28:29]
	v_lshlrev_b32_e32 v20, 16, v14
	v_and_b32_e32 v21, 0xffff0000, v14
	v_lshlrev_b32_e32 v14, 16, v15
	v_and_b32_e32 v15, 0xffff0000, v15
	v_pk_add_f32 v[22:23], v[128:129], v[14:15]
	v_pk_add_f32 v[20:21], v[126:127], v[20:21]
	v_lshlrev_b32_e32 v14, 16, v16
	v_and_b32_e32 v15, 0xffff0000, v16
	v_lshlrev_b32_e32 v16, 16, v17
	v_and_b32_e32 v17, 0xffff0000, v17
	v_pk_add_f32 v[24:25], v[124:125], v[16:17]
	v_pk_add_f32 v[16:17], v[122:123], v[14:15]
	v_mul_f32_e32 v14, v21, v21
	v_mul_f32_e32 v15, v23, v23
	v_fmac_f32_e32 v14, v20, v20
	v_fmac_f32_e32 v15, v22, v22
	v_add_f32_e32 v14, v14, v15
	v_mul_f32_e32 v15, v17, v17
	v_mul_f32_e32 v26, v25, v25
	v_fmac_f32_e32 v15, v16, v16
	v_fmac_f32_e32 v26, v24, v24
	v_add_f32_e32 v15, v15, v26
	v_add_f32_e32 v26, v14, v15
	v_cvt_pk_bf16_f32 v14, v20, v21
	v_mul_f32_e32 v20, 0x41000000, v20
	v_med3_f32 v27, v20, s64, v250
	v_mul_f32_e32 v20, 0x41000000, v21
	v_med3_f32 v21, v20, s64, v250
	v_cvt_pk_fp8_f32 v20, v27, v21
	v_cvt_pk_bf16_f32 v15, v22, v23
	v_mul_f32_e32 v21, 0x41000000, v22
	v_mul_f32_e32 v22, 0x41000000, v23
	v_med3_f32 v21, v21, s64, v250
	v_med3_f32 v22, v22, s64, v250
	v_cvt_pk_fp8_f32 v20, v21, v22 op_sel:[0,0,1]
	v_mul_f32_e32 v21, 0x41000000, v16
	v_med3_f32 v22, v21, s64, v250
	v_mul_f32_e32 v21, 0x41000000, v17
	v_med3_f32 v23, v21, s64, v250
	v_cvt_pk_fp8_f32 v21, v22, v23
	v_mul_f32_e32 v22, 0x41000000, v24
	v_mul_f32_e32 v23, 0x41000000, v25
	v_med3_f32 v22, v22, s64, v250
	v_med3_f32 v23, v23, s64, v250
	v_cvt_pk_fp8_f32 v21, v22, v23 op_sel:[0,0,1]
	v_lshlrev_b64 v[18:19], 10, v[180:181]
; __device__ __forceinline__ u32x4 pack8(const f32x4 a, const f32x4 b) { u32x4 w; w.x = cvt_pk_bf16(a[0], a[1]); w.y = cvt_pk_bf16(a[2], a[3]); w.z = cvt_pk_bf16(b[0], b[1]); w.w = cvt_pk_bf16(b[2], b[3]); return w; }
; __device__ __forceinline__ float sumsq4(const f32x4 v) { return (v[0] * v[0] + v[1] * v[1]) + (v[2] * v[2] + v[3] * v[3]); }
; __device__ __forceinline__ float xor16_add(float v) { return v + __int_as_float(__builtin_amdgcn_ds_swizzle(__float_as_int(v), 0x401F)); }
; __device__ __forceinline__ float xor32_add(float v) { auto rr = __builtin_amdgcn_permlane32_swap(__float_as_uint(v), __float_as_uint(v), false, false); return __uint_as_float(rr[0]) + __uint_as_float(rr[1]); }
; __device__ __forceinline__ f32x4 bf2f_lo(const u32x4 w, int h) { const unsigned a = h ? w.z : w.x, b = h ? w.w : w.y; return (f32x4){__uint_as_float(a << 16), __uint_as_float(a & 0xffff0000u), __uint_as_float(b << 16), __uint_as_float(b & 0xffff0000u)}; }
;     __device__ __forceinline__ void operator()(const f32x4 (&acc)[2][2][4][2], const Unit& u, int wr, int wc, int fr, int fq) const {
;     ...
;             for (int m = 0; m < 4; ++m) {
;                 const int row = row0 + ai * HALF + m * 16; float ss = 0.f;
; #pragma unroll
;                 for (int bj = 0; bj < 2; ++bj) {
;                     const f32x4 v0 = bf2f_lo(old[m][bj], 0) + acc[ai][bj][m][0], v1 = bf2f_lo(old[m][bj], 1) + acc[ai][bj][m][1];
;                     ss += sumsq4(v0) + sumsq4(v1);
;                     *(u32x4*)(xb + (size_t)row * DM + col0 + bj * HALF) = pack8(v0, v1);
;                     { u32x2 w8; w8.x = pack4_fp8_x8(v0); w8.y = pack4_fp8_x8(v1); *(u32x2*)(xq + (size_t)row * DM + col0 + bj * HALF) = w8; }
;                 }
;                 ss = xor32_add(xor16_add(ss));
;                 if (fq == 0) ssx[(size_t)row * 16 + u.pn * 4 + wc] = ss;
	v_cvt_pk_bf16_f32 v16, v16, v17
	v_cvt_pk_bf16_f32 v17, v24, v25
	v_lshl_add_u64 v[18:19], v[30:31], 0, v[18:19]
	global_store_dwordx4 v[182:183], v[14:17], off
	global_store_dwordx2 v[18:19], v[20:21], off
	s_nop 0
	v_lshlrev_b32_e32 v14, 16, v10
	v_and_b32_e32 v15, 0xffff0000, v10
	v_lshlrev_b32_e32 v10, 16, v11
	v_and_b32_e32 v11, 0xffff0000, v11
	v_pk_add_f32 v[16:17], v[120:121], v[10:11]
	v_pk_add_f32 v[14:15], v[118:119], v[14:15]
	v_lshlrev_b32_e32 v10, 16, v12
	v_and_b32_e32 v11, 0xffff0000, v12
	v_lshlrev_b32_e32 v12, 16, v13
	v_and_b32_e32 v13, 0xffff0000, v13
	v_pk_add_f32 v[20:21], v[116:117], v[12:13]
	v_pk_add_f32 v[12:13], v[114:115], v[10:11]
	v_mul_f32_e32 v10, v15, v15
	v_mul_f32_e32 v11, v17, v17
	v_fmac_f32_e32 v10, v14, v14
	v_fmac_f32_e32 v11, v16, v16
	v_add_f32_e32 v10, v10, v11
	v_mul_f32_e32 v11, v13, v13
	v_mul_f32_e32 v22, v21, v21
	v_fmac_f32_e32 v11, v12, v12
	v_fmac_f32_e32 v22, v20, v20
	v_add_f32_e32 v11, v11, v22
	v_add_f32_e32 v10, v10, v11
	v_add_f32_e32 v22, v26, v10
	v_cvt_pk_bf16_f32 v10, v14, v15
	v_mul_f32_e32 v14, 0x41000000, v14
	v_med3_f32 v23, v14, s64, v250
	v_mul_f32_e32 v14, 0x41000000, v15
	v_med3_f32 v15, v14, s64, v250
	v_cvt_pk_fp8_f32 v14, v23, v15
	v_cvt_pk_bf16_f32 v11, v16, v17
	v_mul_f32_e32 v15, 0x41000000, v16
	v_mul_f32_e32 v16, 0x41000000, v17
	v_med3_f32 v15, v15, s64, v250
	v_med3_f32 v16, v16, s64, v250
	v_cvt_pk_fp8_f32 v14, v15, v16 op_sel:[0,0,1]
	v_mul_f32_e32 v15, 0x41000000, v12
	v_med3_f32 v16, v15, s64, v250
	v_mul_f32_e32 v15, 0x41000000, v13
	v_med3_f32 v17, v15, s64, v250
	v_cvt_pk_fp8_f32 v15, v16, v17
	v_mul_f32_e32 v16, 0x41000000, v20
	v_mul_f32_e32 v17, 0x41000000, v21
	v_med3_f32 v16, v16, s64, v250
	v_med3_f32 v17, v17, s64, v250
	v_cvt_pk_fp8_f32 v15, v16, v17 op_sel:[0,0,1]
	ds_swizzle_b32 v16, v22 offset:swizzle(SWAP,16)
	v_cvt_pk_bf16_f32 v12, v12, v13
	v_cvt_pk_bf16_f32 v13, v20, v21
	global_store_dwordx4 v[182:183], v[10:13], off offset:256
	global_store_dwordx2 v[18:19], v[14:15], off offset:128
	s_waitcnt lgkmcnt(0)
	v_add_f32_e32 v10, v22, v16
	v_mov_b32_e32 v11, v10
	s_nop 1
	v_permlane32_swap_b32_e32 v10, v11
	s_and_saveexec_b64 s[28:29], s[2:3]
	s_cbranch_execz .LBB0_1867
	v_lshlrev_b64 v[12:13], 6, v[180:181]
	v_lshl_add_u64 v[12:13], s[26:27], 0, v[12:13]
	v_add_f32_e32 v10, v10, v11
	global_store_dword v[12:13], v10, off
.LBB0_1867:
	s_or_b64 exec, exec, s[28:29]
	v_lshlrev_b32_e32 v12, 16, v6
	v_and_b32_e32 v13, 0xffff0000, v6
	v_lshlrev_b32_e32 v6, 16, v7
	v_and_b32_e32 v7, 0xffff0000, v7
	v_pk_add_f32 v[14:15], v[112:113], v[6:7]
	v_pk_add_f32 v[12:13], v[110:111], v[12:13]
	v_lshlrev_b32_e32 v6, 16, v8
	v_and_b32_e32 v7, 0xffff0000, v8
	v_lshlrev_b32_e32 v8, 16, v9
	v_and_b32_e32 v9, 0xffff0000, v9
	v_pk_add_f32 v[16:17], v[108:109], v[8:9]
	v_pk_add_f32 v[8:9], v[106:107], v[6:7]
	v_mul_f32_e32 v6, v13, v13
	v_mul_f32_e32 v7, v15, v15
	v_fmac_f32_e32 v6, v12, v12
	v_fmac_f32_e32 v7, v14, v14
	v_add_f32_e32 v6, v6, v7
	v_mul_f32_e32 v7, v9, v9
	v_mul_f32_e32 v18, v17, v17
	v_fmac_f32_e32 v7, v8, v8
	v_fmac_f32_e32 v18, v16, v16
	v_add_f32_e32 v7, v7, v18
	v_add_f32_e32 v18, v6, v7
	v_cvt_pk_bf16_f32 v6, v12, v13
	v_mul_f32_e32 v12, 0x41000000, v12
	v_med3_f32 v19, v12, s64, v250
	v_mul_f32_e32 v12, 0x41000000, v13
	v_med3_f32 v13, v12, s64, v250
	v_cvt_pk_fp8_f32 v12, v19, v13
	v_cvt_pk_bf16_f32 v7, v14, v15
	v_mul_f32_e32 v13, 0x41000000, v14
	v_mul_f32_e32 v14, 0x41000000, v15
	v_med3_f32 v13, v13, s64, v250
	v_med3_f32 v14, v14, s64, v250
	v_cvt_pk_fp8_f32 v12, v13, v14 op_sel:[0,0,1]
	v_mul_f32_e32 v13, 0x41000000, v8
	v_med3_f32 v14, v13, s64, v250
	v_mul_f32_e32 v13, 0x41000000, v9
	v_med3_f32 v15, v13, s64, v250
	v_cvt_pk_fp8_f32 v13, v14, v15
	v_mul_f32_e32 v14, 0x41000000, v16
	v_mul_f32_e32 v15, 0x41000000, v17
	v_med3_f32 v14, v14, s64, v250
	v_med3_f32 v15, v15, s64, v250
	v_cvt_pk_fp8_f32 v13, v14, v15 op_sel:[0,0,1]
	v_lshlrev_b64 v[10:11], 10, v[176:177]
	v_cvt_pk_bf16_f32 v8, v8, v9
	v_cvt_pk_bf16_f32 v9, v16, v17
	v_lshl_add_u64 v[10:11], v[30:31], 0, v[10:11]
	global_store_dwordx4 v[178:179], v[6:9], off
	global_store_dwordx2 v[10:11], v[12:13], off
	s_nop 0
	v_lshlrev_b32_e32 v6, 16, v2
	v_and_b32_e32 v7, 0xffff0000, v2
	v_lshlrev_b32_e32 v2, 16, v3
	v_and_b32_e32 v3, 0xffff0000, v3
	v_pk_add_f32 v[8:9], v[104:105], v[2:3]
	v_pk_add_f32 v[6:7], v[102:103], v[6:7]
	v_lshlrev_b32_e32 v2, 16, v4
	v_and_b32_e32 v3, 0xffff0000, v4
	v_lshlrev_b32_e32 v4, 16, v5
	v_and_b32_e32 v5, 0xffff0000, v5
	v_pk_add_f32 v[12:13], v[100:101], v[4:5]
	v_pk_add_f32 v[4:5], v[98:99], v[2:3]
	v_mul_f32_e32 v2, v7, v7
	v_mul_f32_e32 v3, v9, v9
	v_fmac_f32_e32 v2, v6, v6
	v_fmac_f32_e32 v3, v8, v8
	v_add_f32_e32 v2, v2, v3
	v_mul_f32_e32 v3, v5, v5
	v_mul_f32_e32 v14, v13, v13
	v_fmac_f32_e32 v3, v4, v4
	v_fmac_f32_e32 v14, v12, v12
	v_add_f32_e32 v3, v3, v14
	v_add_f32_e32 v2, v2, v3
	v_add_f32_e32 v14, v18, v2
	v_cvt_pk_bf16_f32 v2, v6, v7
	v_mul_f32_e32 v6, 0x41000000, v6
	v_med3_f32 v15, v6, s64, v250
	v_mul_f32_e32 v6, 0x41000000, v7
	v_med3_f32 v7, v6, s64, v250
	v_cvt_pk_fp8_f32 v6, v15, v7
	v_cvt_pk_bf16_f32 v3, v8, v9
	v_mul_f32_e32 v7, 0x41000000, v8
	v_mul_f32_e32 v8, 0x41000000, v9
	v_med3_f32 v7, v7, s64, v250
	v_med3_f32 v8, v8, s64, v250
	v_cvt_pk_fp8_f32 v6, v7, v8 op_sel:[0,0,1]
	v_mul_f32_e32 v7, 0x41000000, v4
	v_med3_f32 v8, v7, s64, v250
	v_mul_f32_e32 v7, 0x41000000, v5
	v_med3_f32 v9, v7, s64, v250
	v_cvt_pk_fp8_f32 v7, v8, v9
	v_mul_f32_e32 v8, 0x41000000, v12
	v_mul_f32_e32 v9, 0x41000000, v13
	v_med3_f32 v8, v8, s64, v250
	v_med3_f32 v9, v9, s64, v250
	v_cvt_pk_fp8_f32 v7, v8, v9 op_sel:[0,0,1]
	ds_swizzle_b32 v8, v14 offset:swizzle(SWAP,16)
	v_cvt_pk_bf16_f32 v4, v4, v5
	v_cvt_pk_bf16_f32 v5, v12, v13
	global_store_dwordx4 v[178:179], v[2:5], off offset:256
	global_store_dwordx2 v[10:11], v[6:7], off offset:128
	s_waitcnt lgkmcnt(0)
	v_add_f32_e32 v2, v14, v8
	v_mov_b32_e32 v3, v2
	s_nop 1
	v_permlane32_swap_b32_e32 v2, v3
	s_and_saveexec_b64 s[28:29], s[2:3]
	s_cbranch_execz .LBB0_1869
	v_lshlrev_b64 v[4:5], 6, v[176:177]
	v_lshl_add_u64 v[4:5], s[26:27], 0, v[4:5]
	v_add_f32_e32 v2, v2, v3
	global_store_dword v[4:5], v2, off
; __device__ __forceinline__ u32x4 pack8(const f32x4 a, const f32x4 b) { u32x4 w; w.x = cvt_pk_bf16(a[0], a[1]); w.y = cvt_pk_bf16(a[2], a[3]); w.z = cvt_pk_bf16(b[0], b[1]); w.w = cvt_pk_bf16(b[2], b[3]); return w; }
; __device__ __forceinline__ float sumsq4(const f32x4 v) { return (v[0] * v[0] + v[1] * v[1]) + (v[2] * v[2] + v[3] * v[3]); }
; __device__ __forceinline__ float xor16_add(float v) { return v + __int_as_float(__builtin_amdgcn_ds_swizzle(__float_as_int(v), 0x401F)); }
; __device__ __forceinline__ float xor32_add(float v) { auto rr = __builtin_amdgcn_permlane32_swap(__float_as_uint(v), __float_as_uint(v), false, false); return __uint_as_float(rr[0]) + __uint_as_float(rr[1]); }
; __device__ __forceinline__ f32x4 bf2f_lo(const u32x4 w, int h) { const unsigned a = h ? w.z : w.x, b = h ? w.w : w.y; return (f32x4){__uint_as_float(a << 16), __uint_as_float(a & 0xffff0000u), __uint_as_float(b << 16), __uint_as_float(b & 0xffff0000u)}; }
;     __device__ __forceinline__ void operator()(const f32x4 (&acc)[2][2][4][2], const Unit& u, int wr, int wc, int fr, int fq) const {
;     ...
;             for (int m = 0; m < 4; ++m) {
;                 const int row = row0 + ai * HALF + m * 16; float ss = 0.f;
; #pragma unroll
;                 for (int bj = 0; bj < 2; ++bj) {
;                     const f32x4 v0 = bf2f_lo(old[m][bj], 0) + acc[ai][bj][m][0], v1 = bf2f_lo(old[m][bj], 1) + acc[ai][bj][m][1];
;                     ss += sumsq4(v0) + sumsq4(v1);
;                     *(u32x4*)(xb + (size_t)row * DM + col0 + bj * HALF) = pack8(v0, v1);
;                     { u32x2 w8; w8.x = pack4_fp8_x8(v0); w8.y = pack4_fp8_x8(v1); *(u32x2*)(xq + (size_t)row * DM + col0 + bj * HALF) = w8; }
;                 }
;                 ss = xor32_add(xor16_add(ss));
;                 if (fq == 0) ssx[(size_t)row * 16 + u.pn * 4 + wc] = ss;
.LBB0_1869:
	s_or_b64 exec, exec, s[28:29]
	v_add_u32_e32 v108, 0x80, v32
	v_ashrrev_i32_e32 v109, 31, v108
	v_lshlrev_b64 v[2:3], 11, v[108:109]
	v_lshl_add_u64 v[110:111], v[174:175], 0, v[2:3]
	global_load_dwordx4 v[114:117], v[110:111], off
	global_load_dwordx4 v[26:29], v[110:111], off offset:256
	v_add_u32_e32 v104, 0x90, v32
	v_ashrrev_i32_e32 v105, 31, v104
	v_add_u32_e32 v100, 0xa0, v32
	v_lshlrev_b64 v[2:3], 11, v[104:105]
	v_ashrrev_i32_e32 v101, 31, v100
	v_add_u32_e32 v32, 0xb0, v32
	v_lshl_add_u64 v[106:107], v[174:175], 0, v[2:3]
	v_lshlrev_b64 v[2:3], 11, v[100:101]
	v_ashrrev_i32_e32 v33, 31, v32
	v_lshl_add_u64 v[102:103], v[174:175], 0, v[2:3]
	v_lshlrev_b64 v[2:3], 11, v[32:33]
	v_lshl_add_u64 v[98:99], v[174:175], 0, v[2:3]
	global_load_dwordx4 v[22:25], v[106:107], off
	global_load_dwordx4 v[18:21], v[106:107], off offset:256
	global_load_dwordx4 v[14:17], v[102:103], off
	global_load_dwordx4 v[10:13], v[102:103], off offset:256
	global_load_dwordx4 v[6:9], v[98:99], off
	global_load_dwordx4 v[2:5], v[98:99], off offset:256
	v_lshlrev_b64 v[112:113], 10, v[108:109]
	v_lshl_add_u64 v[112:113], v[30:31], 0, v[112:113]
	s_waitcnt vmcnt(7)
	v_lshlrev_b32_e32 v118, 16, v114
	v_and_b32_e32 v119, 0xffff0000, v114
	v_lshlrev_b32_e32 v114, 16, v115
	v_and_b32_e32 v115, 0xffff0000, v115
	v_pk_add_f32 v[114:115], v[96:97], v[114:115]
	v_pk_add_f32 v[118:119], v[94:95], v[118:119]
	v_lshlrev_b32_e32 v94, 16, v116
	v_and_b32_e32 v95, 0xffff0000, v116
	v_lshlrev_b32_e32 v96, 16, v117
	v_and_b32_e32 v97, 0xffff0000, v117
	v_pk_add_f32 v[116:117], v[90:91], v[94:95]
	v_mul_f32_e32 v90, v119, v119
	v_mul_f32_e32 v91, v115, v115
	v_pk_add_f32 v[92:93], v[92:93], v[96:97]
	v_fmac_f32_e32 v90, v118, v118
	v_fmac_f32_e32 v91, v114, v114
	v_add_f32_e32 v90, v90, v91
	v_mul_f32_e32 v91, v117, v117
	v_mul_f32_e32 v94, v93, v93
	v_fmac_f32_e32 v91, v116, v116
	v_fmac_f32_e32 v94, v92, v92
	v_add_f32_e32 v91, v91, v94
	v_cvt_pk_bf16_f32 v94, v118, v119
	v_add_f32_e32 v90, v90, v91
	v_cvt_pk_bf16_f32 v95, v114, v115
	v_cvt_pk_bf16_f32 v96, v116, v117
	v_cvt_pk_bf16_f32 v97, v92, v93
	global_store_dwordx4 v[110:111], v[94:97], off
	v_mul_f32_e32 v91, 0x41000000, v118
	v_med3_f32 v91, v91, s64, v250
	v_mul_f32_e32 v94, 0x41000000, v119
	v_med3_f32 v95, v94, s64, v250
	v_cvt_pk_fp8_f32 v94, v91, v95
	v_mul_f32_e32 v91, 0x41000000, v114
	v_mul_f32_e32 v95, 0x41000000, v115
	v_med3_f32 v91, v91, s64, v250
	v_med3_f32 v95, v95, s64, v250
	v_cvt_pk_fp8_f32 v94, v91, v95 op_sel:[0,0,1]
	v_mul_f32_e32 v91, 0x41000000, v116
	v_mul_f32_e32 v95, 0x41000000, v117
	v_med3_f32 v91, v91, s64, v250
	v_med3_f32 v96, v95, s64, v250
	v_cvt_pk_fp8_f32 v95, v91, v96
	v_mul_f32_e32 v91, 0x41000000, v92
	v_mul_f32_e32 v92, 0x41000000, v93
	v_med3_f32 v91, v91, s64, v250
	v_med3_f32 v92, v92, s64, v250
	v_cvt_pk_fp8_f32 v95, v91, v92 op_sel:[0,0,1]
	s_waitcnt vmcnt(7)
	v_lshlrev_b32_e32 v92, 16, v26
	v_and_b32_e32 v93, 0xffff0000, v26
	v_lshlrev_b32_e32 v26, 16, v27
	v_and_b32_e32 v27, 0xffff0000, v27
	v_pk_add_f32 v[26:27], v[88:89], v[26:27]
	v_pk_add_f32 v[86:87], v[86:87], v[92:93]
	v_lshlrev_b32_e32 v88, 16, v28
	v_and_b32_e32 v89, 0xffff0000, v28
	v_lshlrev_b32_e32 v28, 16, v29
	v_and_b32_e32 v29, 0xffff0000, v29
	v_pk_add_f32 v[88:89], v[82:83], v[88:89]
	v_mul_f32_e32 v82, v87, v87
	v_mul_f32_e32 v83, v27, v27
	v_pk_add_f32 v[28:29], v[84:85], v[28:29]
	v_fmac_f32_e32 v82, v86, v86
	v_fmac_f32_e32 v83, v26, v26
	v_add_f32_e32 v82, v82, v83
	v_mul_f32_e32 v83, v89, v89
	v_mul_f32_e32 v84, v29, v29
	v_fmac_f32_e32 v83, v88, v88
	v_fmac_f32_e32 v84, v28, v28
	v_add_f32_e32 v83, v83, v84
	v_add_f32_e32 v82, v82, v83
	global_store_dwordx2 v[112:113], v[94:95], off
	v_add_f32_e32 v90, v90, v82
	v_cvt_pk_bf16_f32 v82, v86, v87
	v_cvt_pk_bf16_f32 v83, v26, v27
	v_cvt_pk_bf16_f32 v84, v88, v89
	v_cvt_pk_bf16_f32 v85, v28, v29
	global_store_dwordx4 v[110:111], v[82:85], off offset:256
	v_mul_f32_e32 v26, 0x41000000, v26
	v_mul_f32_e32 v27, 0x41000000, v27
	v_mul_f32_e32 v82, 0x41000000, v86
	v_med3_f32 v83, v82, s64, v250
	v_mul_f32_e32 v82, 0x41000000, v87
	v_med3_f32 v84, v82, s64, v250
	v_cvt_pk_fp8_f32 v82, v83, v84
	v_med3_f32 v26, v26, s64, v250
	v_med3_f32 v27, v27, s64, v250
	v_cvt_pk_fp8_f32 v82, v26, v27 op_sel:[0,0,1]
	v_mul_f32_e32 v26, 0x41000000, v88
	v_mul_f32_e32 v27, 0x41000000, v89
	v_med3_f32 v26, v26, s64, v250
	v_med3_f32 v27, v27, s64, v250
	v_cvt_pk_fp8_f32 v83, v26, v27
	v_mul_f32_e32 v26, 0x41000000, v28
	v_mul_f32_e32 v27, 0x41000000, v29
	v_med3_f32 v26, v26, s64, v250
	v_med3_f32 v27, v27, s64, v250
	v_cvt_pk_fp8_f32 v83, v26, v27 op_sel:[0,0,1]
	ds_swizzle_b32 v26, v90 offset:swizzle(SWAP,16)
	global_store_dwordx2 v[112:113], v[82:83], off offset:128
	s_waitcnt lgkmcnt(0)
	v_add_f32_e32 v26, v90, v26
	v_mov_b32_e32 v27, v26
	s_nop 1
	v_permlane32_swap_b32_e32 v26, v27
	s_and_saveexec_b64 s[28:29], s[2:3]
	s_cbranch_execz .LBB0_1871
	v_lshlrev_b64 v[28:29], 6, v[108:109]
	v_lshl_add_u64 v[28:29], s[26:27], 0, v[28:29]
	v_add_f32_e32 v26, v26, v27
	global_store_dword v[28:29], v26, off
; __device__ __forceinline__ u32x4 pack8(const f32x4 a, const f32x4 b) { u32x4 w; w.x = cvt_pk_bf16(a[0], a[1]); w.y = cvt_pk_bf16(a[2], a[3]); w.z = cvt_pk_bf16(b[0], b[1]); w.w = cvt_pk_bf16(b[2], b[3]); return w; }
; __device__ __forceinline__ float sumsq4(const f32x4 v) { return (v[0] * v[0] + v[1] * v[1]) + (v[2] * v[2] + v[3] * v[3]); }
; __device__ __forceinline__ float xor16_add(float v) { return v + __int_as_float(__builtin_amdgcn_ds_swizzle(__float_as_int(v), 0x401F)); }
; __device__ __forceinline__ float xor32_add(float v) { auto rr = __builtin_amdgcn_permlane32_swap(__float_as_uint(v), __float_as_uint(v), false, false); return __uint_as_float(rr[0]) + __uint_as_float(rr[1]); }
; __device__ __forceinline__ f32x4 bf2f_lo(const u32x4 w, int h) { const unsigned a = h ? w.z : w.x, b = h ? w.w : w.y; return (f32x4){__uint_as_float(a << 16), __uint_as_float(a & 0xffff0000u), __uint_as_float(b << 16), __uint_as_float(b & 0xffff0000u)}; }
;     __device__ __forceinline__ void operator()(const f32x4 (&acc)[2][2][4][2], const Unit& u, int wr, int wc, int fr, int fq) const {
;     ...
;             for (int m = 0; m < 4; ++m) {
;                 const int row = row0 + ai * HALF + m * 16; float ss = 0.f;
; #pragma unroll
;                 for (int bj = 0; bj < 2; ++bj) {
;                     const f32x4 v0 = bf2f_lo(old[m][bj], 0) + acc[ai][bj][m][0], v1 = bf2f_lo(old[m][bj], 1) + acc[ai][bj][m][1];
;                     ss += sumsq4(v0) + sumsq4(v1);
;                     *(u32x4*)(xb + (size_t)row * DM + col0 + bj * HALF) = pack8(v0, v1);
;                     { u32x2 w8; w8.x = pack4_fp8_x8(v0); w8.y = pack4_fp8_x8(v1); *(u32x2*)(xq + (size_t)row * DM + col0 + bj * HALF) = w8; }
;                 }
;                 ss = xor32_add(xor16_add(ss));
;                 if (fq == 0) ssx[(size_t)row * 16 + u.pn * 4 + wc] = ss;
.LBB0_1871:
	s_or_b64 exec, exec, s[28:29]
	s_waitcnt vmcnt(9)
	v_lshlrev_b32_e32 v28, 16, v22
	v_and_b32_e32 v29, 0xffff0000, v22
	v_lshlrev_b32_e32 v22, 16, v23
	v_and_b32_e32 v23, 0xffff0000, v23
	v_pk_add_f32 v[80:81], v[80:81], v[22:23]
	v_pk_add_f32 v[28:29], v[78:79], v[28:29]
	v_lshlrev_b32_e32 v22, 16, v24
	v_and_b32_e32 v23, 0xffff0000, v24
	v_lshlrev_b32_e32 v24, 16, v25
	v_and_b32_e32 v25, 0xffff0000, v25
	v_pk_add_f32 v[76:77], v[76:77], v[24:25]
	v_pk_add_f32 v[24:25], v[74:75], v[22:23]
	v_mul_f32_e32 v22, v29, v29
	v_mul_f32_e32 v23, v81, v81
	v_fmac_f32_e32 v22, v28, v28
	v_fmac_f32_e32 v23, v80, v80
	v_add_f32_e32 v22, v22, v23
	v_mul_f32_e32 v23, v25, v25
	v_mul_f32_e32 v74, v77, v77
	v_fmac_f32_e32 v23, v24, v24
	v_fmac_f32_e32 v74, v76, v76
	v_add_f32_e32 v23, v23, v74
	v_add_f32_e32 v74, v22, v23
	v_cvt_pk_bf16_f32 v22, v28, v29
	v_mul_f32_e32 v28, 0x41000000, v28
	v_med3_f32 v75, v28, s64, v250
	v_mul_f32_e32 v28, 0x41000000, v29
	v_med3_f32 v29, v28, s64, v250
	v_cvt_pk_fp8_f32 v28, v75, v29
	v_mul_f32_e32 v29, 0x41000000, v80
	v_mul_f32_e32 v75, 0x41000000, v81
	v_med3_f32 v29, v29, s64, v250
	v_med3_f32 v75, v75, s64, v250
	v_cvt_pk_fp8_f32 v28, v29, v75 op_sel:[0,0,1]
	v_mul_f32_e32 v29, 0x41000000, v24
	v_med3_f32 v75, v29, s64, v250
	v_mul_f32_e32 v29, 0x41000000, v25
	v_med3_f32 v78, v29, s64, v250
	v_cvt_pk_fp8_f32 v29, v75, v78
	v_mul_f32_e32 v75, 0x41000000, v76
	v_mul_f32_e32 v78, 0x41000000, v77
	v_med3_f32 v75, v75, s64, v250
	v_med3_f32 v78, v78, s64, v250
	v_cvt_pk_fp8_f32 v29, v75, v78 op_sel:[0,0,1]
	v_lshlrev_b64 v[26:27], 10, v[104:105]
	v_cvt_pk_bf16_f32 v23, v80, v81
	v_cvt_pk_bf16_f32 v24, v24, v25
	v_cvt_pk_bf16_f32 v25, v76, v77
	v_lshl_add_u64 v[26:27], v[30:31], 0, v[26:27]
	global_store_dwordx4 v[106:107], v[22:25], off
	global_store_dwordx2 v[26:27], v[28:29], off
	s_waitcnt vmcnt(10)
	v_lshlrev_b32_e32 v22, 16, v18
	v_and_b32_e32 v23, 0xffff0000, v18
	v_lshlrev_b32_e32 v18, 16, v19
	v_and_b32_e32 v19, 0xffff0000, v19
	v_pk_add_f32 v[24:25], v[72:73], v[18:19]
	v_pk_add_f32 v[22:23], v[70:71], v[22:23]
	v_lshlrev_b32_e32 v18, 16, v20
	v_and_b32_e32 v19, 0xffff0000, v20
	v_lshlrev_b32_e32 v20, 16, v21
	v_and_b32_e32 v21, 0xffff0000, v21
	v_pk_add_f32 v[28:29], v[68:69], v[20:21]
	v_pk_add_f32 v[20:21], v[66:67], v[18:19]
	v_mul_f32_e32 v18, v23, v23
	v_mul_f32_e32 v19, v25, v25
	v_fmac_f32_e32 v18, v22, v22
	v_fmac_f32_e32 v19, v24, v24
	v_add_f32_e32 v18, v18, v19
	v_mul_f32_e32 v19, v21, v21
	v_mul_f32_e32 v66, v29, v29
	v_fmac_f32_e32 v19, v20, v20
	v_fmac_f32_e32 v66, v28, v28
	v_add_f32_e32 v19, v19, v66
	v_add_f32_e32 v18, v18, v19
	v_add_f32_e32 v66, v74, v18
	v_cvt_pk_bf16_f32 v18, v22, v23
	v_mul_f32_e32 v22, 0x41000000, v22
	v_med3_f32 v67, v22, s64, v250
	v_mul_f32_e32 v22, 0x41000000, v23
	v_med3_f32 v23, v22, s64, v250
	v_cvt_pk_fp8_f32 v22, v67, v23
	v_cvt_pk_bf16_f32 v19, v24, v25
	v_mul_f32_e32 v23, 0x41000000, v24
	v_mul_f32_e32 v24, 0x41000000, v25
	v_med3_f32 v23, v23, s64, v250
	v_med3_f32 v24, v24, s64, v250
	v_cvt_pk_fp8_f32 v22, v23, v24 op_sel:[0,0,1]
	v_mul_f32_e32 v23, 0x41000000, v20
	v_med3_f32 v24, v23, s64, v250
	v_mul_f32_e32 v23, 0x41000000, v21
	v_med3_f32 v25, v23, s64, v250
	v_cvt_pk_fp8_f32 v23, v24, v25
	v_mul_f32_e32 v24, 0x41000000, v28
	v_mul_f32_e32 v25, 0x41000000, v29
	v_med3_f32 v24, v24, s64, v250
	v_med3_f32 v25, v25, s64, v250
	v_cvt_pk_fp8_f32 v23, v24, v25 op_sel:[0,0,1]
	ds_swizzle_b32 v24, v66 offset:swizzle(SWAP,16)
	v_cvt_pk_bf16_f32 v20, v20, v21
	v_cvt_pk_bf16_f32 v21, v28, v29
	global_store_dwordx4 v[106:107], v[18:21], off offset:256
	global_store_dwordx2 v[26:27], v[22:23], off offset:128
	s_waitcnt lgkmcnt(0)
	v_add_f32_e32 v18, v66, v24
	v_mov_b32_e32 v19, v18
	s_nop 1
	v_permlane32_swap_b32_e32 v18, v19
	s_and_saveexec_b64 s[28:29], s[2:3]
	s_cbranch_execz .LBB0_1873
	v_lshlrev_b64 v[20:21], 6, v[104:105]
	v_lshl_add_u64 v[20:21], s[26:27], 0, v[20:21]
	v_add_f32_e32 v18, v18, v19
	global_store_dword v[20:21], v18, off
.LBB0_1873:
	s_or_b64 exec, exec, s[28:29]
	s_waitcnt vmcnt(11)
	v_lshlrev_b32_e32 v20, 16, v14
	v_and_b32_e32 v21, 0xffff0000, v14
	v_lshlrev_b32_e32 v14, 16, v15
	v_and_b32_e32 v15, 0xffff0000, v15
	v_pk_add_f32 v[22:23], v[64:65], v[14:15]
	v_pk_add_f32 v[20:21], v[62:63], v[20:21]
	v_lshlrev_b32_e32 v14, 16, v16
	v_and_b32_e32 v15, 0xffff0000, v16
	v_lshlrev_b32_e32 v16, 16, v17
	v_and_b32_e32 v17, 0xffff0000, v17
	v_pk_add_f32 v[24:25], v[60:61], v[16:17]
	v_pk_add_f32 v[16:17], v[58:59], v[14:15]
	v_mul_f32_e32 v14, v21, v21
	v_mul_f32_e32 v15, v23, v23
	v_fmac_f32_e32 v14, v20, v20
	v_fmac_f32_e32 v15, v22, v22
	v_add_f32_e32 v14, v14, v15
	v_mul_f32_e32 v15, v17, v17
	v_mul_f32_e32 v26, v25, v25
	v_fmac_f32_e32 v15, v16, v16
	v_fmac_f32_e32 v26, v24, v24
	v_add_f32_e32 v15, v15, v26
	v_add_f32_e32 v26, v14, v15
	v_cvt_pk_bf16_f32 v14, v20, v21
	v_mul_f32_e32 v20, 0x41000000, v20
	v_med3_f32 v27, v20, s64, v250
	v_mul_f32_e32 v20, 0x41000000, v21
	v_med3_f32 v21, v20, s64, v250
	v_cvt_pk_fp8_f32 v20, v27, v21
	v_cvt_pk_bf16_f32 v15, v22, v23
	v_mul_f32_e32 v21, 0x41000000, v22
	v_mul_f32_e32 v22, 0x41000000, v23
	v_med3_f32 v21, v21, s64, v250
	v_med3_f32 v22, v22, s64, v250
	v_cvt_pk_fp8_f32 v20, v21, v22 op_sel:[0,0,1]
	v_mul_f32_e32 v21, 0x41000000, v16
	v_med3_f32 v22, v21, s64, v250
	v_mul_f32_e32 v21, 0x41000000, v17
	v_med3_f32 v23, v21, s64, v250
	v_cvt_pk_fp8_f32 v21, v22, v23
	v_mul_f32_e32 v22, 0x41000000, v24
	v_mul_f32_e32 v23, 0x41000000, v25
	v_med3_f32 v22, v22, s64, v250
	v_med3_f32 v23, v23, s64, v250
	v_cvt_pk_fp8_f32 v21, v22, v23 op_sel:[0,0,1]
	v_lshlrev_b64 v[18:19], 10, v[100:101]
	v_cvt_pk_bf16_f32 v16, v16, v17
	v_cvt_pk_bf16_f32 v17, v24, v25
	v_lshl_add_u64 v[18:19], v[30:31], 0, v[18:19]
	global_store_dwordx4 v[102:103], v[14:17], off
	global_store_dwordx2 v[18:19], v[20:21], off
	s_waitcnt vmcnt(12)
; __device__ __forceinline__ u32x4 pack8(const f32x4 a, const f32x4 b) { u32x4 w; w.x = cvt_pk_bf16(a[0], a[1]); w.y = cvt_pk_bf16(a[2], a[3]); w.z = cvt_pk_bf16(b[0], b[1]); w.w = cvt_pk_bf16(b[2], b[3]); return w; }
; __device__ __forceinline__ float sumsq4(const f32x4 v) { return (v[0] * v[0] + v[1] * v[1]) + (v[2] * v[2] + v[3] * v[3]); }
; __device__ __forceinline__ float xor16_add(float v) { return v + __int_as_float(__builtin_amdgcn_ds_swizzle(__float_as_int(v), 0x401F)); }
; __device__ __forceinline__ float xor32_add(float v) { auto rr = __builtin_amdgcn_permlane32_swap(__float_as_uint(v), __float_as_uint(v), false, false); return __uint_as_float(rr[0]) + __uint_as_float(rr[1]); }
; __device__ __forceinline__ f32x4 bf2f_lo(const u32x4 w, int h) { const unsigned a = h ? w.z : w.x, b = h ? w.w : w.y; return (f32x4){__uint_as_float(a << 16), __uint_as_float(a & 0xffff0000u), __uint_as_float(b << 16), __uint_as_float(b & 0xffff0000u)}; }
;     __device__ __forceinline__ void operator()(const f32x4 (&acc)[2][2][4][2], const Unit& u, int wr, int wc, int fr, int fq) const {
;     ...
;             for (int m = 0; m < 4; ++m) {
;                 const int row = row0 + ai * HALF + m * 16; float ss = 0.f;
; #pragma unroll
;                 for (int bj = 0; bj < 2; ++bj) {
;                     const f32x4 v0 = bf2f_lo(old[m][bj], 0) + acc[ai][bj][m][0], v1 = bf2f_lo(old[m][bj], 1) + acc[ai][bj][m][1];
;                     ss += sumsq4(v0) + sumsq4(v1);
;                     *(u32x4*)(xb + (size_t)row * DM + col0 + bj * HALF) = pack8(v0, v1);
;                     { u32x2 w8; w8.x = pack4_fp8_x8(v0); w8.y = pack4_fp8_x8(v1); *(u32x2*)(xq + (size_t)row * DM + col0 + bj * HALF) = w8; }
;                 }
;                 ss = xor32_add(xor16_add(ss));
;                 if (fq == 0) ssx[(size_t)row * 16 + u.pn * 4 + wc] = ss;
	v_lshlrev_b32_e32 v14, 16, v10
	v_and_b32_e32 v15, 0xffff0000, v10
	v_lshlrev_b32_e32 v10, 16, v11
	v_and_b32_e32 v11, 0xffff0000, v11
	v_pk_add_f32 v[16:17], v[56:57], v[10:11]
	v_pk_add_f32 v[14:15], v[54:55], v[14:15]
	v_lshlrev_b32_e32 v10, 16, v12
	v_and_b32_e32 v11, 0xffff0000, v12
	v_lshlrev_b32_e32 v12, 16, v13
	v_and_b32_e32 v13, 0xffff0000, v13
	v_pk_add_f32 v[20:21], v[52:53], v[12:13]
	v_pk_add_f32 v[12:13], v[50:51], v[10:11]
	v_mul_f32_e32 v10, v15, v15
	v_mul_f32_e32 v11, v17, v17
	v_fmac_f32_e32 v10, v14, v14
	v_fmac_f32_e32 v11, v16, v16
	v_add_f32_e32 v10, v10, v11
	v_mul_f32_e32 v11, v13, v13
	v_mul_f32_e32 v22, v21, v21
	v_fmac_f32_e32 v11, v12, v12
	v_fmac_f32_e32 v22, v20, v20
	v_add_f32_e32 v11, v11, v22
	v_add_f32_e32 v10, v10, v11
	v_add_f32_e32 v22, v26, v10
	v_cvt_pk_bf16_f32 v10, v14, v15
	v_mul_f32_e32 v14, 0x41000000, v14
	v_med3_f32 v23, v14, s64, v250
	v_mul_f32_e32 v14, 0x41000000, v15
	v_med3_f32 v15, v14, s64, v250
	v_cvt_pk_fp8_f32 v14, v23, v15
	v_cvt_pk_bf16_f32 v11, v16, v17
	v_mul_f32_e32 v15, 0x41000000, v16
	v_mul_f32_e32 v16, 0x41000000, v17
	v_med3_f32 v15, v15, s64, v250
	v_med3_f32 v16, v16, s64, v250
	v_cvt_pk_fp8_f32 v14, v15, v16 op_sel:[0,0,1]
	v_mul_f32_e32 v15, 0x41000000, v12
	v_med3_f32 v16, v15, s64, v250
	v_mul_f32_e32 v15, 0x41000000, v13
	v_med3_f32 v17, v15, s64, v250
	v_cvt_pk_fp8_f32 v15, v16, v17
	v_mul_f32_e32 v16, 0x41000000, v20
	v_mul_f32_e32 v17, 0x41000000, v21
	v_med3_f32 v16, v16, s64, v250
	v_med3_f32 v17, v17, s64, v250
	v_cvt_pk_fp8_f32 v15, v16, v17 op_sel:[0,0,1]
	ds_swizzle_b32 v16, v22 offset:swizzle(SWAP,16)
	v_cvt_pk_bf16_f32 v12, v12, v13
	v_cvt_pk_bf16_f32 v13, v20, v21
	global_store_dwordx4 v[102:103], v[10:13], off offset:256
	global_store_dwordx2 v[18:19], v[14:15], off offset:128
	s_waitcnt lgkmcnt(0)
	v_add_f32_e32 v10, v22, v16
	v_mov_b32_e32 v11, v10
	s_nop 1
	v_permlane32_swap_b32_e32 v10, v11
	s_and_saveexec_b64 s[28:29], s[2:3]
	s_cbranch_execz .LBB0_1875
	v_lshlrev_b64 v[12:13], 6, v[100:101]
	v_lshl_add_u64 v[12:13], s[26:27], 0, v[12:13]
	v_add_f32_e32 v10, v10, v11
	global_store_dword v[12:13], v10, off
.LBB0_1875:
	s_or_b64 exec, exec, s[28:29]
	s_waitcnt vmcnt(13)
	v_lshlrev_b32_e32 v12, 16, v6
	v_and_b32_e32 v13, 0xffff0000, v6
	v_lshlrev_b32_e32 v6, 16, v7
	v_and_b32_e32 v7, 0xffff0000, v7
	v_pk_add_f32 v[14:15], v[48:49], v[6:7]
	v_pk_add_f32 v[12:13], v[46:47], v[12:13]
	v_lshlrev_b32_e32 v6, 16, v8
	v_and_b32_e32 v7, 0xffff0000, v8
	v_lshlrev_b32_e32 v8, 16, v9
	v_and_b32_e32 v9, 0xffff0000, v9
	v_pk_add_f32 v[16:17], v[44:45], v[8:9]
	v_pk_add_f32 v[8:9], v[42:43], v[6:7]
	v_mul_f32_e32 v6, v13, v13
	v_mul_f32_e32 v7, v15, v15
	v_fmac_f32_e32 v6, v12, v12
	v_fmac_f32_e32 v7, v14, v14
	v_add_f32_e32 v6, v6, v7
	v_mul_f32_e32 v7, v9, v9
	v_mul_f32_e32 v18, v17, v17
	v_fmac_f32_e32 v7, v8, v8
	v_fmac_f32_e32 v18, v16, v16
	v_add_f32_e32 v7, v7, v18
	v_add_f32_e32 v18, v6, v7
	v_cvt_pk_bf16_f32 v6, v12, v13
	v_mul_f32_e32 v12, 0x41000000, v12
	v_med3_f32 v19, v12, s64, v250
	v_mul_f32_e32 v12, 0x41000000, v13
	v_med3_f32 v13, v12, s64, v250
	v_cvt_pk_fp8_f32 v12, v19, v13
	v_cvt_pk_bf16_f32 v7, v14, v15
	v_mul_f32_e32 v13, 0x41000000, v14
	v_mul_f32_e32 v14, 0x41000000, v15
	v_med3_f32 v13, v13, s64, v250
	v_med3_f32 v14, v14, s64, v250
	v_cvt_pk_fp8_f32 v12, v13, v14 op_sel:[0,0,1]
	v_mul_f32_e32 v13, 0x41000000, v8
	v_med3_f32 v14, v13, s64, v250
	v_mul_f32_e32 v13, 0x41000000, v9
	v_med3_f32 v15, v13, s64, v250
	v_cvt_pk_fp8_f32 v13, v14, v15
	v_mul_f32_e32 v14, 0x41000000, v16
	v_mul_f32_e32 v15, 0x41000000, v17
	v_med3_f32 v14, v14, s64, v250
	v_med3_f32 v15, v15, s64, v250
	v_cvt_pk_fp8_f32 v13, v14, v15 op_sel:[0,0,1]
	v_lshlrev_b64 v[10:11], 10, v[32:33]
	v_cvt_pk_bf16_f32 v8, v8, v9
	v_cvt_pk_bf16_f32 v9, v16, v17
	v_lshl_add_u64 v[10:11], v[30:31], 0, v[10:11]
	global_store_dwordx4 v[98:99], v[6:9], off
	global_store_dwordx2 v[10:11], v[12:13], off
	s_waitcnt vmcnt(14)
	v_lshlrev_b32_e32 v6, 16, v2
	v_and_b32_e32 v7, 0xffff0000, v2
	v_lshlrev_b32_e32 v2, 16, v3
	v_and_b32_e32 v3, 0xffff0000, v3
	v_pk_add_f32 v[8:9], v[40:41], v[2:3]
	v_pk_add_f32 v[6:7], v[38:39], v[6:7]
	v_lshlrev_b32_e32 v2, 16, v4
	v_and_b32_e32 v3, 0xffff0000, v4
	v_lshlrev_b32_e32 v4, 16, v5
	v_and_b32_e32 v5, 0xffff0000, v5
	v_pk_add_f32 v[12:13], v[36:37], v[4:5]
	v_pk_add_f32 v[4:5], v[34:35], v[2:3]
	v_mul_f32_e32 v2, v7, v7
	v_mul_f32_e32 v3, v9, v9
	v_fmac_f32_e32 v2, v6, v6
	v_fmac_f32_e32 v3, v8, v8
	v_add_f32_e32 v2, v2, v3
	v_mul_f32_e32 v3, v5, v5
	v_mul_f32_e32 v14, v13, v13
	v_fmac_f32_e32 v3, v4, v4
	v_fmac_f32_e32 v14, v12, v12
	v_add_f32_e32 v3, v3, v14
	v_add_f32_e32 v2, v2, v3
	v_add_f32_e32 v14, v18, v2
	v_cvt_pk_bf16_f32 v2, v6, v7
	v_mul_f32_e32 v6, 0x41000000, v6
	v_med3_f32 v15, v6, s64, v250
	v_mul_f32_e32 v6, 0x41000000, v7
	v_med3_f32 v7, v6, s64, v250
	v_cvt_pk_fp8_f32 v6, v15, v7
	v_cvt_pk_bf16_f32 v3, v8, v9
	v_mul_f32_e32 v7, 0x41000000, v8
	v_mul_f32_e32 v8, 0x41000000, v9
	v_med3_f32 v7, v7, s64, v250
	v_med3_f32 v8, v8, s64, v250
	v_cvt_pk_fp8_f32 v6, v7, v8 op_sel:[0,0,1]
	v_mul_f32_e32 v7, 0x41000000, v4
	v_med3_f32 v8, v7, s64, v250
	v_mul_f32_e32 v7, 0x41000000, v5
	v_med3_f32 v9, v7, s64, v250
	v_cvt_pk_fp8_f32 v7, v8, v9
	v_mul_f32_e32 v8, 0x41000000, v12
	v_mul_f32_e32 v9, 0x41000000, v13
	v_med3_f32 v8, v8, s64, v250
	v_med3_f32 v9, v9, s64, v250
	v_cvt_pk_fp8_f32 v7, v8, v9 op_sel:[0,0,1]
	ds_swizzle_b32 v8, v14 offset:swizzle(SWAP,16)
	v_cvt_pk_bf16_f32 v4, v4, v5
	v_cvt_pk_bf16_f32 v5, v12, v13
	global_store_dwordx4 v[98:99], v[2:5], off offset:256
	global_store_dwordx2 v[10:11], v[6:7], off offset:128
	s_waitcnt lgkmcnt(0)
	v_add_f32_e32 v2, v14, v8
	v_mov_b32_e32 v3, v2
	s_nop 1
	v_permlane32_swap_b32_e32 v2, v3
	s_and_saveexec_b64 s[28:29], s[2:3]
	s_cbranch_execz .LBB0_1877
	v_lshlrev_b64 v[4:5], 6, v[32:33]
	v_lshl_add_u64 v[4:5], s[26:27], 0, v[4:5]
	v_add_f32_e32 v2, v2, v3
	global_store_dword v[4:5], v2, off

; #define GAS __attribute__((address_space(1)))
; #define LAS __attribute__((address_space(3)))
; __device__ __forceinline__ void tr_item(const TrJob& J, int item, LAS float* scr, int lane) {
;     ...
;     for (int j = 0; j < 4; ++j) { const int n = (lane >> 3) + 8 * j; const LAS float* s = scr + (8 * c) * 33 + n;
;         if (J.f8) { int w0 = 0, w1 = 0;
;             w0 = __builtin_amdgcn_cvt_pk_fp8_f32(s[0 * 33] * g[0] * 64.0f, s[1 * 33] * g[1] * 64.0f, w0, false); w0 = __builtin_amdgcn_cvt_pk_fp8_f32(s[2 * 33] * g[2] * 64.0f, s[3 * 33] * g[3] * 64.0f, w0, true);
;             w1 = __builtin_amdgcn_cvt_pk_fp8_f32(s[4 * 33] * g[4] * 64.0f, s[5 * 33] * g[5] * 64.0f, w1, false); w1 = __builtin_amdgcn_cvt_pk_fp8_f32(s[6 * 33] * g[6] * 64.0f, s[7 * 33] * g[7] * 64.0f, w1, true);
;             v2u o; o.x = (unsigned)w0; o.y = (unsigned)w1; *(GAS v2u*)((unsigned char*)J.dst + (size_t)tr_dest_row(J.mode, n0, n) * J.K + k0 + 8 * c) = o; }
.LBB0_1964:
	s_waitcnt lgkmcnt(3)
	v_mul_f32_e32 v10, v10, v20
	v_mul_f32_e32 v40, 0x42800000, v40
	v_mul_f32_e32 v20, 0x42800000, v10
	v_cvt_pk_fp8_f32 v10, v40, v20
	v_mul_f32_e32 v20, v39, v21
	s_waitcnt lgkmcnt(2)
	v_mul_f32_e32 v11, v11, v18
	v_mul_f32_e32 v20, 0x42800000, v20
	v_mul_f32_e32 v11, 0x42800000, v11
	v_cvt_pk_fp8_f32 v10, v20, v11 op_sel:[0,0,1]
	v_mul_f32_e32 v11, v14, v19
	v_mul_f32_e32 v14, 0x42800000, v11
	s_waitcnt lgkmcnt(1)
	v_mul_f32_e32 v11, v12, v16
	v_mul_f32_e32 v12, 0x42800000, v11
	v_cvt_pk_fp8_f32 v11, v14, v12
	v_mul_f32_e32 v12, v15, v17
	s_waitcnt lgkmcnt(0)
	v_mul_f32_e32 v0, v13, v0
	v_mul_f32_e32 v12, 0x42800000, v12
	v_mul_f32_e32 v0, 0x42800000, v0
	v_cvt_pk_fp8_f32 v11, v12, v0 op_sel:[0,0,1]
	v_mov_b64_e32 v[12:13], s[16:17]
	v_mad_u64_u32 v[12:13], s[2:3], v41, s44, v[12:13]
	v_ashrrev_i32_e32 v14, 31, v41
	v_mov_b32_e32 v0, v13
	v_mad_u64_u32 v[14:15], s[2:3], v14, s44, v[0:1]
	v_mov_b32_e32 v13, v14
	v_lshl_add_u64 v[12:13], v[12:13], 0, s[22:23]
	v_lshl_add_u64 v[12:13], v[12:13], 0, v[2:3]
	global_store_dwordx2 v[12:13], v[10:11], off

; #define GAS __attribute__((address_space(1)))
; #define LAS __attribute__((address_space(3)))
; __device__ __forceinline__ void tr_item(const TrJob& J, int item, LAS float* scr, int lane) {
;     ...
;     for (int j = 0; j < 4; ++j) { const int n = (lane >> 3) + 8 * j; const LAS float* s = scr + (8 * c) * 33 + n;
;         if (J.f8) { int w0 = 0, w1 = 0;
;             w0 = __builtin_amdgcn_cvt_pk_fp8_f32(s[0 * 33] * g[0] * 64.0f, s[1 * 33] * g[1] * 64.0f, w0, false); w0 = __builtin_amdgcn_cvt_pk_fp8_f32(s[2 * 33] * g[2] * 64.0f, s[3 * 33] * g[3] * 64.0f, w0, true);
;             w1 = __builtin_amdgcn_cvt_pk_fp8_f32(s[4 * 33] * g[4] * 64.0f, s[5 * 33] * g[5] * 64.0f, w1, false); w1 = __builtin_amdgcn_cvt_pk_fp8_f32(s[6 * 33] * g[6] * 64.0f, s[7 * 33] * g[7] * 64.0f, w1, true);
;             v2u o; o.x = (unsigned)w0; o.y = (unsigned)w1; *(GAS v2u*)((unsigned char*)J.dst + (size_t)tr_dest_row(J.mode, n0, n) * J.K + k0 + 8 * c) = o; }
.LBB0_2073:
	s_waitcnt lgkmcnt(3)
	v_mul_f32_e32 v20, v10, v20
	v_mul_f32_e32 v41, 0x42800000, v41
	v_mul_f32_e32 v43, 0x42800000, v20
	v_cvt_pk_fp8_f32 v20, v41, v43
	v_mul_f32_e32 v21, v39, v21
	s_waitcnt lgkmcnt(2)
	v_mul_f32_e32 v18, v11, v18
	v_mul_f32_e32 v21, 0x42800000, v21
	v_mul_f32_e32 v18, 0x42800000, v18
	v_cvt_pk_fp8_f32 v20, v21, v18 op_sel:[0,0,1]
	v_mul_f32_e32 v18, v14, v19
	s_waitcnt lgkmcnt(1)
	v_mul_f32_e32 v16, v12, v16
	v_mul_f32_e32 v18, 0x42800000, v18
	v_mul_f32_e32 v16, 0x42800000, v16
	v_cvt_pk_fp8_f32 v21, v18, v16
	v_mul_f32_e32 v16, v15, v17
	s_waitcnt lgkmcnt(0)
	v_mul_f32_e32 v0, v13, v0
	v_mul_f32_e32 v16, 0x42800000, v16
	v_mul_f32_e32 v0, 0x42800000, v0
	v_cvt_pk_fp8_f32 v21, v16, v0 op_sel:[0,0,1]
	v_mov_b64_e32 v[16:17], s[16:17]
	v_mad_u64_u32 v[16:17], s[26:27], v42, s44, v[16:17]
	v_ashrrev_i32_e32 v18, 31, v42
	v_mov_b32_e32 v0, v17
	v_mad_u64_u32 v[18:19], s[26:27], v18, s44, v[0:1]
	v_mov_b32_e32 v17, v18
	v_lshl_add_u64 v[16:17], v[16:17], 0, s[22:23]
	v_lshl_add_u64 v[16:17], v[16:17], 0, v[2:3]
	global_store_dwordx2 v[16:17], v[20:21], off
